# v28 + weight-conversion (transpose) stores write-through sc1 (less dirty L2 to flush at the grid barriers)
# speedup vs baseline: 1.0014x; 1.0014x over previous
; #define GAS __attribute__((address_space(1)))
; #define LAS __attribute__((address_space(3)))
; #define LDS_WAIT() asm volatile("s_waitcnt lgkmcnt(0)" ::: "memory")
; __device__ __forceinline__ unsigned pk2(float lo, float hi) { unsigned r; asm("v_cvt_pk_bf16_f32 %0, %1, %2" : "=v"(r) : "v"(lo), "v"(hi)); return r; }
; __device__ __forceinline__ void transpose_item(const float* W, int K, int N, bf16* WT, int drow0, int kb, int n0, LAS float* scr, int lane) {
;     const int k0 = 64 * kb; const int c4 = 4 * (lane & 7); const bool ok = (n0 + c4) < N;
;     f32x4 v[8];
; #pragma unroll
;     for (int i = 0; i < 8; ++i) { const int kk = 8 * i + (lane >> 3); v[i] = ok ? *(const f32x4*)(W + (size_t)(k0 + kk) * N + n0 + c4) : (f32x4){0.f, 0.f, 0.f, 0.f}; }
; #pragma unroll
;     for (int i = 0; i < 8; ++i) { const int kk = 8 * i + (lane >> 3); LAS float* d = scr + kk * 33 + c4; d[0] = v[i][0]; d[1] = v[i][1]; d[2] = v[i][2]; d[3] = v[i][3]; }
;     LDS_WAIT(); asm volatile("" ::: "memory");
;     const int c = lane & 7;
; #pragma unroll
;     for (int j = 0; j < 4; ++j) { const int n = (lane >> 3) + 8 * j; const LAS float* s = scr + (8 * c) * 33 + n;
;         v4u o; o.x = pk2(s[0 * 33], s[1 * 33]); o.y = pk2(s[2 * 33], s[3 * 33]); o.z = pk2(s[4 * 33], s[5 * 33]); o.w = pk2(s[6 * 33], s[7 * 33]);
;         *(GAS v4u*)(WT + (size_t)(drow0 + n) * K + k0 + 8 * c) = o; }
;     LDS_WAIT(); asm volatile("" ::: "memory");
; }
; __device__ __forceinline__ void convert_item(const In& I, unsigned char* ws, int it, LAS float* scr, int lane) {
;     ...
;     { const int jk = r >> 3; r &= 7; const int kb = r >> 1, nb = r & 1;
;         transpose_item(I.nsa_w2 + (size_t)jk * 256 * 64, 256, 64, W2t + (size_t)jk * 64 * 256, 32 * nb, kb, 32 * nb, scr, lane); }
.LBB0_13:
	s_add_i32 s58, s40, 0xa800
	s_cmp_gt_i32 s58, 0x83ff
	s_mov_b64 s[0:1], -1
	s_cbranch_scc0 .LBB0_67
	s_cmpk_gt_u32 s58, 0x8eff
	s_cbranch_scc0 .LBB0_48
	s_cmpk_gt_u32 s58, 0x92ff
	s_cbranch_scc0 .LBB0_45
	s_cmpk_gt_u32 s58, 0x9fff
	s_cbranch_scc0 .LBB0_26
	s_cmpk_gt_u32 s58, 0xa3ff
	s_cbranch_scc0 .LBB0_23
	s_cmpk_gt_u32 s58, 0xa7ff
	s_cbranch_scc0 .LBB0_20
	s_lshr_b32 s8, s40, 3
	v_readlane_b32 s60, v253, 16
	s_lshl_b64 s[0:1], s[8:9], 16
	v_readlane_b32 s64, v253, 20
	v_readlane_b32 s65, v253, 21
	s_add_u32 s10, s64, s0
	s_addc_u32 s11, s65, s1
	s_lshl_b64 s[0:1], s[8:9], 15
	s_add_u32 s8, s38, s0
	s_addc_u32 s1, s39, s1
	s_and_b32 s0, s43, 32
	s_and_b32 s12, s43, 0xc0
	s_lshl_b32 s13, s0, 2
	s_add_u32 s10, s10, s13
	v_or_b32_e32 v4, s12, v44
	s_addc_u32 s11, s11, 0
	v_lshl_add_u64 v[2:3], s[10:11], 0, v[36:37]
	v_lshlrev_b32_e32 v4, 8, v4
	v_mov_b32_e32 v5, v37
	v_lshl_add_u64 v[26:27], v[2:3], 0, v[4:5]
	s_movk_i32 s10, 0x1000
	v_add_co_u32_e32 v14, vcc, s10, v26
	s_movk_i32 s10, 0x3000
	s_nop 0
	v_addc_co_u32_e32 v15, vcc, 0, v27, vcc
	v_add_co_u32_e32 v22, vcc, s47, v26
	global_load_dwordx4 v[2:5], v[26:27], off
	global_load_dwordx4 v[6:9], v[26:27], off offset:2048
	v_addc_co_u32_e32 v23, vcc, 0, v27, vcc
	v_add_co_u32_e32 v30, vcc, s10, v26
	global_load_dwordx4 v[10:13], v[22:23], off offset:-4096
	s_nop 0
	global_load_dwordx4 v[14:17], v[14:15], off offset:2048
	s_nop 0
	global_load_dwordx4 v[18:21], v[22:23], off
	s_nop 0
	global_load_dwordx4 v[22:25], v[22:23], off offset:2048
	v_addc_co_u32_e32 v31, vcc, 0, v27, vcc
	global_load_dwordx4 v[26:29], v[30:31], off
	s_nop 0
	global_load_dwordx4 v[30:33], v[30:31], off offset:2048
	s_lshl_b32 s10, s12, 1
	s_add_u32 s10, s8, s10
	v_mov_b32_e32 v39, v37
	v_or_b32_e32 v40, s0, v44
	s_addc_u32 s11, s1, 0
	v_mov_b32_e32 v41, v37
	v_or_b32_e32 v42, s0, v45
	v_or_b32_e32 v64, s0, v46
	v_lshlrev_b32_e32 v40, 9, v40
	v_lshl_add_u64 v[66:67], s[10:11], 0, v[38:39]
	v_mov_b32_e32 v43, v37
	v_mov_b32_e32 v65, v37
	v_lshlrev_b32_e32 v42, 9, v42
	v_lshlrev_b32_e32 v64, 9, v64
	v_lshl_add_u64 v[40:41], v[66:67], 0, v[40:41]
	v_lshl_add_u64 v[42:43], v[66:67], 0, v[42:43]
	v_lshl_add_u64 v[64:65], v[66:67], 0, v[64:65]
	v_readlane_b32 s61, v253, 17
	v_readlane_b32 s62, v253, 18
	v_readlane_b32 s63, v253, 19
	v_readlane_b32 s66, v253, 22
	v_readlane_b32 s67, v253, 23
	v_readlane_b32 s68, v253, 24
	v_readlane_b32 s69, v253, 25
	v_readlane_b32 s70, v253, 26
	v_readlane_b32 s71, v253, 27
	v_readlane_b32 s72, v253, 28
	v_readlane_b32 s73, v253, 29
	v_readlane_b32 s74, v253, 30
	v_readlane_b32 s75, v253, 31
	s_waitcnt vmcnt(7)
	ds_write2_b32 v49, v2, v3 offset1:1
	ds_write2_b32 v49, v4, v5 offset0:2 offset1:3
	s_waitcnt vmcnt(6)
	ds_write2_b32 v50, v6, v7 offset1:1
	ds_write2_b32 v51, v8, v9 offset1:1
	s_waitcnt vmcnt(5)
	ds_write2_b32 v52, v10, v11 offset1:1
	ds_write2_b32 v53, v12, v13 offset1:1
	s_waitcnt vmcnt(4)
	ds_write2_b32 v54, v14, v15 offset1:1
	ds_write2_b32 v55, v16, v17 offset1:1
	s_waitcnt vmcnt(3)
	ds_write2_b32 v56, v18, v19 offset1:1
	ds_write2_b32 v57, v20, v21 offset1:1
	s_waitcnt vmcnt(2)
	ds_write2_b32 v58, v22, v23 offset1:1
	ds_write2_b32 v59, v24, v25 offset1:1
	s_waitcnt vmcnt(1)
	ds_write2_b32 v60, v26, v27 offset1:1
	ds_write2_b32 v61, v28, v29 offset1:1
	s_waitcnt vmcnt(0)
	ds_write2_b32 v62, v30, v31 offset1:1
	ds_write2_b32 v63, v32, v33 offset1:1
	s_waitcnt lgkmcnt(0)
	ds_read2_b32 v[6:7], v48 offset0:33 offset1:41
	ds_read2_b32 v[8:9], v48 offset1:8
	ds_read2_b32 v[10:11], v48 offset0:66 offset1:74
	ds_read2_b32 v[12:13], v48 offset0:99 offset1:107
	ds_read2_b32 v[14:15], v48 offset0:132 offset1:140
	ds_read2_b32 v[16:17], v48 offset0:165 offset1:173
	ds_read2_b32 v[18:19], v48 offset0:198 offset1:206
	ds_read2_b32 v[20:21], v48 offset0:231 offset1:239
	ds_read2_b32 v[22:23], v48 offset0:16 offset1:24
	ds_read2_b32 v[24:25], v48 offset0:49 offset1:57
	ds_read2_b32 v[26:27], v48 offset0:82 offset1:90
	ds_read2_b32 v[28:29], v48 offset0:115 offset1:123
	ds_read2_b32 v[30:31], v48 offset0:148 offset1:156
	ds_read2_b32 v[32:33], v48 offset0:181 offset1:189
	ds_read2_b32 v[68:69], v48 offset0:214 offset1:222
	ds_read2_b32 v[70:71], v48 offset0:247 offset1:255
	s_waitcnt lgkmcnt(14)
	v_cvt_pk_bf16_f32 v2, v8, v6
	s_waitcnt lgkmcnt(12)
	v_cvt_pk_bf16_f32 v3, v10, v12
	s_waitcnt lgkmcnt(10)
	v_cvt_pk_bf16_f32 v4, v14, v16
	s_waitcnt lgkmcnt(8)
	v_cvt_pk_bf16_f32 v5, v18, v20
	v_cvt_pk_bf16_f32 v6, v9, v7
	v_cvt_pk_bf16_f32 v7, v11, v13
	v_cvt_pk_bf16_f32 v8, v15, v17
	v_cvt_pk_bf16_f32 v9, v19, v21
	s_waitcnt lgkmcnt(6)
	v_cvt_pk_bf16_f32 v10, v22, v24
	s_waitcnt lgkmcnt(4)
	v_cvt_pk_bf16_f32 v11, v26, v28
	s_waitcnt lgkmcnt(2)
	v_cvt_pk_bf16_f32 v12, v30, v32
	s_waitcnt lgkmcnt(0)
	v_cvt_pk_bf16_f32 v13, v68, v70
	global_store_dwordx4 v[40:41], v[2:5], off sc1
	global_store_dwordx4 v[42:43], v[6:9], off sc1
	global_store_dwordx4 v[64:65], v[10:13], off sc1
	v_cvt_pk_bf16_f32 v2, v23, v25
	v_cvt_pk_bf16_f32 v3, v27, v29
	v_cvt_pk_bf16_f32 v4, v31, v33
	v_cvt_pk_bf16_f32 v5, v69, v71
	s_nop 0
	v_or_b32_e32 v6, s0, v47
	v_lshlrev_b32_e32 v6, 9, v6
	v_mov_b32_e32 v7, v37
	v_lshl_add_u64 v[6:7], v[66:67], 0, v[6:7]
	global_store_dwordx4 v[6:7], v[2:5], off sc1
	s_waitcnt lgkmcnt(0)
	s_mov_b64 s[0:1], 0
; #define GAS __attribute__((address_space(1)))
; #define LAS __attribute__((address_space(3)))
; #define LDS_WAIT() asm volatile("s_waitcnt lgkmcnt(0)" ::: "memory")
; __device__ __forceinline__ unsigned pk2(float lo, float hi) { unsigned r; asm("v_cvt_pk_bf16_f32 %0, %1, %2" : "=v"(r) : "v"(lo), "v"(hi)); return r; }
; __device__ __forceinline__ void transpose_item(const float* W, int K, int N, bf16* WT, int drow0, int kb, int n0, LAS float* scr, int lane) {
;     const int k0 = 64 * kb; const int c4 = 4 * (lane & 7); const bool ok = (n0 + c4) < N;
;     f32x4 v[8];
; #pragma unroll
;     for (int i = 0; i < 8; ++i) { const int kk = 8 * i + (lane >> 3); v[i] = ok ? *(const f32x4*)(W + (size_t)(k0 + kk) * N + n0 + c4) : (f32x4){0.f, 0.f, 0.f, 0.f}; }
; #pragma unroll
;     for (int i = 0; i < 8; ++i) { const int kk = 8 * i + (lane >> 3); LAS float* d = scr + kk * 33 + c4; d[0] = v[i][0]; d[1] = v[i][1]; d[2] = v[i][2]; d[3] = v[i][3]; }
;     LDS_WAIT(); asm volatile("" ::: "memory");
;     const int c = lane & 7;
; #pragma unroll
;     for (int j = 0; j < 4; ++j) { const int n = (lane >> 3) + 8 * j; const LAS float* s = scr + (8 * c) * 33 + n;
;         v4u o; o.x = pk2(s[0 * 33], s[1 * 33]); o.y = pk2(s[2 * 33], s[3 * 33]); o.z = pk2(s[4 * 33], s[5 * 33]); o.w = pk2(s[6 * 33], s[7 * 33]);
;         *(GAS v4u*)(WT + (size_t)(drow0 + n) * K + k0 + 8 * c) = o; }
;     LDS_WAIT(); asm volatile("" ::: "memory");
; }
.LBB0_20:
	s_andn2_b64 vcc, exec, s[0:1]
	s_cbranch_vccnz .LBB0_22
	s_add_i32 s0, s40, 0x400
	s_lshr_b32 s8, s0, 8
	s_lshl_b64 s[0:1], s[8:9], 21
	v_readlane_b32 s60, v253, 16
	v_readlane_b32 s61, v253, 17
	s_add_u32 s10, s60, s0
	s_addc_u32 s11, s61, s1
	s_lshl_b64 s[0:1], s[8:9], 20
	s_add_u32 s8, s36, s0
	s_addc_u32 s1, s37, s1
	s_and_b32 s0, s43, 0xe0
	s_and_b32 s12, s41, 0x7c0
	s_lshl_b32 s13, s0, 2
	s_add_u32 s10, s10, s13
	v_or_b32_e32 v4, s12, v44
	s_addc_u32 s11, s11, 0
	v_lshl_add_u64 v[2:3], s[10:11], 0, v[36:37]
	v_lshlrev_b32_e32 v4, 10, v4
	v_mov_b32_e32 v5, v37
	v_lshl_add_u64 v[30:31], v[2:3], 0, v[4:5]
	v_add_co_u32_e32 v6, vcc, s47, v30
	s_movk_i32 s10, 0x4000
	s_nop 0
	v_addc_co_u32_e32 v7, vcc, 0, v31, vcc
	v_add_co_u32_e32 v10, vcc, s10, v30
	s_movk_i32 s10, 0x6000
	s_nop 0
	v_addc_co_u32_e32 v11, vcc, 0, v31, vcc
	v_add_co_u32_e32 v14, vcc, s10, v30
	s_mov_b32 s10, 0xa000
	s_nop 0
	v_addc_co_u32_e32 v15, vcc, 0, v31, vcc
	v_add_co_u32_e32 v18, vcc, s48, v30
	global_load_dwordx4 v[2:5], v[30:31], off
	s_nop 0
	global_load_dwordx4 v[6:9], v[6:7], off
	v_addc_co_u32_e32 v19, vcc, 0, v31, vcc
	v_add_co_u32_e32 v22, vcc, s10, v30
	global_load_dwordx4 v[10:13], v[10:11], off
	s_nop 0
	global_load_dwordx4 v[14:17], v[14:15], off
	v_addc_co_u32_e32 v23, vcc, 0, v31, vcc
	global_load_dwordx4 v[18:21], v[18:19], off
	s_nop 0
	global_load_dwordx4 v[22:25], v[22:23], off
	s_mov_b32 s10, 0xc000
	v_add_co_u32_e32 v26, vcc, s10, v30
	s_mov_b32 s10, 0xe000
	s_nop 0
	v_addc_co_u32_e32 v27, vcc, 0, v31, vcc
	global_load_dwordx4 v[26:29], v[26:27], off
	v_add_co_u32_e32 v30, vcc, s10, v30
	s_lshl_b32 s10, s12, 1
	s_nop 0
	v_addc_co_u32_e32 v31, vcc, 0, v31, vcc
	global_load_dwordx4 v[30:33], v[30:31], off
	s_add_u32 s10, s8, s10
	v_mov_b32_e32 v39, v37
	v_or_b32_e32 v40, s0, v44
	s_addc_u32 s11, s1, 0
	v_mov_b32_e32 v41, v37
	v_lshlrev_b32_e32 v40, 12, v40
	v_lshl_add_u64 v[64:65], s[10:11], 0, v[38:39]
	v_lshl_add_u64 v[40:41], v[64:65], 0, v[40:41]
	v_or_b32_e32 v42, s0, v45
	v_mov_b32_e32 v43, v37
	v_lshlrev_b32_e32 v42, 12, v42
	v_lshl_add_u64 v[42:43], v[64:65], 0, v[42:43]
	v_readlane_b32 s62, v253, 18
	v_readlane_b32 s63, v253, 19
	v_readlane_b32 s64, v253, 20
	v_readlane_b32 s65, v253, 21
	v_readlane_b32 s66, v253, 22
	v_readlane_b32 s67, v253, 23
	v_readlane_b32 s68, v253, 24
	v_readlane_b32 s69, v253, 25
	v_readlane_b32 s70, v253, 26
	v_readlane_b32 s71, v253, 27
	v_readlane_b32 s72, v253, 28
	v_readlane_b32 s73, v253, 29
	v_readlane_b32 s74, v253, 30
	v_readlane_b32 s75, v253, 31
	s_waitcnt vmcnt(7)
	ds_write2_b32 v49, v2, v3 offset1:1
	ds_write2_b32 v49, v4, v5 offset0:2 offset1:3
	s_waitcnt vmcnt(6)
	ds_write2_b32 v50, v6, v7 offset1:1
	ds_write2_b32 v51, v8, v9 offset1:1
	s_waitcnt vmcnt(5)
	ds_write2_b32 v52, v10, v11 offset1:1
	ds_write2_b32 v53, v12, v13 offset1:1
	s_waitcnt vmcnt(4)
	ds_write2_b32 v54, v14, v15 offset1:1
	ds_write2_b32 v55, v16, v17 offset1:1
	s_waitcnt vmcnt(3)
	ds_write2_b32 v56, v18, v19 offset1:1
	ds_write2_b32 v57, v20, v21 offset1:1
	s_waitcnt vmcnt(2)
	ds_write2_b32 v58, v22, v23 offset1:1
	ds_write2_b32 v59, v24, v25 offset1:1
	s_waitcnt vmcnt(1)
	ds_write2_b32 v60, v26, v27 offset1:1
	ds_write2_b32 v61, v28, v29 offset1:1
	s_waitcnt vmcnt(0)
	ds_write2_b32 v62, v30, v31 offset1:1
	ds_write2_b32 v63, v32, v33 offset1:1
	s_waitcnt lgkmcnt(0)
	ds_read2_b32 v[6:7], v48 offset0:33 offset1:41
	ds_read2_b32 v[8:9], v48 offset1:8
	ds_read2_b32 v[10:11], v48 offset0:66 offset1:74
	ds_read2_b32 v[12:13], v48 offset0:99 offset1:107
	ds_read2_b32 v[14:15], v48 offset0:132 offset1:140
	ds_read2_b32 v[16:17], v48 offset0:165 offset1:173
	ds_read2_b32 v[18:19], v48 offset0:198 offset1:206
	ds_read2_b32 v[20:21], v48 offset0:231 offset1:239
	ds_read2_b32 v[22:23], v48 offset0:16 offset1:24
	ds_read2_b32 v[24:25], v48 offset0:49 offset1:57
	s_waitcnt lgkmcnt(8)
	v_cvt_pk_bf16_f32 v2, v8, v6
	s_waitcnt lgkmcnt(6)
	v_cvt_pk_bf16_f32 v3, v10, v12
	s_waitcnt lgkmcnt(4)
	v_cvt_pk_bf16_f32 v4, v14, v16
	s_waitcnt lgkmcnt(2)
	v_cvt_pk_bf16_f32 v5, v18, v20
	global_store_dwordx4 v[40:41], v[2:5], off sc1
	v_cvt_pk_bf16_f32 v6, v9, v7
	v_cvt_pk_bf16_f32 v7, v11, v13
	v_cvt_pk_bf16_f32 v8, v15, v17
	v_cvt_pk_bf16_f32 v9, v19, v21
	ds_read2_b32 v[10:11], v48 offset0:82 offset1:90
	ds_read2_b32 v[12:13], v48 offset0:115 offset1:123
	ds_read2_b32 v[14:15], v48 offset0:148 offset1:156
	ds_read2_b32 v[16:17], v48 offset0:181 offset1:189
	ds_read2_b32 v[18:19], v48 offset0:214 offset1:222
	ds_read2_b32 v[20:21], v48 offset0:247 offset1:255
	global_store_dwordx4 v[42:43], v[6:9], off sc1
	s_waitcnt lgkmcnt(6)
	v_cvt_pk_bf16_f32 v2, v22, v24
	s_waitcnt lgkmcnt(4)
	v_cvt_pk_bf16_f32 v3, v10, v12
	s_waitcnt lgkmcnt(2)
	v_cvt_pk_bf16_f32 v4, v14, v16
	s_waitcnt lgkmcnt(0)
	v_cvt_pk_bf16_f32 v5, v18, v20
	v_or_b32_e32 v6, s0, v46
	v_lshlrev_b32_e32 v6, 12, v6
	v_mov_b32_e32 v7, v37
	v_lshl_add_u64 v[6:7], v[64:65], 0, v[6:7]
	global_store_dwordx4 v[6:7], v[2:5], off sc1
	v_or_b32_e32 v6, s0, v47
	v_lshlrev_b32_e32 v6, 12, v6
	v_mov_b32_e32 v7, v37
	v_lshl_add_u64 v[6:7], v[64:65], 0, v[6:7]
	v_cvt_pk_bf16_f32 v2, v23, v25
	v_cvt_pk_bf16_f32 v3, v11, v13
	v_cvt_pk_bf16_f32 v4, v15, v17
	v_cvt_pk_bf16_f32 v5, v19, v21
	global_store_dwordx4 v[6:7], v[2:5], off sc1
	s_waitcnt lgkmcnt(0)

; #define GAS __attribute__((address_space(1)))
; #define LAS __attribute__((address_space(3)))
; #define LDS_WAIT() asm volatile("s_waitcnt lgkmcnt(0)" ::: "memory")
; __device__ __forceinline__ unsigned pk2(float lo, float hi) { unsigned r; asm("v_cvt_pk_bf16_f32 %0, %1, %2" : "=v"(r) : "v"(lo), "v"(hi)); return r; }
; __device__ __forceinline__ void transpose_item(const float* W, int K, int N, bf16* WT, int drow0, int kb, int n0, LAS float* scr, int lane) {
;     const int k0 = 64 * kb; const int c4 = 4 * (lane & 7); const bool ok = (n0 + c4) < N;
;     f32x4 v[8];
; #pragma unroll
;     for (int i = 0; i < 8; ++i) { const int kk = 8 * i + (lane >> 3); v[i] = ok ? *(const f32x4*)(W + (size_t)(k0 + kk) * N + n0 + c4) : (f32x4){0.f, 0.f, 0.f, 0.f}; }
; #pragma unroll
;     for (int i = 0; i < 8; ++i) { const int kk = 8 * i + (lane >> 3); LAS float* d = scr + kk * 33 + c4; d[0] = v[i][0]; d[1] = v[i][1]; d[2] = v[i][2]; d[3] = v[i][3]; }
;     LDS_WAIT(); asm volatile("" ::: "memory");
;     const int c = lane & 7;
; #pragma unroll
;     for (int j = 0; j < 4; ++j) { const int n = (lane >> 3) + 8 * j; const LAS float* s = scr + (8 * c) * 33 + n;
;         v4u o; o.x = pk2(s[0 * 33], s[1 * 33]); o.y = pk2(s[2 * 33], s[3 * 33]); o.z = pk2(s[4 * 33], s[5 * 33]); o.w = pk2(s[6 * 33], s[7 * 33]);
;         *(GAS v4u*)(WT + (size_t)(drow0 + n) * K + k0 + 8 * c) = o; }
;     LDS_WAIT(); asm volatile("" ::: "memory");
; }
.LBB0_23:
	s_andn2_b64 vcc, exec, s[0:1]
	s_cbranch_vccnz .LBB0_25
	s_add_i32 s0, s40, 0x800
	s_lshr_b32 s8, s0, 9
	v_readlane_b32 s60, v253, 16
	s_lshl_b64 s[0:1], s[8:9], 22
	v_readlane_b32 s72, v253, 28
	v_readlane_b32 s73, v253, 29
	s_add_u32 s10, s72, s0
	s_addc_u32 s11, s73, s1
	s_lshl_b64 s[0:1], s[8:9], 21
	s_add_u32 s8, s34, s0
	s_addc_u32 s1, s35, s1
	s_and_b32 s0, s43, 0x3e0
	s_and_b32 s12, s45, 0x3c0
	s_lshl_b32 s13, s0, 2
	s_add_u32 s10, s10, s13
	v_or_b32_e32 v4, s12, v44
	s_addc_u32 s11, s11, 0
	v_lshl_add_u64 v[2:3], s[10:11], 0, v[36:37]
	v_lshlrev_b32_e32 v4, 12, v4
	v_mov_b32_e32 v5, v37
	v_lshl_add_u64 v[30:31], v[2:3], 0, v[4:5]
	v_add_co_u32_e32 v6, vcc, s48, v30
	s_lshl_b32 s10, s12, 1
	s_nop 0
	v_addc_co_u32_e32 v7, vcc, 0, v31, vcc
	v_add_co_u32_e32 v10, vcc, s49, v30
	global_load_dwordx4 v[2:5], v[30:31], off
	s_nop 0
	global_load_dwordx4 v[6:9], v[6:7], off
	v_addc_co_u32_e32 v11, vcc, 0, v31, vcc
	v_add_co_u32_e32 v14, vcc, s50, v30
	s_add_u32 s10, s8, s10
	s_nop 0
	v_addc_co_u32_e32 v15, vcc, 0, v31, vcc
	v_add_co_u32_e32 v18, vcc, s51, v30
	global_load_dwordx4 v[10:13], v[10:11], off
	s_nop 0
	global_load_dwordx4 v[14:17], v[14:15], off
	v_addc_co_u32_e32 v19, vcc, 0, v31, vcc
	v_add_co_u32_e32 v22, vcc, s52, v30
	v_mov_b32_e32 v39, v37
	s_nop 0
	v_addc_co_u32_e32 v23, vcc, 0, v31, vcc
	global_load_dwordx4 v[18:21], v[18:19], off
	s_nop 0
	global_load_dwordx4 v[22:25], v[22:23], off
	v_add_co_u32_e32 v26, vcc, s53, v30
	v_or_b32_e32 v40, s0, v44
	s_nop 0
	v_addc_co_u32_e32 v27, vcc, 0, v31, vcc
	global_load_dwordx4 v[26:29], v[26:27], off
	v_add_co_u32_e32 v30, vcc, s54, v30
	s_addc_u32 s11, s1, 0
	s_nop 0
	v_addc_co_u32_e32 v31, vcc, 0, v31, vcc
	global_load_dwordx4 v[30:33], v[30:31], off
	v_mov_b32_e32 v41, v37
	v_lshlrev_b32_e32 v40, 11, v40
	v_lshl_add_u64 v[64:65], s[10:11], 0, v[38:39]
	v_lshl_add_u64 v[40:41], v[64:65], 0, v[40:41]
	v_or_b32_e32 v42, s0, v45
	v_mov_b32_e32 v43, v37
	v_lshlrev_b32_e32 v42, 11, v42
	v_lshl_add_u64 v[42:43], v[64:65], 0, v[42:43]
	v_readlane_b32 s61, v253, 17
	v_readlane_b32 s62, v253, 18
	v_readlane_b32 s63, v253, 19
	v_readlane_b32 s64, v253, 20
	v_readlane_b32 s65, v253, 21
	v_readlane_b32 s66, v253, 22
	v_readlane_b32 s67, v253, 23
	v_readlane_b32 s68, v253, 24
	v_readlane_b32 s69, v253, 25
	v_readlane_b32 s70, v253, 26
	v_readlane_b32 s71, v253, 27
	v_readlane_b32 s74, v253, 30
	v_readlane_b32 s75, v253, 31
	s_waitcnt vmcnt(7)
	ds_write2_b32 v49, v2, v3 offset1:1
	ds_write2_b32 v49, v4, v5 offset0:2 offset1:3
	s_waitcnt vmcnt(6)
	ds_write2_b32 v50, v6, v7 offset1:1
	ds_write2_b32 v51, v8, v9 offset1:1
	s_waitcnt vmcnt(5)
	ds_write2_b32 v52, v10, v11 offset1:1
	ds_write2_b32 v53, v12, v13 offset1:1
	s_waitcnt vmcnt(4)
	ds_write2_b32 v54, v14, v15 offset1:1
	ds_write2_b32 v55, v16, v17 offset1:1
	s_waitcnt vmcnt(3)
	ds_write2_b32 v56, v18, v19 offset1:1
	ds_write2_b32 v57, v20, v21 offset1:1
	s_waitcnt vmcnt(2)
	ds_write2_b32 v58, v22, v23 offset1:1
	ds_write2_b32 v59, v24, v25 offset1:1
	s_waitcnt vmcnt(1)
	ds_write2_b32 v60, v26, v27 offset1:1
	ds_write2_b32 v61, v28, v29 offset1:1
	s_waitcnt vmcnt(0)
	ds_write2_b32 v62, v30, v31 offset1:1
	ds_write2_b32 v63, v32, v33 offset1:1
	s_waitcnt lgkmcnt(0)
	ds_read2_b32 v[6:7], v48 offset0:33 offset1:41
	ds_read2_b32 v[8:9], v48 offset1:8
	ds_read2_b32 v[10:11], v48 offset0:66 offset1:74
	ds_read2_b32 v[12:13], v48 offset0:99 offset1:107
	ds_read2_b32 v[14:15], v48 offset0:132 offset1:140
	ds_read2_b32 v[16:17], v48 offset0:165 offset1:173
	ds_read2_b32 v[18:19], v48 offset0:198 offset1:206
	ds_read2_b32 v[20:21], v48 offset0:231 offset1:239
	ds_read2_b32 v[22:23], v48 offset0:16 offset1:24
	ds_read2_b32 v[24:25], v48 offset0:49 offset1:57
	s_waitcnt lgkmcnt(8)
	v_cvt_pk_bf16_f32 v2, v8, v6
	s_waitcnt lgkmcnt(6)
	v_cvt_pk_bf16_f32 v3, v10, v12
	s_waitcnt lgkmcnt(4)
	v_cvt_pk_bf16_f32 v4, v14, v16
	s_waitcnt lgkmcnt(2)
	v_cvt_pk_bf16_f32 v5, v18, v20
	global_store_dwordx4 v[40:41], v[2:5], off sc1
	v_cvt_pk_bf16_f32 v6, v9, v7
	v_cvt_pk_bf16_f32 v7, v11, v13
	v_cvt_pk_bf16_f32 v8, v15, v17
	v_cvt_pk_bf16_f32 v9, v19, v21
	ds_read2_b32 v[10:11], v48 offset0:82 offset1:90
	ds_read2_b32 v[12:13], v48 offset0:115 offset1:123
	ds_read2_b32 v[14:15], v48 offset0:148 offset1:156
	ds_read2_b32 v[16:17], v48 offset0:181 offset1:189
	ds_read2_b32 v[18:19], v48 offset0:214 offset1:222
	ds_read2_b32 v[20:21], v48 offset0:247 offset1:255
	global_store_dwordx4 v[42:43], v[6:9], off sc1
	s_waitcnt lgkmcnt(6)
	v_cvt_pk_bf16_f32 v2, v22, v24
	s_waitcnt lgkmcnt(4)
	v_cvt_pk_bf16_f32 v3, v10, v12
	s_waitcnt lgkmcnt(2)
	v_cvt_pk_bf16_f32 v4, v14, v16
	s_waitcnt lgkmcnt(0)
	v_cvt_pk_bf16_f32 v5, v18, v20
	v_or_b32_e32 v6, s0, v46
	v_lshlrev_b32_e32 v6, 11, v6
	v_mov_b32_e32 v7, v37
	v_lshl_add_u64 v[6:7], v[64:65], 0, v[6:7]
	global_store_dwordx4 v[6:7], v[2:5], off sc1
	v_or_b32_e32 v6, s0, v47
	v_lshlrev_b32_e32 v6, 11, v6
	v_mov_b32_e32 v7, v37
	v_lshl_add_u64 v[6:7], v[64:65], 0, v[6:7]
	v_cvt_pk_bf16_f32 v2, v23, v25
	v_cvt_pk_bf16_f32 v3, v11, v13
	v_cvt_pk_bf16_f32 v4, v15, v17
	v_cvt_pk_bf16_f32 v5, v19, v21
	global_store_dwordx4 v[6:7], v[2:5], off sc1
	s_waitcnt lgkmcnt(0)

; #define GAS __attribute__((address_space(1)))
; #define LAS __attribute__((address_space(3)))
; #define LDS_WAIT() asm volatile("s_waitcnt lgkmcnt(0)" ::: "memory")
; __device__ __forceinline__ unsigned pk2(float lo, float hi) { unsigned r; asm("v_cvt_pk_bf16_f32 %0, %1, %2" : "=v"(r) : "v"(lo), "v"(hi)); return r; }
; __device__ __forceinline__ void transpose_item(const float* W, int K, int N, bf16* WT, int drow0, int kb, int n0, LAS float* scr, int lane) {
;     ...
;     for (int i = 0; i < 8; ++i) { const int kk = 8 * i + (lane >> 3); v[i] = ok ? *(const f32x4*)(W + (size_t)(k0 + kk) * N + n0 + c4) : (f32x4){0.f, 0.f, 0.f, 0.f}; }
; #pragma unroll
;     for (int i = 0; i < 8; ++i) { const int kk = 8 * i + (lane >> 3); LAS float* d = scr + kk * 33 + c4; d[0] = v[i][0]; d[1] = v[i][1]; d[2] = v[i][2]; d[3] = v[i][3]; }
;     LDS_WAIT(); asm volatile("" ::: "memory");
;     const int c = lane & 7;
; #pragma unroll
;     for (int j = 0; j < 4; ++j) { const int n = (lane >> 3) + 8 * j; const LAS float* s = scr + (8 * c) * 33 + n;
;         v4u o; o.x = pk2(s[0 * 33], s[1 * 33]); o.y = pk2(s[2 * 33], s[3 * 33]); o.z = pk2(s[4 * 33], s[5 * 33]); o.w = pk2(s[6 * 33], s[7 * 33]);
;         *(GAS v4u*)(WT + (size_t)(drow0 + n) * K + k0 + 8 * c) = o; }
;     LDS_WAIT(); asm volatile("" ::: "memory");
.LBB0_43:
	s_or_b64 exec, exec, s[16:17]
	s_and_b64 s[0:1], s[14:15], exec
	s_cselect_b32 s0, 0x680000, 0
	s_waitcnt vmcnt(0)
	ds_write2_b32 v49, v2, v3 offset1:1
	ds_write2_b32 v49, v4, v5 offset0:2 offset1:3
	ds_write2_b32 v50, v6, v7 offset1:1
	ds_write2_b32 v51, v8, v9 offset1:1
	ds_write2_b32 v52, v14, v15 offset1:1
	ds_write2_b32 v53, v16, v17 offset1:1
	ds_write2_b32 v54, v10, v11 offset1:1
	ds_write2_b32 v55, v12, v13 offset1:1
	ds_write2_b32 v56, v22, v23 offset1:1
	ds_write2_b32 v57, v24, v25 offset1:1
	ds_write2_b32 v58, v18, v19 offset1:1
	ds_write2_b32 v59, v20, v21 offset1:1
	ds_write2_b32 v60, v30, v31 offset1:1
	ds_write2_b32 v61, v32, v33 offset1:1
	ds_write2_b32 v62, v26, v27 offset1:1
	ds_write2_b32 v63, v28, v29 offset1:1
	s_add_u32 s8, s31, s0
	s_waitcnt lgkmcnt(0)
	s_addc_u32 s11, s33, 0
	s_ashr_i32 s13, s12, 31
	s_lshl_b64 s[0:1], s[12:13], 1
	ds_read2_b32 v[6:7], v48 offset0:33 offset1:41
	ds_read2_b32 v[8:9], v48 offset1:8
	ds_read2_b32 v[10:11], v48 offset0:66 offset1:74
	ds_read2_b32 v[12:13], v48 offset0:99 offset1:107
	ds_read2_b32 v[14:15], v48 offset0:132 offset1:140
	ds_read2_b32 v[16:17], v48 offset0:165 offset1:173
	ds_read2_b32 v[18:19], v48 offset0:198 offset1:206
	ds_read2_b32 v[20:21], v48 offset0:231 offset1:239
	s_add_u32 s0, s8, s0
	v_or_b32_e32 v24, s10, v44
	s_addc_u32 s1, s11, s1
	v_mov_b32_e32 v39, v37
	v_ashrrev_i32_e32 v25, 31, v24
	v_lshl_add_u64 v[22:23], s[0:1], 0, v[38:39]
	v_lshlrev_b64 v[24:25], 11, v[24:25]
	s_waitcnt lgkmcnt(6)
	v_cvt_pk_bf16_f32 v2, v8, v6
	v_lshl_add_u64 v[24:25], v[22:23], 0, v[24:25]
	v_or_b32_e32 v6, s10, v45
	s_waitcnt lgkmcnt(4)
	v_cvt_pk_bf16_f32 v3, v10, v12
	s_waitcnt lgkmcnt(2)
	v_cvt_pk_bf16_f32 v4, v14, v16
	s_waitcnt lgkmcnt(0)
	v_cvt_pk_bf16_f32 v5, v18, v20
	global_store_dwordx4 v[24:25], v[2:5], off sc1
	s_nop 1
	v_cvt_pk_bf16_f32 v2, v9, v7
	v_ashrrev_i32_e32 v7, 31, v6
	v_lshlrev_b64 v[6:7], 11, v[6:7]
	v_cvt_pk_bf16_f32 v3, v11, v13
	v_cvt_pk_bf16_f32 v4, v15, v17
	v_cvt_pk_bf16_f32 v5, v19, v21
	v_lshl_add_u64 v[6:7], v[22:23], 0, v[6:7]
	ds_read2_b32 v[8:9], v48 offset0:16 offset1:24
	ds_read2_b32 v[10:11], v48 offset0:49 offset1:57
	ds_read2_b32 v[12:13], v48 offset0:82 offset1:90
	ds_read2_b32 v[14:15], v48 offset0:115 offset1:123
	ds_read2_b32 v[16:17], v48 offset0:148 offset1:156
	ds_read2_b32 v[18:19], v48 offset0:181 offset1:189
	ds_read2_b32 v[20:21], v48 offset0:214 offset1:222
	ds_read2_b32 v[24:25], v48 offset0:247 offset1:255
	global_store_dwordx4 v[6:7], v[2:5], off sc1
	v_or_b32_e32 v6, s10, v46
	v_ashrrev_i32_e32 v7, 31, v6
	v_lshlrev_b64 v[6:7], 11, v[6:7]
	v_lshl_add_u64 v[6:7], v[22:23], 0, v[6:7]
	s_waitcnt lgkmcnt(6)
	v_cvt_pk_bf16_f32 v2, v8, v10
	s_waitcnt lgkmcnt(4)
	v_cvt_pk_bf16_f32 v3, v12, v14
	s_waitcnt lgkmcnt(2)
	v_cvt_pk_bf16_f32 v4, v16, v18
	s_waitcnt lgkmcnt(0)
	v_cvt_pk_bf16_f32 v5, v20, v24
	global_store_dwordx4 v[6:7], v[2:5], off sc1
	v_or_b32_e32 v6, s10, v47
	v_ashrrev_i32_e32 v7, 31, v6
	v_lshlrev_b64 v[6:7], 11, v[6:7]
	v_lshl_add_u64 v[6:7], v[22:23], 0, v[6:7]
	v_cvt_pk_bf16_f32 v2, v9, v11
	v_cvt_pk_bf16_f32 v3, v13, v15
	v_cvt_pk_bf16_f32 v4, v17, v19
	v_cvt_pk_bf16_f32 v5, v21, v25
	global_store_dwordx4 v[6:7], v[2:5], off sc1
	s_waitcnt lgkmcnt(0)

; #define GAS __attribute__((address_space(1)))
; #define LAS __attribute__((address_space(3)))
; #define LDS_WAIT() asm volatile("s_waitcnt lgkmcnt(0)" ::: "memory")
; __device__ __forceinline__ unsigned pk2(float lo, float hi) { unsigned r; asm("v_cvt_pk_bf16_f32 %0, %1, %2" : "=v"(r) : "v"(lo), "v"(hi)); return r; }
; __device__ __forceinline__ void transpose_item(const float* W, int K, int N, bf16* WT, int drow0, int kb, int n0, LAS float* scr, int lane) {
;     const int k0 = 64 * kb; const int c4 = 4 * (lane & 7); const bool ok = (n0 + c4) < N;
;     f32x4 v[8];
; #pragma unroll
;     for (int i = 0; i < 8; ++i) { const int kk = 8 * i + (lane >> 3); v[i] = ok ? *(const f32x4*)(W + (size_t)(k0 + kk) * N + n0 + c4) : (f32x4){0.f, 0.f, 0.f, 0.f}; }
; #pragma unroll
;     for (int i = 0; i < 8; ++i) { const int kk = 8 * i + (lane >> 3); LAS float* d = scr + kk * 33 + c4; d[0] = v[i][0]; d[1] = v[i][1]; d[2] = v[i][2]; d[3] = v[i][3]; }
;     LDS_WAIT(); asm volatile("" ::: "memory");
;     const int c = lane & 7;
; #pragma unroll
;     for (int j = 0; j < 4; ++j) { const int n = (lane >> 3) + 8 * j; const LAS float* s = scr + (8 * c) * 33 + n;
;         v4u o; o.x = pk2(s[0 * 33], s[1 * 33]); o.y = pk2(s[2 * 33], s[3 * 33]); o.z = pk2(s[4 * 33], s[5 * 33]); o.w = pk2(s[6 * 33], s[7 * 33]);
;         *(GAS v4u*)(WT + (size_t)(drow0 + n) * K + k0 + 8 * c) = o; }
;     LDS_WAIT(); asm volatile("" ::: "memory");
; }
.LBB0_45:
	s_andn2_b64 vcc, exec, s[0:1]
	s_cbranch_vccnz .LBB0_47
	s_add_i32 s0, s40, 0x1900
	s_lshr_b32 s8, s0, 9
	v_readlane_b32 s60, v253, 16
	s_lshl_b64 s[0:1], s[8:9], 22
	v_readlane_b32 s66, v253, 22
	v_readlane_b32 s67, v253, 23
	s_add_u32 s10, s66, s0
	s_addc_u32 s11, s67, s1
	s_lshl_b64 s[0:1], s[8:9], 21
	s_add_u32 s8, s29, s0
	s_addc_u32 s1, s30, s1
	s_and_b32 s0, s43, 0x3e0
	s_add_i32 s12, s45, 0xfffee200
	s_and_b32 s12, s12, 0x3c0
	s_lshl_b32 s13, s0, 2
	s_add_u32 s10, s10, s13
	v_or_b32_e32 v4, s12, v44
	s_addc_u32 s11, s11, 0
	v_lshl_add_u64 v[2:3], s[10:11], 0, v[36:37]
	v_lshlrev_b32_e32 v4, 12, v4
	v_mov_b32_e32 v5, v37
	v_lshl_add_u64 v[30:31], v[2:3], 0, v[4:5]
	v_add_co_u32_e32 v6, vcc, s48, v30
	s_lshl_b32 s10, s12, 1
	s_nop 0
	v_addc_co_u32_e32 v7, vcc, 0, v31, vcc
	v_add_co_u32_e32 v10, vcc, s49, v30
	global_load_dwordx4 v[2:5], v[30:31], off
	s_nop 0
	global_load_dwordx4 v[6:9], v[6:7], off
	v_addc_co_u32_e32 v11, vcc, 0, v31, vcc
	v_add_co_u32_e32 v14, vcc, s50, v30
	s_add_u32 s10, s8, s10
	s_nop 0
	v_addc_co_u32_e32 v15, vcc, 0, v31, vcc
	v_add_co_u32_e32 v18, vcc, s51, v30
	global_load_dwordx4 v[10:13], v[10:11], off
	s_nop 0
	global_load_dwordx4 v[14:17], v[14:15], off
	v_addc_co_u32_e32 v19, vcc, 0, v31, vcc
	v_add_co_u32_e32 v22, vcc, s52, v30
	v_mov_b32_e32 v39, v37
	s_nop 0
	v_addc_co_u32_e32 v23, vcc, 0, v31, vcc
	global_load_dwordx4 v[18:21], v[18:19], off
	s_nop 0
	global_load_dwordx4 v[22:25], v[22:23], off
	v_add_co_u32_e32 v26, vcc, s53, v30
	v_or_b32_e32 v40, s0, v44
	s_nop 0
	v_addc_co_u32_e32 v27, vcc, 0, v31, vcc
	global_load_dwordx4 v[26:29], v[26:27], off
	v_add_co_u32_e32 v30, vcc, s54, v30
	s_addc_u32 s11, s1, 0
	s_nop 0
	v_addc_co_u32_e32 v31, vcc, 0, v31, vcc
	global_load_dwordx4 v[30:33], v[30:31], off
	v_mov_b32_e32 v41, v37
	v_lshlrev_b32_e32 v40, 11, v40
	v_lshl_add_u64 v[64:65], s[10:11], 0, v[38:39]
	v_lshl_add_u64 v[40:41], v[64:65], 0, v[40:41]
	v_or_b32_e32 v42, s0, v45
	v_mov_b32_e32 v43, v37
	v_lshlrev_b32_e32 v42, 11, v42
	v_lshl_add_u64 v[42:43], v[64:65], 0, v[42:43]
	v_readlane_b32 s61, v253, 17
	v_readlane_b32 s62, v253, 18
	v_readlane_b32 s63, v253, 19
	v_readlane_b32 s64, v253, 20
	v_readlane_b32 s65, v253, 21
	v_readlane_b32 s68, v253, 24
	v_readlane_b32 s69, v253, 25
	v_readlane_b32 s70, v253, 26
	v_readlane_b32 s71, v253, 27
	v_readlane_b32 s72, v253, 28
	v_readlane_b32 s73, v253, 29
	v_readlane_b32 s74, v253, 30
	v_readlane_b32 s75, v253, 31
	s_waitcnt vmcnt(7)
	ds_write2_b32 v49, v2, v3 offset1:1
	ds_write2_b32 v49, v4, v5 offset0:2 offset1:3
	s_waitcnt vmcnt(6)
	ds_write2_b32 v50, v6, v7 offset1:1
	ds_write2_b32 v51, v8, v9 offset1:1
	s_waitcnt vmcnt(5)
	ds_write2_b32 v52, v10, v11 offset1:1
	ds_write2_b32 v53, v12, v13 offset1:1
	s_waitcnt vmcnt(4)
	ds_write2_b32 v54, v14, v15 offset1:1
	ds_write2_b32 v55, v16, v17 offset1:1
	s_waitcnt vmcnt(3)
	ds_write2_b32 v56, v18, v19 offset1:1
	ds_write2_b32 v57, v20, v21 offset1:1
	s_waitcnt vmcnt(2)
	ds_write2_b32 v58, v22, v23 offset1:1
	ds_write2_b32 v59, v24, v25 offset1:1
	s_waitcnt vmcnt(1)
	ds_write2_b32 v60, v26, v27 offset1:1
	ds_write2_b32 v61, v28, v29 offset1:1
	s_waitcnt vmcnt(0)
	ds_write2_b32 v62, v30, v31 offset1:1
	ds_write2_b32 v63, v32, v33 offset1:1
	s_waitcnt lgkmcnt(0)
	ds_read2_b32 v[6:7], v48 offset0:33 offset1:41
	ds_read2_b32 v[8:9], v48 offset1:8
	ds_read2_b32 v[10:11], v48 offset0:66 offset1:74
	ds_read2_b32 v[12:13], v48 offset0:99 offset1:107
	ds_read2_b32 v[14:15], v48 offset0:132 offset1:140
	ds_read2_b32 v[16:17], v48 offset0:165 offset1:173
	ds_read2_b32 v[18:19], v48 offset0:198 offset1:206
	ds_read2_b32 v[20:21], v48 offset0:231 offset1:239
	ds_read2_b32 v[22:23], v48 offset0:16 offset1:24
	s_waitcnt lgkmcnt(7)
	v_cvt_pk_bf16_f32 v2, v8, v6
	s_waitcnt lgkmcnt(5)
	v_cvt_pk_bf16_f32 v3, v10, v12
	s_waitcnt lgkmcnt(3)
	v_cvt_pk_bf16_f32 v4, v14, v16
	s_waitcnt lgkmcnt(1)
	v_cvt_pk_bf16_f32 v5, v18, v20
	global_store_dwordx4 v[40:41], v[2:5], off sc1
	v_cvt_pk_bf16_f32 v6, v9, v7
	v_cvt_pk_bf16_f32 v7, v11, v13
	v_cvt_pk_bf16_f32 v8, v15, v17
	v_cvt_pk_bf16_f32 v9, v19, v21
	ds_read2_b32 v[10:11], v48 offset0:49 offset1:57
	ds_read2_b32 v[12:13], v48 offset0:82 offset1:90
	ds_read2_b32 v[14:15], v48 offset0:115 offset1:123
	ds_read2_b32 v[16:17], v48 offset0:148 offset1:156
	ds_read2_b32 v[18:19], v48 offset0:181 offset1:189
	ds_read2_b32 v[20:21], v48 offset0:214 offset1:222
	ds_read2_b32 v[24:25], v48 offset0:247 offset1:255
	global_store_dwordx4 v[42:43], v[6:9], off sc1
	s_waitcnt lgkmcnt(6)
	v_cvt_pk_bf16_f32 v2, v22, v10
	s_waitcnt lgkmcnt(4)
	v_cvt_pk_bf16_f32 v3, v12, v14
	s_waitcnt lgkmcnt(2)
	v_cvt_pk_bf16_f32 v4, v16, v18
	s_waitcnt lgkmcnt(0)
	v_cvt_pk_bf16_f32 v5, v20, v24
	v_or_b32_e32 v6, s0, v46
	v_lshlrev_b32_e32 v6, 11, v6
	v_mov_b32_e32 v7, v37
	v_lshl_add_u64 v[6:7], v[64:65], 0, v[6:7]
	global_store_dwordx4 v[6:7], v[2:5], off sc1
	v_or_b32_e32 v6, s0, v47
	v_lshlrev_b32_e32 v6, 11, v6
	v_mov_b32_e32 v7, v37
	v_lshl_add_u64 v[6:7], v[64:65], 0, v[6:7]
	v_cvt_pk_bf16_f32 v2, v23, v11
	v_cvt_pk_bf16_f32 v3, v13, v15
	v_cvt_pk_bf16_f32 v4, v17, v19
	v_cvt_pk_bf16_f32 v5, v21, v25
	global_store_dwordx4 v[6:7], v[2:5], off sc1
	s_waitcnt lgkmcnt(0)

; #define GAS __attribute__((address_space(1)))
; #define LAS __attribute__((address_space(3)))
; #define LDS_WAIT() asm volatile("s_waitcnt lgkmcnt(0)" ::: "memory")
; __device__ __forceinline__ unsigned pk2(float lo, float hi) { unsigned r; asm("v_cvt_pk_bf16_f32 %0, %1, %2" : "=v"(r) : "v"(lo), "v"(hi)); return r; }
; __device__ __forceinline__ void transpose_item(const float* W, int K, int N, bf16* WT, int drow0, int kb, int n0, LAS float* scr, int lane) {
;     ...
;     for (int i = 0; i < 8; ++i) { const int kk = 8 * i + (lane >> 3); v[i] = ok ? *(const f32x4*)(W + (size_t)(k0 + kk) * N + n0 + c4) : (f32x4){0.f, 0.f, 0.f, 0.f}; }
; #pragma unroll
;     for (int i = 0; i < 8; ++i) { const int kk = 8 * i + (lane >> 3); LAS float* d = scr + kk * 33 + c4; d[0] = v[i][0]; d[1] = v[i][1]; d[2] = v[i][2]; d[3] = v[i][3]; }
;     LDS_WAIT(); asm volatile("" ::: "memory");
;     const int c = lane & 7;
; #pragma unroll
;     for (int j = 0; j < 4; ++j) { const int n = (lane >> 3) + 8 * j; const LAS float* s = scr + (8 * c) * 33 + n;
;         v4u o; o.x = pk2(s[0 * 33], s[1 * 33]); o.y = pk2(s[2 * 33], s[3 * 33]); o.z = pk2(s[4 * 33], s[5 * 33]); o.w = pk2(s[6 * 33], s[7 * 33]);
;         *(GAS v4u*)(WT + (size_t)(drow0 + n) * K + k0 + 8 * c) = o; }
;     LDS_WAIT(); asm volatile("" ::: "memory");
.LBB0_65:
	s_or_b64 exec, exec, s[16:17]
	s_and_b64 s[0:1], s[14:15], exec
	s_cselect_b32 s0, 0x580000, 0
	s_waitcnt vmcnt(0)
	ds_write2_b32 v49, v2, v3 offset1:1
	ds_write2_b32 v49, v4, v5 offset0:2 offset1:3
	ds_write2_b32 v50, v6, v7 offset1:1
	ds_write2_b32 v51, v8, v9 offset1:1
	ds_write2_b32 v52, v14, v15 offset1:1
	ds_write2_b32 v53, v16, v17 offset1:1
	ds_write2_b32 v54, v10, v11 offset1:1
	ds_write2_b32 v55, v12, v13 offset1:1
	ds_write2_b32 v56, v22, v23 offset1:1
	ds_write2_b32 v57, v24, v25 offset1:1
	ds_write2_b32 v58, v18, v19 offset1:1
	ds_write2_b32 v59, v20, v21 offset1:1
	ds_write2_b32 v60, v30, v31 offset1:1
	ds_write2_b32 v61, v32, v33 offset1:1
	ds_write2_b32 v62, v26, v27 offset1:1
	ds_write2_b32 v63, v28, v29 offset1:1
	s_add_u32 s8, s27, s0
	s_waitcnt lgkmcnt(0)
	s_addc_u32 s11, s28, 0
	s_ashr_i32 s13, s12, 31
	s_lshl_b64 s[0:1], s[12:13], 1
	ds_read2_b32 v[6:7], v48 offset0:33 offset1:41
	ds_read2_b32 v[8:9], v48 offset1:8
	ds_read2_b32 v[10:11], v48 offset0:66 offset1:74
	ds_read2_b32 v[12:13], v48 offset0:99 offset1:107
	ds_read2_b32 v[14:15], v48 offset0:132 offset1:140
	ds_read2_b32 v[16:17], v48 offset0:165 offset1:173
	ds_read2_b32 v[18:19], v48 offset0:198 offset1:206
	ds_read2_b32 v[20:21], v48 offset0:231 offset1:239
	s_add_u32 s0, s8, s0
	v_or_b32_e32 v24, s10, v44
	s_addc_u32 s1, s11, s1
	v_mov_b32_e32 v39, v37
	v_ashrrev_i32_e32 v25, 31, v24
	v_lshl_add_u64 v[22:23], s[0:1], 0, v[38:39]
	v_lshlrev_b64 v[24:25], 11, v[24:25]
	s_waitcnt lgkmcnt(6)
	v_cvt_pk_bf16_f32 v2, v8, v6
	v_lshl_add_u64 v[24:25], v[22:23], 0, v[24:25]
	v_or_b32_e32 v6, s10, v45
	s_waitcnt lgkmcnt(4)
	v_cvt_pk_bf16_f32 v3, v10, v12
	s_waitcnt lgkmcnt(2)
	v_cvt_pk_bf16_f32 v4, v14, v16
	s_waitcnt lgkmcnt(0)
	v_cvt_pk_bf16_f32 v5, v18, v20
	global_store_dwordx4 v[24:25], v[2:5], off sc1
	s_nop 1
	v_cvt_pk_bf16_f32 v2, v9, v7
	v_ashrrev_i32_e32 v7, 31, v6
	v_lshlrev_b64 v[6:7], 11, v[6:7]
	v_cvt_pk_bf16_f32 v3, v11, v13
	v_cvt_pk_bf16_f32 v4, v15, v17
	v_cvt_pk_bf16_f32 v5, v19, v21
	v_lshl_add_u64 v[6:7], v[22:23], 0, v[6:7]
	ds_read2_b32 v[8:9], v48 offset0:16 offset1:24
	ds_read2_b32 v[10:11], v48 offset0:49 offset1:57
	ds_read2_b32 v[12:13], v48 offset0:82 offset1:90
	ds_read2_b32 v[14:15], v48 offset0:115 offset1:123
	ds_read2_b32 v[16:17], v48 offset0:148 offset1:156
	ds_read2_b32 v[18:19], v48 offset0:181 offset1:189
	ds_read2_b32 v[20:21], v48 offset0:214 offset1:222
	ds_read2_b32 v[24:25], v48 offset0:247 offset1:255
	global_store_dwordx4 v[6:7], v[2:5], off sc1
	v_or_b32_e32 v6, s10, v46
	v_ashrrev_i32_e32 v7, 31, v6
	v_lshlrev_b64 v[6:7], 11, v[6:7]
	v_lshl_add_u64 v[6:7], v[22:23], 0, v[6:7]
	s_waitcnt lgkmcnt(6)
	v_cvt_pk_bf16_f32 v2, v8, v10
	s_waitcnt lgkmcnt(4)
	v_cvt_pk_bf16_f32 v3, v12, v14
	s_waitcnt lgkmcnt(2)
	v_cvt_pk_bf16_f32 v4, v16, v18
	s_waitcnt lgkmcnt(0)
	v_cvt_pk_bf16_f32 v5, v20, v24
	global_store_dwordx4 v[6:7], v[2:5], off sc1
	v_or_b32_e32 v6, s10, v47
	v_ashrrev_i32_e32 v7, 31, v6
	v_lshlrev_b64 v[6:7], 11, v[6:7]
	v_lshl_add_u64 v[6:7], v[22:23], 0, v[6:7]
	v_cvt_pk_bf16_f32 v2, v9, v11
	v_cvt_pk_bf16_f32 v3, v13, v15
	v_cvt_pk_bf16_f32 v4, v17, v19
	v_cvt_pk_bf16_f32 v5, v21, v25
	global_store_dwordx4 v[6:7], v[2:5], off sc1
	s_waitcnt lgkmcnt(0)

; #define GAS __attribute__((address_space(1)))
; #define LAS __attribute__((address_space(3)))
; #define LDS_WAIT() asm volatile("s_waitcnt lgkmcnt(0)" ::: "memory")
; __device__ __forceinline__ unsigned pk2(float lo, float hi) { unsigned r; asm("v_cvt_pk_bf16_f32 %0, %1, %2" : "=v"(r) : "v"(lo), "v"(hi)); return r; }
; __device__ __forceinline__ void transpose_item(const float* W, int K, int N, bf16* WT, int drow0, int kb, int n0, LAS float* scr, int lane) {
;     const int k0 = 64 * kb; const int c4 = 4 * (lane & 7); const bool ok = (n0 + c4) < N;
;     f32x4 v[8];
; #pragma unroll
;     for (int i = 0; i < 8; ++i) { const int kk = 8 * i + (lane >> 3); v[i] = ok ? *(const f32x4*)(W + (size_t)(k0 + kk) * N + n0 + c4) : (f32x4){0.f, 0.f, 0.f, 0.f}; }
; #pragma unroll
;     for (int i = 0; i < 8; ++i) { const int kk = 8 * i + (lane >> 3); LAS float* d = scr + kk * 33 + c4; d[0] = v[i][0]; d[1] = v[i][1]; d[2] = v[i][2]; d[3] = v[i][3]; }
;     LDS_WAIT(); asm volatile("" ::: "memory");
;     const int c = lane & 7;
; #pragma unroll
;     for (int j = 0; j < 4; ++j) { const int n = (lane >> 3) + 8 * j; const LAS float* s = scr + (8 * c) * 33 + n;
;         v4u o; o.x = pk2(s[0 * 33], s[1 * 33]); o.y = pk2(s[2 * 33], s[3 * 33]); o.z = pk2(s[4 * 33], s[5 * 33]); o.w = pk2(s[6 * 33], s[7 * 33]);
;         *(GAS v4u*)(WT + (size_t)(drow0 + n) * K + k0 + 8 * c) = o; }
;     LDS_WAIT(); asm volatile("" ::: "memory");
; }
; __device__ __forceinline__ void convert_item(const In& I, unsigned char* ws, int it, LAS float* scr, int lane) {
;     ...
;     int r = it;
;     if (r < T0) { const int f = r / I_FFN; r -= f * I_FFN;
;         if (r < 2 * I_G) { const int up = r >= I_G; r -= up * I_G; const int kb = r / 88, nb = r % 88;
;             transpose_item((up ? I.w_up : I.w_gate) + (size_t)f * D * FF, D, FF, Wgu + (size_t)f * NGU * D, 256 * (nb >> 2) + 32 * (nb & 3) + 128 * up, kb, 32 * nb, scr, lane); }
;         else { r -= 2 * I_G; const int kb = r / 32, nb = r % 32; transpose_item(I.w_down + (size_t)f * FF * D, FF, D, Wd + (size_t)f * D * FF, 32 * nb, kb, 32 * nb, scr, lane); }
.LBB0_67:
	s_andn2_b64 vcc, exec, s[0:1]
	s_cbranch_vccnz .LBB0_12
	s_mul_hi_i32 s0, s58, 0x3e0f83e1
	s_lshr_b32 s1, s0, 31
	s_ashr_i32 s10, s0, 10
	s_add_i32 s10, s10, s1
	s_mul_i32 s0, s10, 0xffffef80
	s_add_i32 s11, s40, s0
	s_add_i32 s11, s11, 0xa800
	s_cmpk_gt_i32 s11, 0xaff
	s_mov_b64 s[0:1], -1
	s_cbranch_scc0 .LBB0_70
	v_readlane_b32 s60, v253, 0
	s_mul_i32 s1, s10, 0xb00000
	v_readlane_b32 s68, v253, 8
	s_mul_hi_i32 s0, s10, 0xb00000
	v_readlane_b32 s69, v253, 9
	s_add_u32 s1, s68, s1
	s_addc_u32 s13, s69, s0
	s_mul_i32 s8, s10, 0x580000
	s_mul_hi_i32 s0, s10, 0x580000
	s_add_u32 s14, s25, s8
	s_mul_i32 s8, s10, 0xffffdf00
	s_addc_u32 s15, s26, s0
	s_add_i32 s8, s45, s8
	s_andn2_b32 s8, s8, 63
	s_and_b32 s0, s43, 0x3e0
	s_addk_i32 s8, 0xea00
	v_or_b32_e32 v30, s8, v44
	s_lshl_b32 s12, s0, 2
	s_add_u32 s12, s1, s12
	v_or_b32_e32 v4, 8, v30
	v_or_b32_e32 v10, 16, v30
	v_or_b32_e32 v12, 24, v30
	v_or_b32_e32 v18, 32, v30
	v_or_b32_e32 v20, 40, v30
	s_addc_u32 s13, s13, 0
	v_ashrrev_i32_e32 v31, 31, v30
	v_ashrrev_i32_e32 v5, 31, v4
	v_ashrrev_i32_e32 v11, 31, v10
	v_ashrrev_i32_e32 v13, 31, v12
	v_ashrrev_i32_e32 v19, 31, v18
	v_ashrrev_i32_e32 v21, 31, v20
	v_lshl_add_u64 v[32:33], s[12:13], 0, v[36:37]
	v_lshlrev_b64 v[2:3], 12, v[30:31]
	v_lshlrev_b64 v[4:5], 12, v[4:5]
	v_lshlrev_b64 v[10:11], 12, v[10:11]
	v_lshlrev_b64 v[12:13], 12, v[12:13]
	v_lshlrev_b64 v[18:19], 12, v[18:19]
	v_lshlrev_b64 v[20:21], 12, v[20:21]
	v_lshl_add_u64 v[2:3], v[32:33], 0, v[2:3]
	v_lshl_add_u64 v[6:7], v[32:33], 0, v[4:5]
	v_lshl_add_u64 v[10:11], v[32:33], 0, v[10:11]
	v_lshl_add_u64 v[14:15], v[32:33], 0, v[12:13]
	v_lshl_add_u64 v[18:19], v[32:33], 0, v[18:19]
	v_lshl_add_u64 v[22:23], v[32:33], 0, v[20:21]
	global_load_dwordx4 v[2:5], v[2:3], off
	s_nop 0
	global_load_dwordx4 v[6:9], v[6:7], off
	s_nop 0
	global_load_dwordx4 v[10:13], v[10:11], off
	s_nop 0
	global_load_dwordx4 v[14:17], v[14:15], off
	s_nop 0
	global_load_dwordx4 v[18:21], v[18:19], off
	s_nop 0
	global_load_dwordx4 v[22:25], v[22:23], off
	v_or_b32_e32 v26, 48, v30
	v_ashrrev_i32_e32 v27, 31, v26
	v_lshlrev_b64 v[26:27], 12, v[26:27]
	v_or_b32_e32 v30, 56, v30
	v_lshl_add_u64 v[26:27], v[32:33], 0, v[26:27]
	v_ashrrev_i32_e32 v31, 31, v30
	global_load_dwordx4 v[26:29], v[26:27], off
	v_lshlrev_b64 v[30:31], 12, v[30:31]
	v_lshl_add_u64 v[30:31], v[32:33], 0, v[30:31]
	global_load_dwordx4 v[30:33], v[30:31], off
	s_lshl_b64 s[12:13], s[8:9], 1
	s_add_u32 s12, s14, s12
	v_mov_b32_e32 v39, v37
	v_or_b32_e32 v40, s0, v44
	s_addc_u32 s13, s15, s13
	v_mov_b32_e32 v41, v37
	v_mul_u32_u24_e32 v40, 0x1600, v40
	v_lshl_add_u64 v[42:43], s[12:13], 0, v[38:39]
	v_or_b32_e32 v64, s0, v45
	v_readlane_b32 s61, v253, 1
	v_readlane_b32 s62, v253, 2
	v_readlane_b32 s63, v253, 3
	v_readlane_b32 s64, v253, 4
	v_readlane_b32 s65, v253, 5
	v_readlane_b32 s66, v253, 6
	v_readlane_b32 s67, v253, 7
	v_readlane_b32 s70, v253, 10
	v_readlane_b32 s71, v253, 11
	v_readlane_b32 s72, v253, 12
	v_readlane_b32 s73, v253, 13
	v_readlane_b32 s74, v253, 14
	v_readlane_b32 s75, v253, 15
	s_waitcnt vmcnt(7)
	ds_write2_b32 v49, v2, v3 offset1:1
	ds_write2_b32 v49, v4, v5 offset0:2 offset1:3
	s_waitcnt vmcnt(6)
	ds_write2_b32 v50, v6, v7 offset1:1
	ds_write2_b32 v51, v8, v9 offset1:1
	s_waitcnt vmcnt(5)
	ds_write2_b32 v52, v10, v11 offset1:1
	ds_write2_b32 v53, v12, v13 offset1:1
	s_waitcnt vmcnt(4)
	ds_write2_b32 v54, v14, v15 offset1:1
	ds_write2_b32 v55, v16, v17 offset1:1
	s_waitcnt vmcnt(3)
	ds_write2_b32 v56, v18, v19 offset1:1
	ds_write2_b32 v57, v20, v21 offset1:1
	s_waitcnt vmcnt(2)
	ds_write2_b32 v58, v22, v23 offset1:1
	ds_write2_b32 v59, v24, v25 offset1:1
	s_waitcnt vmcnt(1)
	ds_write2_b32 v60, v26, v27 offset1:1
	ds_write2_b32 v61, v28, v29 offset1:1
	s_waitcnt vmcnt(0)
	ds_write2_b32 v62, v30, v31 offset1:1
	ds_write2_b32 v63, v32, v33 offset1:1
	s_waitcnt lgkmcnt(0)
	ds_read2_b32 v[6:7], v48 offset0:33 offset1:41
	ds_read2_b32 v[8:9], v48 offset1:8
	ds_read2_b32 v[10:11], v48 offset0:66 offset1:74
	ds_read2_b32 v[12:13], v48 offset0:99 offset1:107
	ds_read2_b32 v[14:15], v48 offset0:132 offset1:140
	ds_read2_b32 v[16:17], v48 offset0:165 offset1:173
	ds_read2_b32 v[18:19], v48 offset0:198 offset1:206
	ds_read2_b32 v[20:21], v48 offset0:231 offset1:239
	v_lshl_add_u64 v[22:23], v[42:43], 0, v[40:41]
	s_waitcnt lgkmcnt(6)
	v_cvt_pk_bf16_f32 v2, v8, v6
	s_waitcnt lgkmcnt(4)
	v_cvt_pk_bf16_f32 v3, v10, v12
	s_waitcnt lgkmcnt(2)
	v_cvt_pk_bf16_f32 v4, v14, v16
	s_waitcnt lgkmcnt(0)
	v_cvt_pk_bf16_f32 v5, v18, v20
	global_store_dwordx4 v[22:23], v[2:5], off sc1
	v_cvt_pk_bf16_f32 v6, v9, v7
	v_cvt_pk_bf16_f32 v7, v11, v13
	v_cvt_pk_bf16_f32 v8, v15, v17
	v_cvt_pk_bf16_f32 v9, v19, v21
	ds_read2_b32 v[10:11], v48 offset0:16 offset1:24
	ds_read2_b32 v[12:13], v48 offset0:49 offset1:57
	ds_read2_b32 v[14:15], v48 offset0:82 offset1:90
	ds_read2_b32 v[16:17], v48 offset0:115 offset1:123
	ds_read2_b32 v[18:19], v48 offset0:148 offset1:156
	ds_read2_b32 v[20:21], v48 offset0:181 offset1:189
	ds_read2_b32 v[22:23], v48 offset0:214 offset1:222
	ds_read2_b32 v[24:25], v48 offset0:247 offset1:255
	v_mul_u32_u24_e32 v2, 0x1600, v64
	v_mov_b32_e32 v3, v37
	v_lshl_add_u64 v[2:3], v[42:43], 0, v[2:3]
	global_store_dwordx4 v[2:3], v[6:9], off sc1
	s_waitcnt lgkmcnt(6)
	v_cvt_pk_bf16_f32 v2, v10, v12
	s_waitcnt lgkmcnt(4)
	v_cvt_pk_bf16_f32 v3, v14, v16
	s_waitcnt lgkmcnt(2)
	v_cvt_pk_bf16_f32 v4, v18, v20
	s_waitcnt lgkmcnt(0)
	v_cvt_pk_bf16_f32 v5, v22, v24
	v_or_b32_e32 v6, s0, v46
	v_mul_u32_u24_e32 v6, 0x1600, v6
	v_mov_b32_e32 v7, v37
	v_lshl_add_u64 v[6:7], v[42:43], 0, v[6:7]
	global_store_dwordx4 v[6:7], v[2:5], off sc1
	v_or_b32_e32 v6, s0, v47
	v_mul_u32_u24_e32 v6, 0x1600, v6
	v_mov_b32_e32 v7, v37
	v_lshl_add_u64 v[6:7], v[42:43], 0, v[6:7]
	v_cvt_pk_bf16_f32 v2, v11, v13
	v_cvt_pk_bf16_f32 v3, v15, v17
	v_cvt_pk_bf16_f32 v4, v19, v21
	v_cvt_pk_bf16_f32 v5, v23, v25
	global_store_dwordx4 v[6:7], v[2:5], off sc1
	s_waitcnt lgkmcnt(0)
	s_mov_b64 s[0:1], 0
; #define GAS __attribute__((address_space(1)))
; #define LAS __attribute__((address_space(3)))
; #define LDS_WAIT() asm volatile("s_waitcnt lgkmcnt(0)" ::: "memory")
; __device__ __forceinline__ unsigned pk2(float lo, float hi) { unsigned r; asm("v_cvt_pk_bf16_f32 %0, %1, %2" : "=v"(r) : "v"(lo), "v"(hi)); return r; }
; __device__ __forceinline__ void transpose_item(const float* W, int K, int N, bf16* WT, int drow0, int kb, int n0, LAS float* scr, int lane) {
;     const int k0 = 64 * kb; const int c4 = 4 * (lane & 7); const bool ok = (n0 + c4) < N;
;     f32x4 v[8];
; #pragma unroll
;     for (int i = 0; i < 8; ++i) { const int kk = 8 * i + (lane >> 3); v[i] = ok ? *(const f32x4*)(W + (size_t)(k0 + kk) * N + n0 + c4) : (f32x4){0.f, 0.f, 0.f, 0.f}; }
; #pragma unroll
;     for (int i = 0; i < 8; ++i) { const int kk = 8 * i + (lane >> 3); LAS float* d = scr + kk * 33 + c4; d[0] = v[i][0]; d[1] = v[i][1]; d[2] = v[i][2]; d[3] = v[i][3]; }
;     LDS_WAIT(); asm volatile("" ::: "memory");
;     const int c = lane & 7;
; #pragma unroll
;     for (int j = 0; j < 4; ++j) { const int n = (lane >> 3) + 8 * j; const LAS float* s = scr + (8 * c) * 33 + n;
;         v4u o; o.x = pk2(s[0 * 33], s[1 * 33]); o.y = pk2(s[2 * 33], s[3 * 33]); o.z = pk2(s[4 * 33], s[5 * 33]); o.w = pk2(s[6 * 33], s[7 * 33]);
;         *(GAS v4u*)(WT + (size_t)(drow0 + n) * K + k0 + 8 * c) = o; }
;     LDS_WAIT(); asm volatile("" ::: "memory");
; }
; __device__ __forceinline__ void convert_item(const In& I, unsigned char* ws, int it, LAS float* scr, int lane) {
;     ...
;         if (r < 2 * I_G) { const int up = r >= I_G; r -= up * I_G; const int kb = r / 88, nb = r % 88;
;             transpose_item((up ? I.w_up : I.w_gate) + (size_t)f * D * FF, D, FF, Wgu + (size_t)f * NGU * D, 256 * (nb >> 2) + 32 * (nb & 3) + 128 * up, kb, 32 * nb, scr, lane); }
.LBB0_70:
	s_andn2_b64 vcc, exec, s[0:1]
	s_cbranch_vccnz .LBB0_12
	s_cmpk_gt_i32 s11, 0x57f
	v_readlane_b32 s60, v253, 0
	s_cselect_b32 s0, 0xfffffa80, 0
	s_mul_i32 s1, s10, 0x1080
	v_readlane_b32 s64, v253, 4
	v_readlane_b32 s65, v253, 5
	v_readlane_b32 s66, v253, 6
	v_readlane_b32 s67, v253, 7
	s_cselect_b32 s8, 0x80, 0
	s_cselect_b32 s11, s66, s64
	s_cselect_b32 s12, s67, s65
	s_sub_i32 s0, s0, s1
	s_add_i32 s0, s40, s0
	s_add_i32 s0, s0, 0xa800
	s_mul_hi_i32 s1, s0, 0x2e8ba2e9
	s_lshr_b32 s13, s1, 31
	s_ashr_i32 s1, s1, 4
	s_add_i32 s1, s1, s13
	s_mul_i32 s13, s1, 0x58
	s_sub_i32 s0, s0, s13
	s_mul_hi_i32 s13, s10, 0xb00000
	s_mul_i32 s10, s10, 0xb00000
	s_add_u32 s14, s11, s10
	s_addc_u32 s12, s12, s13
	s_add_u32 s15, s23, s10
	s_addc_u32 s13, s24, s13
	s_lshl_b32 s10, s0, 6
	s_and_b32 s11, s10, 0xffffff00
	s_lshl_b32 s10, s0, 5
	s_and_b32 s0, s10, 0x60
	s_or_b32 s0, s0, s8
	s_or_b32 s8, s0, s11
	s_ashr_i32 s11, s10, 31
	s_lshl_b32 s0, s1, 6
	s_lshl_b64 s[10:11], s[10:11], 2
	s_add_u32 s10, s14, s10
	v_or_b32_e32 v32, s0, v44
	s_addc_u32 s11, s12, s11
	v_lshl_add_u64 v[30:31], s[10:11], 0, v[36:37]
	v_or_b32_e32 v4, 8, v32
	v_or_b32_e32 v10, 16, v32
	v_or_b32_e32 v12, 24, v32
	v_or_b32_e32 v18, 32, v32
	v_or_b32_e32 v20, 40, v32
	v_mad_i64_i32 v[2:3], s[10:11], v32, s57, v[30:31]
	v_mad_i64_i32 v[6:7], s[10:11], v4, s57, v[30:31]
	v_mad_i64_i32 v[10:11], s[10:11], v10, s57, v[30:31]
	v_mad_i64_i32 v[14:15], s[10:11], v12, s57, v[30:31]
	v_mad_i64_i32 v[18:19], s[10:11], v18, s57, v[30:31]
	v_mad_i64_i32 v[22:23], s[10:11], v20, s57, v[30:31]
	global_load_dwordx4 v[2:5], v[2:3], off
	s_nop 0
	global_load_dwordx4 v[6:9], v[6:7], off
	s_nop 0
	global_load_dwordx4 v[10:13], v[10:11], off
	s_nop 0
	global_load_dwordx4 v[14:17], v[14:15], off
	s_nop 0
	global_load_dwordx4 v[18:21], v[18:19], off
	s_nop 0
	global_load_dwordx4 v[22:25], v[22:23], off
	v_or_b32_e32 v26, 48, v32
	v_mad_i64_i32 v[26:27], s[10:11], v26, s57, v[30:31]
	global_load_dwordx4 v[26:29], v[26:27], off
	v_or_b32_e32 v32, 56, v32
	v_mad_i64_i32 v[30:31], s[10:11], v32, s57, v[30:31]
	global_load_dwordx4 v[30:33], v[30:31], off
	s_ashr_i32 s1, s0, 31
	s_lshl_b64 s[0:1], s[0:1], 1
	v_or_b32_e32 v40, s8, v44
	s_add_u32 s0, s15, s0
	v_mov_b32_e32 v39, v37
	v_ashrrev_i32_e32 v41, 31, v40
	s_addc_u32 s1, s13, s1
	v_or_b32_e32 v42, s8, v45
	v_lshlrev_b64 v[40:41], 11, v[40:41]
	v_lshl_add_u64 v[64:65], s[0:1], 0, v[38:39]
	v_ashrrev_i32_e32 v43, 31, v42
	v_readlane_b32 s61, v253, 1
	v_readlane_b32 s62, v253, 2
	v_readlane_b32 s63, v253, 3
	v_readlane_b32 s68, v253, 8
	v_readlane_b32 s69, v253, 9
	v_readlane_b32 s70, v253, 10
	v_readlane_b32 s71, v253, 11
	v_readlane_b32 s72, v253, 12
	v_readlane_b32 s73, v253, 13
	v_readlane_b32 s74, v253, 14
	v_readlane_b32 s75, v253, 15
	s_waitcnt vmcnt(7)
	ds_write2_b32 v49, v2, v3 offset1:1
	ds_write2_b32 v49, v4, v5 offset0:2 offset1:3
	s_waitcnt vmcnt(6)
	ds_write2_b32 v50, v6, v7 offset1:1
	ds_write2_b32 v51, v8, v9 offset1:1
	s_waitcnt vmcnt(5)
	ds_write2_b32 v52, v10, v11 offset1:1
	ds_write2_b32 v53, v12, v13 offset1:1
	s_waitcnt vmcnt(4)
	ds_write2_b32 v54, v14, v15 offset1:1
	ds_write2_b32 v55, v16, v17 offset1:1
	s_waitcnt vmcnt(3)
	ds_write2_b32 v56, v18, v19 offset1:1
	ds_write2_b32 v57, v20, v21 offset1:1
	s_waitcnt vmcnt(2)
	ds_write2_b32 v58, v22, v23 offset1:1
	ds_write2_b32 v59, v24, v25 offset1:1
	s_waitcnt vmcnt(1)
	ds_write2_b32 v60, v26, v27 offset1:1
	ds_write2_b32 v61, v28, v29 offset1:1
	s_waitcnt vmcnt(0)
	ds_write2_b32 v62, v30, v31 offset1:1
	ds_write2_b32 v63, v32, v33 offset1:1
	s_waitcnt lgkmcnt(0)
	ds_read2_b32 v[6:7], v48 offset0:33 offset1:41
	ds_read2_b32 v[8:9], v48 offset1:8
	ds_read2_b32 v[10:11], v48 offset0:66 offset1:74
	ds_read2_b32 v[12:13], v48 offset0:99 offset1:107
	ds_read2_b32 v[14:15], v48 offset0:132 offset1:140
	ds_read2_b32 v[16:17], v48 offset0:165 offset1:173
	ds_read2_b32 v[18:19], v48 offset0:198 offset1:206
	ds_read2_b32 v[20:21], v48 offset0:231 offset1:239
	v_lshl_add_u64 v[22:23], v[64:65], 0, v[40:41]
	s_waitcnt lgkmcnt(6)
	v_cvt_pk_bf16_f32 v2, v8, v6
	s_waitcnt lgkmcnt(4)
	v_cvt_pk_bf16_f32 v3, v10, v12
	s_waitcnt lgkmcnt(2)
	v_cvt_pk_bf16_f32 v4, v14, v16
	s_waitcnt lgkmcnt(0)
	v_cvt_pk_bf16_f32 v5, v18, v20
	global_store_dwordx4 v[22:23], v[2:5], off sc1
	v_cvt_pk_bf16_f32 v6, v9, v7
	v_cvt_pk_bf16_f32 v7, v11, v13
	v_cvt_pk_bf16_f32 v8, v15, v17
	v_cvt_pk_bf16_f32 v9, v19, v21
	ds_read2_b32 v[10:11], v48 offset0:16 offset1:24
	ds_read2_b32 v[12:13], v48 offset0:49 offset1:57
	ds_read2_b32 v[14:15], v48 offset0:82 offset1:90
	ds_read2_b32 v[16:17], v48 offset0:115 offset1:123
	ds_read2_b32 v[18:19], v48 offset0:148 offset1:156
	ds_read2_b32 v[20:21], v48 offset0:181 offset1:189
	ds_read2_b32 v[22:23], v48 offset0:214 offset1:222
	ds_read2_b32 v[24:25], v48 offset0:247 offset1:255
	v_lshlrev_b64 v[2:3], 11, v[42:43]
	v_lshl_add_u64 v[2:3], v[64:65], 0, v[2:3]
	global_store_dwordx4 v[2:3], v[6:9], off sc1
	s_waitcnt lgkmcnt(6)
	v_cvt_pk_bf16_f32 v2, v10, v12
	s_waitcnt lgkmcnt(4)
	v_cvt_pk_bf16_f32 v3, v14, v16
	s_waitcnt lgkmcnt(2)
	v_cvt_pk_bf16_f32 v4, v18, v20
	s_waitcnt lgkmcnt(0)
	v_cvt_pk_bf16_f32 v5, v22, v24
	v_or_b32_e32 v6, s8, v46
	v_ashrrev_i32_e32 v7, 31, v6
	v_lshlrev_b64 v[6:7], 11, v[6:7]
	v_lshl_add_u64 v[6:7], v[64:65], 0, v[6:7]
	global_store_dwordx4 v[6:7], v[2:5], off sc1
	v_or_b32_e32 v6, s8, v47
	v_ashrrev_i32_e32 v7, 31, v6
	v_lshlrev_b64 v[6:7], 11, v[6:7]
	v_lshl_add_u64 v[6:7], v[64:65], 0, v[6:7]
	v_cvt_pk_bf16_f32 v2, v11, v13
	v_cvt_pk_bf16_f32 v3, v15, v17
	v_cvt_pk_bf16_f32 v4, v19, v21
	v_cvt_pk_bf16_f32 v5, v23, v25
	global_store_dwordx4 v[6:7], v[2:5], off sc1
	s_waitcnt lgkmcnt(0)
	s_branch .LBB0_12

; __device__ __forceinline__ unsigned pk2(float lo, float hi) { unsigned r; asm("v_cvt_pk_bf16_f32 %0, %1, %2" : "=v"(r) : "v"(lo), "v"(hi)); return r; }
; __device__ __forceinline__ void first_norm_row(const float* xrow, const float* g, bf16* urow, bf16* hrow, int lane) {
;     const f32x4* xp = (const f32x4*)xrow; const f32x4* gp = (const f32x4*)g;
;     f32x4 v[4] = {xp[2 * lane], xp[2 * lane + 1], xp[128 + 2 * lane], xp[128 + 2 * lane + 1]};
;     float ss = 0.f;
; #pragma unroll
;     for (int i = 0; i < 4; ++i) ss += (v[i][0] * v[i][0] + v[i][1] * v[i][1]) + (v[i][2] * v[i][2] + v[i][3] * v[i][3]);
;     const float r = 1.0f / sqrtf(wave_sum(ss) * (1.0f / D) + RMS_EPS);
;     { v4u h0, h1; h0.x = pk2(v[0][0], v[0][1]); h0.y = pk2(v[0][2], v[0][3]); h0.z = pk2(v[1][0], v[1][1]); h0.w = pk2(v[1][2], v[1][3]);
;       h1.x = pk2(v[2][0], v[2][1]); h1.y = pk2(v[2][2], v[2][3]); h1.z = pk2(v[3][0], v[3][1]); h1.w = pk2(v[3][2], v[3][3]);
;       ((v4u*)hrow)[lane] = h0; ((v4u*)hrow)[64 + lane] = h1; }
;     const f32x4 g4[4] = {gp[2 * lane], gp[2 * lane + 1], gp[128 + 2 * lane], gp[128 + 2 * lane + 1]};
; #pragma unroll
;     for (int i = 0; i < 4; ++i) v[i] = v[i] * r * g4[i];
;     v4u o0, o1; o0.x = pk2(v[0][0], v[0][1]); o0.y = pk2(v[0][2], v[0][3]); o0.z = pk2(v[1][0], v[1][1]); o0.w = pk2(v[1][2], v[1][3]);
;     o1.x = pk2(v[2][0], v[2][1]); o1.y = pk2(v[2][2], v[2][3]); o1.z = pk2(v[3][0], v[3][1]); o1.w = pk2(v[3][2], v[3][3]);
;     ((v4u*)urow)[lane] = o0; ((v4u*)urow)[64 + lane] = o1;
; __device__ __forceinline__ void prologue(const Ctx& C, const In& I, unsigned char* ws, bf16* hs0) {
;     ...
;     else for (int m = C.gw; m < M; m += C.ngw) first_norm_row(I.x + (size_t)m * D, I.norm_g, U + (size_t)m * D, hs0 + (size_t)m * D, C.lane);
.LBB0_87:
	s_waitcnt lgkmcnt(0)
	global_load_dwordx4 v[6:9], v[22:23], off
	global_load_dwordx4 v[2:5], v[22:23], off offset:16
	global_load_dwordx4 v[10:13], v[22:23], off offset:2064
	global_load_dwordx4 v[14:17], v[22:23], off offset:2048
	v_lshl_add_u64 v[26:27], s[10:11], 0, v[20:21]
	v_add_co_u32_e32 v34, vcc, s14, v26
	s_add_i32 s20, s20, s4
	s_nop 0
	v_addc_co_u32_e32 v35, vcc, 0, v27, vcc
	v_lshl_add_u64 v[42:43], s[6:7], 0, v[20:21]
	s_add_u32 s6, s6, s8
	s_addc_u32 s7, s7, s9
	s_add_u32 s10, s10, s8
	s_addc_u32 s11, s11, s9
	v_lshl_add_u64 v[22:23], v[22:23], 0, s[12:13]
	s_cmpk_lt_i32 s20, 0x4000
	s_waitcnt vmcnt(0)
	v_cvt_pk_bf16_f32 v26, v6, v7
	v_cvt_pk_bf16_f32 v27, v8, v9
	v_cvt_pk_bf16_f32 v28, v2, v3
	v_cvt_pk_bf16_f32 v29, v4, v5
	v_pk_mul_f32 v[36:37], v[8:9], v[8:9]
	v_pk_mul_f32 v[44:45], v[6:7], v[6:7]
	v_pk_mul_f32 v[38:39], v[4:5], v[4:5]
	v_pk_mul_f32 v[46:47], v[2:3], v[2:3]
	v_mul_f32_e32 v40, v15, v15
	v_cvt_pk_bf16_f32 v30, v14, v15
	v_cvt_pk_bf16_f32 v31, v16, v17
	v_cvt_pk_bf16_f32 v32, v10, v11
	v_cvt_pk_bf16_f32 v33, v12, v13
	global_store_dwordx4 v[34:35], v[26:29], off sc1
	global_store_dwordx4 v[34:35], v[30:33], off offset:1024 sc1
	v_pk_mov_b32 v[50:51], v[44:45], v[36:37] op_sel:[1,0]
	v_mov_b32_e32 v45, v37
	v_pk_mov_b32 v[52:53], v[46:47], v[38:39] op_sel:[1,0]
	v_mov_b32_e32 v47, v39
	v_pk_fma_f32 v[54:55], v[14:15], v[14:15], v[40:41] op_sel_hi:[1,1,0]
	global_load_dwordx4 v[26:29], v[18:19], off
	global_load_dwordx4 v[30:33], v[18:19], off offset:16
	global_load_dwordx4 v[34:37], v[18:19], off offset:2048
	global_load_dwordx4 v[38:41], v[18:19], off offset:2064
	v_mul_f32_e32 v48, v17, v17
	v_pk_add_f32 v[44:45], v[50:51], v[44:45]
	v_pk_add_f32 v[46:47], v[52:53], v[46:47]
	v_mul_f32_e32 v56, v10, v10
	v_mul_f32_e32 v57, v11, v11
	v_mul_f32_e32 v58, v12, v12
	v_mul_f32_e32 v59, v13, v13
	v_pk_fma_f32 v[48:49], v[16:17], v[16:17], v[48:49] op_sel_hi:[1,1,0]
	v_pk_add_f32 v[44:45], v[44:45], v[44:45] op_sel:[0,1] op_sel_hi:[1,0]
	v_pk_add_f32 v[46:47], v[46:47], v[46:47] op_sel:[0,1] op_sel_hi:[1,0]
	v_mov_b32_e32 v55, v58
	v_mov_b32_e32 v49, v59
	v_mov_b32_e32 v45, v56
	v_mov_b32_e32 v47, v57
	v_pk_add_f32 v[48:49], v[54:55], v[48:49]
	v_pk_add_f32 v[44:45], v[44:45], v[46:47]
	s_nop 0
	v_pk_add_f32 v[44:45], v[44:45], v[48:49]
	s_nop 0
	v_add_f32_e32 v44, v44, v45
	s_nop 1
	v_add_f32_dpp v44, v44, v44 quad_perm:[1,0,3,2] row_mask:0xf bank_mask:0xf bound_ctrl:1
	s_nop 1
	v_add_f32_dpp v44, v44, v44 quad_perm:[2,3,0,1] row_mask:0xf bank_mask:0xf bound_ctrl:1
	s_nop 1
	v_add_f32_dpp v44, v44, v44 row_half_mirror row_mask:0xf bank_mask:0xf bound_ctrl:1
	s_nop 1
	v_add_f32_dpp v44, v44, v44 row_mirror row_mask:0xf bank_mask:0xf bound_ctrl:1
	s_nop 0
	v_readlane_b32 s16, v44, 16
	v_readlane_b32 s17, v44, 48
	v_readlane_b32 s0, v44, 0
	v_readlane_b32 s1, v44, 32
	v_mov_b32_e32 v44, s16
	v_mov_b32_e32 v45, s17
	v_pk_add_f32 v[44:45], s[0:1], v[44:45]
	s_nop 0
	v_add_f32_e32 v44, v44, v45
	v_fmamk_f32 v44, v44, 0x3a800000, v24
	v_mul_f32_e32 v45, 0x4f800000, v44
	v_cmp_gt_f32_e32 vcc, s5, v44
	s_nop 1
	v_cndmask_b32_e32 v44, v44, v45, vcc
	v_sqrt_f32_e32 v45, v44
	s_nop 0
	v_add_u32_e32 v46, -1, v45
	v_add_u32_e32 v47, 1, v45
	v_fma_f32 v48, -v46, v45, v44
	v_fma_f32 v49, -v47, v45, v44
	v_cmp_ge_f32_e64 s[0:1], 0, v48
	s_nop 1
	v_cndmask_b32_e64 v45, v45, v46, s[0:1]
	v_cmp_lt_f32_e64 s[0:1], 0, v49
	s_nop 1
	v_cndmask_b32_e64 v45, v45, v47, s[0:1]
	v_mul_f32_e32 v46, 0x37800000, v45
	v_cndmask_b32_e32 v45, v45, v46, vcc
	v_cmp_class_f32_e32 vcc, v44, v25
	s_nop 1
	v_cndmask_b32_e32 v44, v45, v44, vcc
	v_div_scale_f32 v45, s[0:1], v44, v44, 1.0
	v_rcp_f32_e32 v47, v45
	v_div_scale_f32 v46, vcc, 1.0, v44, 1.0
	v_fma_f32 v48, -v45, v47, 1.0
	v_fmac_f32_e32 v47, v48, v47
	v_mul_f32_e32 v48, v46, v47
	v_fma_f32 v49, -v45, v48, v46
	v_fmac_f32_e32 v48, v49, v47
	v_fma_f32 v45, -v45, v48, v46
	v_div_fmas_f32 v45, v45, v47, v48
	v_div_fixup_f32 v44, v45, v44, 1.0
	v_pk_mul_f32 v[6:7], v[6:7], v[44:45] op_sel_hi:[1,0]
	v_pk_mul_f32 v[2:3], v[2:3], v[44:45] op_sel_hi:[1,0]
	v_pk_mul_f32 v[4:5], v[4:5], v[44:45] op_sel_hi:[1,0]
	v_add_co_u32_e32 v42, vcc, s15, v42
	v_pk_mul_f32 v[8:9], v[8:9], v[44:45] op_sel_hi:[1,0]
	s_waitcnt vmcnt(3)
	v_pk_mul_f32 v[6:7], v[6:7], v[26:27]
	s_waitcnt vmcnt(2)
	v_pk_mul_f32 v[26:27], v[4:5], v[32:33]
	v_pk_mul_f32 v[4:5], v[2:3], v[30:31]
	v_addc_co_u32_e32 v43, vcc, 0, v43, vcc
	v_pk_mul_f32 v[14:15], v[14:15], v[44:45] op_sel_hi:[1,0]
	v_pk_mul_f32 v[16:17], v[16:17], v[44:45] op_sel_hi:[1,0]
	v_pk_mul_f32 v[10:11], v[10:11], v[44:45] op_sel_hi:[1,0]
	v_pk_mul_f32 v[12:13], v[12:13], v[44:45] op_sel_hi:[1,0]
	v_pk_mul_f32 v[8:9], v[8:9], v[28:29]
	v_cvt_pk_bf16_f32 v2, v6, v7
	v_cvt_pk_bf16_f32 v4, v4, v5
	v_cvt_pk_bf16_f32 v5, v26, v27
	s_waitcnt vmcnt(1)
	v_pk_mul_f32 v[16:17], v[16:17], v[36:37]
	v_cvt_pk_bf16_f32 v3, v8, v9
	v_pk_mul_f32 v[14:15], v[14:15], v[34:35]
	s_waitcnt vmcnt(0)
	v_pk_mul_f32 v[12:13], v[12:13], v[40:41]
	v_pk_mul_f32 v[10:11], v[10:11], v[38:39]
	v_cvt_pk_bf16_f32 v6, v14, v15
	v_cvt_pk_bf16_f32 v7, v16, v17
	v_cvt_pk_bf16_f32 v9, v12, v13
	s_nop 0
	v_cvt_pk_bf16_f32 v8, v10, v11
	flat_store_dwordx4 v[42:43], v[2:5]
	flat_store_dwordx4 v[42:43], v[6:9] offset:1024
	s_cbranch_scc1 .LBB0_87

; __device__ __forceinline__ unsigned pk2(float lo, float hi) { unsigned r; asm("v_cvt_pk_bf16_f32 %0, %1, %2" : "=v"(r) : "v"(lo), "v"(hi)); return r; }
; __device__ __forceinline__ void first_norm_row(const float* xrow, const float* g, bf16* urow, bf16* hrow, int lane) {
;     const f32x4* xp = (const f32x4*)xrow; const f32x4* gp = (const f32x4*)g;
;     f32x4 v[4] = {xp[2 * lane], xp[2 * lane + 1], xp[128 + 2 * lane], xp[128 + 2 * lane + 1]};
;     float ss = 0.f;
; #pragma unroll
;     for (int i = 0; i < 4; ++i) ss += (v[i][0] * v[i][0] + v[i][1] * v[i][1]) + (v[i][2] * v[i][2] + v[i][3] * v[i][3]);
;     const float r = 1.0f / sqrtf(wave_sum(ss) * (1.0f / D) + RMS_EPS);
;     { v4u h0, h1; h0.x = pk2(v[0][0], v[0][1]); h0.y = pk2(v[0][2], v[0][3]); h0.z = pk2(v[1][0], v[1][1]); h0.w = pk2(v[1][2], v[1][3]);
;       h1.x = pk2(v[2][0], v[2][1]); h1.y = pk2(v[2][2], v[2][3]); h1.z = pk2(v[3][0], v[3][1]); h1.w = pk2(v[3][2], v[3][3]);
;       ((v4u*)hrow)[lane] = h0; ((v4u*)hrow)[64 + lane] = h1; }
;     const f32x4 g4[4] = {gp[2 * lane], gp[2 * lane + 1], gp[128 + 2 * lane], gp[128 + 2 * lane + 1]};
; #pragma unroll
;     for (int i = 0; i < 4; ++i) v[i] = v[i] * r * g4[i];
;     v4u o0, o1; o0.x = pk2(v[0][0], v[0][1]); o0.y = pk2(v[0][2], v[0][3]); o0.z = pk2(v[1][0], v[1][1]); o0.w = pk2(v[1][2], v[1][3]);
;     o1.x = pk2(v[2][0], v[2][1]); o1.y = pk2(v[2][2], v[2][3]); o1.z = pk2(v[3][0], v[3][1]); o1.w = pk2(v[3][2], v[3][3]);
;     ((v4u*)urow)[lane] = o0; ((v4u*)urow)[64 + lane] = o1;
; __device__ __forceinline__ void prologue(const Ctx& C, const In& I, unsigned char* ws, bf16* hs0) {
;     ...
;     if (C.G == 256) { const int mb = 2048 * (C.bx & 7) + 64 * (C.bx >> 3) + 8 * C.wave;
;         for (int m = mb; m < mb + 8; ++m) first_norm_row(I.x + (size_t)m * D, I.norm_g, U + (size_t)m * D, hs0 + (size_t)m * D, C.lane); }
.LBB0_91:
	s_waitcnt lgkmcnt(0)
	global_load_dwordx4 v[6:9], v[22:23], off
	global_load_dwordx4 v[2:5], v[22:23], off offset:16
	global_load_dwordx4 v[10:13], v[22:23], off offset:2064
	global_load_dwordx4 v[14:17], v[22:23], off offset:2048
	v_lshl_add_u64 v[26:27], s[4:5], 0, v[20:21]
	v_add_co_u32_e32 v34, vcc, s11, v26
	s_add_i32 s9, s9, 1
	s_nop 0
	v_addc_co_u32_e32 v35, vcc, 0, v27, vcc
	v_lshl_add_u64 v[42:43], s[2:3], 0, v[20:21]
	s_add_u32 s2, s2, 0x800
	s_addc_u32 s3, s3, 0
	s_add_u32 s4, s4, 0x800
	s_addc_u32 s5, s5, 0
	v_lshl_add_u64 v[22:23], v[22:23], 0, s[6:7]
	s_cmp_ge_i32 s9, s8
	s_waitcnt vmcnt(0)
	v_cvt_pk_bf16_f32 v26, v6, v7
	v_cvt_pk_bf16_f32 v27, v8, v9
	v_cvt_pk_bf16_f32 v28, v2, v3
	v_cvt_pk_bf16_f32 v29, v4, v5
	v_pk_mul_f32 v[36:37], v[8:9], v[8:9]
	v_pk_mul_f32 v[44:45], v[6:7], v[6:7]
	v_pk_mul_f32 v[38:39], v[4:5], v[4:5]
	v_pk_mul_f32 v[46:47], v[2:3], v[2:3]
	v_mul_f32_e32 v40, v15, v15
	v_cvt_pk_bf16_f32 v30, v14, v15
	v_cvt_pk_bf16_f32 v31, v16, v17
	v_cvt_pk_bf16_f32 v32, v10, v11
	v_cvt_pk_bf16_f32 v33, v12, v13
	global_store_dwordx4 v[34:35], v[26:29], off sc1
	global_store_dwordx4 v[34:35], v[30:33], off offset:1024 sc1
	v_pk_mov_b32 v[50:51], v[44:45], v[36:37] op_sel:[1,0]
	v_mov_b32_e32 v45, v37
	v_pk_mov_b32 v[52:53], v[46:47], v[38:39] op_sel:[1,0]
	v_mov_b32_e32 v47, v39
	v_pk_fma_f32 v[54:55], v[14:15], v[14:15], v[40:41] op_sel_hi:[1,1,0]
	global_load_dwordx4 v[26:29], v[18:19], off
	global_load_dwordx4 v[30:33], v[18:19], off offset:16
	global_load_dwordx4 v[34:37], v[18:19], off offset:2048
	global_load_dwordx4 v[38:41], v[18:19], off offset:2064
	v_mul_f32_e32 v48, v17, v17
	v_pk_add_f32 v[44:45], v[50:51], v[44:45]
	v_pk_add_f32 v[46:47], v[52:53], v[46:47]
	v_mul_f32_e32 v25, v10, v10
	v_mul_f32_e32 v56, v11, v11
	v_mul_f32_e32 v57, v12, v12
	v_mul_f32_e32 v58, v13, v13
	v_pk_fma_f32 v[48:49], v[16:17], v[16:17], v[48:49] op_sel_hi:[1,1,0]
	v_pk_add_f32 v[44:45], v[44:45], v[44:45] op_sel:[0,1] op_sel_hi:[1,0]
	v_pk_add_f32 v[46:47], v[46:47], v[46:47] op_sel:[0,1] op_sel_hi:[1,0]
	v_mov_b32_e32 v55, v57
	v_mov_b32_e32 v49, v58
	v_mov_b32_e32 v45, v25
	v_mov_b32_e32 v47, v56
	v_pk_add_f32 v[48:49], v[54:55], v[48:49]
	v_pk_add_f32 v[44:45], v[44:45], v[46:47]
	s_nop 0
	v_pk_add_f32 v[44:45], v[44:45], v[48:49]
	s_nop 0
	v_add_f32_e32 v25, v44, v45
	s_nop 1
	v_add_f32_dpp v25, v25, v25 quad_perm:[1,0,3,2] row_mask:0xf bank_mask:0xf bound_ctrl:1
	s_nop 1
	v_add_f32_dpp v25, v25, v25 quad_perm:[2,3,0,1] row_mask:0xf bank_mask:0xf bound_ctrl:1
	s_nop 1
	v_add_f32_dpp v25, v25, v25 row_half_mirror row_mask:0xf bank_mask:0xf bound_ctrl:1
	s_nop 1
	v_add_f32_dpp v25, v25, v25 row_mirror row_mask:0xf bank_mask:0xf bound_ctrl:1
	s_nop 0
	v_readlane_b32 s13, v25, 16
	v_readlane_b32 s14, v25, 48
	v_readlane_b32 s0, v25, 0
	v_readlane_b32 s1, v25, 32
	v_mov_b32_e32 v44, s13
	v_mov_b32_e32 v45, s14
	v_pk_add_f32 v[44:45], s[0:1], v[44:45]
	s_nop 0
	v_add_f32_e32 v25, v44, v45
	v_fmamk_f32 v25, v25, 0x3a800000, v1
	v_mul_f32_e32 v44, 0x4f800000, v25
	v_cmp_gt_f32_e32 vcc, s10, v25
	s_nop 1
	v_cndmask_b32_e32 v25, v25, v44, vcc
	v_sqrt_f32_e32 v44, v25
	s_nop 0
	v_add_u32_e32 v45, -1, v44
	v_add_u32_e32 v46, 1, v44
	v_fma_f32 v47, -v45, v44, v25
	v_fma_f32 v48, -v46, v44, v25
	v_cmp_ge_f32_e64 s[0:1], 0, v47
	s_nop 1
	v_cndmask_b32_e64 v44, v44, v45, s[0:1]
	v_cmp_lt_f32_e64 s[0:1], 0, v48
	s_nop 1
	v_cndmask_b32_e64 v44, v44, v46, s[0:1]
	v_mul_f32_e32 v45, 0x37800000, v44
	v_cndmask_b32_e32 v44, v44, v45, vcc
	v_cmp_class_f32_e32 vcc, v25, v24
	s_nop 1
	v_cndmask_b32_e32 v25, v44, v25, vcc
	v_div_scale_f32 v44, s[0:1], v25, v25, 1.0
	v_rcp_f32_e32 v46, v44
	v_div_scale_f32 v45, vcc, 1.0, v25, 1.0
	v_fma_f32 v47, -v44, v46, 1.0
	v_fmac_f32_e32 v46, v47, v46
	v_mul_f32_e32 v47, v45, v46
	v_fma_f32 v48, -v44, v47, v45
	v_fmac_f32_e32 v47, v48, v46
	v_fma_f32 v44, -v44, v47, v45
	v_div_fmas_f32 v44, v44, v46, v47
	v_div_fixup_f32 v44, v44, v25, 1.0
	v_pk_mul_f32 v[6:7], v[6:7], v[44:45] op_sel_hi:[1,0]
	v_pk_mul_f32 v[2:3], v[2:3], v[44:45] op_sel_hi:[1,0]
	v_pk_mul_f32 v[4:5], v[4:5], v[44:45] op_sel_hi:[1,0]
	v_add_co_u32_e32 v42, vcc, s12, v42
	v_pk_mul_f32 v[8:9], v[8:9], v[44:45] op_sel_hi:[1,0]
	s_waitcnt vmcnt(3)
	v_pk_mul_f32 v[6:7], v[6:7], v[26:27]
	s_waitcnt vmcnt(2)
	v_pk_mul_f32 v[26:27], v[4:5], v[32:33]
	v_pk_mul_f32 v[4:5], v[2:3], v[30:31]
	v_addc_co_u32_e32 v43, vcc, 0, v43, vcc
	v_pk_mul_f32 v[14:15], v[14:15], v[44:45] op_sel_hi:[1,0]
	v_pk_mul_f32 v[16:17], v[16:17], v[44:45] op_sel_hi:[1,0]
	v_pk_mul_f32 v[10:11], v[10:11], v[44:45] op_sel_hi:[1,0]
	v_pk_mul_f32 v[12:13], v[12:13], v[44:45] op_sel_hi:[1,0]
	v_pk_mul_f32 v[8:9], v[8:9], v[28:29]
	v_cvt_pk_bf16_f32 v2, v6, v7
	v_cvt_pk_bf16_f32 v4, v4, v5
	v_cvt_pk_bf16_f32 v5, v26, v27
	s_waitcnt vmcnt(1)
	v_pk_mul_f32 v[16:17], v[16:17], v[36:37]
	v_cvt_pk_bf16_f32 v3, v8, v9
	v_pk_mul_f32 v[14:15], v[14:15], v[34:35]
	s_waitcnt vmcnt(0)
	v_pk_mul_f32 v[12:13], v[12:13], v[40:41]
	v_pk_mul_f32 v[10:11], v[10:11], v[38:39]
	v_cvt_pk_bf16_f32 v6, v14, v15
	v_cvt_pk_bf16_f32 v7, v16, v17
	v_cvt_pk_bf16_f32 v9, v12, v13
	s_nop 0
	v_cvt_pk_bf16_f32 v8, v10, v11
	flat_store_dwordx4 v[42:43], v[2:5]
	flat_store_dwordx4 v[42:43], v[6:9] offset:1024
	s_cbranch_scc0 .LBB0_91

; #define GAS __attribute__((address_space(1)))
; #define LAS __attribute__((address_space(3)))
; #define LDS_WAIT() asm volatile("s_waitcnt lgkmcnt(0)" ::: "memory")
; __device__ __forceinline__ unsigned pk2(float lo, float hi) { unsigned r; asm("v_cvt_pk_bf16_f32 %0, %1, %2" : "=v"(r) : "v"(lo), "v"(hi)); return r; }
; __device__ __forceinline__ void transpose_item(const float* W, int K, int N, bf16* WT, int drow0, int kb, int n0, LAS float* scr, int lane) {
;     const int k0 = 64 * kb; const int c4 = 4 * (lane & 7); const bool ok = (n0 + c4) < N;
;     f32x4 v[8];
; #pragma unroll
;     for (int i = 0; i < 8; ++i) { const int kk = 8 * i + (lane >> 3); v[i] = ok ? *(const f32x4*)(W + (size_t)(k0 + kk) * N + n0 + c4) : (f32x4){0.f, 0.f, 0.f, 0.f}; }
; #pragma unroll
;     for (int i = 0; i < 8; ++i) { const int kk = 8 * i + (lane >> 3); LAS float* d = scr + kk * 33 + c4; d[0] = v[i][0]; d[1] = v[i][1]; d[2] = v[i][2]; d[3] = v[i][3]; }
;     LDS_WAIT(); asm volatile("" ::: "memory");
;     const int c = lane & 7;
; #pragma unroll
;     for (int j = 0; j < 4; ++j) { const int n = (lane >> 3) + 8 * j; const LAS float* s = scr + (8 * c) * 33 + n;
;         v4u o; o.x = pk2(s[0 * 33], s[1 * 33]); o.y = pk2(s[2 * 33], s[3 * 33]); o.z = pk2(s[4 * 33], s[5 * 33]); o.w = pk2(s[6 * 33], s[7 * 33]);
;         *(GAS v4u*)(WT + (size_t)(drow0 + n) * K + k0 + 8 * c) = o; }
;     LDS_WAIT(); asm volatile("" ::: "memory");
; }
; __device__ __forceinline__ void convert_item(const In& I, unsigned char* ws, int it, LAS float* scr, int lane) {
;     ...
;     if (r < 4 * I_W1) { const int jk = r / I_W1; r -= jk * I_W1; const int kb = r / 8, nb = r % 8;
;         transpose_item(I.nsa_w1 + (size_t)jk * 2048 * 256, 2048, 256, W1t + (size_t)jk * 256 * 2048, 32 * nb, kb, 32 * nb, scr, lane); return; }
.LBB0_174:
	s_andn2_b64 vcc, exec, s[2:3]
	s_cbranch_vccnz .LBB0_176
	s_add_i32 s2, s40, 0x400
	s_lshr_b32 s68, s2, 8
	s_lshl_b64 s[2:3], s[68:69], 21
	v_readlane_b32 s48, v253, 16
	v_readlane_b32 s49, v253, 17
	s_add_u32 s6, s48, s2
	s_addc_u32 s7, s49, s3
	s_lshl_b64 s[2:3], s[68:69], 20
	s_add_u32 s8, s33, s2
	s_addc_u32 s3, s34, s3
	s_and_b32 s2, s42, 0xe0
	s_and_b32 s9, s41, 0x7c0
	s_lshl_b32 s10, s2, 2
	s_add_u32 s6, s6, s10
	v_or_b32_e32 v6, s9, v39
	s_addc_u32 s7, s7, 0
	v_lshlrev_b32_e32 v2, 2, v36
	v_lshl_add_u64 v[4:5], s[6:7], 0, v[2:3]
	v_lshlrev_b32_e32 v2, 10, v6
	v_lshl_add_u64 v[32:33], v[4:5], 0, v[2:3]
	v_add_co_u32_e32 v8, vcc, s74, v32
	global_load_dwordx4 v[4:7], v[32:33], off
	s_nop 0
	v_addc_co_u32_e32 v9, vcc, 0, v33, vcc
	s_movk_i32 s6, 0x4000
	global_load_dwordx4 v[8:11], v[8:9], off
	v_add_co_u32_e32 v12, vcc, s6, v32
	s_movk_i32 s6, 0x6000
	s_nop 0
	v_addc_co_u32_e32 v13, vcc, 0, v33, vcc
	global_load_dwordx4 v[12:15], v[12:13], off
	v_add_co_u32_e32 v16, vcc, s6, v32
	s_mov_b32 s6, 0xa000
	s_nop 0
	v_addc_co_u32_e32 v17, vcc, 0, v33, vcc
	global_load_dwordx4 v[16:19], v[16:17], off
	v_add_co_u32_e32 v20, vcc, s81, v32
	v_add_u32_e32 v2, v44, v45
	s_nop 0
	v_addc_co_u32_e32 v21, vcc, 0, v33, vcc
	global_load_dwordx4 v[20:23], v[20:21], off
	v_add_co_u32_e32 v24, vcc, s6, v32
	s_mov_b32 s6, 0xc000
	s_nop 0
	v_addc_co_u32_e32 v25, vcc, 0, v33, vcc
	global_load_dwordx4 v[24:27], v[24:25], off
	v_add_co_u32_e32 v28, vcc, s6, v32
	s_mov_b32 s6, 0xe000
	s_nop 0
	v_addc_co_u32_e32 v29, vcc, 0, v33, vcc
	global_load_dwordx4 v[28:31], v[28:29], off
	v_add_co_u32_e32 v32, vcc, s6, v32
	s_lshl_b32 s6, s9, 1
	s_nop 0
	v_addc_co_u32_e32 v33, vcc, 0, v33, vcc
	global_load_dwordx4 v[32:35], v[32:33], off
	s_add_u32 s6, s8, s6
	s_addc_u32 s7, s3, 0
	v_readlane_b32 s50, v253, 18
	v_readlane_b32 s51, v253, 19
	v_readlane_b32 s52, v253, 20
	v_readlane_b32 s53, v253, 21
	v_readlane_b32 s54, v253, 22
	v_readlane_b32 s55, v253, 23
	v_readlane_b32 s56, v253, 24
	v_readlane_b32 s57, v253, 25
	v_readlane_b32 s58, v253, 26
	v_readlane_b32 s59, v253, 27
	v_readlane_b32 s60, v253, 28
	v_readlane_b32 s61, v253, 29
	v_readlane_b32 s62, v253, 30
	v_readlane_b32 s63, v253, 31
	s_waitcnt vmcnt(0)
	ds_write2_b32 v2, v4, v5 offset1:1
	ds_write2_b32 v2, v6, v7 offset0:2 offset1:3
	v_add_u32_e32 v4, 0x420, v2
	ds_write2_b32 v4, v8, v9 offset1:1
	v_add_u32_e32 v4, 0x428, v2
	ds_write2_b32 v4, v10, v11 offset1:1
	v_add_u32_e32 v4, 0x840, v2
	ds_write2_b32 v4, v12, v13 offset1:1
	v_add_u32_e32 v4, 0x848, v2
	ds_write2_b32 v4, v14, v15 offset1:1
	v_add_u32_e32 v4, 0xc60, v2
	ds_write2_b32 v4, v16, v17 offset1:1
	v_add_u32_e32 v4, 0xc68, v2
	ds_write2_b32 v4, v18, v19 offset1:1
	v_add_u32_e32 v4, 0x1080, v2
	ds_write2_b32 v4, v20, v21 offset1:1
	v_add_u32_e32 v4, 0x1088, v2
	ds_write2_b32 v4, v22, v23 offset1:1
	v_add_u32_e32 v4, 0x14a0, v2
	ds_write2_b32 v4, v24, v25 offset1:1
	v_add_u32_e32 v4, 0x14a8, v2
	ds_write2_b32 v4, v26, v27 offset1:1
	v_add_u32_e32 v4, 0x18c0, v2
	ds_write2_b32 v4, v28, v29 offset1:1
	v_add_u32_e32 v4, 0x18c8, v2
	ds_write2_b32 v4, v30, v31 offset1:1
	v_add_u32_e32 v4, 0x1ce0, v2
	v_add_u32_e32 v2, 0x1ce8, v2
	ds_write2_b32 v4, v32, v33 offset1:1
	ds_write2_b32 v2, v34, v35 offset1:1
	s_waitcnt lgkmcnt(0)
	ds_read2_b32 v[10:11], v49 offset0:33 offset1:41
	ds_read2_b32 v[12:13], v49 offset1:8
	v_lshlrev_b32_e32 v2, 1, v38
	ds_read2_b32 v[14:15], v49 offset0:66 offset1:74
	ds_read2_b32 v[16:17], v49 offset0:99 offset1:107
	ds_read2_b32 v[18:19], v49 offset0:132 offset1:140
	ds_read2_b32 v[20:21], v49 offset0:165 offset1:173
	ds_read2_b32 v[22:23], v49 offset0:198 offset1:206
	ds_read2_b32 v[24:25], v49 offset0:231 offset1:239
	v_lshl_add_u64 v[8:9], s[6:7], 0, v[2:3]
	v_or_b32_e32 v2, s2, v39
	v_lshlrev_b32_e32 v2, 12, v2
	v_lshl_add_u64 v[26:27], v[8:9], 0, v[2:3]
	v_or_b32_e32 v2, s2, v46
	s_waitcnt lgkmcnt(0)
	v_cvt_pk_bf16_f32 v4, v12, v10
	v_lshlrev_b32_e32 v2, 12, v2
	v_cvt_pk_bf16_f32 v5, v14, v16
	v_cvt_pk_bf16_f32 v6, v18, v20
	v_cvt_pk_bf16_f32 v7, v22, v24
	global_store_dwordx4 v[26:27], v[4:7], off sc1
	s_nop 1
	v_cvt_pk_bf16_f32 v4, v13, v11
	v_lshl_add_u64 v[10:11], v[8:9], 0, v[2:3]
	v_cvt_pk_bf16_f32 v5, v15, v17
	v_cvt_pk_bf16_f32 v6, v19, v21
	v_cvt_pk_bf16_f32 v7, v23, v25
	global_store_dwordx4 v[10:11], v[4:7], off sc1
	ds_read2_b32 v[10:11], v49 offset0:16 offset1:24
	ds_read2_b32 v[12:13], v49 offset0:49 offset1:57
	ds_read2_b32 v[14:15], v49 offset0:82 offset1:90
	ds_read2_b32 v[16:17], v49 offset0:115 offset1:123
	ds_read2_b32 v[18:19], v49 offset0:148 offset1:156
	ds_read2_b32 v[20:21], v49 offset0:181 offset1:189
	ds_read2_b32 v[22:23], v49 offset0:214 offset1:222
	ds_read2_b32 v[24:25], v49 offset0:247 offset1:255
	v_or_b32_e32 v2, s2, v47
	v_lshlrev_b32_e32 v2, 12, v2
	v_lshl_add_u64 v[26:27], v[8:9], 0, v[2:3]
	v_or_b32_e32 v2, s2, v48
	v_lshlrev_b32_e32 v2, 12, v2
	s_waitcnt lgkmcnt(6)
	v_cvt_pk_bf16_f32 v4, v10, v12
	s_waitcnt lgkmcnt(4)
	v_cvt_pk_bf16_f32 v5, v14, v16
	s_waitcnt lgkmcnt(2)
	v_cvt_pk_bf16_f32 v6, v18, v20
	s_waitcnt lgkmcnt(0)
	v_cvt_pk_bf16_f32 v7, v22, v24
	v_lshl_add_u64 v[8:9], v[8:9], 0, v[2:3]
	global_store_dwordx4 v[26:27], v[4:7], off sc1
	s_nop 1
	v_cvt_pk_bf16_f32 v4, v11, v13
	v_cvt_pk_bf16_f32 v5, v15, v17
	v_cvt_pk_bf16_f32 v6, v19, v21
	v_cvt_pk_bf16_f32 v7, v23, v25
	global_store_dwordx4 v[8:9], v[4:7], off sc1
	s_waitcnt lgkmcnt(0)

; #define GAS __attribute__((address_space(1)))
; #define LAS __attribute__((address_space(3)))
; #define LDS_WAIT() asm volatile("s_waitcnt lgkmcnt(0)" ::: "memory")
; __device__ __forceinline__ unsigned pk2(float lo, float hi) { unsigned r; asm("v_cvt_pk_bf16_f32 %0, %1, %2" : "=v"(r) : "v"(lo), "v"(hi)); return r; }
; __device__ __forceinline__ void transpose_item(const float* W, int K, int N, bf16* WT, int drow0, int kb, int n0, LAS float* scr, int lane) {
;     const int k0 = 64 * kb; const int c4 = 4 * (lane & 7); const bool ok = (n0 + c4) < N;
;     f32x4 v[8];
; #pragma unroll
;     for (int i = 0; i < 8; ++i) { const int kk = 8 * i + (lane >> 3); v[i] = ok ? *(const f32x4*)(W + (size_t)(k0 + kk) * N + n0 + c4) : (f32x4){0.f, 0.f, 0.f, 0.f}; }
; #pragma unroll
;     for (int i = 0; i < 8; ++i) { const int kk = 8 * i + (lane >> 3); LAS float* d = scr + kk * 33 + c4; d[0] = v[i][0]; d[1] = v[i][1]; d[2] = v[i][2]; d[3] = v[i][3]; }
;     LDS_WAIT(); asm volatile("" ::: "memory");
;     const int c = lane & 7;
; #pragma unroll
;     for (int j = 0; j < 4; ++j) { const int n = (lane >> 3) + 8 * j; const LAS float* s = scr + (8 * c) * 33 + n;
;         v4u o; o.x = pk2(s[0 * 33], s[1 * 33]); o.y = pk2(s[2 * 33], s[3 * 33]); o.z = pk2(s[4 * 33], s[5 * 33]); o.w = pk2(s[6 * 33], s[7 * 33]);
;         *(GAS v4u*)(WT + (size_t)(drow0 + n) * K + k0 + 8 * c) = o; }
;     LDS_WAIT(); asm volatile("" ::: "memory");
; }
; __device__ __forceinline__ void convert_item(const In& I, unsigned char* ws, int it, LAS float* scr, int lane) {
;     ...
;     if (r < 2 * I_SQ) { const int j = r / I_SQ; r -= j * I_SQ; const int kb = r / 32, nb = r % 32;
;         transpose_item(I.nsa_w_out + (size_t)j * D * D, D, D, Wnout + (size_t)j * D * D, 32 * nb, kb, 32 * nb, scr, lane); return; }
.LBB0_177:
	s_andn2_b64 vcc, exec, s[2:3]
	s_cbranch_vccnz .LBB0_179
	s_add_i32 s2, s40, 0x800
	s_lshr_b32 s68, s2, 9
	v_readlane_b32 s48, v253, 16
	s_lshl_b64 s[2:3], s[68:69], 22
	v_readlane_b32 s60, v253, 28
	v_readlane_b32 s61, v253, 29
	s_add_u32 s6, s60, s2
	s_addc_u32 s7, s61, s3
	s_lshl_b64 s[2:3], s[68:69], 21
	s_add_u32 s8, s27, s2
	s_addc_u32 s3, s31, s3
	s_and_b32 s2, s42, 0x3e0
	s_add_i32 s9, s43, s44
	s_and_b32 s9, s9, 0x3c0
	s_lshl_b32 s10, s2, 2
	s_add_u32 s6, s6, s10
	v_or_b32_e32 v6, s9, v39
	s_addc_u32 s7, s7, 0
	v_lshlrev_b32_e32 v2, 2, v36
	v_lshl_add_u64 v[4:5], s[6:7], 0, v[2:3]
	v_lshlrev_b32_e32 v2, 12, v6
	v_lshl_add_u64 v[32:33], v[4:5], 0, v[2:3]
	v_add_co_u32_e32 v8, vcc, s81, v32
	global_load_dwordx4 v[4:7], v[32:33], off
	s_nop 0
	v_addc_co_u32_e32 v9, vcc, 0, v33, vcc
	global_load_dwordx4 v[8:11], v[8:9], off
	v_add_co_u32_e32 v12, vcc, s79, v32
	v_add_u32_e32 v2, v44, v45
	s_nop 0
	v_addc_co_u32_e32 v13, vcc, 0, v33, vcc
	global_load_dwordx4 v[12:15], v[12:13], off
	v_add_co_u32_e32 v16, vcc, s80, v32
	s_lshl_b32 s6, s9, 1
	s_nop 0
	v_addc_co_u32_e32 v17, vcc, 0, v33, vcc
	global_load_dwordx4 v[16:19], v[16:17], off
	v_add_co_u32_e32 v20, vcc, s85, v32
	s_add_u32 s6, s8, s6
	s_nop 0
	v_addc_co_u32_e32 v21, vcc, 0, v33, vcc
	global_load_dwordx4 v[20:23], v[20:21], off
	v_add_co_u32_e32 v24, vcc, s86, v32
	s_addc_u32 s7, s3, 0
	s_nop 0
	v_addc_co_u32_e32 v25, vcc, 0, v33, vcc
	global_load_dwordx4 v[24:27], v[24:25], off
	v_add_co_u32_e32 v28, vcc, s87, v32
	v_readlane_b32 s49, v253, 17
	s_nop 0
	v_addc_co_u32_e32 v29, vcc, 0, v33, vcc
	global_load_dwordx4 v[28:31], v[28:29], off
	v_add_co_u32_e32 v32, vcc, s89, v32
	v_readlane_b32 s50, v253, 18
	s_nop 0
	v_addc_co_u32_e32 v33, vcc, 0, v33, vcc
	global_load_dwordx4 v[32:35], v[32:33], off
	v_readlane_b32 s51, v253, 19
	v_readlane_b32 s52, v253, 20
	v_readlane_b32 s53, v253, 21
	v_readlane_b32 s54, v253, 22
	v_readlane_b32 s55, v253, 23
	v_readlane_b32 s56, v253, 24
	v_readlane_b32 s57, v253, 25
	v_readlane_b32 s58, v253, 26
	v_readlane_b32 s59, v253, 27
	v_readlane_b32 s62, v253, 30
	v_readlane_b32 s63, v253, 31
	s_waitcnt vmcnt(0)
	ds_write2_b32 v2, v4, v5 offset1:1
	ds_write2_b32 v2, v6, v7 offset0:2 offset1:3
	v_add_u32_e32 v4, 0x420, v2
	ds_write2_b32 v4, v8, v9 offset1:1
	v_add_u32_e32 v4, 0x428, v2
	ds_write2_b32 v4, v10, v11 offset1:1
	v_add_u32_e32 v4, 0x840, v2
	ds_write2_b32 v4, v12, v13 offset1:1
	v_add_u32_e32 v4, 0x848, v2
	ds_write2_b32 v4, v14, v15 offset1:1
	v_add_u32_e32 v4, 0xc60, v2
	ds_write2_b32 v4, v16, v17 offset1:1
	v_add_u32_e32 v4, 0xc68, v2
	ds_write2_b32 v4, v18, v19 offset1:1
	v_add_u32_e32 v4, 0x1080, v2
	ds_write2_b32 v4, v20, v21 offset1:1
	v_add_u32_e32 v4, 0x1088, v2
	ds_write2_b32 v4, v22, v23 offset1:1
	v_add_u32_e32 v4, 0x14a0, v2
	ds_write2_b32 v4, v24, v25 offset1:1
	v_add_u32_e32 v4, 0x14a8, v2
	ds_write2_b32 v4, v26, v27 offset1:1
	v_add_u32_e32 v4, 0x18c0, v2
	ds_write2_b32 v4, v28, v29 offset1:1
	v_add_u32_e32 v4, 0x18c8, v2
	ds_write2_b32 v4, v30, v31 offset1:1
	v_add_u32_e32 v4, 0x1ce0, v2
	v_add_u32_e32 v2, 0x1ce8, v2
	ds_write2_b32 v4, v32, v33 offset1:1
	ds_write2_b32 v2, v34, v35 offset1:1
	s_waitcnt lgkmcnt(0)
	ds_read2_b32 v[10:11], v49 offset0:33 offset1:41
	ds_read2_b32 v[12:13], v49 offset1:8
	v_lshlrev_b32_e32 v2, 1, v38
	ds_read2_b32 v[14:15], v49 offset0:66 offset1:74
	ds_read2_b32 v[16:17], v49 offset0:99 offset1:107
	ds_read2_b32 v[18:19], v49 offset0:132 offset1:140
	ds_read2_b32 v[20:21], v49 offset0:165 offset1:173
	ds_read2_b32 v[22:23], v49 offset0:198 offset1:206
	ds_read2_b32 v[24:25], v49 offset0:231 offset1:239
	v_lshl_add_u64 v[8:9], s[6:7], 0, v[2:3]
	v_or_b32_e32 v2, s2, v39
	v_lshlrev_b32_e32 v2, 11, v2
	v_lshl_add_u64 v[26:27], v[8:9], 0, v[2:3]
	v_or_b32_e32 v2, s2, v46
	s_waitcnt lgkmcnt(0)
	v_cvt_pk_bf16_f32 v4, v12, v10
	v_lshlrev_b32_e32 v2, 11, v2
	v_cvt_pk_bf16_f32 v5, v14, v16
	v_cvt_pk_bf16_f32 v6, v18, v20
	v_cvt_pk_bf16_f32 v7, v22, v24
	global_store_dwordx4 v[26:27], v[4:7], off sc1
	s_nop 1
	v_cvt_pk_bf16_f32 v4, v13, v11
	v_lshl_add_u64 v[10:11], v[8:9], 0, v[2:3]
	v_cvt_pk_bf16_f32 v5, v15, v17
	v_cvt_pk_bf16_f32 v6, v19, v21
	v_cvt_pk_bf16_f32 v7, v23, v25
	global_store_dwordx4 v[10:11], v[4:7], off sc1
	ds_read2_b32 v[10:11], v49 offset0:16 offset1:24
	ds_read2_b32 v[12:13], v49 offset0:49 offset1:57
	ds_read2_b32 v[14:15], v49 offset0:82 offset1:90
	ds_read2_b32 v[16:17], v49 offset0:115 offset1:123
	ds_read2_b32 v[18:19], v49 offset0:148 offset1:156
	ds_read2_b32 v[20:21], v49 offset0:181 offset1:189
	ds_read2_b32 v[22:23], v49 offset0:214 offset1:222
	ds_read2_b32 v[24:25], v49 offset0:247 offset1:255
	v_or_b32_e32 v2, s2, v47
	v_lshlrev_b32_e32 v2, 11, v2
	v_lshl_add_u64 v[26:27], v[8:9], 0, v[2:3]
	v_or_b32_e32 v2, s2, v48
	v_lshlrev_b32_e32 v2, 11, v2
	s_waitcnt lgkmcnt(6)
	v_cvt_pk_bf16_f32 v4, v10, v12
	s_waitcnt lgkmcnt(4)
	v_cvt_pk_bf16_f32 v5, v14, v16
	s_waitcnt lgkmcnt(2)
	v_cvt_pk_bf16_f32 v6, v18, v20
	s_waitcnt lgkmcnt(0)
	v_cvt_pk_bf16_f32 v7, v22, v24
	v_lshl_add_u64 v[8:9], v[8:9], 0, v[2:3]
	global_store_dwordx4 v[26:27], v[4:7], off sc1
	s_nop 1
	v_cvt_pk_bf16_f32 v4, v11, v13
	v_cvt_pk_bf16_f32 v5, v15, v17
	v_cvt_pk_bf16_f32 v6, v19, v21
	v_cvt_pk_bf16_f32 v7, v23, v25
	global_store_dwordx4 v[8:9], v[4:7], off sc1
	s_waitcnt lgkmcnt(0)

; #define GAS __attribute__((address_space(1)))
; #define LAS __attribute__((address_space(3)))
; #define LDS_WAIT() asm volatile("s_waitcnt lgkmcnt(0)" ::: "memory")
; __device__ __forceinline__ unsigned pk2(float lo, float hi) { unsigned r; asm("v_cvt_pk_bf16_f32 %0, %1, %2" : "=v"(r) : "v"(lo), "v"(hi)); return r; }
; __device__ __forceinline__ void transpose_item(const float* W, int K, int N, bf16* WT, int drow0, int kb, int n0, LAS float* scr, int lane) {
;     ...
;     for (int i = 0; i < 8; ++i) { const int kk = 8 * i + (lane >> 3); v[i] = ok ? *(const f32x4*)(W + (size_t)(k0 + kk) * N + n0 + c4) : (f32x4){0.f, 0.f, 0.f, 0.f}; }
; #pragma unroll
;     for (int i = 0; i < 8; ++i) { const int kk = 8 * i + (lane >> 3); LAS float* d = scr + kk * 33 + c4; d[0] = v[i][0]; d[1] = v[i][1]; d[2] = v[i][2]; d[3] = v[i][3]; }
;     LDS_WAIT(); asm volatile("" ::: "memory");
;     const int c = lane & 7;
; #pragma unroll
;     for (int j = 0; j < 4; ++j) { const int n = (lane >> 3) + 8 * j; const LAS float* s = scr + (8 * c) * 33 + n;
;         v4u o; o.x = pk2(s[0 * 33], s[1 * 33]); o.y = pk2(s[2 * 33], s[3 * 33]); o.z = pk2(s[4 * 33], s[5 * 33]); o.w = pk2(s[6 * 33], s[7 * 33]);
;         *(GAS v4u*)(WT + (size_t)(drow0 + n) * K + k0 + 8 * c) = o; }
;     LDS_WAIT(); asm volatile("" ::: "memory");
; __device__ __forceinline__ void convert_item(const In& I, unsigned char* ws, int it, LAS float* scr, int lane) {
;     ...
;     if (r < 2 * I_FIN) { const int j = r / I_FIN; r -= j * I_FIN; const int kb = r / 104, nb = r % 104;
;         transpose_item(I.fox_w_in + (size_t)j * D * FOX_IN, D, FOX_IN, Wfin + (size_t)j * FOX_IN_PAD * D, 32 * nb, kb, 32 * nb, scr, lane); return; }
.LBB0_197:
	s_or_b64 exec, exec, s[12:13]
	v_add_u32_e32 v2, v44, v45
	s_waitcnt vmcnt(0)
	ds_write2_b32 v2, v8, v9 offset1:1
	ds_write2_b32 v2, v10, v11 offset0:2 offset1:3
	v_add_u32_e32 v8, 0x420, v2
	ds_write2_b32 v8, v4, v5 offset1:1
	v_add_u32_e32 v4, 0x428, v2
	ds_write2_b32 v4, v6, v7 offset1:1
	v_add_u32_e32 v4, 0x840, v2
	ds_write2_b32 v4, v16, v17 offset1:1
	v_add_u32_e32 v4, 0x848, v2
	ds_write2_b32 v4, v18, v19 offset1:1
	v_add_u32_e32 v4, 0xc60, v2
	ds_write2_b32 v4, v12, v13 offset1:1
	v_add_u32_e32 v4, 0xc68, v2
	ds_write2_b32 v4, v14, v15 offset1:1
	v_add_u32_e32 v4, 0x1080, v2
	ds_write2_b32 v4, v24, v25 offset1:1
	v_add_u32_e32 v4, 0x1088, v2
	ds_write2_b32 v4, v26, v27 offset1:1
	v_add_u32_e32 v4, 0x14a0, v2
	ds_write2_b32 v4, v20, v21 offset1:1
	v_add_u32_e32 v4, 0x14a8, v2
	ds_write2_b32 v4, v22, v23 offset1:1
	v_add_u32_e32 v4, 0x18c0, v2
	ds_write2_b32 v4, v32, v33 offset1:1
	v_add_u32_e32 v4, 0x18c8, v2
	s_and_b64 s[2:3], s[10:11], exec
	ds_write2_b32 v4, v34, v35 offset1:1
	v_add_u32_e32 v4, 0x1ce0, v2
	v_add_u32_e32 v2, 0x1ce8, v2
	s_cselect_b32 s2, 0x680000, 0
	ds_write2_b32 v4, v28, v29 offset1:1
	ds_write2_b32 v2, v30, v31 offset1:1
	s_add_u32 s7, s25, s2
	s_waitcnt lgkmcnt(0)
	s_addc_u32 s10, s26, 0
	s_ashr_i32 s9, s8, 31
	s_lshl_b64 s[2:3], s[8:9], 1
	ds_read2_b32 v[8:9], v49 offset0:33 offset1:41
	ds_read2_b32 v[10:11], v49 offset1:8
	ds_read2_b32 v[12:13], v49 offset0:66 offset1:74
	ds_read2_b32 v[14:15], v49 offset0:99 offset1:107
	ds_read2_b32 v[16:17], v49 offset0:132 offset1:140
	ds_read2_b32 v[18:19], v49 offset0:165 offset1:173
	ds_read2_b32 v[20:21], v49 offset0:198 offset1:206
	ds_read2_b32 v[22:23], v49 offset0:231 offset1:239
	s_add_u32 s2, s7, s2
	v_or_b32_e32 v26, s6, v39
	s_addc_u32 s3, s10, s3
	v_lshlrev_b32_e32 v2, 1, v38
	v_ashrrev_i32_e32 v27, 31, v26
	v_lshl_add_u64 v[24:25], s[2:3], 0, v[2:3]
	v_lshlrev_b64 v[26:27], 11, v[26:27]
	s_waitcnt lgkmcnt(0)
	v_cvt_pk_bf16_f32 v4, v10, v8
	v_lshl_add_u64 v[26:27], v[24:25], 0, v[26:27]
	v_or_b32_e32 v8, s6, v46
	v_cvt_pk_bf16_f32 v5, v12, v14
	v_cvt_pk_bf16_f32 v6, v16, v18
	v_cvt_pk_bf16_f32 v7, v20, v22
	global_store_dwordx4 v[26:27], v[4:7], off sc1
	s_nop 1
	v_cvt_pk_bf16_f32 v4, v11, v9
	v_ashrrev_i32_e32 v9, 31, v8
	v_lshlrev_b64 v[8:9], 11, v[8:9]
	v_cvt_pk_bf16_f32 v5, v13, v15
	v_cvt_pk_bf16_f32 v6, v17, v19
	v_cvt_pk_bf16_f32 v7, v21, v23
	v_lshl_add_u64 v[8:9], v[24:25], 0, v[8:9]
	ds_read2_b32 v[10:11], v49 offset0:16 offset1:24
	ds_read2_b32 v[12:13], v49 offset0:49 offset1:57
	ds_read2_b32 v[14:15], v49 offset0:82 offset1:90
	ds_read2_b32 v[16:17], v49 offset0:115 offset1:123
	ds_read2_b32 v[18:19], v49 offset0:148 offset1:156
	ds_read2_b32 v[20:21], v49 offset0:181 offset1:189
	ds_read2_b32 v[22:23], v49 offset0:214 offset1:222
	ds_read2_b32 v[26:27], v49 offset0:247 offset1:255
	global_store_dwordx4 v[8:9], v[4:7], off sc1
	v_or_b32_e32 v8, s6, v47
	v_ashrrev_i32_e32 v9, 31, v8
	v_lshlrev_b64 v[8:9], 11, v[8:9]
	v_lshl_add_u64 v[8:9], v[24:25], 0, v[8:9]
	s_waitcnt lgkmcnt(6)
	v_cvt_pk_bf16_f32 v4, v10, v12
	s_waitcnt lgkmcnt(4)
	v_cvt_pk_bf16_f32 v5, v14, v16
	s_waitcnt lgkmcnt(2)
	v_cvt_pk_bf16_f32 v6, v18, v20
	s_waitcnt lgkmcnt(0)
	v_cvt_pk_bf16_f32 v7, v22, v26
	global_store_dwordx4 v[8:9], v[4:7], off sc1
	v_or_b32_e32 v8, s6, v48
	v_ashrrev_i32_e32 v9, 31, v8
	v_lshlrev_b64 v[8:9], 11, v[8:9]
	v_lshl_add_u64 v[8:9], v[24:25], 0, v[8:9]
	v_cvt_pk_bf16_f32 v4, v11, v13
	v_cvt_pk_bf16_f32 v5, v15, v17
	v_cvt_pk_bf16_f32 v6, v19, v21
	v_cvt_pk_bf16_f32 v7, v23, v27
	global_store_dwordx4 v[8:9], v[4:7], off sc1
	s_waitcnt lgkmcnt(0)

; #define GAS __attribute__((address_space(1)))
; #define LAS __attribute__((address_space(3)))
; #define LDS_WAIT() asm volatile("s_waitcnt lgkmcnt(0)" ::: "memory")
; __device__ __forceinline__ unsigned pk2(float lo, float hi) { unsigned r; asm("v_cvt_pk_bf16_f32 %0, %1, %2" : "=v"(r) : "v"(lo), "v"(hi)); return r; }
; __device__ __forceinline__ void transpose_item(const float* W, int K, int N, bf16* WT, int drow0, int kb, int n0, LAS float* scr, int lane) {
;     const int k0 = 64 * kb; const int c4 = 4 * (lane & 7); const bool ok = (n0 + c4) < N;
;     f32x4 v[8];
; #pragma unroll
;     for (int i = 0; i < 8; ++i) { const int kk = 8 * i + (lane >> 3); v[i] = ok ? *(const f32x4*)(W + (size_t)(k0 + kk) * N + n0 + c4) : (f32x4){0.f, 0.f, 0.f, 0.f}; }
; #pragma unroll
;     for (int i = 0; i < 8; ++i) { const int kk = 8 * i + (lane >> 3); LAS float* d = scr + kk * 33 + c4; d[0] = v[i][0]; d[1] = v[i][1]; d[2] = v[i][2]; d[3] = v[i][3]; }
;     LDS_WAIT(); asm volatile("" ::: "memory");
;     const int c = lane & 7;
; #pragma unroll
;     for (int j = 0; j < 4; ++j) { const int n = (lane >> 3) + 8 * j; const LAS float* s = scr + (8 * c) * 33 + n;
;         v4u o; o.x = pk2(s[0 * 33], s[1 * 33]); o.y = pk2(s[2 * 33], s[3 * 33]); o.z = pk2(s[4 * 33], s[5 * 33]); o.w = pk2(s[6 * 33], s[7 * 33]);
;         *(GAS v4u*)(WT + (size_t)(drow0 + n) * K + k0 + 8 * c) = o; }
;     LDS_WAIT(); asm volatile("" ::: "memory");
; }
; __device__ __forceinline__ void convert_item(const In& I, unsigned char* ws, int it, LAS float* scr, int lane) {
;     ...
;     if (r < 2 * I_SQ) { const int j = r / I_SQ; r -= j * I_SQ; const int kb = r / 32, nb = r % 32;
;         transpose_item(I.fox_w_out + (size_t)j * D * D, D, D, Wfout + (size_t)j * D * D, 32 * nb, kb, 32 * nb, scr, lane); return; }
.LBB0_199:
	s_andn2_b64 vcc, exec, s[2:3]
	s_cbranch_vccnz .LBB0_201
	s_add_i32 s2, s40, 0x1900
	s_lshr_b32 s68, s2, 9
	v_readlane_b32 s48, v253, 16
	s_lshl_b64 s[2:3], s[68:69], 22
	v_readlane_b32 s54, v253, 22
	v_readlane_b32 s55, v253, 23
	s_add_u32 s6, s54, s2
	s_addc_u32 s7, s55, s3
	s_lshl_b64 s[2:3], s[68:69], 21
	s_add_u32 s8, s23, s2
	s_addc_u32 s3, s24, s3
	s_add_i32 s9, s43, s44
	s_and_b32 s2, s42, 0x3e0
	s_add_i32 s9, s9, 0xfffee200
	s_and_b32 s9, s9, 0x3c0
	s_lshl_b32 s10, s2, 2
	s_add_u32 s6, s6, s10
	v_or_b32_e32 v6, s9, v39
	s_addc_u32 s7, s7, 0
	v_lshlrev_b32_e32 v2, 2, v36
	v_lshl_add_u64 v[4:5], s[6:7], 0, v[2:3]
	v_lshlrev_b32_e32 v2, 12, v6
	v_lshl_add_u64 v[32:33], v[4:5], 0, v[2:3]
	v_add_co_u32_e32 v8, vcc, s81, v32
	global_load_dwordx4 v[4:7], v[32:33], off
	s_nop 0
	v_addc_co_u32_e32 v9, vcc, 0, v33, vcc
	global_load_dwordx4 v[8:11], v[8:9], off
	v_add_co_u32_e32 v12, vcc, s79, v32
	v_add_u32_e32 v2, v44, v45
	s_nop 0
	v_addc_co_u32_e32 v13, vcc, 0, v33, vcc
	global_load_dwordx4 v[12:15], v[12:13], off
	v_add_co_u32_e32 v16, vcc, s80, v32
	s_lshl_b32 s6, s9, 1
	s_nop 0
	v_addc_co_u32_e32 v17, vcc, 0, v33, vcc
	global_load_dwordx4 v[16:19], v[16:17], off
	v_add_co_u32_e32 v20, vcc, s85, v32
	s_add_u32 s6, s8, s6
	s_nop 0
	v_addc_co_u32_e32 v21, vcc, 0, v33, vcc
	global_load_dwordx4 v[20:23], v[20:21], off
	v_add_co_u32_e32 v24, vcc, s86, v32
	s_addc_u32 s7, s3, 0
	s_nop 0
	v_addc_co_u32_e32 v25, vcc, 0, v33, vcc
	global_load_dwordx4 v[24:27], v[24:25], off
	v_add_co_u32_e32 v28, vcc, s87, v32
	v_readlane_b32 s49, v253, 17
	s_nop 0
	v_addc_co_u32_e32 v29, vcc, 0, v33, vcc
	global_load_dwordx4 v[28:31], v[28:29], off
	v_add_co_u32_e32 v32, vcc, s89, v32
	v_readlane_b32 s50, v253, 18
	s_nop 0
	v_addc_co_u32_e32 v33, vcc, 0, v33, vcc
	global_load_dwordx4 v[32:35], v[32:33], off
	v_readlane_b32 s51, v253, 19
	v_readlane_b32 s52, v253, 20
	v_readlane_b32 s53, v253, 21
	v_readlane_b32 s56, v253, 24
	v_readlane_b32 s57, v253, 25
	v_readlane_b32 s58, v253, 26
	v_readlane_b32 s59, v253, 27
	v_readlane_b32 s60, v253, 28
	v_readlane_b32 s61, v253, 29
	v_readlane_b32 s62, v253, 30
	v_readlane_b32 s63, v253, 31
	s_waitcnt vmcnt(0)
	ds_write2_b32 v2, v4, v5 offset1:1
	ds_write2_b32 v2, v6, v7 offset0:2 offset1:3
	v_add_u32_e32 v4, 0x420, v2
	ds_write2_b32 v4, v8, v9 offset1:1
	v_add_u32_e32 v4, 0x428, v2
	ds_write2_b32 v4, v10, v11 offset1:1
	v_add_u32_e32 v4, 0x840, v2
	ds_write2_b32 v4, v12, v13 offset1:1
	v_add_u32_e32 v4, 0x848, v2
	ds_write2_b32 v4, v14, v15 offset1:1
	v_add_u32_e32 v4, 0xc60, v2
	ds_write2_b32 v4, v16, v17 offset1:1
	v_add_u32_e32 v4, 0xc68, v2
	ds_write2_b32 v4, v18, v19 offset1:1
	v_add_u32_e32 v4, 0x1080, v2
	ds_write2_b32 v4, v20, v21 offset1:1
	v_add_u32_e32 v4, 0x1088, v2
	ds_write2_b32 v4, v22, v23 offset1:1
	v_add_u32_e32 v4, 0x14a0, v2
	ds_write2_b32 v4, v24, v25 offset1:1
	v_add_u32_e32 v4, 0x14a8, v2
	ds_write2_b32 v4, v26, v27 offset1:1
	v_add_u32_e32 v4, 0x18c0, v2
	ds_write2_b32 v4, v28, v29 offset1:1
	v_add_u32_e32 v4, 0x18c8, v2
	ds_write2_b32 v4, v30, v31 offset1:1
	v_add_u32_e32 v4, 0x1ce0, v2
	v_add_u32_e32 v2, 0x1ce8, v2
	ds_write2_b32 v4, v32, v33 offset1:1
	ds_write2_b32 v2, v34, v35 offset1:1
	s_waitcnt lgkmcnt(0)
	ds_read2_b32 v[10:11], v49 offset0:33 offset1:41
	ds_read2_b32 v[12:13], v49 offset1:8
	v_lshlrev_b32_e32 v2, 1, v38
	ds_read2_b32 v[14:15], v49 offset0:66 offset1:74
	ds_read2_b32 v[16:17], v49 offset0:99 offset1:107
	ds_read2_b32 v[18:19], v49 offset0:132 offset1:140
	ds_read2_b32 v[20:21], v49 offset0:165 offset1:173
	ds_read2_b32 v[22:23], v49 offset0:198 offset1:206
	ds_read2_b32 v[24:25], v49 offset0:231 offset1:239
	v_lshl_add_u64 v[8:9], s[6:7], 0, v[2:3]
	v_or_b32_e32 v2, s2, v39
	v_lshlrev_b32_e32 v2, 11, v2
	v_lshl_add_u64 v[26:27], v[8:9], 0, v[2:3]
	v_or_b32_e32 v2, s2, v46
	s_waitcnt lgkmcnt(0)
	v_cvt_pk_bf16_f32 v4, v12, v10
	v_lshlrev_b32_e32 v2, 11, v2
	v_cvt_pk_bf16_f32 v5, v14, v16
	v_cvt_pk_bf16_f32 v6, v18, v20
	v_cvt_pk_bf16_f32 v7, v22, v24
	global_store_dwordx4 v[26:27], v[4:7], off sc1
	s_nop 1
	v_cvt_pk_bf16_f32 v4, v13, v11
	v_lshl_add_u64 v[10:11], v[8:9], 0, v[2:3]
	v_cvt_pk_bf16_f32 v5, v15, v17
	v_cvt_pk_bf16_f32 v6, v19, v21
	v_cvt_pk_bf16_f32 v7, v23, v25
	global_store_dwordx4 v[10:11], v[4:7], off sc1
	ds_read2_b32 v[10:11], v49 offset0:16 offset1:24
	ds_read2_b32 v[12:13], v49 offset0:49 offset1:57
	ds_read2_b32 v[14:15], v49 offset0:82 offset1:90
	ds_read2_b32 v[16:17], v49 offset0:115 offset1:123
	ds_read2_b32 v[18:19], v49 offset0:148 offset1:156
	ds_read2_b32 v[20:21], v49 offset0:181 offset1:189
	ds_read2_b32 v[22:23], v49 offset0:214 offset1:222
	ds_read2_b32 v[24:25], v49 offset0:247 offset1:255
	v_or_b32_e32 v2, s2, v47
	v_lshlrev_b32_e32 v2, 11, v2
	v_lshl_add_u64 v[26:27], v[8:9], 0, v[2:3]
	v_or_b32_e32 v2, s2, v48
	v_lshlrev_b32_e32 v2, 11, v2
	s_waitcnt lgkmcnt(6)
	v_cvt_pk_bf16_f32 v4, v10, v12
	s_waitcnt lgkmcnt(4)
	v_cvt_pk_bf16_f32 v5, v14, v16
	s_waitcnt lgkmcnt(2)
	v_cvt_pk_bf16_f32 v6, v18, v20
	s_waitcnt lgkmcnt(0)
	v_cvt_pk_bf16_f32 v7, v22, v24
	v_lshl_add_u64 v[8:9], v[8:9], 0, v[2:3]
	global_store_dwordx4 v[26:27], v[4:7], off sc1
	s_nop 1
	v_cvt_pk_bf16_f32 v4, v11, v13
	v_cvt_pk_bf16_f32 v5, v15, v17
	v_cvt_pk_bf16_f32 v6, v19, v21
	v_cvt_pk_bf16_f32 v7, v23, v25
	global_store_dwordx4 v[8:9], v[4:7], off sc1
	s_waitcnt lgkmcnt(0)

; #define GAS __attribute__((address_space(1)))
; #define LAS __attribute__((address_space(3)))
; #define LDS_WAIT() asm volatile("s_waitcnt lgkmcnt(0)" ::: "memory")
; __device__ __forceinline__ unsigned pk2(float lo, float hi) { unsigned r; asm("v_cvt_pk_bf16_f32 %0, %1, %2" : "=v"(r) : "v"(lo), "v"(hi)); return r; }
; __device__ __forceinline__ void transpose_item(const float* W, int K, int N, bf16* WT, int drow0, int kb, int n0, LAS float* scr, int lane) {
;     ...
;     for (int i = 0; i < 8; ++i) { const int kk = 8 * i + (lane >> 3); v[i] = ok ? *(const f32x4*)(W + (size_t)(k0 + kk) * N + n0 + c4) : (f32x4){0.f, 0.f, 0.f, 0.f}; }
; #pragma unroll
;     for (int i = 0; i < 8; ++i) { const int kk = 8 * i + (lane >> 3); LAS float* d = scr + kk * 33 + c4; d[0] = v[i][0]; d[1] = v[i][1]; d[2] = v[i][2]; d[3] = v[i][3]; }
;     LDS_WAIT(); asm volatile("" ::: "memory");
;     const int c = lane & 7;
; #pragma unroll
;     for (int j = 0; j < 4; ++j) { const int n = (lane >> 3) + 8 * j; const LAS float* s = scr + (8 * c) * 33 + n;
;         v4u o; o.x = pk2(s[0 * 33], s[1 * 33]); o.y = pk2(s[2 * 33], s[3 * 33]); o.z = pk2(s[4 * 33], s[5 * 33]); o.w = pk2(s[6 * 33], s[7 * 33]);
;         *(GAS v4u*)(WT + (size_t)(drow0 + n) * K + k0 + 8 * c) = o; }
;     LDS_WAIT(); asm volatile("" ::: "memory");
; __device__ __forceinline__ void convert_item(const In& I, unsigned char* ws, int it, LAS float* scr, int lane) {
;     ...
;     if (r < 2 * I_NIN) { const int j = r / I_NIN; r -= j * I_NIN; const int kb = r / 88, nb = r % 88;
;         transpose_item(I.nsa_w_in + (size_t)j * D * NSA_IN, D, NSA_IN, Wnin + (size_t)j * NSA_IN_PAD * D, 32 * nb, kb, 32 * nb, scr, lane); return; }
.LBB0_219:
	s_or_b64 exec, exec, s[12:13]
	v_add_u32_e32 v2, v44, v45
	s_waitcnt vmcnt(0)
	ds_write2_b32 v2, v4, v5 offset1:1
	ds_write2_b32 v2, v6, v7 offset0:2 offset1:3
	v_add_u32_e32 v4, 0x420, v2
	ds_write2_b32 v4, v8, v9 offset1:1
	v_add_u32_e32 v4, 0x428, v2
	ds_write2_b32 v4, v10, v11 offset1:1
	v_add_u32_e32 v4, 0x840, v2
	ds_write2_b32 v4, v16, v17 offset1:1
	v_add_u32_e32 v4, 0x848, v2
	ds_write2_b32 v4, v18, v19 offset1:1
	v_add_u32_e32 v4, 0xc60, v2
	ds_write2_b32 v4, v12, v13 offset1:1
	v_add_u32_e32 v4, 0xc68, v2
	ds_write2_b32 v4, v14, v15 offset1:1
	v_add_u32_e32 v4, 0x1080, v2
	ds_write2_b32 v4, v24, v25 offset1:1
	v_add_u32_e32 v4, 0x1088, v2
	ds_write2_b32 v4, v26, v27 offset1:1
	v_add_u32_e32 v4, 0x14a0, v2
	ds_write2_b32 v4, v20, v21 offset1:1
	v_add_u32_e32 v4, 0x14a8, v2
	ds_write2_b32 v4, v22, v23 offset1:1
	v_add_u32_e32 v4, 0x18c0, v2
	ds_write2_b32 v4, v32, v33 offset1:1
	v_add_u32_e32 v4, 0x18c8, v2
	s_and_b64 s[2:3], s[10:11], exec
	ds_write2_b32 v4, v34, v35 offset1:1
	v_add_u32_e32 v4, 0x1ce0, v2
	v_add_u32_e32 v2, 0x1ce8, v2
	s_cselect_b32 s2, 0x580000, 0
	ds_write2_b32 v4, v28, v29 offset1:1
	ds_write2_b32 v2, v30, v31 offset1:1
	s_add_u32 s7, s21, s2
	s_waitcnt lgkmcnt(0)
	s_addc_u32 s10, s22, 0
	s_ashr_i32 s9, s8, 31
	s_lshl_b64 s[2:3], s[8:9], 1
	ds_read2_b32 v[8:9], v49 offset0:33 offset1:41
	ds_read2_b32 v[10:11], v49 offset1:8
	ds_read2_b32 v[12:13], v49 offset0:66 offset1:74
	ds_read2_b32 v[14:15], v49 offset0:99 offset1:107
	ds_read2_b32 v[16:17], v49 offset0:132 offset1:140
	ds_read2_b32 v[18:19], v49 offset0:165 offset1:173
	ds_read2_b32 v[20:21], v49 offset0:198 offset1:206
	ds_read2_b32 v[22:23], v49 offset0:231 offset1:239
	s_add_u32 s2, s7, s2
	v_or_b32_e32 v26, s6, v39
	s_addc_u32 s3, s10, s3
	v_lshlrev_b32_e32 v2, 1, v38
	v_ashrrev_i32_e32 v27, 31, v26
	v_lshl_add_u64 v[24:25], s[2:3], 0, v[2:3]
	v_lshlrev_b64 v[26:27], 11, v[26:27]
	s_waitcnt lgkmcnt(0)
	v_cvt_pk_bf16_f32 v4, v10, v8
	v_lshl_add_u64 v[26:27], v[24:25], 0, v[26:27]
	v_or_b32_e32 v8, s6, v46
	v_cvt_pk_bf16_f32 v5, v12, v14
	v_cvt_pk_bf16_f32 v6, v16, v18
	v_cvt_pk_bf16_f32 v7, v20, v22
	global_store_dwordx4 v[26:27], v[4:7], off sc1
	s_nop 1
	v_cvt_pk_bf16_f32 v4, v11, v9
	v_ashrrev_i32_e32 v9, 31, v8
	v_lshlrev_b64 v[8:9], 11, v[8:9]
	v_cvt_pk_bf16_f32 v5, v13, v15
	v_cvt_pk_bf16_f32 v6, v17, v19
	v_cvt_pk_bf16_f32 v7, v21, v23
	v_lshl_add_u64 v[8:9], v[24:25], 0, v[8:9]
	ds_read2_b32 v[10:11], v49 offset0:16 offset1:24
	ds_read2_b32 v[12:13], v49 offset0:49 offset1:57
	ds_read2_b32 v[14:15], v49 offset0:82 offset1:90
	ds_read2_b32 v[16:17], v49 offset0:115 offset1:123
	ds_read2_b32 v[18:19], v49 offset0:148 offset1:156
	ds_read2_b32 v[20:21], v49 offset0:181 offset1:189
	ds_read2_b32 v[22:23], v49 offset0:214 offset1:222
	ds_read2_b32 v[26:27], v49 offset0:247 offset1:255
	global_store_dwordx4 v[8:9], v[4:7], off sc1
	v_or_b32_e32 v8, s6, v47
	v_ashrrev_i32_e32 v9, 31, v8
	v_lshlrev_b64 v[8:9], 11, v[8:9]
	v_lshl_add_u64 v[8:9], v[24:25], 0, v[8:9]
	s_waitcnt lgkmcnt(6)
	v_cvt_pk_bf16_f32 v4, v10, v12
	s_waitcnt lgkmcnt(4)
	v_cvt_pk_bf16_f32 v5, v14, v16
	s_waitcnt lgkmcnt(2)
	v_cvt_pk_bf16_f32 v6, v18, v20
	s_waitcnt lgkmcnt(0)
	v_cvt_pk_bf16_f32 v7, v22, v26
	global_store_dwordx4 v[8:9], v[4:7], off sc1
	v_or_b32_e32 v8, s6, v48
	v_ashrrev_i32_e32 v9, 31, v8
	v_lshlrev_b64 v[8:9], 11, v[8:9]
	v_lshl_add_u64 v[8:9], v[24:25], 0, v[8:9]
	v_cvt_pk_bf16_f32 v4, v11, v13
	v_cvt_pk_bf16_f32 v5, v15, v17
	v_cvt_pk_bf16_f32 v6, v19, v21
	v_cvt_pk_bf16_f32 v7, v23, v27
	global_store_dwordx4 v[8:9], v[4:7], off sc1
	s_waitcnt lgkmcnt(0)

; #define GAS __attribute__((address_space(1)))
; #define LAS __attribute__((address_space(3)))
; #define LDS_WAIT() asm volatile("s_waitcnt lgkmcnt(0)" ::: "memory")
; __device__ __forceinline__ unsigned pk2(float lo, float hi) { unsigned r; asm("v_cvt_pk_bf16_f32 %0, %1, %2" : "=v"(r) : "v"(lo), "v"(hi)); return r; }
; __device__ __forceinline__ void transpose_item(const float* W, int K, int N, bf16* WT, int drow0, int kb, int n0, LAS float* scr, int lane) {
;     const int k0 = 64 * kb; const int c4 = 4 * (lane & 7); const bool ok = (n0 + c4) < N;
;     f32x4 v[8];
; #pragma unroll
;     for (int i = 0; i < 8; ++i) { const int kk = 8 * i + (lane >> 3); v[i] = ok ? *(const f32x4*)(W + (size_t)(k0 + kk) * N + n0 + c4) : (f32x4){0.f, 0.f, 0.f, 0.f}; }
; #pragma unroll
;     for (int i = 0; i < 8; ++i) { const int kk = 8 * i + (lane >> 3); LAS float* d = scr + kk * 33 + c4; d[0] = v[i][0]; d[1] = v[i][1]; d[2] = v[i][2]; d[3] = v[i][3]; }
;     LDS_WAIT(); asm volatile("" ::: "memory");
;     const int c = lane & 7;
; #pragma unroll
;     for (int j = 0; j < 4; ++j) { const int n = (lane >> 3) + 8 * j; const LAS float* s = scr + (8 * c) * 33 + n;
;         v4u o; o.x = pk2(s[0 * 33], s[1 * 33]); o.y = pk2(s[2 * 33], s[3 * 33]); o.z = pk2(s[4 * 33], s[5 * 33]); o.w = pk2(s[6 * 33], s[7 * 33]);
;         *(GAS v4u*)(WT + (size_t)(drow0 + n) * K + k0 + 8 * c) = o; }
;     LDS_WAIT(); asm volatile("" ::: "memory");
; }
; __device__ __forceinline__ void convert_item(const In& I, unsigned char* ws, int it, LAS float* scr, int lane) {
;     ...
;     int r = it;
;     if (r < T0) { const int f = r / I_FFN; r -= f * I_FFN;
;         if (r < 2 * I_G) { const int up = r >= I_G; r -= up * I_G; const int kb = r / 88, nb = r % 88;
;             transpose_item((up ? I.w_up : I.w_gate) + (size_t)f * D * FF, D, FF, Wgu + (size_t)f * NGU * D, 256 * (nb >> 2) + 32 * (nb & 3) + 128 * up, kb, 32 * nb, scr, lane); }
;         else { r -= 2 * I_G; const int kb = r / 32, nb = r % 32; transpose_item(I.w_down + (size_t)f * FF * D, FF, D, Wd + (size_t)f * D * FF, 32 * nb, kb, 32 * nb, scr, lane); }
.LBB0_221:
	s_andn2_b64 vcc, exec, s[2:3]
	s_cbranch_vccnz .LBB0_166
	s_mul_hi_i32 s2, s45, 0x3e0f83e1
	s_lshr_b32 s3, s2, 31
	s_ashr_i32 s6, s2, 10
	s_add_i32 s6, s6, s3
	s_mul_i32 s2, s6, 0xffffef80
	s_add_i32 s7, s40, s2
	s_add_i32 s7, s7, 0xa800
	s_cmpk_gt_i32 s7, 0xaff
	s_mov_b64 s[2:3], -1
	s_cbranch_scc0 .LBB0_224
	v_readlane_b32 s48, v253, 0
	v_readlane_b32 s49, v253, 1
	v_readlane_b32 s50, v253, 2
	v_readlane_b32 s51, v253, 3
	v_readlane_b32 s52, v253, 4
	v_readlane_b32 s53, v253, 5
	v_readlane_b32 s54, v253, 6
	v_readlane_b32 s55, v253, 7
	v_readlane_b32 s56, v253, 8
	v_readlane_b32 s57, v253, 9
	s_mov_b64 s[48:49], s[52:53]
	s_mul_i32 s3, s6, 0xb00000
	s_mov_b64 s[50:51], s[54:55]
	s_mov_b64 s[52:53], s[56:57]
	s_mul_hi_i32 s2, s6, 0xb00000
	s_add_u32 s9, s52, s3
	s_addc_u32 s11, s53, s2
	s_mul_i32 s3, s6, 0x580000
	s_mul_hi_i32 s2, s6, 0x580000
	s_add_u32 s3, s19, s3
	s_addc_u32 s8, s20, s2
	s_mul_i32 s10, s6, 0xffffdf00
	s_add_i32 s12, s43, s44
	s_add_i32 s10, s12, s10
	s_and_b32 s2, s42, 0x3e0
	s_andn2_b32 s10, s10, 63
	s_add_i32 s68, s10, 0xffffea00
	s_lshl_b32 s10, s2, 2
	v_or_b32_e32 v32, s68, v39
	s_add_u32 s10, s9, s10
	s_addc_u32 s11, s11, 0
	v_lshlrev_b32_e32 v2, 2, v36
	v_ashrrev_i32_e32 v33, 31, v32
	v_or_b32_e32 v8, 8, v32
	v_lshl_add_u64 v[34:35], s[10:11], 0, v[2:3]
	v_lshlrev_b64 v[4:5], 12, v[32:33]
	v_ashrrev_i32_e32 v9, 31, v8
	v_lshl_add_u64 v[4:5], v[34:35], 0, v[4:5]
	v_lshlrev_b64 v[8:9], 12, v[8:9]
	v_or_b32_e32 v12, 16, v32
	global_load_dwordx4 v[4:7], v[4:5], off
	v_lshl_add_u64 v[8:9], v[34:35], 0, v[8:9]
	v_ashrrev_i32_e32 v13, 31, v12
	global_load_dwordx4 v[8:11], v[8:9], off
	v_lshlrev_b64 v[12:13], 12, v[12:13]
	v_or_b32_e32 v16, 24, v32
	v_lshl_add_u64 v[12:13], v[34:35], 0, v[12:13]
	v_ashrrev_i32_e32 v17, 31, v16
	global_load_dwordx4 v[12:15], v[12:13], off
	v_lshlrev_b64 v[16:17], 12, v[16:17]
	v_or_b32_e32 v20, 32, v32
	v_lshl_add_u64 v[16:17], v[34:35], 0, v[16:17]
	v_ashrrev_i32_e32 v21, 31, v20
	global_load_dwordx4 v[16:19], v[16:17], off
	v_lshlrev_b64 v[20:21], 12, v[20:21]
	v_or_b32_e32 v24, 40, v32
	v_lshl_add_u64 v[20:21], v[34:35], 0, v[20:21]
	v_ashrrev_i32_e32 v25, 31, v24
	global_load_dwordx4 v[20:23], v[20:21], off
	v_lshlrev_b64 v[24:25], 12, v[24:25]
	v_or_b32_e32 v28, 48, v32
	v_lshl_add_u64 v[24:25], v[34:35], 0, v[24:25]
	v_ashrrev_i32_e32 v29, 31, v28
	global_load_dwordx4 v[24:27], v[24:25], off
	v_lshlrev_b64 v[28:29], 12, v[28:29]
	v_or_b32_e32 v32, 56, v32
	v_lshl_add_u64 v[28:29], v[34:35], 0, v[28:29]
	v_ashrrev_i32_e32 v33, 31, v32
	global_load_dwordx4 v[28:31], v[28:29], off
	v_lshlrev_b64 v[32:33], 12, v[32:33]
	v_lshl_add_u64 v[32:33], v[34:35], 0, v[32:33]
	global_load_dwordx4 v[32:35], v[32:33], off
	v_add_u32_e32 v2, v44, v45
	s_lshl_b64 s[10:11], s[68:69], 1
	s_add_u32 s10, s3, s10
	s_addc_u32 s11, s8, s11
	v_readlane_b32 s58, v253, 10
	v_readlane_b32 s59, v253, 11
	v_readlane_b32 s60, v253, 12
	v_readlane_b32 s61, v253, 13
	v_readlane_b32 s62, v253, 14
	v_readlane_b32 s63, v253, 15
	s_waitcnt vmcnt(0)
	ds_write2_b32 v2, v4, v5 offset1:1
	ds_write2_b32 v2, v6, v7 offset0:2 offset1:3
	v_add_u32_e32 v4, 0x420, v2
	ds_write2_b32 v4, v8, v9 offset1:1
	v_add_u32_e32 v4, 0x428, v2
	ds_write2_b32 v4, v10, v11 offset1:1
	v_add_u32_e32 v4, 0x840, v2
	ds_write2_b32 v4, v12, v13 offset1:1
	v_add_u32_e32 v4, 0x848, v2
	ds_write2_b32 v4, v14, v15 offset1:1
	v_add_u32_e32 v4, 0xc60, v2
	ds_write2_b32 v4, v16, v17 offset1:1
	v_add_u32_e32 v4, 0xc68, v2
	ds_write2_b32 v4, v18, v19 offset1:1
	v_add_u32_e32 v4, 0x1080, v2
	ds_write2_b32 v4, v20, v21 offset1:1
	v_add_u32_e32 v4, 0x1088, v2
	ds_write2_b32 v4, v22, v23 offset1:1
	v_add_u32_e32 v4, 0x14a0, v2
	ds_write2_b32 v4, v24, v25 offset1:1
	v_add_u32_e32 v4, 0x14a8, v2
	ds_write2_b32 v4, v26, v27 offset1:1
	v_add_u32_e32 v4, 0x18c0, v2
	ds_write2_b32 v4, v28, v29 offset1:1
	v_add_u32_e32 v4, 0x18c8, v2
	ds_write2_b32 v4, v30, v31 offset1:1
	v_add_u32_e32 v4, 0x1ce0, v2
	v_add_u32_e32 v2, 0x1ce8, v2
	ds_write2_b32 v4, v32, v33 offset1:1
	ds_write2_b32 v2, v34, v35 offset1:1
	s_waitcnt lgkmcnt(0)
	ds_read2_b32 v[10:11], v49 offset0:33 offset1:41
	ds_read2_b32 v[12:13], v49 offset1:8
	v_lshlrev_b32_e32 v2, 1, v38
	ds_read2_b32 v[14:15], v49 offset0:66 offset1:74
	ds_read2_b32 v[16:17], v49 offset0:99 offset1:107
	ds_read2_b32 v[18:19], v49 offset0:132 offset1:140
	ds_read2_b32 v[20:21], v49 offset0:165 offset1:173
	ds_read2_b32 v[22:23], v49 offset0:198 offset1:206
	ds_read2_b32 v[24:25], v49 offset0:231 offset1:239
	v_lshl_add_u64 v[8:9], s[10:11], 0, v[2:3]
	v_or_b32_e32 v2, s2, v39
	v_mul_u32_u24_e32 v2, 0x1600, v2
	v_lshl_add_u64 v[26:27], v[8:9], 0, v[2:3]
	v_or_b32_e32 v2, s2, v46
	s_waitcnt lgkmcnt(0)
	v_cvt_pk_bf16_f32 v4, v12, v10
	v_mul_u32_u24_e32 v2, 0x1600, v2
	v_cvt_pk_bf16_f32 v5, v14, v16
	v_cvt_pk_bf16_f32 v6, v18, v20
	v_cvt_pk_bf16_f32 v7, v22, v24
	global_store_dwordx4 v[26:27], v[4:7], off sc1
	s_nop 1
	v_cvt_pk_bf16_f32 v4, v13, v11
	v_lshl_add_u64 v[10:11], v[8:9], 0, v[2:3]
	v_cvt_pk_bf16_f32 v5, v15, v17
	v_cvt_pk_bf16_f32 v6, v19, v21
	v_cvt_pk_bf16_f32 v7, v23, v25
	global_store_dwordx4 v[10:11], v[4:7], off sc1
	ds_read2_b32 v[10:11], v49 offset0:16 offset1:24
	ds_read2_b32 v[12:13], v49 offset0:49 offset1:57
	ds_read2_b32 v[14:15], v49 offset0:82 offset1:90
	ds_read2_b32 v[16:17], v49 offset0:115 offset1:123
	ds_read2_b32 v[18:19], v49 offset0:148 offset1:156
	ds_read2_b32 v[20:21], v49 offset0:181 offset1:189
	ds_read2_b32 v[22:23], v49 offset0:214 offset1:222
	ds_read2_b32 v[24:25], v49 offset0:247 offset1:255
	v_or_b32_e32 v2, s2, v47
	v_mul_u32_u24_e32 v2, 0x1600, v2
	v_lshl_add_u64 v[26:27], v[8:9], 0, v[2:3]
	v_or_b32_e32 v2, s2, v48
	v_mul_u32_u24_e32 v2, 0x1600, v2
	s_waitcnt lgkmcnt(6)
	v_cvt_pk_bf16_f32 v4, v10, v12
	s_waitcnt lgkmcnt(4)
	v_cvt_pk_bf16_f32 v5, v14, v16
	s_waitcnt lgkmcnt(2)
	v_cvt_pk_bf16_f32 v6, v18, v20
	s_waitcnt lgkmcnt(0)
	v_cvt_pk_bf16_f32 v7, v22, v24
	v_lshl_add_u64 v[8:9], v[8:9], 0, v[2:3]
	global_store_dwordx4 v[26:27], v[4:7], off sc1
	s_mov_b64 s[2:3], 0
	s_nop 0
	v_cvt_pk_bf16_f32 v4, v11, v13
	v_cvt_pk_bf16_f32 v5, v15, v17
	v_cvt_pk_bf16_f32 v6, v19, v21
	v_cvt_pk_bf16_f32 v7, v23, v25
	global_store_dwordx4 v[8:9], v[4:7], off sc1
	s_waitcnt lgkmcnt(0)
; #define GAS __attribute__((address_space(1)))
; #define LAS __attribute__((address_space(3)))
; #define LDS_WAIT() asm volatile("s_waitcnt lgkmcnt(0)" ::: "memory")
; __device__ __forceinline__ unsigned pk2(float lo, float hi) { unsigned r; asm("v_cvt_pk_bf16_f32 %0, %1, %2" : "=v"(r) : "v"(lo), "v"(hi)); return r; }
; __device__ __forceinline__ void transpose_item(const float* W, int K, int N, bf16* WT, int drow0, int kb, int n0, LAS float* scr, int lane) {
;     const int k0 = 64 * kb; const int c4 = 4 * (lane & 7); const bool ok = (n0 + c4) < N;
;     f32x4 v[8];
; #pragma unroll
;     for (int i = 0; i < 8; ++i) { const int kk = 8 * i + (lane >> 3); v[i] = ok ? *(const f32x4*)(W + (size_t)(k0 + kk) * N + n0 + c4) : (f32x4){0.f, 0.f, 0.f, 0.f}; }
; #pragma unroll
;     for (int i = 0; i < 8; ++i) { const int kk = 8 * i + (lane >> 3); LAS float* d = scr + kk * 33 + c4; d[0] = v[i][0]; d[1] = v[i][1]; d[2] = v[i][2]; d[3] = v[i][3]; }
;     LDS_WAIT(); asm volatile("" ::: "memory");
;     const int c = lane & 7;
; #pragma unroll
;     for (int j = 0; j < 4; ++j) { const int n = (lane >> 3) + 8 * j; const LAS float* s = scr + (8 * c) * 33 + n;
;         v4u o; o.x = pk2(s[0 * 33], s[1 * 33]); o.y = pk2(s[2 * 33], s[3 * 33]); o.z = pk2(s[4 * 33], s[5 * 33]); o.w = pk2(s[6 * 33], s[7 * 33]);
;         *(GAS v4u*)(WT + (size_t)(drow0 + n) * K + k0 + 8 * c) = o; }
;     LDS_WAIT(); asm volatile("" ::: "memory");
; }
; __device__ __forceinline__ void convert_item(const In& I, unsigned char* ws, int it, LAS float* scr, int lane) {
;     ...
;         if (r < 2 * I_G) { const int up = r >= I_G; r -= up * I_G; const int kb = r / 88, nb = r % 88;
;             transpose_item((up ? I.w_up : I.w_gate) + (size_t)f * D * FF, D, FF, Wgu + (size_t)f * NGU * D, 256 * (nb >> 2) + 32 * (nb & 3) + 128 * up, kb, 32 * nb, scr, lane); }
.LBB0_224:
	s_andn2_b64 vcc, exec, s[2:3]
	s_cbranch_vccnz .LBB0_166
	v_readlane_b32 s48, v253, 0
	v_readlane_b32 s49, v253, 1
	v_readlane_b32 s50, v253, 2
	v_readlane_b32 s51, v253, 3
	v_readlane_b32 s52, v253, 4
	v_readlane_b32 s53, v253, 5
	s_cmpk_gt_i32 s7, 0x57f
	v_readlane_b32 s54, v253, 6
	v_readlane_b32 s55, v253, 7
	v_readlane_b32 s56, v253, 8
	v_readlane_b32 s57, v253, 9
	s_mov_b64 s[48:49], s[52:53]
	s_cselect_b32 s2, 0xfffffa80, 0
	s_mul_i32 s3, s6, 0x1080
	s_mov_b64 s[50:51], s[54:55]
	s_cselect_b32 s7, 0x80, 0
	s_cselect_b32 s8, s50, s48
	s_cselect_b32 s9, s51, s49
	s_sub_i32 s2, s2, s3
	s_add_i32 s2, s40, s2
	s_add_i32 s2, s2, 0xa800
	s_mul_hi_i32 s3, s2, 0x2e8ba2e9
	s_lshr_b32 s10, s3, 31
	s_ashr_i32 s3, s3, 4
	s_add_i32 s3, s3, s10
	s_mul_i32 s10, s3, 0x58
	s_sub_i32 s2, s2, s10
	s_mul_hi_i32 s10, s6, 0xb00000
	s_mul_i32 s6, s6, 0xb00000
	s_add_u32 s11, s8, s6
	s_addc_u32 s12, s9, s10
	s_add_u32 s13, s28, s6
	s_addc_u32 s10, s29, s10
	s_lshl_b32 s8, s2, 5
	s_lshl_b32 s6, s2, 6
	s_and_b32 s2, s8, 0x60
	s_and_b32 s6, s6, 0xffffff00
	s_or_b32 s2, s2, s7
	s_ashr_i32 s9, s8, 31
	s_or_b32 s6, s2, s6
	s_lshl_b32 s2, s3, 6
	s_lshl_b64 s[8:9], s[8:9], 2
	s_add_u32 s8, s11, s8
	s_addc_u32 s9, s12, s9
	v_lshlrev_b32_e32 v2, 2, v36
	v_or_b32_e32 v34, s2, v39
	v_lshl_add_u64 v[32:33], s[8:9], 0, v[2:3]
	s_movk_i32 s3, 0x2c00
	v_mad_i64_i32 v[4:5], s[8:9], v34, s3, v[32:33]
	v_or_b32_e32 v2, 8, v34
	global_load_dwordx4 v[4:7], v[4:5], off
	v_mad_i64_i32 v[8:9], s[8:9], v2, s3, v[32:33]
	global_load_dwordx4 v[8:11], v[8:9], off
	v_or_b32_e32 v2, 16, v34
	v_mad_i64_i32 v[12:13], s[8:9], v2, s3, v[32:33]
	global_load_dwordx4 v[12:15], v[12:13], off
	v_or_b32_e32 v2, 24, v34
	v_mad_i64_i32 v[16:17], s[8:9], v2, s3, v[32:33]
	global_load_dwordx4 v[16:19], v[16:17], off
	v_or_b32_e32 v2, 32, v34
	v_mad_i64_i32 v[20:21], s[8:9], v2, s3, v[32:33]
	global_load_dwordx4 v[20:23], v[20:21], off
	v_or_b32_e32 v2, 40, v34
	v_mad_i64_i32 v[24:25], s[8:9], v2, s3, v[32:33]
	global_load_dwordx4 v[24:27], v[24:25], off
	v_or_b32_e32 v2, 48, v34
	v_mad_i64_i32 v[28:29], s[8:9], v2, s3, v[32:33]
	global_load_dwordx4 v[28:31], v[28:29], off
	v_or_b32_e32 v2, 56, v34
	v_mad_i64_i32 v[32:33], s[8:9], v2, s3, v[32:33]
	global_load_dwordx4 v[32:35], v[32:33], off
	v_add_u32_e32 v2, v44, v45
	s_ashr_i32 s3, s2, 31
	s_lshl_b64 s[2:3], s[2:3], 1
	s_add_u32 s2, s13, s2
	s_addc_u32 s3, s10, s3
	v_readlane_b32 s58, v253, 10
	v_readlane_b32 s59, v253, 11
	v_readlane_b32 s60, v253, 12
	v_readlane_b32 s61, v253, 13
	v_readlane_b32 s62, v253, 14
	v_readlane_b32 s63, v253, 15
	s_mov_b64 s[52:53], s[56:57]
	s_waitcnt vmcnt(0)
	ds_write2_b32 v2, v4, v5 offset1:1
	ds_write2_b32 v2, v6, v7 offset0:2 offset1:3
	v_add_u32_e32 v4, 0x420, v2
	ds_write2_b32 v4, v8, v9 offset1:1
	v_add_u32_e32 v4, 0x428, v2
	ds_write2_b32 v4, v10, v11 offset1:1
	v_add_u32_e32 v4, 0x840, v2
	ds_write2_b32 v4, v12, v13 offset1:1
	v_add_u32_e32 v4, 0x848, v2
	ds_write2_b32 v4, v14, v15 offset1:1
	v_add_u32_e32 v4, 0xc60, v2
	ds_write2_b32 v4, v16, v17 offset1:1
	v_add_u32_e32 v4, 0xc68, v2
	ds_write2_b32 v4, v18, v19 offset1:1
	v_add_u32_e32 v4, 0x1080, v2
	ds_write2_b32 v4, v20, v21 offset1:1
	v_add_u32_e32 v4, 0x1088, v2
	ds_write2_b32 v4, v22, v23 offset1:1
	v_add_u32_e32 v4, 0x14a0, v2
	ds_write2_b32 v4, v24, v25 offset1:1
	v_add_u32_e32 v4, 0x14a8, v2
	ds_write2_b32 v4, v26, v27 offset1:1
	v_add_u32_e32 v4, 0x18c0, v2
	ds_write2_b32 v4, v28, v29 offset1:1
	v_add_u32_e32 v4, 0x18c8, v2
	ds_write2_b32 v4, v30, v31 offset1:1
	v_add_u32_e32 v4, 0x1ce0, v2
	v_add_u32_e32 v2, 0x1ce8, v2
	ds_write2_b32 v4, v32, v33 offset1:1
	ds_write2_b32 v2, v34, v35 offset1:1
	s_waitcnt lgkmcnt(0)
	ds_read2_b32 v[10:11], v49 offset0:33 offset1:41
	ds_read2_b32 v[12:13], v49 offset1:8
	ds_read2_b32 v[14:15], v49 offset0:66 offset1:74
	ds_read2_b32 v[16:17], v49 offset0:99 offset1:107
	ds_read2_b32 v[18:19], v49 offset0:132 offset1:140
	ds_read2_b32 v[20:21], v49 offset0:165 offset1:173
	ds_read2_b32 v[22:23], v49 offset0:198 offset1:206
	ds_read2_b32 v[24:25], v49 offset0:231 offset1:239
	v_or_b32_e32 v26, s6, v39
	v_lshlrev_b32_e32 v2, 1, v38
	v_ashrrev_i32_e32 v27, 31, v26
	v_lshl_add_u64 v[8:9], s[2:3], 0, v[2:3]
	v_lshlrev_b64 v[26:27], 11, v[26:27]
	s_waitcnt lgkmcnt(0)
	v_cvt_pk_bf16_f32 v4, v12, v10
	v_lshl_add_u64 v[26:27], v[8:9], 0, v[26:27]
	v_or_b32_e32 v10, s6, v46
	v_cvt_pk_bf16_f32 v5, v14, v16
	v_cvt_pk_bf16_f32 v6, v18, v20
	v_cvt_pk_bf16_f32 v7, v22, v24
	global_store_dwordx4 v[26:27], v[4:7], off sc1
	v_or_b32_e32 v26, s6, v47
	v_ashrrev_i32_e32 v27, 31, v26
	v_cvt_pk_bf16_f32 v4, v13, v11
	v_ashrrev_i32_e32 v11, 31, v10
	v_lshlrev_b64 v[10:11], 11, v[10:11]
	v_lshl_add_u64 v[10:11], v[8:9], 0, v[10:11]
	v_cvt_pk_bf16_f32 v5, v15, v17
	v_cvt_pk_bf16_f32 v6, v19, v21
	v_cvt_pk_bf16_f32 v7, v23, v25
	global_store_dwordx4 v[10:11], v[4:7], off sc1
	ds_read2_b32 v[10:11], v49 offset0:16 offset1:24
	ds_read2_b32 v[12:13], v49 offset0:49 offset1:57
	ds_read2_b32 v[14:15], v49 offset0:82 offset1:90
	ds_read2_b32 v[16:17], v49 offset0:115 offset1:123
	ds_read2_b32 v[18:19], v49 offset0:148 offset1:156
	ds_read2_b32 v[20:21], v49 offset0:181 offset1:189
	ds_read2_b32 v[22:23], v49 offset0:214 offset1:222
	ds_read2_b32 v[24:25], v49 offset0:247 offset1:255
	v_lshlrev_b64 v[26:27], 11, v[26:27]
	s_waitcnt lgkmcnt(6)
	v_cvt_pk_bf16_f32 v4, v10, v12
	v_lshl_add_u64 v[26:27], v[8:9], 0, v[26:27]
	v_or_b32_e32 v10, s6, v48
	s_waitcnt lgkmcnt(4)
	v_cvt_pk_bf16_f32 v5, v14, v16
	s_waitcnt lgkmcnt(2)
	v_cvt_pk_bf16_f32 v6, v18, v20
	s_waitcnt lgkmcnt(0)
	v_cvt_pk_bf16_f32 v7, v22, v24
	global_store_dwordx4 v[26:27], v[4:7], off sc1
	s_nop 1
	v_cvt_pk_bf16_f32 v4, v11, v13
	v_ashrrev_i32_e32 v11, 31, v10
	v_lshlrev_b64 v[10:11], 11, v[10:11]
	v_lshl_add_u64 v[8:9], v[8:9], 0, v[10:11]
	v_cvt_pk_bf16_f32 v5, v15, v17
	v_cvt_pk_bf16_f32 v6, v19, v21
	v_cvt_pk_bf16_f32 v7, v23, v25
	global_store_dwordx4 v[8:9], v[4:7], off sc1
	s_waitcnt lgkmcnt(0)
	s_branch .LBB0_166

; #define GAS __attribute__((address_space(1)))
; #define LAS __attribute__((address_space(3)))
; #define LDS_WAIT() asm volatile("s_waitcnt lgkmcnt(0)" ::: "memory")
; __device__ __forceinline__ unsigned pk2(float lo, float hi) { unsigned r; asm("v_cvt_pk_bf16_f32 %0, %1, %2" : "=v"(r) : "v"(lo), "v"(hi)); return r; }
; __device__ __forceinline__ void transpose_item(const float* W, int K, int N, bf16* WT, int drow0, int kb, int n0, LAS float* scr, int lane) {
;     const int k0 = 64 * kb; const int c4 = 4 * (lane & 7); const bool ok = (n0 + c4) < N;
;     f32x4 v[8];
; #pragma unroll
;     for (int i = 0; i < 8; ++i) { const int kk = 8 * i + (lane >> 3); v[i] = ok ? *(const f32x4*)(W + (size_t)(k0 + kk) * N + n0 + c4) : (f32x4){0.f, 0.f, 0.f, 0.f}; }
; #pragma unroll
;     for (int i = 0; i < 8; ++i) { const int kk = 8 * i + (lane >> 3); LAS float* d = scr + kk * 33 + c4; d[0] = v[i][0]; d[1] = v[i][1]; d[2] = v[i][2]; d[3] = v[i][3]; }
;     LDS_WAIT(); asm volatile("" ::: "memory");
;     const int c = lane & 7;
; #pragma unroll
;     for (int j = 0; j < 4; ++j) { const int n = (lane >> 3) + 8 * j; const LAS float* s = scr + (8 * c) * 33 + n;
;         v4u o; o.x = pk2(s[0 * 33], s[1 * 33]); o.y = pk2(s[2 * 33], s[3 * 33]); o.z = pk2(s[4 * 33], s[5 * 33]); o.w = pk2(s[6 * 33], s[7 * 33]);
;         *(GAS v4u*)(WT + (size_t)(drow0 + n) * K + k0 + 8 * c) = o; }
;     LDS_WAIT(); asm volatile("" ::: "memory");
; }
; __device__ __forceinline__ void convert_item(const In& I, unsigned char* ws, int it, LAS float* scr, int lane) {
;     ...
;     if (r < 4 * I_W1) { const int jk = r / I_W1; r -= jk * I_W1; const int kb = r / 8, nb = r % 8;
;         transpose_item(I.nsa_w1 + (size_t)jk * 2048 * 256, 2048, 256, W1t + (size_t)jk * 256 * 2048, 32 * nb, kb, 32 * nb, scr, lane); return; }
;     r -= 4 * I_W1;
;     { const int jk = r >> 3; r &= 7; const int kb = r >> 1, nb = r & 1;
;         transpose_item(I.nsa_w2 + (size_t)jk * 256 * 64, 256, 64, W2t + (size_t)jk * 64 * 256, 32 * nb, kb, 32 * nb, scr, lane); }
.LBB0_229:
	s_add_i32 s44, s40, 0xa800
	s_cmp_gt_i32 s44, 0x83ff
	s_mov_b64 s[2:3], -1
	s_cbranch_scc0 .LBB0_283
	s_cmpk_gt_u32 s44, 0x8eff
	s_cbranch_scc0 .LBB0_264
	s_cmpk_gt_u32 s44, 0x92ff
	s_cbranch_scc0 .LBB0_261
	s_cmpk_gt_u32 s44, 0x9fff
	s_cbranch_scc0 .LBB0_242
	s_cmpk_gt_u32 s44, 0xa3ff
	s_cbranch_scc0 .LBB0_239
	s_cmpk_gt_u32 s44, 0xa7ff
	s_cbranch_scc0 .LBB0_236
	s_lshr_b32 s68, s40, 3
	v_readlane_b32 s48, v253, 16
	s_lshl_b64 s[2:3], s[68:69], 16
	v_readlane_b32 s52, v253, 20
	v_readlane_b32 s53, v253, 21
	s_add_u32 s6, s52, s2
	s_addc_u32 s7, s53, s3
	s_lshl_b64 s[2:3], s[68:69], 15
	s_add_u32 s8, s35, s2
	s_addc_u32 s3, s39, s3
	s_and_b32 s2, s42, 32
	s_and_b32 s9, s42, 0xc0
	s_lshl_b32 s10, s2, 2
	s_add_u32 s6, s6, s10
	v_or_b32_e32 v6, s9, v39
	s_addc_u32 s7, s7, 0
	v_lshlrev_b32_e32 v2, 2, v36
	v_lshl_add_u64 v[4:5], s[6:7], 0, v[2:3]
	v_lshlrev_b32_e32 v2, 8, v6
	v_lshl_add_u64 v[28:29], v[4:5], 0, v[2:3]
	global_load_dwordx4 v[4:7], v[28:29], off
	global_load_dwordx4 v[8:11], v[28:29], off offset:2048
	v_add_co_u32_e32 v16, vcc, s84, v28
	s_movk_i32 s6, 0x3000
	s_nop 0
	v_addc_co_u32_e32 v17, vcc, 0, v29, vcc
	v_add_co_u32_e32 v24, vcc, s74, v28
	v_add_u32_e32 v2, v44, v45
	s_nop 0
	v_addc_co_u32_e32 v25, vcc, 0, v29, vcc
	global_load_dwordx4 v[12:15], v[24:25], off offset:-4096
	s_nop 0
	global_load_dwordx4 v[16:19], v[16:17], off offset:2048
	s_nop 0
	global_load_dwordx4 v[20:23], v[24:25], off
	s_nop 0
	global_load_dwordx4 v[24:27], v[24:25], off offset:2048
	v_add_co_u32_e32 v32, vcc, s6, v28
	s_lshl_b32 s6, s9, 1
	s_nop 0
	v_addc_co_u32_e32 v33, vcc, 0, v29, vcc
	global_load_dwordx4 v[28:31], v[32:33], off
	s_nop 0
	global_load_dwordx4 v[32:35], v[32:33], off offset:2048
	s_add_u32 s6, s8, s6
	s_addc_u32 s7, s3, 0
	v_readlane_b32 s49, v253, 17
	v_readlane_b32 s50, v253, 18
	v_readlane_b32 s51, v253, 19
	v_readlane_b32 s54, v253, 22
	v_readlane_b32 s55, v253, 23
	v_readlane_b32 s56, v253, 24
	v_readlane_b32 s57, v253, 25
	v_readlane_b32 s58, v253, 26
	v_readlane_b32 s59, v253, 27
	v_readlane_b32 s60, v253, 28
	v_readlane_b32 s61, v253, 29
	v_readlane_b32 s62, v253, 30
	v_readlane_b32 s63, v253, 31
	s_waitcnt vmcnt(0)
	ds_write2_b32 v2, v4, v5 offset1:1
	ds_write2_b32 v2, v6, v7 offset0:2 offset1:3
	v_add_u32_e32 v4, 0x420, v2
	ds_write2_b32 v4, v8, v9 offset1:1
	v_add_u32_e32 v4, 0x428, v2
	ds_write2_b32 v4, v10, v11 offset1:1
	v_add_u32_e32 v4, 0x840, v2
	ds_write2_b32 v4, v12, v13 offset1:1
	v_add_u32_e32 v4, 0x848, v2
	ds_write2_b32 v4, v14, v15 offset1:1
	v_add_u32_e32 v4, 0xc60, v2
	ds_write2_b32 v4, v16, v17 offset1:1
	v_add_u32_e32 v4, 0xc68, v2
	ds_write2_b32 v4, v18, v19 offset1:1
	v_add_u32_e32 v4, 0x1080, v2
	ds_write2_b32 v4, v20, v21 offset1:1
	v_add_u32_e32 v4, 0x1088, v2
	ds_write2_b32 v4, v22, v23 offset1:1
	v_add_u32_e32 v4, 0x14a0, v2
	ds_write2_b32 v4, v24, v25 offset1:1
	v_add_u32_e32 v4, 0x14a8, v2
	ds_write2_b32 v4, v26, v27 offset1:1
	v_add_u32_e32 v4, 0x18c0, v2
	ds_write2_b32 v4, v28, v29 offset1:1
	v_add_u32_e32 v4, 0x18c8, v2
	ds_write2_b32 v4, v30, v31 offset1:1
	v_add_u32_e32 v4, 0x1ce0, v2
	v_add_u32_e32 v2, 0x1ce8, v2
	ds_write2_b32 v4, v32, v33 offset1:1
	ds_write2_b32 v2, v34, v35 offset1:1
	s_waitcnt lgkmcnt(0)
	ds_read2_b32 v[10:11], v49 offset0:33 offset1:41
	ds_read2_b32 v[12:13], v49 offset1:8
	v_lshlrev_b32_e32 v2, 1, v38
	ds_read2_b32 v[14:15], v49 offset0:66 offset1:74
	ds_read2_b32 v[16:17], v49 offset0:99 offset1:107
	ds_read2_b32 v[18:19], v49 offset0:132 offset1:140
	ds_read2_b32 v[20:21], v49 offset0:165 offset1:173
	ds_read2_b32 v[22:23], v49 offset0:198 offset1:206
	ds_read2_b32 v[24:25], v49 offset0:231 offset1:239
	v_lshl_add_u64 v[4:5], s[6:7], 0, v[2:3]
	v_or_b32_e32 v2, s2, v39
	v_lshlrev_b32_e32 v2, 9, v2
	v_lshl_add_u64 v[26:27], v[4:5], 0, v[2:3]
	v_or_b32_e32 v2, s2, v46
	s_waitcnt lgkmcnt(0)
	v_cvt_pk_bf16_f32 v6, v12, v10
	v_lshlrev_b32_e32 v2, 9, v2
	v_cvt_pk_bf16_f32 v7, v14, v16
	v_cvt_pk_bf16_f32 v8, v18, v20
	v_cvt_pk_bf16_f32 v9, v22, v24
	global_store_dwordx4 v[26:27], v[6:9], off sc1
	s_nop 1
	v_cvt_pk_bf16_f32 v6, v13, v11
	v_lshl_add_u64 v[10:11], v[4:5], 0, v[2:3]
	v_cvt_pk_bf16_f32 v7, v15, v17
	v_cvt_pk_bf16_f32 v8, v19, v21
	v_cvt_pk_bf16_f32 v9, v23, v25
	global_store_dwordx4 v[10:11], v[6:9], off sc1
	ds_read2_b32 v[10:11], v49 offset0:16 offset1:24
	ds_read2_b32 v[12:13], v49 offset0:49 offset1:57
	ds_read2_b32 v[14:15], v49 offset0:82 offset1:90
	ds_read2_b32 v[16:17], v49 offset0:115 offset1:123
	ds_read2_b32 v[18:19], v49 offset0:148 offset1:156
	ds_read2_b32 v[20:21], v49 offset0:181 offset1:189
	ds_read2_b32 v[22:23], v49 offset0:214 offset1:222
	ds_read2_b32 v[24:25], v49 offset0:247 offset1:255
	v_or_b32_e32 v2, s2, v47
	v_lshlrev_b32_e32 v2, 9, v2
	v_lshl_add_u64 v[26:27], v[4:5], 0, v[2:3]
	v_or_b32_e32 v2, s2, v48
	v_lshlrev_b32_e32 v2, 9, v2
	s_waitcnt lgkmcnt(6)
	v_cvt_pk_bf16_f32 v6, v10, v12
	s_waitcnt lgkmcnt(4)
	v_cvt_pk_bf16_f32 v7, v14, v16
	s_waitcnt lgkmcnt(2)
	v_cvt_pk_bf16_f32 v8, v18, v20
	s_waitcnt lgkmcnt(0)
	v_cvt_pk_bf16_f32 v9, v22, v24
	v_lshl_add_u64 v[4:5], v[4:5], 0, v[2:3]
	global_store_dwordx4 v[26:27], v[6:9], off sc1
	s_mov_b64 s[2:3], 0
	s_nop 0
	v_cvt_pk_bf16_f32 v6, v11, v13
	v_cvt_pk_bf16_f32 v7, v15, v17
	v_cvt_pk_bf16_f32 v8, v19, v21
	v_cvt_pk_bf16_f32 v9, v23, v25
	global_store_dwordx4 v[4:5], v[6:9], off sc1
	s_waitcnt lgkmcnt(0)

; #define GAS __attribute__((address_space(1)))
; #define LAS __attribute__((address_space(3)))
; #define LDS_WAIT() asm volatile("s_waitcnt lgkmcnt(0)" ::: "memory")
; __device__ __forceinline__ unsigned pk2(float lo, float hi) { unsigned r; asm("v_cvt_pk_bf16_f32 %0, %1, %2" : "=v"(r) : "v"(lo), "v"(hi)); return r; }
; __device__ __forceinline__ void transpose_item(const float* W, int K, int N, bf16* WT, int drow0, int kb, int n0, LAS float* scr, int lane) {
;     const int k0 = 64 * kb; const int c4 = 4 * (lane & 7); const bool ok = (n0 + c4) < N;
;     f32x4 v[8];
; #pragma unroll
;     for (int i = 0; i < 8; ++i) { const int kk = 8 * i + (lane >> 3); v[i] = ok ? *(const f32x4*)(W + (size_t)(k0 + kk) * N + n0 + c4) : (f32x4){0.f, 0.f, 0.f, 0.f}; }
; #pragma unroll
;     for (int i = 0; i < 8; ++i) { const int kk = 8 * i + (lane >> 3); LAS float* d = scr + kk * 33 + c4; d[0] = v[i][0]; d[1] = v[i][1]; d[2] = v[i][2]; d[3] = v[i][3]; }
;     LDS_WAIT(); asm volatile("" ::: "memory");
;     const int c = lane & 7;
; #pragma unroll
;     for (int j = 0; j < 4; ++j) { const int n = (lane >> 3) + 8 * j; const LAS float* s = scr + (8 * c) * 33 + n;
;         v4u o; o.x = pk2(s[0 * 33], s[1 * 33]); o.y = pk2(s[2 * 33], s[3 * 33]); o.z = pk2(s[4 * 33], s[5 * 33]); o.w = pk2(s[6 * 33], s[7 * 33]);
;         *(GAS v4u*)(WT + (size_t)(drow0 + n) * K + k0 + 8 * c) = o; }
;     LDS_WAIT(); asm volatile("" ::: "memory");
; }
; __device__ __forceinline__ void convert_item(const In& I, unsigned char* ws, int it, LAS float* scr, int lane) {
;     ...
;     if (r < 2 * I_SQ) { const int j = r / I_SQ; r -= j * I_SQ; const int kb = r / 32, nb = r % 32;
;         transpose_item(I.nsa_w_out + (size_t)j * D * D, D, D, Wnout + (size_t)j * D * D, 32 * nb, kb, 32 * nb, scr, lane); return; }
.LBB0_239:
	s_andn2_b64 vcc, exec, s[2:3]
	s_cbranch_vccnz .LBB0_241
	s_add_i32 s2, s40, 0x800
	s_lshr_b32 s68, s2, 9
	v_readlane_b32 s48, v253, 16
	s_lshl_b64 s[2:3], s[68:69], 22
	v_readlane_b32 s60, v253, 28
	v_readlane_b32 s61, v253, 29
	s_add_u32 s6, s60, s2
	s_addc_u32 s7, s61, s3
	s_lshl_b64 s[2:3], s[68:69], 21
	s_add_u32 s8, s27, s2
	s_addc_u32 s3, s31, s3
	s_and_b32 s2, s42, 0x3e0
	s_add_i32 s9, s43, 0x13800
	s_and_b32 s9, s9, 0x3c0
	s_lshl_b32 s10, s2, 2
	s_add_u32 s6, s6, s10
	v_or_b32_e32 v6, s9, v39
	s_addc_u32 s7, s7, 0
	v_lshlrev_b32_e32 v2, 2, v36
	v_lshl_add_u64 v[4:5], s[6:7], 0, v[2:3]
	v_lshlrev_b32_e32 v2, 12, v6
	v_lshl_add_u64 v[32:33], v[4:5], 0, v[2:3]
	v_add_co_u32_e32 v8, vcc, s81, v32
	global_load_dwordx4 v[4:7], v[32:33], off
	s_nop 0
	v_addc_co_u32_e32 v9, vcc, 0, v33, vcc
	global_load_dwordx4 v[8:11], v[8:9], off
	v_add_co_u32_e32 v12, vcc, s79, v32
	v_add_u32_e32 v2, v44, v45
	s_nop 0
	v_addc_co_u32_e32 v13, vcc, 0, v33, vcc
	global_load_dwordx4 v[12:15], v[12:13], off
	v_add_co_u32_e32 v16, vcc, s80, v32
	s_lshl_b32 s6, s9, 1
	s_nop 0
	v_addc_co_u32_e32 v17, vcc, 0, v33, vcc
	global_load_dwordx4 v[16:19], v[16:17], off
	v_add_co_u32_e32 v20, vcc, s85, v32
	s_add_u32 s6, s8, s6
	s_nop 0
	v_addc_co_u32_e32 v21, vcc, 0, v33, vcc
	global_load_dwordx4 v[20:23], v[20:21], off
	v_add_co_u32_e32 v24, vcc, s86, v32
	s_addc_u32 s7, s3, 0
	s_nop 0
	v_addc_co_u32_e32 v25, vcc, 0, v33, vcc
	global_load_dwordx4 v[24:27], v[24:25], off
	v_add_co_u32_e32 v28, vcc, s87, v32
	v_readlane_b32 s49, v253, 17
	s_nop 0
	v_addc_co_u32_e32 v29, vcc, 0, v33, vcc
	global_load_dwordx4 v[28:31], v[28:29], off
	v_add_co_u32_e32 v32, vcc, s89, v32
	v_readlane_b32 s50, v253, 18
	s_nop 0
	v_addc_co_u32_e32 v33, vcc, 0, v33, vcc
	global_load_dwordx4 v[32:35], v[32:33], off
	v_readlane_b32 s51, v253, 19
	v_readlane_b32 s52, v253, 20
	v_readlane_b32 s53, v253, 21
	v_readlane_b32 s54, v253, 22
	v_readlane_b32 s55, v253, 23
	v_readlane_b32 s56, v253, 24
	v_readlane_b32 s57, v253, 25
	v_readlane_b32 s58, v253, 26
	v_readlane_b32 s59, v253, 27
	v_readlane_b32 s62, v253, 30
	v_readlane_b32 s63, v253, 31
	s_waitcnt vmcnt(0)
	ds_write2_b32 v2, v4, v5 offset1:1
	ds_write2_b32 v2, v6, v7 offset0:2 offset1:3
	v_add_u32_e32 v4, 0x420, v2
	ds_write2_b32 v4, v8, v9 offset1:1
	v_add_u32_e32 v4, 0x428, v2
	ds_write2_b32 v4, v10, v11 offset1:1
	v_add_u32_e32 v4, 0x840, v2
	ds_write2_b32 v4, v12, v13 offset1:1
	v_add_u32_e32 v4, 0x848, v2
	ds_write2_b32 v4, v14, v15 offset1:1
	v_add_u32_e32 v4, 0xc60, v2
	ds_write2_b32 v4, v16, v17 offset1:1
	v_add_u32_e32 v4, 0xc68, v2
	ds_write2_b32 v4, v18, v19 offset1:1
	v_add_u32_e32 v4, 0x1080, v2
	ds_write2_b32 v4, v20, v21 offset1:1
	v_add_u32_e32 v4, 0x1088, v2
	ds_write2_b32 v4, v22, v23 offset1:1
	v_add_u32_e32 v4, 0x14a0, v2
	ds_write2_b32 v4, v24, v25 offset1:1
	v_add_u32_e32 v4, 0x14a8, v2
	ds_write2_b32 v4, v26, v27 offset1:1
	v_add_u32_e32 v4, 0x18c0, v2
	ds_write2_b32 v4, v28, v29 offset1:1
	v_add_u32_e32 v4, 0x18c8, v2
	ds_write2_b32 v4, v30, v31 offset1:1
	v_add_u32_e32 v4, 0x1ce0, v2
	v_add_u32_e32 v2, 0x1ce8, v2
	ds_write2_b32 v4, v32, v33 offset1:1
	ds_write2_b32 v2, v34, v35 offset1:1
	s_waitcnt lgkmcnt(0)
	ds_read2_b32 v[10:11], v49 offset0:33 offset1:41
	ds_read2_b32 v[12:13], v49 offset1:8
	v_lshlrev_b32_e32 v2, 1, v38
	ds_read2_b32 v[14:15], v49 offset0:66 offset1:74
	ds_read2_b32 v[16:17], v49 offset0:99 offset1:107
	ds_read2_b32 v[18:19], v49 offset0:132 offset1:140
	ds_read2_b32 v[20:21], v49 offset0:165 offset1:173
	ds_read2_b32 v[22:23], v49 offset0:198 offset1:206
	ds_read2_b32 v[24:25], v49 offset0:231 offset1:239
	v_lshl_add_u64 v[8:9], s[6:7], 0, v[2:3]
	v_or_b32_e32 v2, s2, v39
	v_lshlrev_b32_e32 v2, 11, v2
	v_lshl_add_u64 v[26:27], v[8:9], 0, v[2:3]
	v_or_b32_e32 v2, s2, v46
	s_waitcnt lgkmcnt(0)
	v_cvt_pk_bf16_f32 v4, v12, v10
	v_lshlrev_b32_e32 v2, 11, v2
	v_cvt_pk_bf16_f32 v5, v14, v16
	v_cvt_pk_bf16_f32 v6, v18, v20
	v_cvt_pk_bf16_f32 v7, v22, v24
	global_store_dwordx4 v[26:27], v[4:7], off sc1
	s_nop 1
	v_cvt_pk_bf16_f32 v4, v13, v11
	v_lshl_add_u64 v[10:11], v[8:9], 0, v[2:3]
	v_cvt_pk_bf16_f32 v5, v15, v17
	v_cvt_pk_bf16_f32 v6, v19, v21
	v_cvt_pk_bf16_f32 v7, v23, v25
	global_store_dwordx4 v[10:11], v[4:7], off sc1
	ds_read2_b32 v[10:11], v49 offset0:16 offset1:24
	ds_read2_b32 v[12:13], v49 offset0:49 offset1:57
	ds_read2_b32 v[14:15], v49 offset0:82 offset1:90
	ds_read2_b32 v[16:17], v49 offset0:115 offset1:123
	ds_read2_b32 v[18:19], v49 offset0:148 offset1:156
	ds_read2_b32 v[20:21], v49 offset0:181 offset1:189
	ds_read2_b32 v[22:23], v49 offset0:214 offset1:222
	ds_read2_b32 v[24:25], v49 offset0:247 offset1:255
	v_or_b32_e32 v2, s2, v47
	v_lshlrev_b32_e32 v2, 11, v2
	v_lshl_add_u64 v[26:27], v[8:9], 0, v[2:3]
	v_or_b32_e32 v2, s2, v48
	v_lshlrev_b32_e32 v2, 11, v2
	s_waitcnt lgkmcnt(6)
	v_cvt_pk_bf16_f32 v4, v10, v12
	s_waitcnt lgkmcnt(4)
	v_cvt_pk_bf16_f32 v5, v14, v16
	s_waitcnt lgkmcnt(2)
	v_cvt_pk_bf16_f32 v6, v18, v20
	s_waitcnt lgkmcnt(0)
	v_cvt_pk_bf16_f32 v7, v22, v24
	v_lshl_add_u64 v[8:9], v[8:9], 0, v[2:3]
	global_store_dwordx4 v[26:27], v[4:7], off sc1
	s_nop 1
	v_cvt_pk_bf16_f32 v4, v11, v13
	v_cvt_pk_bf16_f32 v5, v15, v17
	v_cvt_pk_bf16_f32 v6, v19, v21
	v_cvt_pk_bf16_f32 v7, v23, v25
	global_store_dwordx4 v[8:9], v[4:7], off sc1
	s_waitcnt lgkmcnt(0)

; #define GAS __attribute__((address_space(1)))
; #define LAS __attribute__((address_space(3)))
; #define LDS_WAIT() asm volatile("s_waitcnt lgkmcnt(0)" ::: "memory")
; __device__ __forceinline__ unsigned pk2(float lo, float hi) { unsigned r; asm("v_cvt_pk_bf16_f32 %0, %1, %2" : "=v"(r) : "v"(lo), "v"(hi)); return r; }
; __device__ __forceinline__ void transpose_item(const float* W, int K, int N, bf16* WT, int drow0, int kb, int n0, LAS float* scr, int lane) {
;     const int k0 = 64 * kb; const int c4 = 4 * (lane & 7); const bool ok = (n0 + c4) < N;
;     f32x4 v[8];
; #pragma unroll
;     for (int i = 0; i < 8; ++i) { const int kk = 8 * i + (lane >> 3); v[i] = ok ? *(const f32x4*)(W + (size_t)(k0 + kk) * N + n0 + c4) : (f32x4){0.f, 0.f, 0.f, 0.f}; }
; #pragma unroll
;     for (int i = 0; i < 8; ++i) { const int kk = 8 * i + (lane >> 3); LAS float* d = scr + kk * 33 + c4; d[0] = v[i][0]; d[1] = v[i][1]; d[2] = v[i][2]; d[3] = v[i][3]; }
;     LDS_WAIT(); asm volatile("" ::: "memory");
;     const int c = lane & 7;
; #pragma unroll
;     for (int j = 0; j < 4; ++j) { const int n = (lane >> 3) + 8 * j; const LAS float* s = scr + (8 * c) * 33 + n;
;         v4u o; o.x = pk2(s[0 * 33], s[1 * 33]); o.y = pk2(s[2 * 33], s[3 * 33]); o.z = pk2(s[4 * 33], s[5 * 33]); o.w = pk2(s[6 * 33], s[7 * 33]);
;         *(GAS v4u*)(WT + (size_t)(drow0 + n) * K + k0 + 8 * c) = o; }
;     LDS_WAIT(); asm volatile("" ::: "memory");
; }
; __device__ __forceinline__ void convert_item(const In& I, unsigned char* ws, int it, LAS float* scr, int lane) {
;     ...
;     if (r < 2 * I_SQ) { const int j = r / I_SQ; r -= j * I_SQ; const int kb = r / 32, nb = r % 32;
;         transpose_item(I.fox_w_out + (size_t)j * D * D, D, D, Wfout + (size_t)j * D * D, 32 * nb, kb, 32 * nb, scr, lane); return; }
.LBB0_261:
	s_andn2_b64 vcc, exec, s[2:3]
	s_cbranch_vccnz .LBB0_263
	s_add_i32 s2, s40, 0x1900
	s_lshr_b32 s68, s2, 9
	v_readlane_b32 s48, v253, 16
	s_lshl_b64 s[2:3], s[68:69], 22
	v_readlane_b32 s54, v253, 22
	v_readlane_b32 s55, v253, 23
	s_add_u32 s6, s54, s2
	s_addc_u32 s7, s55, s3
	s_lshl_b64 s[2:3], s[68:69], 21
	s_add_u32 s8, s23, s2
	s_addc_u32 s3, s24, s3
	s_and_b32 s2, s42, 0x3e0
	s_add_i32 s9, s43, 0x1a00
	s_and_b32 s9, s9, 0x3c0
	s_lshl_b32 s10, s2, 2
	s_add_u32 s6, s6, s10
	v_or_b32_e32 v6, s9, v39
	s_addc_u32 s7, s7, 0
	v_lshlrev_b32_e32 v2, 2, v36
	v_lshl_add_u64 v[4:5], s[6:7], 0, v[2:3]
	v_lshlrev_b32_e32 v2, 12, v6
	v_lshl_add_u64 v[32:33], v[4:5], 0, v[2:3]
	v_add_co_u32_e32 v8, vcc, s81, v32
	global_load_dwordx4 v[4:7], v[32:33], off
	s_nop 0
	v_addc_co_u32_e32 v9, vcc, 0, v33, vcc
	global_load_dwordx4 v[8:11], v[8:9], off
	v_add_co_u32_e32 v12, vcc, s79, v32
	v_add_u32_e32 v2, v44, v45
	s_nop 0
	v_addc_co_u32_e32 v13, vcc, 0, v33, vcc
	global_load_dwordx4 v[12:15], v[12:13], off
	v_add_co_u32_e32 v16, vcc, s80, v32
	s_lshl_b32 s6, s9, 1
	s_nop 0
	v_addc_co_u32_e32 v17, vcc, 0, v33, vcc
	global_load_dwordx4 v[16:19], v[16:17], off
	v_add_co_u32_e32 v20, vcc, s85, v32
	s_add_u32 s6, s8, s6
	s_nop 0
	v_addc_co_u32_e32 v21, vcc, 0, v33, vcc
	global_load_dwordx4 v[20:23], v[20:21], off
	v_add_co_u32_e32 v24, vcc, s86, v32
	s_addc_u32 s7, s3, 0
	s_nop 0
	v_addc_co_u32_e32 v25, vcc, 0, v33, vcc
	global_load_dwordx4 v[24:27], v[24:25], off
	v_add_co_u32_e32 v28, vcc, s87, v32
	v_readlane_b32 s49, v253, 17
	s_nop 0
	v_addc_co_u32_e32 v29, vcc, 0, v33, vcc
	global_load_dwordx4 v[28:31], v[28:29], off
	v_add_co_u32_e32 v32, vcc, s89, v32
	v_readlane_b32 s50, v253, 18
	s_nop 0
	v_addc_co_u32_e32 v33, vcc, 0, v33, vcc
	global_load_dwordx4 v[32:35], v[32:33], off
	v_readlane_b32 s51, v253, 19
	v_readlane_b32 s52, v253, 20
	v_readlane_b32 s53, v253, 21
	v_readlane_b32 s56, v253, 24
	v_readlane_b32 s57, v253, 25
	v_readlane_b32 s58, v253, 26
	v_readlane_b32 s59, v253, 27
	v_readlane_b32 s60, v253, 28
	v_readlane_b32 s61, v253, 29
	v_readlane_b32 s62, v253, 30
	v_readlane_b32 s63, v253, 31
	s_waitcnt vmcnt(0)
	ds_write2_b32 v2, v4, v5 offset1:1
	ds_write2_b32 v2, v6, v7 offset0:2 offset1:3
	v_add_u32_e32 v4, 0x420, v2
	ds_write2_b32 v4, v8, v9 offset1:1
	v_add_u32_e32 v4, 0x428, v2
	ds_write2_b32 v4, v10, v11 offset1:1
	v_add_u32_e32 v4, 0x840, v2
	ds_write2_b32 v4, v12, v13 offset1:1
	v_add_u32_e32 v4, 0x848, v2
	ds_write2_b32 v4, v14, v15 offset1:1
	v_add_u32_e32 v4, 0xc60, v2
	ds_write2_b32 v4, v16, v17 offset1:1
	v_add_u32_e32 v4, 0xc68, v2
	ds_write2_b32 v4, v18, v19 offset1:1
	v_add_u32_e32 v4, 0x1080, v2
	ds_write2_b32 v4, v20, v21 offset1:1
	v_add_u32_e32 v4, 0x1088, v2
	ds_write2_b32 v4, v22, v23 offset1:1
	v_add_u32_e32 v4, 0x14a0, v2
	ds_write2_b32 v4, v24, v25 offset1:1
	v_add_u32_e32 v4, 0x14a8, v2
	ds_write2_b32 v4, v26, v27 offset1:1
	v_add_u32_e32 v4, 0x18c0, v2
	ds_write2_b32 v4, v28, v29 offset1:1
	v_add_u32_e32 v4, 0x18c8, v2
	ds_write2_b32 v4, v30, v31 offset1:1
	v_add_u32_e32 v4, 0x1ce0, v2
	v_add_u32_e32 v2, 0x1ce8, v2
	ds_write2_b32 v4, v32, v33 offset1:1
	ds_write2_b32 v2, v34, v35 offset1:1
	s_waitcnt lgkmcnt(0)
	ds_read2_b32 v[10:11], v49 offset0:33 offset1:41
	ds_read2_b32 v[12:13], v49 offset1:8
	v_lshlrev_b32_e32 v2, 1, v38
	ds_read2_b32 v[14:15], v49 offset0:66 offset1:74
	ds_read2_b32 v[16:17], v49 offset0:99 offset1:107
	ds_read2_b32 v[18:19], v49 offset0:132 offset1:140
	ds_read2_b32 v[20:21], v49 offset0:165 offset1:173
	ds_read2_b32 v[22:23], v49 offset0:198 offset1:206
	ds_read2_b32 v[24:25], v49 offset0:231 offset1:239
	v_lshl_add_u64 v[8:9], s[6:7], 0, v[2:3]
	v_or_b32_e32 v2, s2, v39
	v_lshlrev_b32_e32 v2, 11, v2
	v_lshl_add_u64 v[26:27], v[8:9], 0, v[2:3]
	v_or_b32_e32 v2, s2, v46
	s_waitcnt lgkmcnt(0)
	v_cvt_pk_bf16_f32 v4, v12, v10
	v_lshlrev_b32_e32 v2, 11, v2
	v_cvt_pk_bf16_f32 v5, v14, v16
	v_cvt_pk_bf16_f32 v6, v18, v20
	v_cvt_pk_bf16_f32 v7, v22, v24
	global_store_dwordx4 v[26:27], v[4:7], off sc1
	s_nop 1
	v_cvt_pk_bf16_f32 v4, v13, v11
	v_lshl_add_u64 v[10:11], v[8:9], 0, v[2:3]
	v_cvt_pk_bf16_f32 v5, v15, v17
	v_cvt_pk_bf16_f32 v6, v19, v21
	v_cvt_pk_bf16_f32 v7, v23, v25
	global_store_dwordx4 v[10:11], v[4:7], off sc1
	ds_read2_b32 v[10:11], v49 offset0:16 offset1:24
	ds_read2_b32 v[12:13], v49 offset0:49 offset1:57
	ds_read2_b32 v[14:15], v49 offset0:82 offset1:90
	ds_read2_b32 v[16:17], v49 offset0:115 offset1:123
	ds_read2_b32 v[18:19], v49 offset0:148 offset1:156
	ds_read2_b32 v[20:21], v49 offset0:181 offset1:189
	ds_read2_b32 v[22:23], v49 offset0:214 offset1:222
	ds_read2_b32 v[24:25], v49 offset0:247 offset1:255
	v_or_b32_e32 v2, s2, v47
	v_lshlrev_b32_e32 v2, 11, v2
	v_lshl_add_u64 v[26:27], v[8:9], 0, v[2:3]
	v_or_b32_e32 v2, s2, v48
	v_lshlrev_b32_e32 v2, 11, v2
	s_waitcnt lgkmcnt(6)
	v_cvt_pk_bf16_f32 v4, v10, v12
	s_waitcnt lgkmcnt(4)
	v_cvt_pk_bf16_f32 v5, v14, v16
	s_waitcnt lgkmcnt(2)
	v_cvt_pk_bf16_f32 v6, v18, v20
	s_waitcnt lgkmcnt(0)
	v_cvt_pk_bf16_f32 v7, v22, v24
	v_lshl_add_u64 v[8:9], v[8:9], 0, v[2:3]
	global_store_dwordx4 v[26:27], v[4:7], off sc1
	s_nop 1
	v_cvt_pk_bf16_f32 v4, v11, v13
	v_cvt_pk_bf16_f32 v5, v15, v17
	v_cvt_pk_bf16_f32 v6, v19, v21
	v_cvt_pk_bf16_f32 v7, v23, v25
	global_store_dwordx4 v[8:9], v[4:7], off sc1
	s_waitcnt lgkmcnt(0)

; #define GAS __attribute__((address_space(1)))
; #define LAS __attribute__((address_space(3)))
; #define LDS_WAIT() asm volatile("s_waitcnt lgkmcnt(0)" ::: "memory")
; __device__ __forceinline__ unsigned pk2(float lo, float hi) { unsigned r; asm("v_cvt_pk_bf16_f32 %0, %1, %2" : "=v"(r) : "v"(lo), "v"(hi)); return r; }
; __device__ __forceinline__ void transpose_item(const float* W, int K, int N, bf16* WT, int drow0, int kb, int n0, LAS float* scr, int lane) {
;     const int k0 = 64 * kb; const int c4 = 4 * (lane & 7); const bool ok = (n0 + c4) < N;
;     f32x4 v[8];
; #pragma unroll
;     for (int i = 0; i < 8; ++i) { const int kk = 8 * i + (lane >> 3); v[i] = ok ? *(const f32x4*)(W + (size_t)(k0 + kk) * N + n0 + c4) : (f32x4){0.f, 0.f, 0.f, 0.f}; }
; #pragma unroll
;     for (int i = 0; i < 8; ++i) { const int kk = 8 * i + (lane >> 3); LAS float* d = scr + kk * 33 + c4; d[0] = v[i][0]; d[1] = v[i][1]; d[2] = v[i][2]; d[3] = v[i][3]; }
;     LDS_WAIT(); asm volatile("" ::: "memory");
;     const int c = lane & 7;
; #pragma unroll
;     for (int j = 0; j < 4; ++j) { const int n = (lane >> 3) + 8 * j; const LAS float* s = scr + (8 * c) * 33 + n;
;         v4u o; o.x = pk2(s[0 * 33], s[1 * 33]); o.y = pk2(s[2 * 33], s[3 * 33]); o.z = pk2(s[4 * 33], s[5 * 33]); o.w = pk2(s[6 * 33], s[7 * 33]);
;         *(GAS v4u*)(WT + (size_t)(drow0 + n) * K + k0 + 8 * c) = o; }
;     LDS_WAIT(); asm volatile("" ::: "memory");
; }
; __device__ __forceinline__ void convert_item(const In& I, unsigned char* ws, int it, LAS float* scr, int lane) {
;     ...
;     int r = it;
;     if (r < T0) { const int f = r / I_FFN; r -= f * I_FFN;
;         if (r < 2 * I_G) { const int up = r >= I_G; r -= up * I_G; const int kb = r / 88, nb = r % 88;
;             transpose_item((up ? I.w_up : I.w_gate) + (size_t)f * D * FF, D, FF, Wgu + (size_t)f * NGU * D, 256 * (nb >> 2) + 32 * (nb & 3) + 128 * up, kb, 32 * nb, scr, lane); }
;         else { r -= 2 * I_G; const int kb = r / 32, nb = r % 32; transpose_item(I.w_down + (size_t)f * FF * D, FF, D, Wd + (size_t)f * D * FF, 32 * nb, kb, 32 * nb, scr, lane); }
.LBB0_283:
	s_andn2_b64 vcc, exec, s[2:3]
	s_cbranch_vccnz .LBB0_228
	s_mul_hi_i32 s2, s44, 0x3e0f83e1
	s_lshr_b32 s3, s2, 31
	s_ashr_i32 s6, s2, 10
	s_add_i32 s6, s6, s3
	s_mul_i32 s2, s6, 0xffffef80
	s_add_i32 s7, s40, s2
	s_add_i32 s7, s7, 0xa800
	s_cmpk_gt_i32 s7, 0xaff
	s_mov_b64 s[2:3], -1
	s_cbranch_scc0 .LBB0_286
	v_readlane_b32 s48, v253, 0
	v_readlane_b32 s49, v253, 1
	v_readlane_b32 s50, v253, 2
	v_readlane_b32 s51, v253, 3
	v_readlane_b32 s52, v253, 4
	v_readlane_b32 s53, v253, 5
	v_readlane_b32 s54, v253, 6
	v_readlane_b32 s55, v253, 7
	v_readlane_b32 s56, v253, 8
	v_readlane_b32 s57, v253, 9
	s_mov_b64 s[48:49], s[52:53]
	s_mul_i32 s3, s6, 0xb00000
	s_mov_b64 s[50:51], s[54:55]
	s_mov_b64 s[52:53], s[56:57]
	s_mul_hi_i32 s2, s6, 0xb00000
	s_add_u32 s9, s52, s3
	s_addc_u32 s11, s53, s2
	s_mul_i32 s3, s6, 0x580000
	s_mul_hi_i32 s2, s6, 0x580000
	s_add_u32 s3, s19, s3
	s_mul_i32 s10, s6, 0xffffdf00
	s_addc_u32 s8, s20, s2
	s_add_i32 s10, s43, s10
	s_add_i32 s10, s10, 0x13800
	s_and_b32 s2, s42, 0x3e0
	s_andn2_b32 s10, s10, 63
	s_add_i32 s68, s10, 0xffffea00
	s_lshl_b32 s10, s2, 2
	v_or_b32_e32 v32, s68, v39
	s_add_u32 s10, s9, s10
	s_addc_u32 s11, s11, 0
	v_lshlrev_b32_e32 v2, 2, v36
	v_ashrrev_i32_e32 v33, 31, v32
	v_or_b32_e32 v8, 8, v32
	v_lshl_add_u64 v[34:35], s[10:11], 0, v[2:3]
	v_lshlrev_b64 v[4:5], 12, v[32:33]
	v_ashrrev_i32_e32 v9, 31, v8
	v_lshl_add_u64 v[4:5], v[34:35], 0, v[4:5]
	v_lshlrev_b64 v[8:9], 12, v[8:9]
	v_or_b32_e32 v12, 16, v32
	global_load_dwordx4 v[4:7], v[4:5], off
	v_lshl_add_u64 v[8:9], v[34:35], 0, v[8:9]
	v_ashrrev_i32_e32 v13, 31, v12
	global_load_dwordx4 v[8:11], v[8:9], off
	v_lshlrev_b64 v[12:13], 12, v[12:13]
	v_or_b32_e32 v16, 24, v32
	v_lshl_add_u64 v[12:13], v[34:35], 0, v[12:13]
	v_ashrrev_i32_e32 v17, 31, v16
	global_load_dwordx4 v[12:15], v[12:13], off
	v_lshlrev_b64 v[16:17], 12, v[16:17]
	v_or_b32_e32 v20, 32, v32
	v_lshl_add_u64 v[16:17], v[34:35], 0, v[16:17]
	v_ashrrev_i32_e32 v21, 31, v20
	global_load_dwordx4 v[16:19], v[16:17], off
	v_lshlrev_b64 v[20:21], 12, v[20:21]
	v_or_b32_e32 v24, 40, v32
	v_lshl_add_u64 v[20:21], v[34:35], 0, v[20:21]
	v_ashrrev_i32_e32 v25, 31, v24
	global_load_dwordx4 v[20:23], v[20:21], off
	v_lshlrev_b64 v[24:25], 12, v[24:25]
	v_or_b32_e32 v28, 48, v32
	v_lshl_add_u64 v[24:25], v[34:35], 0, v[24:25]
	v_ashrrev_i32_e32 v29, 31, v28
	global_load_dwordx4 v[24:27], v[24:25], off
	v_lshlrev_b64 v[28:29], 12, v[28:29]
	v_or_b32_e32 v32, 56, v32
	v_lshl_add_u64 v[28:29], v[34:35], 0, v[28:29]
	v_ashrrev_i32_e32 v33, 31, v32
	global_load_dwordx4 v[28:31], v[28:29], off
	v_lshlrev_b64 v[32:33], 12, v[32:33]
	v_lshl_add_u64 v[32:33], v[34:35], 0, v[32:33]
	global_load_dwordx4 v[32:35], v[32:33], off
	v_add_u32_e32 v2, v44, v45
	s_lshl_b64 s[10:11], s[68:69], 1
	s_add_u32 s10, s3, s10
	s_addc_u32 s11, s8, s11
	v_readlane_b32 s58, v253, 10
	v_readlane_b32 s59, v253, 11
	v_readlane_b32 s60, v253, 12
	v_readlane_b32 s61, v253, 13
	v_readlane_b32 s62, v253, 14
	v_readlane_b32 s63, v253, 15
	s_waitcnt vmcnt(0)
	ds_write2_b32 v2, v4, v5 offset1:1
	ds_write2_b32 v2, v6, v7 offset0:2 offset1:3
	v_add_u32_e32 v4, 0x420, v2
	ds_write2_b32 v4, v8, v9 offset1:1
	v_add_u32_e32 v4, 0x428, v2
	ds_write2_b32 v4, v10, v11 offset1:1
	v_add_u32_e32 v4, 0x840, v2
	ds_write2_b32 v4, v12, v13 offset1:1
	v_add_u32_e32 v4, 0x848, v2
	ds_write2_b32 v4, v14, v15 offset1:1
	v_add_u32_e32 v4, 0xc60, v2
	ds_write2_b32 v4, v16, v17 offset1:1
	v_add_u32_e32 v4, 0xc68, v2
	ds_write2_b32 v4, v18, v19 offset1:1
	v_add_u32_e32 v4, 0x1080, v2
	ds_write2_b32 v4, v20, v21 offset1:1
	v_add_u32_e32 v4, 0x1088, v2
	ds_write2_b32 v4, v22, v23 offset1:1
	v_add_u32_e32 v4, 0x14a0, v2
	ds_write2_b32 v4, v24, v25 offset1:1
	v_add_u32_e32 v4, 0x14a8, v2
	ds_write2_b32 v4, v26, v27 offset1:1
	v_add_u32_e32 v4, 0x18c0, v2
	ds_write2_b32 v4, v28, v29 offset1:1
	v_add_u32_e32 v4, 0x18c8, v2
	ds_write2_b32 v4, v30, v31 offset1:1
	v_add_u32_e32 v4, 0x1ce0, v2
	v_add_u32_e32 v2, 0x1ce8, v2
	ds_write2_b32 v4, v32, v33 offset1:1
	ds_write2_b32 v2, v34, v35 offset1:1
	s_waitcnt lgkmcnt(0)
	ds_read2_b32 v[10:11], v49 offset0:33 offset1:41
	ds_read2_b32 v[12:13], v49 offset1:8
	v_lshlrev_b32_e32 v2, 1, v38
	ds_read2_b32 v[14:15], v49 offset0:66 offset1:74
	ds_read2_b32 v[16:17], v49 offset0:99 offset1:107
	ds_read2_b32 v[18:19], v49 offset0:132 offset1:140
	ds_read2_b32 v[20:21], v49 offset0:165 offset1:173
	ds_read2_b32 v[22:23], v49 offset0:198 offset1:206
	ds_read2_b32 v[24:25], v49 offset0:231 offset1:239
	v_lshl_add_u64 v[8:9], s[10:11], 0, v[2:3]
	v_or_b32_e32 v2, s2, v39
	v_mul_u32_u24_e32 v2, 0x1600, v2
	v_lshl_add_u64 v[26:27], v[8:9], 0, v[2:3]
	v_or_b32_e32 v2, s2, v46
	s_waitcnt lgkmcnt(0)
	v_cvt_pk_bf16_f32 v4, v12, v10
	v_mul_u32_u24_e32 v2, 0x1600, v2
	v_cvt_pk_bf16_f32 v5, v14, v16
	v_cvt_pk_bf16_f32 v6, v18, v20
	v_cvt_pk_bf16_f32 v7, v22, v24
	global_store_dwordx4 v[26:27], v[4:7], off sc1
	s_nop 1
	v_cvt_pk_bf16_f32 v4, v13, v11
	v_lshl_add_u64 v[10:11], v[8:9], 0, v[2:3]
	v_cvt_pk_bf16_f32 v5, v15, v17
	v_cvt_pk_bf16_f32 v6, v19, v21
	v_cvt_pk_bf16_f32 v7, v23, v25
	global_store_dwordx4 v[10:11], v[4:7], off sc1
	ds_read2_b32 v[10:11], v49 offset0:16 offset1:24
	ds_read2_b32 v[12:13], v49 offset0:49 offset1:57
	ds_read2_b32 v[14:15], v49 offset0:82 offset1:90
	ds_read2_b32 v[16:17], v49 offset0:115 offset1:123
	ds_read2_b32 v[18:19], v49 offset0:148 offset1:156
	ds_read2_b32 v[20:21], v49 offset0:181 offset1:189
	ds_read2_b32 v[22:23], v49 offset0:214 offset1:222
	ds_read2_b32 v[24:25], v49 offset0:247 offset1:255
	v_or_b32_e32 v2, s2, v47
	v_mul_u32_u24_e32 v2, 0x1600, v2
	v_lshl_add_u64 v[26:27], v[8:9], 0, v[2:3]
	v_or_b32_e32 v2, s2, v48
	v_mul_u32_u24_e32 v2, 0x1600, v2
	s_waitcnt lgkmcnt(6)
	v_cvt_pk_bf16_f32 v4, v10, v12
	s_waitcnt lgkmcnt(4)
	v_cvt_pk_bf16_f32 v5, v14, v16
	s_waitcnt lgkmcnt(2)
	v_cvt_pk_bf16_f32 v6, v18, v20
	s_waitcnt lgkmcnt(0)
	v_cvt_pk_bf16_f32 v7, v22, v24
	v_lshl_add_u64 v[8:9], v[8:9], 0, v[2:3]
	global_store_dwordx4 v[26:27], v[4:7], off sc1
	s_mov_b64 s[2:3], 0
	s_nop 0
	v_cvt_pk_bf16_f32 v4, v11, v13
	v_cvt_pk_bf16_f32 v5, v15, v17
	v_cvt_pk_bf16_f32 v6, v19, v21
	v_cvt_pk_bf16_f32 v7, v23, v25
	global_store_dwordx4 v[8:9], v[4:7], off sc1
	s_waitcnt lgkmcnt(0)

; #define GAS __attribute__((address_space(1)))
; #define LAS __attribute__((address_space(3)))
; #define LDS_WAIT() asm volatile("s_waitcnt lgkmcnt(0)" ::: "memory")
; __device__ __forceinline__ unsigned pk2(float lo, float hi) { unsigned r; asm("v_cvt_pk_bf16_f32 %0, %1, %2" : "=v"(r) : "v"(lo), "v"(hi)); return r; }
; __device__ __forceinline__ void transpose_item(const float* W, int K, int N, bf16* WT, int drow0, int kb, int n0, LAS float* scr, int lane) {
;     const int k0 = 64 * kb; const int c4 = 4 * (lane & 7); const bool ok = (n0 + c4) < N;
;     f32x4 v[8];
; #pragma unroll
;     for (int i = 0; i < 8; ++i) { const int kk = 8 * i + (lane >> 3); v[i] = ok ? *(const f32x4*)(W + (size_t)(k0 + kk) * N + n0 + c4) : (f32x4){0.f, 0.f, 0.f, 0.f}; }
; #pragma unroll
;     for (int i = 0; i < 8; ++i) { const int kk = 8 * i + (lane >> 3); LAS float* d = scr + kk * 33 + c4; d[0] = v[i][0]; d[1] = v[i][1]; d[2] = v[i][2]; d[3] = v[i][3]; }
;     LDS_WAIT(); asm volatile("" ::: "memory");
;     const int c = lane & 7;
; #pragma unroll
;     for (int j = 0; j < 4; ++j) { const int n = (lane >> 3) + 8 * j; const LAS float* s = scr + (8 * c) * 33 + n;
;         v4u o; o.x = pk2(s[0 * 33], s[1 * 33]); o.y = pk2(s[2 * 33], s[3 * 33]); o.z = pk2(s[4 * 33], s[5 * 33]); o.w = pk2(s[6 * 33], s[7 * 33]);
;         *(GAS v4u*)(WT + (size_t)(drow0 + n) * K + k0 + 8 * c) = o; }
;     LDS_WAIT(); asm volatile("" ::: "memory");
; }
; __device__ __forceinline__ void convert_item(const In& I, unsigned char* ws, int it, LAS float* scr, int lane) {
;     ...
;     if (r < 2 * I_SQ) { const int j = r / I_SQ; r -= j * I_SQ; const int kb = r / 32, nb = r % 32;
;         transpose_item(I.nsa_w_out + (size_t)j * D * D, D, D, Wnout + (size_t)j * D * D, 32 * nb, kb, 32 * nb, scr, lane); return; }
.LBB0_303:
	s_andn2_b64 vcc, exec, s[2:3]
	s_cbranch_vccnz .LBB0_305
	s_add_i32 s2, s40, 0x800
	s_lshr_b32 s68, s2, 9
	v_readlane_b32 s48, v253, 16
	s_lshl_b64 s[2:3], s[68:69], 22
	v_readlane_b32 s60, v253, 28
	v_readlane_b32 s61, v253, 29
	s_add_u32 s6, s60, s2
	s_addc_u32 s7, s61, s3
	s_lshl_b64 s[2:3], s[68:69], 21
	s_add_u32 s8, s27, s2
	s_addc_u32 s3, s31, s3
	s_and_b32 s2, s42, 0x3e0
	s_add_i32 s9, s43, 0x10000
	s_and_b32 s9, s9, 0x3c0
	s_lshl_b32 s10, s2, 2
	s_add_u32 s6, s6, s10
	v_or_b32_e32 v6, s9, v39
	s_addc_u32 s7, s7, 0
	v_lshlrev_b32_e32 v2, 2, v36
	v_lshl_add_u64 v[4:5], s[6:7], 0, v[2:3]
	v_lshlrev_b32_e32 v2, 12, v6
	v_lshl_add_u64 v[32:33], v[4:5], 0, v[2:3]
	v_add_co_u32_e32 v8, vcc, s81, v32
	global_load_dwordx4 v[4:7], v[32:33], off
	s_nop 0
	v_addc_co_u32_e32 v9, vcc, 0, v33, vcc
	global_load_dwordx4 v[8:11], v[8:9], off
	v_add_co_u32_e32 v12, vcc, s79, v32
	v_add_u32_e32 v2, v44, v45
	s_nop 0
	v_addc_co_u32_e32 v13, vcc, 0, v33, vcc
	global_load_dwordx4 v[12:15], v[12:13], off
	v_add_co_u32_e32 v16, vcc, s80, v32
	s_lshl_b32 s6, s9, 1
	s_nop 0
	v_addc_co_u32_e32 v17, vcc, 0, v33, vcc
	global_load_dwordx4 v[16:19], v[16:17], off
	v_add_co_u32_e32 v20, vcc, s85, v32
	s_add_u32 s6, s8, s6
	s_nop 0
	v_addc_co_u32_e32 v21, vcc, 0, v33, vcc
	global_load_dwordx4 v[20:23], v[20:21], off
	v_add_co_u32_e32 v24, vcc, s86, v32
	s_addc_u32 s7, s3, 0
	s_nop 0
	v_addc_co_u32_e32 v25, vcc, 0, v33, vcc
	global_load_dwordx4 v[24:27], v[24:25], off
	v_add_co_u32_e32 v28, vcc, s87, v32
	v_readlane_b32 s49, v253, 17
	s_nop 0
	v_addc_co_u32_e32 v29, vcc, 0, v33, vcc
	global_load_dwordx4 v[28:31], v[28:29], off
	v_add_co_u32_e32 v32, vcc, s89, v32
	v_readlane_b32 s50, v253, 18
	s_nop 0
	v_addc_co_u32_e32 v33, vcc, 0, v33, vcc
	global_load_dwordx4 v[32:35], v[32:33], off
	v_readlane_b32 s51, v253, 19
	v_readlane_b32 s52, v253, 20
	v_readlane_b32 s53, v253, 21
	v_readlane_b32 s54, v253, 22
	v_readlane_b32 s55, v253, 23
	v_readlane_b32 s56, v253, 24
	v_readlane_b32 s57, v253, 25
	v_readlane_b32 s58, v253, 26
	v_readlane_b32 s59, v253, 27
	v_readlane_b32 s62, v253, 30
	v_readlane_b32 s63, v253, 31
	s_waitcnt vmcnt(0)
	ds_write2_b32 v2, v4, v5 offset1:1
	ds_write2_b32 v2, v6, v7 offset0:2 offset1:3
	v_add_u32_e32 v4, 0x420, v2
	ds_write2_b32 v4, v8, v9 offset1:1
	v_add_u32_e32 v4, 0x428, v2
	ds_write2_b32 v4, v10, v11 offset1:1
	v_add_u32_e32 v4, 0x840, v2
	ds_write2_b32 v4, v12, v13 offset1:1
	v_add_u32_e32 v4, 0x848, v2
	ds_write2_b32 v4, v14, v15 offset1:1
	v_add_u32_e32 v4, 0xc60, v2
	ds_write2_b32 v4, v16, v17 offset1:1
	v_add_u32_e32 v4, 0xc68, v2
	ds_write2_b32 v4, v18, v19 offset1:1
	v_add_u32_e32 v4, 0x1080, v2
	ds_write2_b32 v4, v20, v21 offset1:1
	v_add_u32_e32 v4, 0x1088, v2
	ds_write2_b32 v4, v22, v23 offset1:1
	v_add_u32_e32 v4, 0x14a0, v2
	ds_write2_b32 v4, v24, v25 offset1:1
	v_add_u32_e32 v4, 0x14a8, v2
	ds_write2_b32 v4, v26, v27 offset1:1
	v_add_u32_e32 v4, 0x18c0, v2
	ds_write2_b32 v4, v28, v29 offset1:1
	v_add_u32_e32 v4, 0x18c8, v2
	ds_write2_b32 v4, v30, v31 offset1:1
	v_add_u32_e32 v4, 0x1ce0, v2
	v_add_u32_e32 v2, 0x1ce8, v2
	ds_write2_b32 v4, v32, v33 offset1:1
	ds_write2_b32 v2, v34, v35 offset1:1
	s_waitcnt lgkmcnt(0)
	ds_read2_b32 v[10:11], v49 offset0:33 offset1:41
	ds_read2_b32 v[12:13], v49 offset1:8
	v_lshlrev_b32_e32 v2, 1, v38
	ds_read2_b32 v[14:15], v49 offset0:66 offset1:74
	ds_read2_b32 v[16:17], v49 offset0:99 offset1:107
	ds_read2_b32 v[18:19], v49 offset0:132 offset1:140
	ds_read2_b32 v[20:21], v49 offset0:165 offset1:173
	ds_read2_b32 v[22:23], v49 offset0:198 offset1:206
	ds_read2_b32 v[24:25], v49 offset0:231 offset1:239
	v_lshl_add_u64 v[8:9], s[6:7], 0, v[2:3]
	v_or_b32_e32 v2, s2, v39
	v_lshlrev_b32_e32 v2, 11, v2
	v_lshl_add_u64 v[26:27], v[8:9], 0, v[2:3]
	v_or_b32_e32 v2, s2, v46
	s_waitcnt lgkmcnt(0)
	v_cvt_pk_bf16_f32 v4, v12, v10
	v_lshlrev_b32_e32 v2, 11, v2
	v_cvt_pk_bf16_f32 v5, v14, v16
	v_cvt_pk_bf16_f32 v6, v18, v20
	v_cvt_pk_bf16_f32 v7, v22, v24
	global_store_dwordx4 v[26:27], v[4:7], off sc1
	s_nop 1
	v_cvt_pk_bf16_f32 v4, v13, v11
	v_lshl_add_u64 v[10:11], v[8:9], 0, v[2:3]
	v_cvt_pk_bf16_f32 v5, v15, v17
	v_cvt_pk_bf16_f32 v6, v19, v21
	v_cvt_pk_bf16_f32 v7, v23, v25
	global_store_dwordx4 v[10:11], v[4:7], off sc1
	ds_read2_b32 v[10:11], v49 offset0:16 offset1:24
	ds_read2_b32 v[12:13], v49 offset0:49 offset1:57
	ds_read2_b32 v[14:15], v49 offset0:82 offset1:90
	ds_read2_b32 v[16:17], v49 offset0:115 offset1:123
	ds_read2_b32 v[18:19], v49 offset0:148 offset1:156
	ds_read2_b32 v[20:21], v49 offset0:181 offset1:189
	ds_read2_b32 v[22:23], v49 offset0:214 offset1:222
	ds_read2_b32 v[24:25], v49 offset0:247 offset1:255
	v_or_b32_e32 v2, s2, v47
	v_lshlrev_b32_e32 v2, 11, v2
	v_lshl_add_u64 v[26:27], v[8:9], 0, v[2:3]
	v_or_b32_e32 v2, s2, v48
	v_lshlrev_b32_e32 v2, 11, v2
	s_waitcnt lgkmcnt(6)
	v_cvt_pk_bf16_f32 v4, v10, v12
	s_waitcnt lgkmcnt(4)
	v_cvt_pk_bf16_f32 v5, v14, v16
	s_waitcnt lgkmcnt(2)
	v_cvt_pk_bf16_f32 v6, v18, v20
	s_waitcnt lgkmcnt(0)
	v_cvt_pk_bf16_f32 v7, v22, v24
	v_lshl_add_u64 v[8:9], v[8:9], 0, v[2:3]
	global_store_dwordx4 v[26:27], v[4:7], off sc1
	s_nop 1
	v_cvt_pk_bf16_f32 v4, v11, v13
	v_cvt_pk_bf16_f32 v5, v15, v17
	v_cvt_pk_bf16_f32 v6, v19, v21
	v_cvt_pk_bf16_f32 v7, v23, v25
	global_store_dwordx4 v[8:9], v[4:7], off sc1
	s_waitcnt lgkmcnt(0)

; #define GAS __attribute__((address_space(1)))
; #define LAS __attribute__((address_space(3)))
; #define LDS_WAIT() asm volatile("s_waitcnt lgkmcnt(0)" ::: "memory")
; __device__ __forceinline__ unsigned pk2(float lo, float hi) { unsigned r; asm("v_cvt_pk_bf16_f32 %0, %1, %2" : "=v"(r) : "v"(lo), "v"(hi)); return r; }
; __device__ __forceinline__ void transpose_item(const float* W, int K, int N, bf16* WT, int drow0, int kb, int n0, LAS float* scr, int lane) {
;     const int k0 = 64 * kb; const int c4 = 4 * (lane & 7); const bool ok = (n0 + c4) < N;
;     f32x4 v[8];
; #pragma unroll
;     for (int i = 0; i < 8; ++i) { const int kk = 8 * i + (lane >> 3); v[i] = ok ? *(const f32x4*)(W + (size_t)(k0 + kk) * N + n0 + c4) : (f32x4){0.f, 0.f, 0.f, 0.f}; }
; #pragma unroll
;     for (int i = 0; i < 8; ++i) { const int kk = 8 * i + (lane >> 3); LAS float* d = scr + kk * 33 + c4; d[0] = v[i][0]; d[1] = v[i][1]; d[2] = v[i][2]; d[3] = v[i][3]; }
;     LDS_WAIT(); asm volatile("" ::: "memory");
;     const int c = lane & 7;
; #pragma unroll
;     for (int j = 0; j < 4; ++j) { const int n = (lane >> 3) + 8 * j; const LAS float* s = scr + (8 * c) * 33 + n;
;         v4u o; o.x = pk2(s[0 * 33], s[1 * 33]); o.y = pk2(s[2 * 33], s[3 * 33]); o.z = pk2(s[4 * 33], s[5 * 33]); o.w = pk2(s[6 * 33], s[7 * 33]);
;         *(GAS v4u*)(WT + (size_t)(drow0 + n) * K + k0 + 8 * c) = o; }
;     LDS_WAIT(); asm volatile("" ::: "memory");
; }
; __device__ __forceinline__ void convert_item(const In& I, unsigned char* ws, int it, LAS float* scr, int lane) {
;     ...
;     if (r < 2 * I_SQ) { const int j = r / I_SQ; r -= j * I_SQ; const int kb = r / 32, nb = r % 32;
;         transpose_item(I.fox_w_out + (size_t)j * D * D, D, D, Wfout + (size_t)j * D * D, 32 * nb, kb, 32 * nb, scr, lane); return; }
.LBB0_325:
	s_andn2_b64 vcc, exec, s[2:3]
	s_cbranch_vccnz .LBB0_327
	s_add_i32 s2, s40, 0x1900
	s_lshr_b32 s68, s2, 9
	v_readlane_b32 s48, v253, 16
	s_lshl_b64 s[2:3], s[68:69], 22
	v_readlane_b32 s54, v253, 22
	v_readlane_b32 s55, v253, 23
	s_add_u32 s6, s54, s2
	s_addc_u32 s7, s55, s3
	s_lshl_b64 s[2:3], s[68:69], 21
	s_add_u32 s8, s23, s2
	s_addc_u32 s3, s24, s3
	s_and_b32 s2, s42, 0x3e0
	s_add_i32 s9, s43, 0xffffe200
	s_and_b32 s9, s9, 0x3c0
	s_lshl_b32 s10, s2, 2
	s_add_u32 s6, s6, s10
	v_or_b32_e32 v6, s9, v39
	s_addc_u32 s7, s7, 0
	v_lshlrev_b32_e32 v2, 2, v36
	v_lshl_add_u64 v[4:5], s[6:7], 0, v[2:3]
	v_lshlrev_b32_e32 v2, 12, v6
	v_lshl_add_u64 v[32:33], v[4:5], 0, v[2:3]
	v_add_co_u32_e32 v8, vcc, s81, v32
	global_load_dwordx4 v[4:7], v[32:33], off
	s_nop 0
	v_addc_co_u32_e32 v9, vcc, 0, v33, vcc
	global_load_dwordx4 v[8:11], v[8:9], off
	v_add_co_u32_e32 v12, vcc, s79, v32
	v_add_u32_e32 v2, v44, v45
	s_nop 0
	v_addc_co_u32_e32 v13, vcc, 0, v33, vcc
	global_load_dwordx4 v[12:15], v[12:13], off
	v_add_co_u32_e32 v16, vcc, s80, v32
	s_lshl_b32 s6, s9, 1
	s_nop 0
	v_addc_co_u32_e32 v17, vcc, 0, v33, vcc
	global_load_dwordx4 v[16:19], v[16:17], off
	v_add_co_u32_e32 v20, vcc, s85, v32
	s_add_u32 s6, s8, s6
	s_nop 0
	v_addc_co_u32_e32 v21, vcc, 0, v33, vcc
	global_load_dwordx4 v[20:23], v[20:21], off
	v_add_co_u32_e32 v24, vcc, s86, v32
	s_addc_u32 s7, s3, 0
	s_nop 0
	v_addc_co_u32_e32 v25, vcc, 0, v33, vcc
	global_load_dwordx4 v[24:27], v[24:25], off
	v_add_co_u32_e32 v28, vcc, s87, v32
	v_readlane_b32 s49, v253, 17
	s_nop 0
	v_addc_co_u32_e32 v29, vcc, 0, v33, vcc
	global_load_dwordx4 v[28:31], v[28:29], off
	v_add_co_u32_e32 v32, vcc, s89, v32
	v_readlane_b32 s50, v253, 18
	s_nop 0
	v_addc_co_u32_e32 v33, vcc, 0, v33, vcc
	global_load_dwordx4 v[32:35], v[32:33], off
	v_readlane_b32 s51, v253, 19
	v_readlane_b32 s52, v253, 20
	v_readlane_b32 s53, v253, 21
	v_readlane_b32 s56, v253, 24
	v_readlane_b32 s57, v253, 25
	v_readlane_b32 s58, v253, 26
	v_readlane_b32 s59, v253, 27
	v_readlane_b32 s60, v253, 28
	v_readlane_b32 s61, v253, 29
	v_readlane_b32 s62, v253, 30
	v_readlane_b32 s63, v253, 31
	s_waitcnt vmcnt(0)
	ds_write2_b32 v2, v4, v5 offset1:1
	ds_write2_b32 v2, v6, v7 offset0:2 offset1:3
	v_add_u32_e32 v4, 0x420, v2
	ds_write2_b32 v4, v8, v9 offset1:1
	v_add_u32_e32 v4, 0x428, v2
	ds_write2_b32 v4, v10, v11 offset1:1
	v_add_u32_e32 v4, 0x840, v2
	ds_write2_b32 v4, v12, v13 offset1:1
	v_add_u32_e32 v4, 0x848, v2
	ds_write2_b32 v4, v14, v15 offset1:1
	v_add_u32_e32 v4, 0xc60, v2
	ds_write2_b32 v4, v16, v17 offset1:1
	v_add_u32_e32 v4, 0xc68, v2
	ds_write2_b32 v4, v18, v19 offset1:1
	v_add_u32_e32 v4, 0x1080, v2
	ds_write2_b32 v4, v20, v21 offset1:1
	v_add_u32_e32 v4, 0x1088, v2
	ds_write2_b32 v4, v22, v23 offset1:1
	v_add_u32_e32 v4, 0x14a0, v2
	ds_write2_b32 v4, v24, v25 offset1:1
	v_add_u32_e32 v4, 0x14a8, v2
	ds_write2_b32 v4, v26, v27 offset1:1
	v_add_u32_e32 v4, 0x18c0, v2
	ds_write2_b32 v4, v28, v29 offset1:1
	v_add_u32_e32 v4, 0x18c8, v2
	ds_write2_b32 v4, v30, v31 offset1:1
	v_add_u32_e32 v4, 0x1ce0, v2
	v_add_u32_e32 v2, 0x1ce8, v2
	ds_write2_b32 v4, v32, v33 offset1:1
	ds_write2_b32 v2, v34, v35 offset1:1
	s_waitcnt lgkmcnt(0)
	ds_read2_b32 v[10:11], v49 offset0:33 offset1:41
	ds_read2_b32 v[12:13], v49 offset1:8
	v_lshlrev_b32_e32 v2, 1, v38
	ds_read2_b32 v[14:15], v49 offset0:66 offset1:74
	ds_read2_b32 v[16:17], v49 offset0:99 offset1:107
	ds_read2_b32 v[18:19], v49 offset0:132 offset1:140
	ds_read2_b32 v[20:21], v49 offset0:165 offset1:173
	ds_read2_b32 v[22:23], v49 offset0:198 offset1:206
	ds_read2_b32 v[24:25], v49 offset0:231 offset1:239
	v_lshl_add_u64 v[8:9], s[6:7], 0, v[2:3]
	v_or_b32_e32 v2, s2, v39
	v_lshlrev_b32_e32 v2, 11, v2
	v_lshl_add_u64 v[26:27], v[8:9], 0, v[2:3]
	v_or_b32_e32 v2, s2, v46
	s_waitcnt lgkmcnt(0)
	v_cvt_pk_bf16_f32 v4, v12, v10
	v_lshlrev_b32_e32 v2, 11, v2
	v_cvt_pk_bf16_f32 v5, v14, v16
	v_cvt_pk_bf16_f32 v6, v18, v20
	v_cvt_pk_bf16_f32 v7, v22, v24
	global_store_dwordx4 v[26:27], v[4:7], off sc1
	s_nop 1
	v_cvt_pk_bf16_f32 v4, v13, v11
	v_lshl_add_u64 v[10:11], v[8:9], 0, v[2:3]
	v_cvt_pk_bf16_f32 v5, v15, v17
	v_cvt_pk_bf16_f32 v6, v19, v21
	v_cvt_pk_bf16_f32 v7, v23, v25
	global_store_dwordx4 v[10:11], v[4:7], off sc1
	ds_read2_b32 v[10:11], v49 offset0:16 offset1:24
	ds_read2_b32 v[12:13], v49 offset0:49 offset1:57
	ds_read2_b32 v[14:15], v49 offset0:82 offset1:90
	ds_read2_b32 v[16:17], v49 offset0:115 offset1:123
	ds_read2_b32 v[18:19], v49 offset0:148 offset1:156
	ds_read2_b32 v[20:21], v49 offset0:181 offset1:189
	ds_read2_b32 v[22:23], v49 offset0:214 offset1:222
	ds_read2_b32 v[24:25], v49 offset0:247 offset1:255
	v_or_b32_e32 v2, s2, v47
	v_lshlrev_b32_e32 v2, 11, v2
	v_lshl_add_u64 v[26:27], v[8:9], 0, v[2:3]
	v_or_b32_e32 v2, s2, v48
	v_lshlrev_b32_e32 v2, 11, v2
	s_waitcnt lgkmcnt(6)
	v_cvt_pk_bf16_f32 v4, v10, v12
	s_waitcnt lgkmcnt(4)
	v_cvt_pk_bf16_f32 v5, v14, v16
	s_waitcnt lgkmcnt(2)
	v_cvt_pk_bf16_f32 v6, v18, v20
	s_waitcnt lgkmcnt(0)
	v_cvt_pk_bf16_f32 v7, v22, v24
	v_lshl_add_u64 v[8:9], v[8:9], 0, v[2:3]
	global_store_dwordx4 v[26:27], v[4:7], off sc1
	s_nop 1
	v_cvt_pk_bf16_f32 v4, v11, v13
	v_cvt_pk_bf16_f32 v5, v15, v17
	v_cvt_pk_bf16_f32 v6, v19, v21
	v_cvt_pk_bf16_f32 v7, v23, v25
	global_store_dwordx4 v[8:9], v[4:7], off sc1
	s_waitcnt lgkmcnt(0)

; #define GAS __attribute__((address_space(1)))
; #define LAS __attribute__((address_space(3)))
; #define LDS_WAIT() asm volatile("s_waitcnt lgkmcnt(0)" ::: "memory")
; __device__ __forceinline__ unsigned pk2(float lo, float hi) { unsigned r; asm("v_cvt_pk_bf16_f32 %0, %1, %2" : "=v"(r) : "v"(lo), "v"(hi)); return r; }
; __device__ __forceinline__ void transpose_item(const float* W, int K, int N, bf16* WT, int drow0, int kb, int n0, LAS float* scr, int lane) {
;     const int k0 = 64 * kb; const int c4 = 4 * (lane & 7); const bool ok = (n0 + c4) < N;
;     f32x4 v[8];
; #pragma unroll
;     for (int i = 0; i < 8; ++i) { const int kk = 8 * i + (lane >> 3); v[i] = ok ? *(const f32x4*)(W + (size_t)(k0 + kk) * N + n0 + c4) : (f32x4){0.f, 0.f, 0.f, 0.f}; }
; #pragma unroll
;     for (int i = 0; i < 8; ++i) { const int kk = 8 * i + (lane >> 3); LAS float* d = scr + kk * 33 + c4; d[0] = v[i][0]; d[1] = v[i][1]; d[2] = v[i][2]; d[3] = v[i][3]; }
;     LDS_WAIT(); asm volatile("" ::: "memory");
;     const int c = lane & 7;
; #pragma unroll
;     for (int j = 0; j < 4; ++j) { const int n = (lane >> 3) + 8 * j; const LAS float* s = scr + (8 * c) * 33 + n;
;         v4u o; o.x = pk2(s[0 * 33], s[1 * 33]); o.y = pk2(s[2 * 33], s[3 * 33]); o.z = pk2(s[4 * 33], s[5 * 33]); o.w = pk2(s[6 * 33], s[7 * 33]);
;         *(GAS v4u*)(WT + (size_t)(drow0 + n) * K + k0 + 8 * c) = o; }
;     LDS_WAIT(); asm volatile("" ::: "memory");
; }
; __device__ __forceinline__ void convert_item(const In& I, unsigned char* ws, int it, LAS float* scr, int lane) {
;     ...
;     int r = it;
;     if (r < T0) { const int f = r / I_FFN; r -= f * I_FFN;
;         if (r < 2 * I_G) { const int up = r >= I_G; r -= up * I_G; const int kb = r / 88, nb = r % 88;
;             transpose_item((up ? I.w_up : I.w_gate) + (size_t)f * D * FF, D, FF, Wgu + (size_t)f * NGU * D, 256 * (nb >> 2) + 32 * (nb & 3) + 128 * up, kb, 32 * nb, scr, lane); }
;         else { r -= 2 * I_G; const int kb = r / 32, nb = r % 32; transpose_item(I.w_down + (size_t)f * FF * D, FF, D, Wd + (size_t)f * D * FF, 32 * nb, kb, 32 * nb, scr, lane); }
.LBB0_347:
	s_andn2_b64 vcc, exec, s[2:3]
	s_cbranch_vccnz .LBB0_292
	s_mul_hi_i32 s2, s44, 0x3e0f83e1
	s_lshr_b32 s3, s2, 31
	s_ashr_i32 s6, s2, 10
	s_add_i32 s6, s6, s3
	s_mul_i32 s2, s6, 0xffffef80
	s_add_i32 s7, s40, s2
	s_add_i32 s7, s7, 0xa800
	s_cmpk_gt_i32 s7, 0xaff
	s_mov_b64 s[2:3], -1
	s_cbranch_scc0 .LBB0_350
	v_readlane_b32 s48, v253, 0
	v_readlane_b32 s49, v253, 1
	v_readlane_b32 s50, v253, 2
	v_readlane_b32 s51, v253, 3
	v_readlane_b32 s52, v253, 4
	v_readlane_b32 s53, v253, 5
	v_readlane_b32 s54, v253, 6
	v_readlane_b32 s55, v253, 7
	v_readlane_b32 s56, v253, 8
	v_readlane_b32 s57, v253, 9
	s_mov_b64 s[48:49], s[52:53]
	s_mul_i32 s3, s6, 0xb00000
	s_mov_b64 s[50:51], s[54:55]
	s_mov_b64 s[52:53], s[56:57]
	s_mul_hi_i32 s2, s6, 0xb00000
	s_add_u32 s9, s52, s3
	s_addc_u32 s11, s53, s2
	s_mul_i32 s3, s6, 0x580000
	s_mul_hi_i32 s2, s6, 0x580000
	s_add_u32 s3, s19, s3
	s_mul_i32 s10, s6, 0xffffdf00
	s_addc_u32 s8, s20, s2
	s_add_i32 s10, s43, s10
	s_add_i32 s10, s10, 0x10000
	s_and_b32 s2, s42, 0x3e0
	s_andn2_b32 s10, s10, 63
	s_add_i32 s68, s10, 0xffffea00
	s_lshl_b32 s10, s2, 2
	v_or_b32_e32 v32, s68, v39
	s_add_u32 s10, s9, s10
	s_addc_u32 s11, s11, 0
	v_lshlrev_b32_e32 v2, 2, v36
	v_ashrrev_i32_e32 v33, 31, v32
	v_or_b32_e32 v8, 8, v32
	v_lshl_add_u64 v[34:35], s[10:11], 0, v[2:3]
	v_lshlrev_b64 v[4:5], 12, v[32:33]
	v_ashrrev_i32_e32 v9, 31, v8
	v_lshl_add_u64 v[4:5], v[34:35], 0, v[4:5]
	v_lshlrev_b64 v[8:9], 12, v[8:9]
	v_or_b32_e32 v12, 16, v32
	global_load_dwordx4 v[4:7], v[4:5], off
	v_lshl_add_u64 v[8:9], v[34:35], 0, v[8:9]
	v_ashrrev_i32_e32 v13, 31, v12
	global_load_dwordx4 v[8:11], v[8:9], off
	v_lshlrev_b64 v[12:13], 12, v[12:13]
	v_or_b32_e32 v16, 24, v32
	v_lshl_add_u64 v[12:13], v[34:35], 0, v[12:13]
	v_ashrrev_i32_e32 v17, 31, v16
	global_load_dwordx4 v[12:15], v[12:13], off
	v_lshlrev_b64 v[16:17], 12, v[16:17]
	v_or_b32_e32 v20, 32, v32
	v_lshl_add_u64 v[16:17], v[34:35], 0, v[16:17]
	v_ashrrev_i32_e32 v21, 31, v20
	global_load_dwordx4 v[16:19], v[16:17], off
	v_lshlrev_b64 v[20:21], 12, v[20:21]
	v_or_b32_e32 v24, 40, v32
	v_lshl_add_u64 v[20:21], v[34:35], 0, v[20:21]
	v_ashrrev_i32_e32 v25, 31, v24
	global_load_dwordx4 v[20:23], v[20:21], off
	v_lshlrev_b64 v[24:25], 12, v[24:25]
	v_or_b32_e32 v28, 48, v32
	v_lshl_add_u64 v[24:25], v[34:35], 0, v[24:25]
	v_ashrrev_i32_e32 v29, 31, v28
	global_load_dwordx4 v[24:27], v[24:25], off
	v_lshlrev_b64 v[28:29], 12, v[28:29]
	v_or_b32_e32 v32, 56, v32
	v_lshl_add_u64 v[28:29], v[34:35], 0, v[28:29]
	v_ashrrev_i32_e32 v33, 31, v32
	global_load_dwordx4 v[28:31], v[28:29], off
	v_lshlrev_b64 v[32:33], 12, v[32:33]
	v_lshl_add_u64 v[32:33], v[34:35], 0, v[32:33]
	global_load_dwordx4 v[32:35], v[32:33], off
	v_add_u32_e32 v2, v44, v45
	s_lshl_b64 s[10:11], s[68:69], 1
	s_add_u32 s10, s3, s10
	s_addc_u32 s11, s8, s11
	v_readlane_b32 s58, v253, 10
	v_readlane_b32 s59, v253, 11
	v_readlane_b32 s60, v253, 12
	v_readlane_b32 s61, v253, 13
	v_readlane_b32 s62, v253, 14
	v_readlane_b32 s63, v253, 15
	s_waitcnt vmcnt(0)
	ds_write2_b32 v2, v4, v5 offset1:1
	ds_write2_b32 v2, v6, v7 offset0:2 offset1:3
	v_add_u32_e32 v4, 0x420, v2
	ds_write2_b32 v4, v8, v9 offset1:1
	v_add_u32_e32 v4, 0x428, v2
	ds_write2_b32 v4, v10, v11 offset1:1
	v_add_u32_e32 v4, 0x840, v2
	ds_write2_b32 v4, v12, v13 offset1:1
	v_add_u32_e32 v4, 0x848, v2
	ds_write2_b32 v4, v14, v15 offset1:1
	v_add_u32_e32 v4, 0xc60, v2
	ds_write2_b32 v4, v16, v17 offset1:1
	v_add_u32_e32 v4, 0xc68, v2
	ds_write2_b32 v4, v18, v19 offset1:1
	v_add_u32_e32 v4, 0x1080, v2
	ds_write2_b32 v4, v20, v21 offset1:1
	v_add_u32_e32 v4, 0x1088, v2
	ds_write2_b32 v4, v22, v23 offset1:1
	v_add_u32_e32 v4, 0x14a0, v2
	ds_write2_b32 v4, v24, v25 offset1:1
	v_add_u32_e32 v4, 0x14a8, v2
	ds_write2_b32 v4, v26, v27 offset1:1
	v_add_u32_e32 v4, 0x18c0, v2
	ds_write2_b32 v4, v28, v29 offset1:1
	v_add_u32_e32 v4, 0x18c8, v2
	ds_write2_b32 v4, v30, v31 offset1:1
	v_add_u32_e32 v4, 0x1ce0, v2
	v_add_u32_e32 v2, 0x1ce8, v2
	ds_write2_b32 v4, v32, v33 offset1:1
	ds_write2_b32 v2, v34, v35 offset1:1
	s_waitcnt lgkmcnt(0)
	ds_read2_b32 v[10:11], v49 offset0:33 offset1:41
	ds_read2_b32 v[12:13], v49 offset1:8
	v_lshlrev_b32_e32 v2, 1, v38
	ds_read2_b32 v[14:15], v49 offset0:66 offset1:74
	ds_read2_b32 v[16:17], v49 offset0:99 offset1:107
	ds_read2_b32 v[18:19], v49 offset0:132 offset1:140
	ds_read2_b32 v[20:21], v49 offset0:165 offset1:173
	ds_read2_b32 v[22:23], v49 offset0:198 offset1:206
	ds_read2_b32 v[24:25], v49 offset0:231 offset1:239
	v_lshl_add_u64 v[8:9], s[10:11], 0, v[2:3]
	v_or_b32_e32 v2, s2, v39
	v_mul_u32_u24_e32 v2, 0x1600, v2
	v_lshl_add_u64 v[26:27], v[8:9], 0, v[2:3]
	v_or_b32_e32 v2, s2, v46
	s_waitcnt lgkmcnt(0)
	v_cvt_pk_bf16_f32 v4, v12, v10
	v_mul_u32_u24_e32 v2, 0x1600, v2
	v_cvt_pk_bf16_f32 v5, v14, v16
	v_cvt_pk_bf16_f32 v6, v18, v20
	v_cvt_pk_bf16_f32 v7, v22, v24
	global_store_dwordx4 v[26:27], v[4:7], off sc1
	s_nop 1
	v_cvt_pk_bf16_f32 v4, v13, v11
	v_lshl_add_u64 v[10:11], v[8:9], 0, v[2:3]
	v_cvt_pk_bf16_f32 v5, v15, v17
	v_cvt_pk_bf16_f32 v6, v19, v21
	v_cvt_pk_bf16_f32 v7, v23, v25
	global_store_dwordx4 v[10:11], v[4:7], off sc1
	ds_read2_b32 v[10:11], v49 offset0:16 offset1:24
	ds_read2_b32 v[12:13], v49 offset0:49 offset1:57
	ds_read2_b32 v[14:15], v49 offset0:82 offset1:90
	ds_read2_b32 v[16:17], v49 offset0:115 offset1:123
	ds_read2_b32 v[18:19], v49 offset0:148 offset1:156
	ds_read2_b32 v[20:21], v49 offset0:181 offset1:189
	ds_read2_b32 v[22:23], v49 offset0:214 offset1:222
	ds_read2_b32 v[24:25], v49 offset0:247 offset1:255
	v_or_b32_e32 v2, s2, v47
	v_mul_u32_u24_e32 v2, 0x1600, v2
	v_lshl_add_u64 v[26:27], v[8:9], 0, v[2:3]
	v_or_b32_e32 v2, s2, v48
	v_mul_u32_u24_e32 v2, 0x1600, v2
	s_waitcnt lgkmcnt(6)
	v_cvt_pk_bf16_f32 v4, v10, v12
	s_waitcnt lgkmcnt(4)
	v_cvt_pk_bf16_f32 v5, v14, v16
	s_waitcnt lgkmcnt(2)
	v_cvt_pk_bf16_f32 v6, v18, v20
	s_waitcnt lgkmcnt(0)
	v_cvt_pk_bf16_f32 v7, v22, v24
	v_lshl_add_u64 v[8:9], v[8:9], 0, v[2:3]
	global_store_dwordx4 v[26:27], v[4:7], off sc1
	s_mov_b64 s[2:3], 0
	s_nop 0
	v_cvt_pk_bf16_f32 v4, v11, v13
	v_cvt_pk_bf16_f32 v5, v15, v17
	v_cvt_pk_bf16_f32 v6, v19, v21
	v_cvt_pk_bf16_f32 v7, v23, v25
	global_store_dwordx4 v[8:9], v[4:7], off sc1
	s_waitcnt lgkmcnt(0)

; #define GAS __attribute__((address_space(1)))
; #define LAS __attribute__((address_space(3)))
; #define LDS_WAIT() asm volatile("s_waitcnt lgkmcnt(0)" ::: "memory")
; __device__ __forceinline__ unsigned pk2(float lo, float hi) { unsigned r; asm("v_cvt_pk_bf16_f32 %0, %1, %2" : "=v"(r) : "v"(lo), "v"(hi)); return r; }
; __device__ __forceinline__ void transpose_item(const float* W, int K, int N, bf16* WT, int drow0, int kb, int n0, LAS float* scr, int lane) {
;     const int k0 = 64 * kb; const int c4 = 4 * (lane & 7); const bool ok = (n0 + c4) < N;
;     f32x4 v[8];
; #pragma unroll
;     for (int i = 0; i < 8; ++i) { const int kk = 8 * i + (lane >> 3); v[i] = ok ? *(const f32x4*)(W + (size_t)(k0 + kk) * N + n0 + c4) : (f32x4){0.f, 0.f, 0.f, 0.f}; }
; #pragma unroll
;     for (int i = 0; i < 8; ++i) { const int kk = 8 * i + (lane >> 3); LAS float* d = scr + kk * 33 + c4; d[0] = v[i][0]; d[1] = v[i][1]; d[2] = v[i][2]; d[3] = v[i][3]; }
;     LDS_WAIT(); asm volatile("" ::: "memory");
;     const int c = lane & 7;
; #pragma unroll
;     for (int j = 0; j < 4; ++j) { const int n = (lane >> 3) + 8 * j; const LAS float* s = scr + (8 * c) * 33 + n;
;         v4u o; o.x = pk2(s[0 * 33], s[1 * 33]); o.y = pk2(s[2 * 33], s[3 * 33]); o.z = pk2(s[4 * 33], s[5 * 33]); o.w = pk2(s[6 * 33], s[7 * 33]);
;         *(GAS v4u*)(WT + (size_t)(drow0 + n) * K + k0 + 8 * c) = o; }
;     LDS_WAIT(); asm volatile("" ::: "memory");
; }
; __device__ __forceinline__ void convert_item(const In& I, unsigned char* ws, int it, LAS float* scr, int lane) {
;     ...
;     { const int jk = r >> 3; r &= 7; const int kb = r >> 1, nb = r & 1;
;         transpose_item(I.nsa_w2 + (size_t)jk * 256 * 64, 256, 64, W2t + (size_t)jk * 64 * 256, 32 * nb, kb, 32 * nb, scr, lane); }
.LBB0_355:
	s_add_i32 s45, s41, 0xa800
	s_cmp_gt_i32 s45, 0x83ff
	s_mov_b64 s[2:3], -1
	s_cbranch_scc0 .LBB0_409
	s_cmpk_gt_u32 s45, 0x8eff
	s_cbranch_scc0 .LBB0_390
	s_cmpk_gt_u32 s45, 0x92ff
	s_cbranch_scc0 .LBB0_387
	s_cmpk_gt_u32 s45, 0x9fff
	s_cbranch_scc0 .LBB0_368
	s_cmpk_gt_u32 s45, 0xa3ff
	s_cbranch_scc0 .LBB0_365
	s_cmpk_gt_u32 s45, 0xa7ff
	s_cbranch_scc0 .LBB0_362
	s_lshr_b32 s68, s41, 3
	v_readlane_b32 s48, v253, 16
	s_lshl_b64 s[2:3], s[68:69], 16
	v_readlane_b32 s52, v253, 20
	v_readlane_b32 s53, v253, 21
	s_add_u32 s6, s52, s2
	s_addc_u32 s7, s53, s3
	s_lshl_b64 s[2:3], s[68:69], 15
	s_add_u32 s8, s34, s2
	s_addc_u32 s3, s35, s3
	s_and_b32 s2, s43, 32
	s_and_b32 s9, s43, 0xc0
	s_lshl_b32 s10, s2, 2
	s_add_u32 s6, s6, s10
	v_or_b32_e32 v6, s9, v39
	s_addc_u32 s7, s7, 0
	v_lshlrev_b32_e32 v2, 2, v36
	v_lshl_add_u64 v[4:5], s[6:7], 0, v[2:3]
	v_lshlrev_b32_e32 v2, 8, v6
	v_lshl_add_u64 v[28:29], v[4:5], 0, v[2:3]
	v_add_co_u32_e32 v16, vcc, s84, v28
	global_load_dwordx4 v[4:7], v[28:29], off
	global_load_dwordx4 v[8:11], v[28:29], off offset:2048
	v_addc_co_u32_e32 v17, vcc, 0, v29, vcc
	v_add_co_u32_e32 v24, vcc, s74, v28
	s_movk_i32 s6, 0x3000
	s_nop 0
	v_addc_co_u32_e32 v25, vcc, 0, v29, vcc
	global_load_dwordx4 v[12:15], v[24:25], off offset:-4096
	s_nop 0
	global_load_dwordx4 v[16:19], v[16:17], off offset:2048
	s_nop 0
	global_load_dwordx4 v[20:23], v[24:25], off
	s_nop 0
	global_load_dwordx4 v[24:27], v[24:25], off offset:2048
	v_add_co_u32_e32 v32, vcc, s6, v28
	v_add_u32_e32 v2, v44, v47
	s_nop 0
	v_addc_co_u32_e32 v33, vcc, 0, v29, vcc
	global_load_dwordx4 v[28:31], v[32:33], off
	s_nop 0
	global_load_dwordx4 v[32:35], v[32:33], off offset:2048
	s_lshl_b32 s6, s9, 1
	s_add_u32 s6, s8, s6
	s_addc_u32 s7, s3, 0
	v_readlane_b32 s49, v253, 17
	v_readlane_b32 s50, v253, 18
	v_readlane_b32 s51, v253, 19
	v_readlane_b32 s54, v253, 22
	v_readlane_b32 s55, v253, 23
	v_readlane_b32 s56, v253, 24
	v_readlane_b32 s57, v253, 25
	v_readlane_b32 s58, v253, 26
	v_readlane_b32 s59, v253, 27
	v_readlane_b32 s60, v253, 28
	v_readlane_b32 s61, v253, 29
	v_readlane_b32 s62, v253, 30
	v_readlane_b32 s63, v253, 31
	s_waitcnt vmcnt(0)
	ds_write2_b32 v45, v4, v5 offset1:1
	ds_write2_b32 v45, v6, v7 offset0:2 offset1:3
	v_add_u32_e32 v4, 0x420, v2
	ds_write2_b32 v2, v8, v9 offset1:1
	ds_write2_b32 v2, v10, v11 offset0:2 offset1:3
	ds_write2_b32 v4, v12, v13 offset1:1
	v_add_u32_e32 v4, 0x428, v2
	ds_write2_b32 v4, v14, v15 offset1:1
	v_add_u32_e32 v4, 0x840, v2
	v_add_u32_e32 v2, 0x848, v2
	ds_write2_b32 v2, v18, v19 offset1:1
	v_add_u32_e32 v2, 0x1080, v45
	ds_write2_b32 v2, v20, v21 offset1:1
	v_add_u32_e32 v2, 0x1088, v45
	ds_write2_b32 v2, v22, v23 offset1:1
	v_add_u32_e32 v2, 0x14a0, v45
	ds_write2_b32 v2, v24, v25 offset1:1
	v_add_u32_e32 v2, 0x14a8, v45
	ds_write2_b32 v2, v26, v27 offset1:1
	v_add_u32_e32 v2, 0x18c0, v45
	ds_write2_b32 v2, v28, v29 offset1:1
	v_add_u32_e32 v2, 0x18c8, v45
	ds_write2_b32 v2, v30, v31 offset1:1
	v_add_u32_e32 v2, 0x1ce0, v45
	ds_write2_b32 v2, v32, v33 offset1:1
	v_add_u32_e32 v2, 0x1ce8, v45
	ds_write2_b32 v4, v16, v17 offset1:1
	ds_write2_b32 v2, v34, v35 offset1:1
	s_waitcnt lgkmcnt(0)
	ds_read2_b32 v[10:11], v50 offset0:33 offset1:41
	ds_read2_b32 v[12:13], v50 offset1:8
	v_lshlrev_b32_e32 v2, 1, v38
	ds_read2_b32 v[14:15], v50 offset0:66 offset1:74
	ds_read2_b32 v[16:17], v50 offset0:99 offset1:107
	ds_read2_b32 v[18:19], v50 offset0:132 offset1:140
	ds_read2_b32 v[20:21], v50 offset0:165 offset1:173
	ds_read2_b32 v[22:23], v50 offset0:198 offset1:206
	ds_read2_b32 v[24:25], v50 offset0:231 offset1:239
	v_lshl_add_u64 v[4:5], s[6:7], 0, v[2:3]
	v_or_b32_e32 v2, s2, v39
	v_lshlrev_b32_e32 v2, 9, v2
	v_lshl_add_u64 v[26:27], v[4:5], 0, v[2:3]
	v_or_b32_e32 v2, s2, v46
	s_waitcnt lgkmcnt(0)
	v_cvt_pk_bf16_f32 v6, v12, v10
	v_lshlrev_b32_e32 v2, 9, v2
	v_cvt_pk_bf16_f32 v7, v14, v16
	v_cvt_pk_bf16_f32 v8, v18, v20
	v_cvt_pk_bf16_f32 v9, v22, v24
	global_store_dwordx4 v[26:27], v[6:9], off sc1
	s_nop 1
	v_cvt_pk_bf16_f32 v6, v13, v11
	v_lshl_add_u64 v[10:11], v[4:5], 0, v[2:3]
	v_cvt_pk_bf16_f32 v7, v15, v17
	v_cvt_pk_bf16_f32 v8, v19, v21
	v_cvt_pk_bf16_f32 v9, v23, v25
	global_store_dwordx4 v[10:11], v[6:9], off sc1
	ds_read2_b32 v[10:11], v50 offset0:16 offset1:24
	ds_read2_b32 v[12:13], v50 offset0:49 offset1:57
	ds_read2_b32 v[14:15], v50 offset0:82 offset1:90
	ds_read2_b32 v[16:17], v50 offset0:115 offset1:123
	ds_read2_b32 v[18:19], v50 offset0:148 offset1:156
	ds_read2_b32 v[20:21], v50 offset0:181 offset1:189
	ds_read2_b32 v[22:23], v50 offset0:214 offset1:222
	ds_read2_b32 v[24:25], v50 offset0:247 offset1:255
	v_or_b32_e32 v2, s2, v48
	v_lshlrev_b32_e32 v2, 9, v2
	v_lshl_add_u64 v[26:27], v[4:5], 0, v[2:3]
	v_or_b32_e32 v2, s2, v49
	v_lshlrev_b32_e32 v2, 9, v2
	s_waitcnt lgkmcnt(6)
	v_cvt_pk_bf16_f32 v6, v10, v12
	s_waitcnt lgkmcnt(4)
	v_cvt_pk_bf16_f32 v7, v14, v16
	s_waitcnt lgkmcnt(2)
	v_cvt_pk_bf16_f32 v8, v18, v20
	s_waitcnt lgkmcnt(0)
	v_cvt_pk_bf16_f32 v9, v22, v24
	v_lshl_add_u64 v[4:5], v[4:5], 0, v[2:3]
	global_store_dwordx4 v[26:27], v[6:9], off sc1
	s_mov_b64 s[2:3], 0
	s_nop 0
	v_cvt_pk_bf16_f32 v6, v11, v13
	v_cvt_pk_bf16_f32 v7, v15, v17
	v_cvt_pk_bf16_f32 v8, v19, v21
	v_cvt_pk_bf16_f32 v9, v23, v25
	global_store_dwordx4 v[4:5], v[6:9], off sc1
	s_waitcnt lgkmcnt(0)
; #define GAS __attribute__((address_space(1)))
; #define LAS __attribute__((address_space(3)))
; #define LDS_WAIT() asm volatile("s_waitcnt lgkmcnt(0)" ::: "memory")
; __device__ __forceinline__ unsigned pk2(float lo, float hi) { unsigned r; asm("v_cvt_pk_bf16_f32 %0, %1, %2" : "=v"(r) : "v"(lo), "v"(hi)); return r; }
; __device__ __forceinline__ void transpose_item(const float* W, int K, int N, bf16* WT, int drow0, int kb, int n0, LAS float* scr, int lane) {
;     const int k0 = 64 * kb; const int c4 = 4 * (lane & 7); const bool ok = (n0 + c4) < N;
;     f32x4 v[8];
; #pragma unroll
;     for (int i = 0; i < 8; ++i) { const int kk = 8 * i + (lane >> 3); v[i] = ok ? *(const f32x4*)(W + (size_t)(k0 + kk) * N + n0 + c4) : (f32x4){0.f, 0.f, 0.f, 0.f}; }
; #pragma unroll
;     for (int i = 0; i < 8; ++i) { const int kk = 8 * i + (lane >> 3); LAS float* d = scr + kk * 33 + c4; d[0] = v[i][0]; d[1] = v[i][1]; d[2] = v[i][2]; d[3] = v[i][3]; }
;     LDS_WAIT(); asm volatile("" ::: "memory");
;     const int c = lane & 7;
; #pragma unroll
;     for (int j = 0; j < 4; ++j) { const int n = (lane >> 3) + 8 * j; const LAS float* s = scr + (8 * c) * 33 + n;
;         v4u o; o.x = pk2(s[0 * 33], s[1 * 33]); o.y = pk2(s[2 * 33], s[3 * 33]); o.z = pk2(s[4 * 33], s[5 * 33]); o.w = pk2(s[6 * 33], s[7 * 33]);
;         *(GAS v4u*)(WT + (size_t)(drow0 + n) * K + k0 + 8 * c) = o; }
;     LDS_WAIT(); asm volatile("" ::: "memory");
; }
; __device__ __forceinline__ void convert_item(const In& I, unsigned char* ws, int it, LAS float* scr, int lane) {
;     ...
;     if (r < 4 * I_W1) { const int jk = r / I_W1; r -= jk * I_W1; const int kb = r / 8, nb = r % 8;
;         transpose_item(I.nsa_w1 + (size_t)jk * 2048 * 256, 2048, 256, W1t + (size_t)jk * 256 * 2048, 32 * nb, kb, 32 * nb, scr, lane); return; }
.LBB0_362:
	s_andn2_b64 vcc, exec, s[2:3]
	s_cbranch_vccnz .LBB0_364
	s_add_i32 s2, s41, 0x400
	s_lshr_b32 s68, s2, 8
	s_lshl_b64 s[2:3], s[68:69], 21
	v_readlane_b32 s48, v253, 16
	v_readlane_b32 s49, v253, 17
	s_add_u32 s6, s48, s2
	s_addc_u32 s7, s49, s3
	s_lshl_b64 s[2:3], s[68:69], 20
	s_add_u32 s8, s31, s2
	s_addc_u32 s3, s33, s3
	s_and_b32 s2, s43, 0xe0
	s_and_b32 s9, s42, 0x7c0
	s_lshl_b32 s10, s2, 2
	s_add_u32 s6, s6, s10
	v_or_b32_e32 v6, s9, v39
	s_addc_u32 s7, s7, 0
	v_lshlrev_b32_e32 v2, 2, v36
	v_lshl_add_u64 v[4:5], s[6:7], 0, v[2:3]
	v_lshlrev_b32_e32 v2, 10, v6
	v_lshl_add_u64 v[32:33], v[4:5], 0, v[2:3]
	v_add_co_u32_e32 v8, vcc, s74, v32
	s_movk_i32 s6, 0x4000
	s_nop 0
	v_addc_co_u32_e32 v9, vcc, 0, v33, vcc
	v_add_co_u32_e32 v12, vcc, s6, v32
	s_movk_i32 s6, 0x6000
	s_nop 0
	v_addc_co_u32_e32 v13, vcc, 0, v33, vcc
	global_load_dwordx4 v[4:7], v[32:33], off
	v_add_co_u32_e32 v16, vcc, s6, v32
	global_load_dwordx4 v[8:11], v[8:9], off
	s_nop 0
	v_addc_co_u32_e32 v17, vcc, 0, v33, vcc
	global_load_dwordx4 v[12:15], v[12:13], off
	v_add_co_u32_e32 v20, vcc, s81, v32
	global_load_dwordx4 v[16:19], v[16:17], off
	s_nop 0
	v_addc_co_u32_e32 v21, vcc, 0, v33, vcc
	s_mov_b32 s6, 0xa000
	global_load_dwordx4 v[20:23], v[20:21], off
	v_add_co_u32_e32 v24, vcc, s6, v32
	s_mov_b32 s6, 0xc000
	s_nop 0
	v_addc_co_u32_e32 v25, vcc, 0, v33, vcc
	global_load_dwordx4 v[24:27], v[24:25], off
	v_add_co_u32_e32 v28, vcc, s6, v32
	s_mov_b32 s6, 0xe000
	s_nop 0
	v_addc_co_u32_e32 v29, vcc, 0, v33, vcc
	global_load_dwordx4 v[28:31], v[28:29], off
	v_add_co_u32_e32 v32, vcc, s6, v32
	v_add_u32_e32 v2, v44, v47
	s_nop 0
	v_addc_co_u32_e32 v33, vcc, 0, v33, vcc
	global_load_dwordx4 v[32:35], v[32:33], off
	s_lshl_b32 s6, s9, 1
	s_add_u32 s6, s8, s6
	s_addc_u32 s7, s3, 0
	v_readlane_b32 s50, v253, 18
	v_readlane_b32 s51, v253, 19
	v_readlane_b32 s52, v253, 20
	v_readlane_b32 s53, v253, 21
	v_readlane_b32 s54, v253, 22
	v_readlane_b32 s55, v253, 23
	v_readlane_b32 s56, v253, 24
	v_readlane_b32 s57, v253, 25
	v_readlane_b32 s58, v253, 26
	v_readlane_b32 s59, v253, 27
	v_readlane_b32 s60, v253, 28
	v_readlane_b32 s61, v253, 29
	v_readlane_b32 s62, v253, 30
	v_readlane_b32 s63, v253, 31
	s_waitcnt vmcnt(0)
	ds_write2_b32 v45, v4, v5 offset1:1
	ds_write2_b32 v45, v6, v7 offset0:2 offset1:3
	v_add_u32_e32 v4, 0x420, v2
	ds_write2_b32 v2, v8, v9 offset1:1
	ds_write2_b32 v2, v10, v11 offset0:2 offset1:3
	ds_write2_b32 v4, v12, v13 offset1:1
	v_add_u32_e32 v4, 0x428, v2
	ds_write2_b32 v4, v14, v15 offset1:1
	v_add_u32_e32 v4, 0x840, v2
	v_add_u32_e32 v2, 0x848, v2
	ds_write2_b32 v2, v18, v19 offset1:1
	v_add_u32_e32 v2, 0x1080, v45
	ds_write2_b32 v2, v20, v21 offset1:1
	v_add_u32_e32 v2, 0x1088, v45
	ds_write2_b32 v2, v22, v23 offset1:1
	v_add_u32_e32 v2, 0x14a0, v45
	ds_write2_b32 v4, v16, v17 offset1:1
	ds_write2_b32 v2, v24, v25 offset1:1
	v_add_u32_e32 v2, 0x14a8, v45
	ds_write2_b32 v2, v26, v27 offset1:1
	v_add_u32_e32 v2, 0x18c0, v45
	ds_write2_b32 v2, v28, v29 offset1:1
	v_add_u32_e32 v2, 0x18c8, v45
	ds_write2_b32 v2, v30, v31 offset1:1
	v_add_u32_e32 v2, 0x1ce0, v45
	ds_write2_b32 v2, v32, v33 offset1:1
	v_add_u32_e32 v2, 0x1ce8, v45
	ds_write2_b32 v2, v34, v35 offset1:1
	s_waitcnt lgkmcnt(0)
	ds_read2_b32 v[10:11], v50 offset0:33 offset1:41
	ds_read2_b32 v[12:13], v50 offset1:8
	v_lshlrev_b32_e32 v2, 1, v38
	ds_read2_b32 v[14:15], v50 offset0:66 offset1:74
	ds_read2_b32 v[16:17], v50 offset0:99 offset1:107
	ds_read2_b32 v[18:19], v50 offset0:132 offset1:140
	ds_read2_b32 v[20:21], v50 offset0:165 offset1:173
	ds_read2_b32 v[22:23], v50 offset0:198 offset1:206
	ds_read2_b32 v[24:25], v50 offset0:231 offset1:239
	v_lshl_add_u64 v[4:5], s[6:7], 0, v[2:3]
	v_or_b32_e32 v2, s2, v39
	v_lshlrev_b32_e32 v2, 12, v2
	v_lshl_add_u64 v[26:27], v[4:5], 0, v[2:3]
	v_or_b32_e32 v2, s2, v46
	s_waitcnt lgkmcnt(0)
	v_cvt_pk_bf16_f32 v6, v12, v10
	v_lshlrev_b32_e32 v2, 12, v2
	v_cvt_pk_bf16_f32 v7, v14, v16
	v_cvt_pk_bf16_f32 v8, v18, v20
	v_cvt_pk_bf16_f32 v9, v22, v24
	global_store_dwordx4 v[26:27], v[6:9], off sc1
	s_nop 1
	v_cvt_pk_bf16_f32 v6, v13, v11
	v_lshl_add_u64 v[10:11], v[4:5], 0, v[2:3]
	v_cvt_pk_bf16_f32 v7, v15, v17
	v_cvt_pk_bf16_f32 v8, v19, v21
	v_cvt_pk_bf16_f32 v9, v23, v25
	global_store_dwordx4 v[10:11], v[6:9], off sc1
	ds_read2_b32 v[10:11], v50 offset0:16 offset1:24
	ds_read2_b32 v[12:13], v50 offset0:49 offset1:57
	ds_read2_b32 v[14:15], v50 offset0:82 offset1:90
	ds_read2_b32 v[16:17], v50 offset0:115 offset1:123
	ds_read2_b32 v[18:19], v50 offset0:148 offset1:156
	ds_read2_b32 v[20:21], v50 offset0:181 offset1:189
	ds_read2_b32 v[22:23], v50 offset0:214 offset1:222
	ds_read2_b32 v[24:25], v50 offset0:247 offset1:255
	v_or_b32_e32 v2, s2, v48
	v_lshlrev_b32_e32 v2, 12, v2
	v_lshl_add_u64 v[26:27], v[4:5], 0, v[2:3]
	v_or_b32_e32 v2, s2, v49
	v_lshlrev_b32_e32 v2, 12, v2
	s_waitcnt lgkmcnt(6)
	v_cvt_pk_bf16_f32 v6, v10, v12
	s_waitcnt lgkmcnt(4)
	v_cvt_pk_bf16_f32 v7, v14, v16
	s_waitcnt lgkmcnt(2)
	v_cvt_pk_bf16_f32 v8, v18, v20
	s_waitcnt lgkmcnt(0)
	v_cvt_pk_bf16_f32 v9, v22, v24
	v_lshl_add_u64 v[4:5], v[4:5], 0, v[2:3]
	global_store_dwordx4 v[26:27], v[6:9], off sc1
	s_nop 1
	v_cvt_pk_bf16_f32 v6, v11, v13
	v_cvt_pk_bf16_f32 v7, v15, v17
	v_cvt_pk_bf16_f32 v8, v19, v21
	v_cvt_pk_bf16_f32 v9, v23, v25
	global_store_dwordx4 v[4:5], v[6:9], off sc1
	s_waitcnt lgkmcnt(0)

; #define GAS __attribute__((address_space(1)))
; #define LAS __attribute__((address_space(3)))
; #define LDS_WAIT() asm volatile("s_waitcnt lgkmcnt(0)" ::: "memory")
; __device__ __forceinline__ unsigned pk2(float lo, float hi) { unsigned r; asm("v_cvt_pk_bf16_f32 %0, %1, %2" : "=v"(r) : "v"(lo), "v"(hi)); return r; }
; __device__ __forceinline__ void transpose_item(const float* W, int K, int N, bf16* WT, int drow0, int kb, int n0, LAS float* scr, int lane) {
;     const int k0 = 64 * kb; const int c4 = 4 * (lane & 7); const bool ok = (n0 + c4) < N;
;     f32x4 v[8];
; #pragma unroll
;     for (int i = 0; i < 8; ++i) { const int kk = 8 * i + (lane >> 3); v[i] = ok ? *(const f32x4*)(W + (size_t)(k0 + kk) * N + n0 + c4) : (f32x4){0.f, 0.f, 0.f, 0.f}; }
; #pragma unroll
;     for (int i = 0; i < 8; ++i) { const int kk = 8 * i + (lane >> 3); LAS float* d = scr + kk * 33 + c4; d[0] = v[i][0]; d[1] = v[i][1]; d[2] = v[i][2]; d[3] = v[i][3]; }
;     LDS_WAIT(); asm volatile("" ::: "memory");
;     const int c = lane & 7;
; #pragma unroll
;     for (int j = 0; j < 4; ++j) { const int n = (lane >> 3) + 8 * j; const LAS float* s = scr + (8 * c) * 33 + n;
;         v4u o; o.x = pk2(s[0 * 33], s[1 * 33]); o.y = pk2(s[2 * 33], s[3 * 33]); o.z = pk2(s[4 * 33], s[5 * 33]); o.w = pk2(s[6 * 33], s[7 * 33]);
;         *(GAS v4u*)(WT + (size_t)(drow0 + n) * K + k0 + 8 * c) = o; }
;     LDS_WAIT(); asm volatile("" ::: "memory");
; }
; __device__ __forceinline__ void convert_item(const In& I, unsigned char* ws, int it, LAS float* scr, int lane) {
;     ...
;     if (r < 2 * I_SQ) { const int j = r / I_SQ; r -= j * I_SQ; const int kb = r / 32, nb = r % 32;
;         transpose_item(I.fox_w_out + (size_t)j * D * D, D, D, Wfout + (size_t)j * D * D, 32 * nb, kb, 32 * nb, scr, lane); return; }
.LBB0_365:
	s_andn2_b64 vcc, exec, s[2:3]
	s_cbranch_vccnz .LBB0_367
	s_add_i32 s2, s41, 0x800
	s_lshr_b32 s68, s2, 9
	v_readlane_b32 s48, v253, 16
	s_lshl_b64 s[2:3], s[68:69], 22
	v_readlane_b32 s60, v253, 28
	v_readlane_b32 s61, v253, 29
	s_add_u32 s8, s60, s2
	s_addc_u32 s9, s61, s3
	s_lshl_b64 s[6:7], s[68:69], 21
	s_add_u32 s3, s26, s6
	s_addc_u32 s6, s27, s7
	s_and_b32 s2, s43, 0x3e0
	s_add_i32 s7, s44, 0x11600
	s_and_b32 s7, s7, 0x3c0
	s_lshl_b32 s10, s2, 2
	s_add_u32 s8, s8, s10
	v_or_b32_e32 v6, s7, v39
	s_addc_u32 s9, s9, 0
	v_lshlrev_b32_e32 v2, 2, v36
	v_lshl_add_u64 v[4:5], s[8:9], 0, v[2:3]
	v_lshlrev_b32_e32 v2, 12, v6
	v_lshl_add_u64 v[32:33], v[4:5], 0, v[2:3]
	v_add_co_u32_e32 v8, vcc, s81, v32
	global_load_dwordx4 v[4:7], v[32:33], off
	s_nop 0
	v_addc_co_u32_e32 v9, vcc, 0, v33, vcc
	v_add_co_u32_e32 v12, vcc, s79, v32
	global_load_dwordx4 v[8:11], v[8:9], off
	s_nop 0
	v_addc_co_u32_e32 v13, vcc, 0, v33, vcc
	v_add_co_u32_e32 v16, vcc, s80, v32
	global_load_dwordx4 v[12:15], v[12:13], off
	s_nop 0
	v_addc_co_u32_e32 v17, vcc, 0, v33, vcc
	v_add_co_u32_e32 v20, vcc, s85, v32
	global_load_dwordx4 v[16:19], v[16:17], off
	s_nop 0
	v_addc_co_u32_e32 v21, vcc, 0, v33, vcc
	global_load_dwordx4 v[20:23], v[20:21], off
	v_add_co_u32_e32 v24, vcc, s86, v32
	v_add_u32_e32 v2, v44, v47
	s_nop 0
	v_addc_co_u32_e32 v25, vcc, 0, v33, vcc
	global_load_dwordx4 v[24:27], v[24:25], off
	v_add_co_u32_e32 v28, vcc, s87, v32
	s_lshl_b32 s7, s7, 1
	s_nop 0
	v_addc_co_u32_e32 v29, vcc, 0, v33, vcc
	global_load_dwordx4 v[28:31], v[28:29], off
	v_add_co_u32_e32 v32, vcc, s89, v32
	s_add_u32 s8, s3, s7
	s_nop 0
	v_addc_co_u32_e32 v33, vcc, 0, v33, vcc
	global_load_dwordx4 v[32:35], v[32:33], off
	s_addc_u32 s9, s6, 0
	v_readlane_b32 s49, v253, 17
	v_readlane_b32 s50, v253, 18
	v_readlane_b32 s51, v253, 19
	v_readlane_b32 s52, v253, 20
	v_readlane_b32 s53, v253, 21
	v_readlane_b32 s54, v253, 22
	v_readlane_b32 s55, v253, 23
	v_readlane_b32 s56, v253, 24
	v_readlane_b32 s57, v253, 25
	v_readlane_b32 s58, v253, 26
	v_readlane_b32 s59, v253, 27
	v_readlane_b32 s62, v253, 30
	v_readlane_b32 s63, v253, 31
	s_waitcnt vmcnt(0)
	ds_write2_b32 v45, v4, v5 offset1:1
	ds_write2_b32 v45, v6, v7 offset0:2 offset1:3
	v_add_u32_e32 v4, 0x420, v2
	ds_write2_b32 v2, v8, v9 offset1:1
	ds_write2_b32 v2, v10, v11 offset0:2 offset1:3
	ds_write2_b32 v4, v12, v13 offset1:1
	v_add_u32_e32 v4, 0x428, v2
	ds_write2_b32 v4, v14, v15 offset1:1
	v_add_u32_e32 v4, 0x840, v2
	v_add_u32_e32 v2, 0x848, v2
	ds_write2_b32 v2, v18, v19 offset1:1
	v_add_u32_e32 v2, 0x1080, v45
	ds_write2_b32 v4, v16, v17 offset1:1
	ds_write2_b32 v2, v20, v21 offset1:1
	v_add_u32_e32 v2, 0x1088, v45
	ds_write2_b32 v2, v22, v23 offset1:1
	v_add_u32_e32 v2, 0x14a0, v45
	ds_write2_b32 v2, v24, v25 offset1:1
	v_add_u32_e32 v2, 0x14a8, v45
	ds_write2_b32 v2, v26, v27 offset1:1
	v_add_u32_e32 v2, 0x18c0, v45
	ds_write2_b32 v2, v28, v29 offset1:1
	v_add_u32_e32 v2, 0x18c8, v45
	ds_write2_b32 v2, v30, v31 offset1:1
	v_add_u32_e32 v2, 0x1ce0, v45
	ds_write2_b32 v2, v32, v33 offset1:1
	v_add_u32_e32 v2, 0x1ce8, v45
	ds_write2_b32 v2, v34, v35 offset1:1
	s_waitcnt lgkmcnt(0)
	ds_read2_b32 v[10:11], v50 offset0:33 offset1:41
	ds_read2_b32 v[12:13], v50 offset1:8
	v_lshlrev_b32_e32 v2, 1, v38
	ds_read2_b32 v[14:15], v50 offset0:66 offset1:74
	ds_read2_b32 v[16:17], v50 offset0:99 offset1:107
	ds_read2_b32 v[18:19], v50 offset0:132 offset1:140
	ds_read2_b32 v[20:21], v50 offset0:165 offset1:173
	ds_read2_b32 v[22:23], v50 offset0:198 offset1:206
	ds_read2_b32 v[24:25], v50 offset0:231 offset1:239
	v_lshl_add_u64 v[8:9], s[8:9], 0, v[2:3]
	v_or_b32_e32 v2, s2, v39
	v_lshlrev_b32_e32 v2, 11, v2
	v_lshl_add_u64 v[26:27], v[8:9], 0, v[2:3]
	v_or_b32_e32 v2, s2, v46
	s_waitcnt lgkmcnt(0)
	v_cvt_pk_bf16_f32 v4, v12, v10
	v_lshlrev_b32_e32 v2, 11, v2
	v_cvt_pk_bf16_f32 v5, v14, v16
	v_cvt_pk_bf16_f32 v6, v18, v20
	v_cvt_pk_bf16_f32 v7, v22, v24
	global_store_dwordx4 v[26:27], v[4:7], off sc1
	s_nop 1
	v_cvt_pk_bf16_f32 v4, v13, v11
	v_lshl_add_u64 v[10:11], v[8:9], 0, v[2:3]
	v_cvt_pk_bf16_f32 v5, v15, v17
	v_cvt_pk_bf16_f32 v6, v19, v21
	v_cvt_pk_bf16_f32 v7, v23, v25
	global_store_dwordx4 v[10:11], v[4:7], off sc1
	ds_read2_b32 v[10:11], v50 offset0:16 offset1:24
	ds_read2_b32 v[12:13], v50 offset0:49 offset1:57
	ds_read2_b32 v[14:15], v50 offset0:82 offset1:90
	ds_read2_b32 v[16:17], v50 offset0:115 offset1:123
	ds_read2_b32 v[18:19], v50 offset0:148 offset1:156
	ds_read2_b32 v[20:21], v50 offset0:181 offset1:189
	ds_read2_b32 v[22:23], v50 offset0:214 offset1:222
	ds_read2_b32 v[24:25], v50 offset0:247 offset1:255
	v_or_b32_e32 v2, s2, v48
	v_lshlrev_b32_e32 v2, 11, v2
	v_lshl_add_u64 v[26:27], v[8:9], 0, v[2:3]
	v_or_b32_e32 v2, s2, v49
	v_lshlrev_b32_e32 v2, 11, v2
	s_waitcnt lgkmcnt(6)
	v_cvt_pk_bf16_f32 v4, v10, v12
	s_waitcnt lgkmcnt(4)
	v_cvt_pk_bf16_f32 v5, v14, v16
	s_waitcnt lgkmcnt(2)
	v_cvt_pk_bf16_f32 v6, v18, v20
	s_waitcnt lgkmcnt(0)
	v_cvt_pk_bf16_f32 v7, v22, v24
	v_lshl_add_u64 v[8:9], v[8:9], 0, v[2:3]
	global_store_dwordx4 v[26:27], v[4:7], off sc1
	s_nop 1
	v_cvt_pk_bf16_f32 v4, v11, v13
	v_cvt_pk_bf16_f32 v5, v15, v17
	v_cvt_pk_bf16_f32 v6, v19, v21
	v_cvt_pk_bf16_f32 v7, v23, v25
	global_store_dwordx4 v[8:9], v[4:7], off sc1
	s_waitcnt lgkmcnt(0)

; #define GAS __attribute__((address_space(1)))
; #define LAS __attribute__((address_space(3)))
; #define LDS_WAIT() asm volatile("s_waitcnt lgkmcnt(0)" ::: "memory")
; __device__ __forceinline__ unsigned pk2(float lo, float hi) { unsigned r; asm("v_cvt_pk_bf16_f32 %0, %1, %2" : "=v"(r) : "v"(lo), "v"(hi)); return r; }
; __device__ __forceinline__ void transpose_item(const float* W, int K, int N, bf16* WT, int drow0, int kb, int n0, LAS float* scr, int lane) {
;     const int k0 = 64 * kb; const int c4 = 4 * (lane & 7); const bool ok = (n0 + c4) < N;
;     f32x4 v[8];
; #pragma unroll
;     for (int i = 0; i < 8; ++i) { const int kk = 8 * i + (lane >> 3); v[i] = ok ? *(const f32x4*)(W + (size_t)(k0 + kk) * N + n0 + c4) : (f32x4){0.f, 0.f, 0.f, 0.f}; }
; #pragma unroll
;     for (int i = 0; i < 8; ++i) { const int kk = 8 * i + (lane >> 3); LAS float* d = scr + kk * 33 + c4; d[0] = v[i][0]; d[1] = v[i][1]; d[2] = v[i][2]; d[3] = v[i][3]; }
;     LDS_WAIT(); asm volatile("" ::: "memory");
;     const int c = lane & 7;
; #pragma unroll
;     for (int j = 0; j < 4; ++j) { const int n = (lane >> 3) + 8 * j; const LAS float* s = scr + (8 * c) * 33 + n;
;         v4u o; o.x = pk2(s[0 * 33], s[1 * 33]); o.y = pk2(s[2 * 33], s[3 * 33]); o.z = pk2(s[4 * 33], s[5 * 33]); o.w = pk2(s[6 * 33], s[7 * 33]);
;         *(GAS v4u*)(WT + (size_t)(drow0 + n) * K + k0 + 8 * c) = o; }
;     LDS_WAIT(); asm volatile("" ::: "memory");
; }
; __device__ __forceinline__ void convert_item(const In& I, unsigned char* ws, int it, LAS float* scr, int lane) {
;     ...
;     if (r < 2 * I_FIN) { const int j = r / I_FIN; r -= j * I_FIN; const int kb = r / 104, nb = r % 104;
;         transpose_item(I.fox_w_in + (size_t)j * D * FOX_IN, D, FOX_IN, Wfin + (size_t)j * FOX_IN_PAD * D, 32 * nb, kb, 32 * nb, scr, lane); return; }
.LBB0_385:
	s_or_b64 exec, exec, s[12:13]
	v_add_u32_e32 v2, v44, v47
	s_waitcnt vmcnt(0)
	ds_write2_b32 v45, v4, v5 offset1:1
	ds_write2_b32 v45, v6, v7 offset0:2 offset1:3
	v_add_u32_e32 v4, 0x420, v2
	ds_write2_b32 v2, v8, v9 offset1:1
	ds_write2_b32 v2, v10, v11 offset0:2 offset1:3
	ds_write2_b32 v4, v16, v17 offset1:1
	v_add_u32_e32 v4, 0x428, v2
	ds_write2_b32 v4, v18, v19 offset1:1
	v_add_u32_e32 v4, 0x840, v2
	v_add_u32_e32 v2, 0x848, v2
	ds_write2_b32 v2, v14, v15 offset1:1
	v_add_u32_e32 v2, 0x1080, v45
	ds_write2_b32 v2, v24, v25 offset1:1
	v_add_u32_e32 v2, 0x1088, v45
	ds_write2_b32 v2, v26, v27 offset1:1
	v_add_u32_e32 v2, 0x14a0, v45
	ds_write2_b32 v2, v20, v21 offset1:1
	v_add_u32_e32 v2, 0x14a8, v45
	ds_write2_b32 v2, v22, v23 offset1:1
	v_add_u32_e32 v2, 0x18c0, v45
	ds_write2_b32 v2, v32, v33 offset1:1
	v_add_u32_e32 v2, 0x18c8, v45
	ds_write2_b32 v2, v34, v35 offset1:1
	v_add_u32_e32 v2, 0x1ce0, v45
	s_and_b64 s[2:3], s[10:11], exec
	ds_write2_b32 v2, v28, v29 offset1:1
	v_add_u32_e32 v2, 0x1ce8, v45
	s_cselect_b32 s2, 0x680000, 0
	ds_write2_b32 v4, v12, v13 offset1:1
	ds_write2_b32 v2, v30, v31 offset1:1
	s_add_u32 s7, s24, s2
	s_waitcnt lgkmcnt(0)
	s_addc_u32 s10, s25, 0
	s_ashr_i32 s9, s8, 31
	s_lshl_b64 s[2:3], s[8:9], 1
	ds_read2_b32 v[8:9], v50 offset0:33 offset1:41
	ds_read2_b32 v[10:11], v50 offset1:8
	ds_read2_b32 v[12:13], v50 offset0:66 offset1:74
	ds_read2_b32 v[14:15], v50 offset0:99 offset1:107
	ds_read2_b32 v[16:17], v50 offset0:132 offset1:140
	ds_read2_b32 v[18:19], v50 offset0:165 offset1:173
	ds_read2_b32 v[20:21], v50 offset0:198 offset1:206
	ds_read2_b32 v[22:23], v50 offset0:231 offset1:239
	s_add_u32 s2, s7, s2
	v_or_b32_e32 v26, s6, v39
	s_addc_u32 s3, s10, s3
	v_lshlrev_b32_e32 v2, 1, v38
	v_ashrrev_i32_e32 v27, 31, v26
	v_lshl_add_u64 v[24:25], s[2:3], 0, v[2:3]
	v_lshlrev_b64 v[26:27], 11, v[26:27]
	s_waitcnt lgkmcnt(0)
	v_cvt_pk_bf16_f32 v4, v10, v8
	v_lshl_add_u64 v[26:27], v[24:25], 0, v[26:27]
	v_or_b32_e32 v8, s6, v46
	v_cvt_pk_bf16_f32 v5, v12, v14
	v_cvt_pk_bf16_f32 v6, v16, v18
	v_cvt_pk_bf16_f32 v7, v20, v22
	global_store_dwordx4 v[26:27], v[4:7], off sc1
	s_nop 1
	v_cvt_pk_bf16_f32 v4, v11, v9
	v_ashrrev_i32_e32 v9, 31, v8
	v_lshlrev_b64 v[8:9], 11, v[8:9]
	v_cvt_pk_bf16_f32 v5, v13, v15
	v_cvt_pk_bf16_f32 v6, v17, v19
	v_cvt_pk_bf16_f32 v7, v21, v23
	v_lshl_add_u64 v[8:9], v[24:25], 0, v[8:9]
	ds_read2_b32 v[10:11], v50 offset0:16 offset1:24
	ds_read2_b32 v[12:13], v50 offset0:49 offset1:57
	ds_read2_b32 v[14:15], v50 offset0:82 offset1:90
	ds_read2_b32 v[16:17], v50 offset0:115 offset1:123
	ds_read2_b32 v[18:19], v50 offset0:148 offset1:156
	ds_read2_b32 v[20:21], v50 offset0:181 offset1:189
	ds_read2_b32 v[22:23], v50 offset0:214 offset1:222
	ds_read2_b32 v[26:27], v50 offset0:247 offset1:255
	global_store_dwordx4 v[8:9], v[4:7], off sc1
	v_or_b32_e32 v8, s6, v48
	v_ashrrev_i32_e32 v9, 31, v8
	v_lshlrev_b64 v[8:9], 11, v[8:9]
	v_lshl_add_u64 v[8:9], v[24:25], 0, v[8:9]
	s_waitcnt lgkmcnt(6)
	v_cvt_pk_bf16_f32 v4, v10, v12
	s_waitcnt lgkmcnt(4)
	v_cvt_pk_bf16_f32 v5, v14, v16
	s_waitcnt lgkmcnt(2)
	v_cvt_pk_bf16_f32 v6, v18, v20
	s_waitcnt lgkmcnt(0)
	v_cvt_pk_bf16_f32 v7, v22, v26
	global_store_dwordx4 v[8:9], v[4:7], off sc1
	v_or_b32_e32 v8, s6, v49
	v_ashrrev_i32_e32 v9, 31, v8
	v_lshlrev_b64 v[8:9], 11, v[8:9]
	v_lshl_add_u64 v[8:9], v[24:25], 0, v[8:9]
	v_cvt_pk_bf16_f32 v4, v11, v13
	v_cvt_pk_bf16_f32 v5, v15, v17
	v_cvt_pk_bf16_f32 v6, v19, v21
	v_cvt_pk_bf16_f32 v7, v23, v27
	global_store_dwordx4 v[8:9], v[4:7], off sc1
	s_waitcnt lgkmcnt(0)

; #define GAS __attribute__((address_space(1)))
; #define LAS __attribute__((address_space(3)))
; #define LDS_WAIT() asm volatile("s_waitcnt lgkmcnt(0)" ::: "memory")
; __device__ __forceinline__ unsigned pk2(float lo, float hi) { unsigned r; asm("v_cvt_pk_bf16_f32 %0, %1, %2" : "=v"(r) : "v"(lo), "v"(hi)); return r; }
; __device__ __forceinline__ void transpose_item(const float* W, int K, int N, bf16* WT, int drow0, int kb, int n0, LAS float* scr, int lane) {
;     const int k0 = 64 * kb; const int c4 = 4 * (lane & 7); const bool ok = (n0 + c4) < N;
;     f32x4 v[8];
; #pragma unroll
;     for (int i = 0; i < 8; ++i) { const int kk = 8 * i + (lane >> 3); v[i] = ok ? *(const f32x4*)(W + (size_t)(k0 + kk) * N + n0 + c4) : (f32x4){0.f, 0.f, 0.f, 0.f}; }
; #pragma unroll
;     for (int i = 0; i < 8; ++i) { const int kk = 8 * i + (lane >> 3); LAS float* d = scr + kk * 33 + c4; d[0] = v[i][0]; d[1] = v[i][1]; d[2] = v[i][2]; d[3] = v[i][3]; }
;     LDS_WAIT(); asm volatile("" ::: "memory");
;     const int c = lane & 7;
; #pragma unroll
;     for (int j = 0; j < 4; ++j) { const int n = (lane >> 3) + 8 * j; const LAS float* s = scr + (8 * c) * 33 + n;
;         v4u o; o.x = pk2(s[0 * 33], s[1 * 33]); o.y = pk2(s[2 * 33], s[3 * 33]); o.z = pk2(s[4 * 33], s[5 * 33]); o.w = pk2(s[6 * 33], s[7 * 33]);
;         *(GAS v4u*)(WT + (size_t)(drow0 + n) * K + k0 + 8 * c) = o; }
;     LDS_WAIT(); asm volatile("" ::: "memory");
; }
; __device__ __forceinline__ void convert_item(const In& I, unsigned char* ws, int it, LAS float* scr, int lane) {
;     ...
;     if (r < 2 * I_SQ) { const int j = r / I_SQ; r -= j * I_SQ; const int kb = r / 32, nb = r % 32;
;         transpose_item(I.nsa_w_out + (size_t)j * D * D, D, D, Wnout + (size_t)j * D * D, 32 * nb, kb, 32 * nb, scr, lane); return; }
.LBB0_387:
	s_andn2_b64 vcc, exec, s[2:3]
	s_cbranch_vccnz .LBB0_389
	s_add_i32 s2, s41, 0x1900
	s_lshr_b32 s68, s2, 9
	v_readlane_b32 s48, v253, 16
	s_lshl_b64 s[2:3], s[68:69], 22
	v_readlane_b32 s54, v253, 22
	v_readlane_b32 s55, v253, 23
	s_add_u32 s8, s54, s2
	s_addc_u32 s9, s55, s3
	s_lshl_b64 s[6:7], s[68:69], 21
	s_add_u32 s3, s22, s6
	s_addc_u32 s6, s23, s7
	s_and_b32 s2, s43, 0x3e0
	s_add_i32 s7, s44, 0xfffff800
	s_and_b32 s7, s7, 0x3c0
	s_lshl_b32 s10, s2, 2
	s_add_u32 s8, s8, s10
	v_or_b32_e32 v6, s7, v39
	s_addc_u32 s9, s9, 0
	v_lshlrev_b32_e32 v2, 2, v36
	v_lshl_add_u64 v[4:5], s[8:9], 0, v[2:3]
	v_lshlrev_b32_e32 v2, 12, v6
	v_lshl_add_u64 v[32:33], v[4:5], 0, v[2:3]
	v_add_co_u32_e32 v8, vcc, s81, v32
	global_load_dwordx4 v[4:7], v[32:33], off
	s_nop 0
	v_addc_co_u32_e32 v9, vcc, 0, v33, vcc
	v_add_co_u32_e32 v12, vcc, s79, v32
	global_load_dwordx4 v[8:11], v[8:9], off
	s_nop 0
	v_addc_co_u32_e32 v13, vcc, 0, v33, vcc
	v_add_co_u32_e32 v16, vcc, s80, v32
	global_load_dwordx4 v[12:15], v[12:13], off
	s_nop 0
	v_addc_co_u32_e32 v17, vcc, 0, v33, vcc
	v_add_co_u32_e32 v20, vcc, s85, v32
	global_load_dwordx4 v[16:19], v[16:17], off
	s_nop 0
	v_addc_co_u32_e32 v21, vcc, 0, v33, vcc
	global_load_dwordx4 v[20:23], v[20:21], off
	v_add_co_u32_e32 v24, vcc, s86, v32
	v_add_u32_e32 v2, v44, v47
	s_nop 0
	v_addc_co_u32_e32 v25, vcc, 0, v33, vcc
	global_load_dwordx4 v[24:27], v[24:25], off
	v_add_co_u32_e32 v28, vcc, s87, v32
	s_lshl_b32 s7, s7, 1
	s_nop 0
	v_addc_co_u32_e32 v29, vcc, 0, v33, vcc
	global_load_dwordx4 v[28:31], v[28:29], off
	v_add_co_u32_e32 v32, vcc, s89, v32
	s_add_u32 s8, s3, s7
	s_nop 0
	v_addc_co_u32_e32 v33, vcc, 0, v33, vcc
	global_load_dwordx4 v[32:35], v[32:33], off
	s_addc_u32 s9, s6, 0
	v_readlane_b32 s49, v253, 17
	v_readlane_b32 s50, v253, 18
	v_readlane_b32 s51, v253, 19
	v_readlane_b32 s52, v253, 20
	v_readlane_b32 s53, v253, 21
	v_readlane_b32 s56, v253, 24
	v_readlane_b32 s57, v253, 25
	v_readlane_b32 s58, v253, 26
	v_readlane_b32 s59, v253, 27
	v_readlane_b32 s60, v253, 28
	v_readlane_b32 s61, v253, 29
	v_readlane_b32 s62, v253, 30
	v_readlane_b32 s63, v253, 31
	s_waitcnt vmcnt(0)
	ds_write2_b32 v45, v4, v5 offset1:1
	ds_write2_b32 v45, v6, v7 offset0:2 offset1:3
	v_add_u32_e32 v4, 0x420, v2
	ds_write2_b32 v2, v8, v9 offset1:1
	ds_write2_b32 v2, v10, v11 offset0:2 offset1:3
	ds_write2_b32 v4, v12, v13 offset1:1
	v_add_u32_e32 v4, 0x428, v2
	ds_write2_b32 v4, v14, v15 offset1:1
	v_add_u32_e32 v4, 0x840, v2
	v_add_u32_e32 v2, 0x848, v2
	ds_write2_b32 v2, v18, v19 offset1:1
	v_add_u32_e32 v2, 0x1080, v45
	ds_write2_b32 v4, v16, v17 offset1:1
	ds_write2_b32 v2, v20, v21 offset1:1
	v_add_u32_e32 v2, 0x1088, v45
	ds_write2_b32 v2, v22, v23 offset1:1
	v_add_u32_e32 v2, 0x14a0, v45
	ds_write2_b32 v2, v24, v25 offset1:1
	v_add_u32_e32 v2, 0x14a8, v45
	ds_write2_b32 v2, v26, v27 offset1:1
	v_add_u32_e32 v2, 0x18c0, v45
	ds_write2_b32 v2, v28, v29 offset1:1
	v_add_u32_e32 v2, 0x18c8, v45
	ds_write2_b32 v2, v30, v31 offset1:1
	v_add_u32_e32 v2, 0x1ce0, v45
	ds_write2_b32 v2, v32, v33 offset1:1
	v_add_u32_e32 v2, 0x1ce8, v45
	ds_write2_b32 v2, v34, v35 offset1:1
	s_waitcnt lgkmcnt(0)
	ds_read2_b32 v[10:11], v50 offset0:33 offset1:41
	ds_read2_b32 v[12:13], v50 offset1:8
	v_lshlrev_b32_e32 v2, 1, v38
	ds_read2_b32 v[14:15], v50 offset0:66 offset1:74
	ds_read2_b32 v[16:17], v50 offset0:99 offset1:107
	ds_read2_b32 v[18:19], v50 offset0:132 offset1:140
	ds_read2_b32 v[20:21], v50 offset0:165 offset1:173
	ds_read2_b32 v[22:23], v50 offset0:198 offset1:206
	ds_read2_b32 v[24:25], v50 offset0:231 offset1:239
	v_lshl_add_u64 v[8:9], s[8:9], 0, v[2:3]
	v_or_b32_e32 v2, s2, v39
	v_lshlrev_b32_e32 v2, 11, v2
	v_lshl_add_u64 v[26:27], v[8:9], 0, v[2:3]
	v_or_b32_e32 v2, s2, v46
	s_waitcnt lgkmcnt(0)
	v_cvt_pk_bf16_f32 v4, v12, v10
	v_lshlrev_b32_e32 v2, 11, v2
	v_cvt_pk_bf16_f32 v5, v14, v16
	v_cvt_pk_bf16_f32 v6, v18, v20
	v_cvt_pk_bf16_f32 v7, v22, v24
	global_store_dwordx4 v[26:27], v[4:7], off sc1
	s_nop 1
	v_cvt_pk_bf16_f32 v4, v13, v11
	v_lshl_add_u64 v[10:11], v[8:9], 0, v[2:3]
	v_cvt_pk_bf16_f32 v5, v15, v17
	v_cvt_pk_bf16_f32 v6, v19, v21
	v_cvt_pk_bf16_f32 v7, v23, v25
	global_store_dwordx4 v[10:11], v[4:7], off sc1
	ds_read2_b32 v[10:11], v50 offset0:16 offset1:24
	ds_read2_b32 v[12:13], v50 offset0:49 offset1:57
	ds_read2_b32 v[14:15], v50 offset0:82 offset1:90
	ds_read2_b32 v[16:17], v50 offset0:115 offset1:123
	ds_read2_b32 v[18:19], v50 offset0:148 offset1:156
	ds_read2_b32 v[20:21], v50 offset0:181 offset1:189
	ds_read2_b32 v[22:23], v50 offset0:214 offset1:222
	ds_read2_b32 v[24:25], v50 offset0:247 offset1:255
	v_or_b32_e32 v2, s2, v48
	v_lshlrev_b32_e32 v2, 11, v2
	v_lshl_add_u64 v[26:27], v[8:9], 0, v[2:3]
	v_or_b32_e32 v2, s2, v49
	v_lshlrev_b32_e32 v2, 11, v2
	s_waitcnt lgkmcnt(6)
	v_cvt_pk_bf16_f32 v4, v10, v12
	s_waitcnt lgkmcnt(4)
	v_cvt_pk_bf16_f32 v5, v14, v16
	s_waitcnt lgkmcnt(2)
	v_cvt_pk_bf16_f32 v6, v18, v20
	s_waitcnt lgkmcnt(0)
	v_cvt_pk_bf16_f32 v7, v22, v24
	v_lshl_add_u64 v[8:9], v[8:9], 0, v[2:3]
	global_store_dwordx4 v[26:27], v[4:7], off sc1
	s_nop 1
	v_cvt_pk_bf16_f32 v4, v11, v13
	v_cvt_pk_bf16_f32 v5, v15, v17
	v_cvt_pk_bf16_f32 v6, v19, v21
	v_cvt_pk_bf16_f32 v7, v23, v25
	global_store_dwordx4 v[8:9], v[4:7], off sc1
	s_waitcnt lgkmcnt(0)

; #define GAS __attribute__((address_space(1)))
; #define LAS __attribute__((address_space(3)))
; #define LDS_WAIT() asm volatile("s_waitcnt lgkmcnt(0)" ::: "memory")
; __device__ __forceinline__ unsigned pk2(float lo, float hi) { unsigned r; asm("v_cvt_pk_bf16_f32 %0, %1, %2" : "=v"(r) : "v"(lo), "v"(hi)); return r; }
; __device__ __forceinline__ void transpose_item(const float* W, int K, int N, bf16* WT, int drow0, int kb, int n0, LAS float* scr, int lane) {
;     const int k0 = 64 * kb; const int c4 = 4 * (lane & 7); const bool ok = (n0 + c4) < N;
;     f32x4 v[8];
; #pragma unroll
;     for (int i = 0; i < 8; ++i) { const int kk = 8 * i + (lane >> 3); v[i] = ok ? *(const f32x4*)(W + (size_t)(k0 + kk) * N + n0 + c4) : (f32x4){0.f, 0.f, 0.f, 0.f}; }
; #pragma unroll
;     for (int i = 0; i < 8; ++i) { const int kk = 8 * i + (lane >> 3); LAS float* d = scr + kk * 33 + c4; d[0] = v[i][0]; d[1] = v[i][1]; d[2] = v[i][2]; d[3] = v[i][3]; }
;     LDS_WAIT(); asm volatile("" ::: "memory");
;     const int c = lane & 7;
; #pragma unroll
;     for (int j = 0; j < 4; ++j) { const int n = (lane >> 3) + 8 * j; const LAS float* s = scr + (8 * c) * 33 + n;
;         v4u o; o.x = pk2(s[0 * 33], s[1 * 33]); o.y = pk2(s[2 * 33], s[3 * 33]); o.z = pk2(s[4 * 33], s[5 * 33]); o.w = pk2(s[6 * 33], s[7 * 33]);
;         *(GAS v4u*)(WT + (size_t)(drow0 + n) * K + k0 + 8 * c) = o; }
;     LDS_WAIT(); asm volatile("" ::: "memory");
; }
; __device__ __forceinline__ void convert_item(const In& I, unsigned char* ws, int it, LAS float* scr, int lane) {
;     ...
;     if (r < 2 * I_NIN) { const int j = r / I_NIN; r -= j * I_NIN; const int kb = r / 88, nb = r % 88;
;         transpose_item(I.nsa_w_in + (size_t)j * D * NSA_IN, D, NSA_IN, Wnin + (size_t)j * NSA_IN_PAD * D, 32 * nb, kb, 32 * nb, scr, lane); return; }
.LBB0_407:
	s_or_b64 exec, exec, s[12:13]
	v_add_u32_e32 v2, v44, v47
	s_waitcnt vmcnt(0)
	ds_write2_b32 v45, v4, v5 offset1:1
	ds_write2_b32 v45, v6, v7 offset0:2 offset1:3
	v_add_u32_e32 v4, 0x420, v2
	ds_write2_b32 v2, v8, v9 offset1:1
	ds_write2_b32 v2, v10, v11 offset0:2 offset1:3
	ds_write2_b32 v4, v16, v17 offset1:1
	v_add_u32_e32 v4, 0x428, v2
	ds_write2_b32 v4, v18, v19 offset1:1
	v_add_u32_e32 v4, 0x840, v2
	v_add_u32_e32 v2, 0x848, v2
	ds_write2_b32 v2, v14, v15 offset1:1
	v_add_u32_e32 v2, 0x1080, v45
	ds_write2_b32 v2, v24, v25 offset1:1
	v_add_u32_e32 v2, 0x1088, v45
	ds_write2_b32 v2, v26, v27 offset1:1
	v_add_u32_e32 v2, 0x14a0, v45
	ds_write2_b32 v2, v20, v21 offset1:1
	v_add_u32_e32 v2, 0x14a8, v45
	ds_write2_b32 v2, v22, v23 offset1:1
	v_add_u32_e32 v2, 0x18c0, v45
	ds_write2_b32 v2, v32, v33 offset1:1
	v_add_u32_e32 v2, 0x18c8, v45
	ds_write2_b32 v2, v34, v35 offset1:1
	v_add_u32_e32 v2, 0x1ce0, v45
	s_and_b64 s[2:3], s[10:11], exec
	ds_write2_b32 v2, v28, v29 offset1:1
	v_add_u32_e32 v2, 0x1ce8, v45
	s_cselect_b32 s2, 0x580000, 0
	ds_write2_b32 v4, v12, v13 offset1:1
	ds_write2_b32 v2, v30, v31 offset1:1
	s_add_u32 s7, s20, s2
	s_waitcnt lgkmcnt(0)
	s_addc_u32 s10, s21, 0
	s_ashr_i32 s9, s8, 31
	s_lshl_b64 s[2:3], s[8:9], 1
	ds_read2_b32 v[8:9], v50 offset0:33 offset1:41
	ds_read2_b32 v[10:11], v50 offset1:8
	ds_read2_b32 v[12:13], v50 offset0:66 offset1:74
	ds_read2_b32 v[14:15], v50 offset0:99 offset1:107
	ds_read2_b32 v[16:17], v50 offset0:132 offset1:140
	ds_read2_b32 v[18:19], v50 offset0:165 offset1:173
	ds_read2_b32 v[20:21], v50 offset0:198 offset1:206
	ds_read2_b32 v[22:23], v50 offset0:231 offset1:239
	s_add_u32 s2, s7, s2
	v_or_b32_e32 v26, s6, v39
	s_addc_u32 s3, s10, s3
	v_lshlrev_b32_e32 v2, 1, v38
	v_ashrrev_i32_e32 v27, 31, v26
	v_lshl_add_u64 v[24:25], s[2:3], 0, v[2:3]
	v_lshlrev_b64 v[26:27], 11, v[26:27]
	s_waitcnt lgkmcnt(0)
	v_cvt_pk_bf16_f32 v4, v10, v8
	v_lshl_add_u64 v[26:27], v[24:25], 0, v[26:27]
	v_or_b32_e32 v8, s6, v46
	v_cvt_pk_bf16_f32 v5, v12, v14
	v_cvt_pk_bf16_f32 v6, v16, v18
	v_cvt_pk_bf16_f32 v7, v20, v22
	global_store_dwordx4 v[26:27], v[4:7], off sc1
	s_nop 1
	v_cvt_pk_bf16_f32 v4, v11, v9
	v_ashrrev_i32_e32 v9, 31, v8
	v_lshlrev_b64 v[8:9], 11, v[8:9]
	v_cvt_pk_bf16_f32 v5, v13, v15
	v_cvt_pk_bf16_f32 v6, v17, v19
	v_cvt_pk_bf16_f32 v7, v21, v23
	v_lshl_add_u64 v[8:9], v[24:25], 0, v[8:9]
	ds_read2_b32 v[10:11], v50 offset0:16 offset1:24
	ds_read2_b32 v[12:13], v50 offset0:49 offset1:57
	ds_read2_b32 v[14:15], v50 offset0:82 offset1:90
	ds_read2_b32 v[16:17], v50 offset0:115 offset1:123
	ds_read2_b32 v[18:19], v50 offset0:148 offset1:156
	ds_read2_b32 v[20:21], v50 offset0:181 offset1:189
	ds_read2_b32 v[22:23], v50 offset0:214 offset1:222
	ds_read2_b32 v[26:27], v50 offset0:247 offset1:255
	global_store_dwordx4 v[8:9], v[4:7], off sc1
	v_or_b32_e32 v8, s6, v48
	v_ashrrev_i32_e32 v9, 31, v8
	v_lshlrev_b64 v[8:9], 11, v[8:9]
	v_lshl_add_u64 v[8:9], v[24:25], 0, v[8:9]
	s_waitcnt lgkmcnt(6)
	v_cvt_pk_bf16_f32 v4, v10, v12
	s_waitcnt lgkmcnt(4)
	v_cvt_pk_bf16_f32 v5, v14, v16
	s_waitcnt lgkmcnt(2)
	v_cvt_pk_bf16_f32 v6, v18, v20
	s_waitcnt lgkmcnt(0)
	v_cvt_pk_bf16_f32 v7, v22, v26
	global_store_dwordx4 v[8:9], v[4:7], off sc1
	v_or_b32_e32 v8, s6, v49
	v_ashrrev_i32_e32 v9, 31, v8
	v_lshlrev_b64 v[8:9], 11, v[8:9]
	v_lshl_add_u64 v[8:9], v[24:25], 0, v[8:9]
	v_cvt_pk_bf16_f32 v4, v11, v13
	v_cvt_pk_bf16_f32 v5, v15, v17
	v_cvt_pk_bf16_f32 v6, v19, v21
	v_cvt_pk_bf16_f32 v7, v23, v27
	global_store_dwordx4 v[8:9], v[4:7], off sc1
	s_waitcnt lgkmcnt(0)

; #define GAS __attribute__((address_space(1)))
; #define LAS __attribute__((address_space(3)))
; #define LDS_WAIT() asm volatile("s_waitcnt lgkmcnt(0)" ::: "memory")
; __device__ __forceinline__ unsigned pk2(float lo, float hi) { unsigned r; asm("v_cvt_pk_bf16_f32 %0, %1, %2" : "=v"(r) : "v"(lo), "v"(hi)); return r; }
; __device__ __forceinline__ void transpose_item(const float* W, int K, int N, bf16* WT, int drow0, int kb, int n0, LAS float* scr, int lane) {
;     const int k0 = 64 * kb; const int c4 = 4 * (lane & 7); const bool ok = (n0 + c4) < N;
;     f32x4 v[8];
; #pragma unroll
;     for (int i = 0; i < 8; ++i) { const int kk = 8 * i + (lane >> 3); v[i] = ok ? *(const f32x4*)(W + (size_t)(k0 + kk) * N + n0 + c4) : (f32x4){0.f, 0.f, 0.f, 0.f}; }
; #pragma unroll
;     for (int i = 0; i < 8; ++i) { const int kk = 8 * i + (lane >> 3); LAS float* d = scr + kk * 33 + c4; d[0] = v[i][0]; d[1] = v[i][1]; d[2] = v[i][2]; d[3] = v[i][3]; }
;     LDS_WAIT(); asm volatile("" ::: "memory");
;     const int c = lane & 7;
; #pragma unroll
;     for (int j = 0; j < 4; ++j) { const int n = (lane >> 3) + 8 * j; const LAS float* s = scr + (8 * c) * 33 + n;
;         v4u o; o.x = pk2(s[0 * 33], s[1 * 33]); o.y = pk2(s[2 * 33], s[3 * 33]); o.z = pk2(s[4 * 33], s[5 * 33]); o.w = pk2(s[6 * 33], s[7 * 33]);
;         *(GAS v4u*)(WT + (size_t)(drow0 + n) * K + k0 + 8 * c) = o; }
;     LDS_WAIT(); asm volatile("" ::: "memory");
; }
; __device__ __forceinline__ void convert_item(const In& I, unsigned char* ws, int it, LAS float* scr, int lane) {
;     ...
;     if (r < T0) { const int f = r / I_FFN; r -= f * I_FFN;
;         if (r < 2 * I_G) { const int up = r >= I_G; r -= up * I_G; const int kb = r / 88, nb = r % 88;
;             transpose_item((up ? I.w_up : I.w_gate) + (size_t)f * D * FF, D, FF, Wgu + (size_t)f * NGU * D, 256 * (nb >> 2) + 32 * (nb & 3) + 128 * up, kb, 32 * nb, scr, lane); }
;         else { r -= 2 * I_G; const int kb = r / 32, nb = r % 32; transpose_item(I.w_down + (size_t)f * FF * D, FF, D, Wd + (size_t)f * D * FF, 32 * nb, kb, 32 * nb, scr, lane); }
.LBB0_409:
	s_andn2_b64 vcc, exec, s[2:3]
	s_cbranch_vccnz .LBB0_354
	s_mul_hi_i32 s2, s45, 0x3e0f83e1
	s_lshr_b32 s3, s2, 31
	s_ashr_i32 s6, s2, 10
	s_add_i32 s6, s6, s3
	s_mul_i32 s2, s6, 0xffffef80
	s_add_i32 s7, s41, s2
	s_add_i32 s7, s7, 0xa800
	s_cmpk_gt_i32 s7, 0xaff
	s_mov_b64 s[2:3], -1
	s_cbranch_scc0 .LBB0_412
	v_readlane_b32 s48, v253, 0
	v_readlane_b32 s49, v253, 1
	v_readlane_b32 s50, v253, 2
	v_readlane_b32 s51, v253, 3
	v_readlane_b32 s52, v253, 4
	v_readlane_b32 s53, v253, 5
	v_readlane_b32 s54, v253, 6
	v_readlane_b32 s55, v253, 7
	v_readlane_b32 s56, v253, 8
	v_readlane_b32 s57, v253, 9
	s_mov_b64 s[48:49], s[52:53]
	s_mul_i32 s3, s6, 0xb00000
	s_mov_b64 s[50:51], s[54:55]
	s_mov_b64 s[52:53], s[56:57]
	s_mul_hi_i32 s2, s6, 0xb00000
	s_add_u32 s9, s52, s3
	s_addc_u32 s11, s53, s2
	s_mul_i32 s3, s6, 0x580000
	s_mul_hi_i32 s2, s6, 0x580000
	s_add_u32 s3, s1, s3
	s_mul_i32 s10, s6, 0xffffdf00
	s_addc_u32 s8, s19, s2
	s_add_i32 s10, s44, s10
	s_add_i32 s10, s10, 0x11600
	s_and_b32 s2, s43, 0x3e0
	s_andn2_b32 s10, s10, 63
	s_add_i32 s68, s10, 0xffffea00
	s_lshl_b32 s10, s2, 2
	v_or_b32_e32 v32, s68, v39
	s_add_u32 s10, s9, s10
	s_addc_u32 s11, s11, 0
	v_lshlrev_b32_e32 v2, 2, v36
	v_ashrrev_i32_e32 v33, 31, v32
	v_or_b32_e32 v8, 8, v32
	v_or_b32_e32 v12, 16, v32
	v_lshl_add_u64 v[34:35], s[10:11], 0, v[2:3]
	v_lshlrev_b64 v[4:5], 12, v[32:33]
	v_ashrrev_i32_e32 v9, 31, v8
	v_ashrrev_i32_e32 v13, 31, v12
	v_lshl_add_u64 v[4:5], v[34:35], 0, v[4:5]
	v_lshlrev_b64 v[8:9], 12, v[8:9]
	v_lshlrev_b64 v[12:13], 12, v[12:13]
	v_or_b32_e32 v16, 24, v32
	global_load_dwordx4 v[4:7], v[4:5], off
	v_lshl_add_u64 v[8:9], v[34:35], 0, v[8:9]
	v_lshl_add_u64 v[12:13], v[34:35], 0, v[12:13]
	v_ashrrev_i32_e32 v17, 31, v16
	v_or_b32_e32 v20, 32, v32
	global_load_dwordx4 v[8:11], v[8:9], off
	v_lshlrev_b64 v[16:17], 12, v[16:17]
	global_load_dwordx4 v[12:15], v[12:13], off
	v_ashrrev_i32_e32 v21, 31, v20
	v_lshl_add_u64 v[16:17], v[34:35], 0, v[16:17]
	v_lshlrev_b64 v[20:21], 12, v[20:21]
	v_or_b32_e32 v24, 40, v32
	global_load_dwordx4 v[16:19], v[16:17], off
	v_lshl_add_u64 v[20:21], v[34:35], 0, v[20:21]
	v_ashrrev_i32_e32 v25, 31, v24
	global_load_dwordx4 v[20:23], v[20:21], off
	v_lshlrev_b64 v[24:25], 12, v[24:25]
	v_or_b32_e32 v28, 48, v32
	v_lshl_add_u64 v[24:25], v[34:35], 0, v[24:25]
	v_ashrrev_i32_e32 v29, 31, v28
	global_load_dwordx4 v[24:27], v[24:25], off
	v_lshlrev_b64 v[28:29], 12, v[28:29]
	v_or_b32_e32 v32, 56, v32
	v_lshl_add_u64 v[28:29], v[34:35], 0, v[28:29]
	v_ashrrev_i32_e32 v33, 31, v32
	global_load_dwordx4 v[28:31], v[28:29], off
	v_lshlrev_b64 v[32:33], 12, v[32:33]
	v_lshl_add_u64 v[32:33], v[34:35], 0, v[32:33]
	global_load_dwordx4 v[32:35], v[32:33], off
	v_add_u32_e32 v2, v44, v47
	s_lshl_b64 s[10:11], s[68:69], 1
	s_add_u32 s10, s3, s10
	s_addc_u32 s11, s8, s11
	v_readlane_b32 s58, v253, 10
	v_readlane_b32 s59, v253, 11
	v_readlane_b32 s60, v253, 12
	v_readlane_b32 s61, v253, 13
	v_readlane_b32 s62, v253, 14
	v_readlane_b32 s63, v253, 15
	s_waitcnt vmcnt(0)
	ds_write2_b32 v45, v4, v5 offset1:1
	ds_write2_b32 v45, v6, v7 offset0:2 offset1:3
	v_add_u32_e32 v4, 0x420, v2
	ds_write2_b32 v2, v8, v9 offset1:1
	ds_write2_b32 v2, v10, v11 offset0:2 offset1:3
	ds_write2_b32 v4, v12, v13 offset1:1
	v_add_u32_e32 v4, 0x428, v2
	ds_write2_b32 v4, v14, v15 offset1:1
	v_add_u32_e32 v4, 0x840, v2
	v_add_u32_e32 v2, 0x848, v2
	ds_write2_b32 v2, v18, v19 offset1:1
	v_add_u32_e32 v2, 0x1080, v45
	ds_write2_b32 v4, v16, v17 offset1:1
	ds_write2_b32 v2, v20, v21 offset1:1
	v_add_u32_e32 v2, 0x1088, v45
	ds_write2_b32 v2, v22, v23 offset1:1
	v_add_u32_e32 v2, 0x14a0, v45
	ds_write2_b32 v2, v24, v25 offset1:1
	v_add_u32_e32 v2, 0x14a8, v45
	ds_write2_b32 v2, v26, v27 offset1:1
	v_add_u32_e32 v2, 0x18c0, v45
	ds_write2_b32 v2, v28, v29 offset1:1
	v_add_u32_e32 v2, 0x18c8, v45
	ds_write2_b32 v2, v30, v31 offset1:1
	v_add_u32_e32 v2, 0x1ce0, v45
	ds_write2_b32 v2, v32, v33 offset1:1
	v_add_u32_e32 v2, 0x1ce8, v45
	ds_write2_b32 v2, v34, v35 offset1:1
	s_waitcnt lgkmcnt(0)
	ds_read2_b32 v[10:11], v50 offset0:33 offset1:41
	ds_read2_b32 v[12:13], v50 offset1:8
	v_lshlrev_b32_e32 v2, 1, v38
	ds_read2_b32 v[14:15], v50 offset0:66 offset1:74
	ds_read2_b32 v[16:17], v50 offset0:99 offset1:107
	ds_read2_b32 v[18:19], v50 offset0:132 offset1:140
	ds_read2_b32 v[20:21], v50 offset0:165 offset1:173
	ds_read2_b32 v[22:23], v50 offset0:198 offset1:206
	ds_read2_b32 v[24:25], v50 offset0:231 offset1:239
	v_lshl_add_u64 v[8:9], s[10:11], 0, v[2:3]
	v_or_b32_e32 v2, s2, v39
	v_mul_u32_u24_e32 v2, 0x1600, v2
	v_lshl_add_u64 v[26:27], v[8:9], 0, v[2:3]
	v_or_b32_e32 v2, s2, v46
	s_waitcnt lgkmcnt(0)
	v_cvt_pk_bf16_f32 v4, v12, v10
	v_mul_u32_u24_e32 v2, 0x1600, v2
	v_cvt_pk_bf16_f32 v5, v14, v16
	v_cvt_pk_bf16_f32 v6, v18, v20
	v_cvt_pk_bf16_f32 v7, v22, v24
	global_store_dwordx4 v[26:27], v[4:7], off sc1
	s_nop 1
	v_cvt_pk_bf16_f32 v4, v13, v11
	v_lshl_add_u64 v[10:11], v[8:9], 0, v[2:3]
	v_cvt_pk_bf16_f32 v5, v15, v17
	v_cvt_pk_bf16_f32 v6, v19, v21
	v_cvt_pk_bf16_f32 v7, v23, v25
	global_store_dwordx4 v[10:11], v[4:7], off sc1
	ds_read2_b32 v[10:11], v50 offset0:16 offset1:24
	ds_read2_b32 v[12:13], v50 offset0:49 offset1:57
	ds_read2_b32 v[14:15], v50 offset0:82 offset1:90
	ds_read2_b32 v[16:17], v50 offset0:115 offset1:123
	ds_read2_b32 v[18:19], v50 offset0:148 offset1:156
	ds_read2_b32 v[20:21], v50 offset0:181 offset1:189
	ds_read2_b32 v[22:23], v50 offset0:214 offset1:222
	ds_read2_b32 v[24:25], v50 offset0:247 offset1:255
	v_or_b32_e32 v2, s2, v48
	v_mul_u32_u24_e32 v2, 0x1600, v2
	v_lshl_add_u64 v[26:27], v[8:9], 0, v[2:3]
	v_or_b32_e32 v2, s2, v49
	v_mul_u32_u24_e32 v2, 0x1600, v2
	s_waitcnt lgkmcnt(6)
	v_cvt_pk_bf16_f32 v4, v10, v12
	s_waitcnt lgkmcnt(4)
	v_cvt_pk_bf16_f32 v5, v14, v16
	s_waitcnt lgkmcnt(2)
	v_cvt_pk_bf16_f32 v6, v18, v20
	s_waitcnt lgkmcnt(0)
	v_cvt_pk_bf16_f32 v7, v22, v24
	v_lshl_add_u64 v[8:9], v[8:9], 0, v[2:3]
	global_store_dwordx4 v[26:27], v[4:7], off sc1
	s_mov_b64 s[2:3], 0
	s_nop 0
	v_cvt_pk_bf16_f32 v4, v11, v13
	v_cvt_pk_bf16_f32 v5, v15, v17
	v_cvt_pk_bf16_f32 v6, v19, v21
	v_cvt_pk_bf16_f32 v7, v23, v25
	global_store_dwordx4 v[8:9], v[4:7], off sc1
	s_waitcnt lgkmcnt(0)
; #define GAS __attribute__((address_space(1)))
; #define LAS __attribute__((address_space(3)))
; #define LDS_WAIT() asm volatile("s_waitcnt lgkmcnt(0)" ::: "memory")
; __device__ __forceinline__ unsigned pk2(float lo, float hi) { unsigned r; asm("v_cvt_pk_bf16_f32 %0, %1, %2" : "=v"(r) : "v"(lo), "v"(hi)); return r; }
; __device__ __forceinline__ void transpose_item(const float* W, int K, int N, bf16* WT, int drow0, int kb, int n0, LAS float* scr, int lane) {
;     const int k0 = 64 * kb; const int c4 = 4 * (lane & 7); const bool ok = (n0 + c4) < N;
;     f32x4 v[8];
; #pragma unroll
;     for (int i = 0; i < 8; ++i) { const int kk = 8 * i + (lane >> 3); v[i] = ok ? *(const f32x4*)(W + (size_t)(k0 + kk) * N + n0 + c4) : (f32x4){0.f, 0.f, 0.f, 0.f}; }
; #pragma unroll
;     for (int i = 0; i < 8; ++i) { const int kk = 8 * i + (lane >> 3); LAS float* d = scr + kk * 33 + c4; d[0] = v[i][0]; d[1] = v[i][1]; d[2] = v[i][2]; d[3] = v[i][3]; }
;     LDS_WAIT(); asm volatile("" ::: "memory");
;     const int c = lane & 7;
; #pragma unroll
;     for (int j = 0; j < 4; ++j) { const int n = (lane >> 3) + 8 * j; const LAS float* s = scr + (8 * c) * 33 + n;
;         v4u o; o.x = pk2(s[0 * 33], s[1 * 33]); o.y = pk2(s[2 * 33], s[3 * 33]); o.z = pk2(s[4 * 33], s[5 * 33]); o.w = pk2(s[6 * 33], s[7 * 33]);
;         *(GAS v4u*)(WT + (size_t)(drow0 + n) * K + k0 + 8 * c) = o; }
;     LDS_WAIT(); asm volatile("" ::: "memory");
; }
; __device__ __forceinline__ void convert_item(const In& I, unsigned char* ws, int it, LAS float* scr, int lane) {
;     ...
;         if (r < 2 * I_G) { const int up = r >= I_G; r -= up * I_G; const int kb = r / 88, nb = r % 88;
;             transpose_item((up ? I.w_up : I.w_gate) + (size_t)f * D * FF, D, FF, Wgu + (size_t)f * NGU * D, 256 * (nb >> 2) + 32 * (nb & 3) + 128 * up, kb, 32 * nb, scr, lane); }
.LBB0_412:
	s_andn2_b64 vcc, exec, s[2:3]
	s_cbranch_vccnz .LBB0_354
	v_readlane_b32 s48, v253, 0
	v_readlane_b32 s49, v253, 1
	v_readlane_b32 s50, v253, 2
	v_readlane_b32 s51, v253, 3
	v_readlane_b32 s52, v253, 4
	v_readlane_b32 s53, v253, 5
	s_cmpk_gt_i32 s7, 0x57f
	v_readlane_b32 s54, v253, 6
	v_readlane_b32 s55, v253, 7
	v_readlane_b32 s56, v253, 8
	v_readlane_b32 s57, v253, 9
	s_mov_b64 s[48:49], s[52:53]
	s_cselect_b32 s2, 0xfffffa80, 0
	s_mul_i32 s3, s6, 0x1080
	s_mov_b64 s[50:51], s[54:55]
	s_cselect_b32 s9, 0x80, 0
	s_cselect_b32 s7, s50, s48
	s_cselect_b32 s8, s51, s49
	s_sub_i32 s2, s2, s3
	s_add_i32 s2, s41, s2
	s_add_i32 s2, s2, 0xa800
	s_mul_hi_i32 s3, s2, 0x2e8ba2e9
	s_lshr_b32 s10, s3, 31
	s_ashr_i32 s3, s3, 4
	s_add_i32 s3, s3, s10
	s_mul_i32 s10, s3, 0x58
	s_sub_i32 s2, s2, s10
	s_mul_hi_i32 s10, s6, 0xb00000
	s_mul_i32 s6, s6, 0xb00000
	s_add_u32 s12, s7, s6
	s_addc_u32 s13, s8, s10
	s_add_u32 s7, s28, s6
	s_addc_u32 s8, s29, s10
	s_lshl_b32 s10, s2, 5
	s_lshl_b32 s6, s2, 6
	s_and_b32 s2, s10, 0x60
	s_and_b32 s6, s6, 0xffffff00
	s_or_b32 s2, s2, s9
	s_ashr_i32 s11, s10, 31
	s_or_b32 s6, s2, s6
	s_lshl_b32 s2, s3, 6
	s_lshl_b64 s[10:11], s[10:11], 2
	s_add_u32 s10, s12, s10
	v_or_b32_e32 v34, s2, v39
	s_addc_u32 s11, s13, s11
	v_lshlrev_b32_e32 v2, 2, v36
	v_lshl_add_u64 v[32:33], s[10:11], 0, v[2:3]
	s_movk_i32 s3, 0x2c00
	v_or_b32_e32 v2, 8, v34
	v_mad_i64_i32 v[4:5], s[10:11], v34, s3, v[32:33]
	v_mad_i64_i32 v[8:9], s[10:11], v2, s3, v[32:33]
	v_or_b32_e32 v2, 16, v34
	global_load_dwordx4 v[4:7], v[4:5], off
	v_mad_i64_i32 v[12:13], s[10:11], v2, s3, v[32:33]
	global_load_dwordx4 v[8:11], v[8:9], off
	v_or_b32_e32 v2, 24, v34
	global_load_dwordx4 v[12:15], v[12:13], off
	v_mad_i64_i32 v[16:17], s[10:11], v2, s3, v[32:33]
	v_or_b32_e32 v2, 32, v34
	global_load_dwordx4 v[16:19], v[16:17], off
	v_mad_i64_i32 v[20:21], s[10:11], v2, s3, v[32:33]
	global_load_dwordx4 v[20:23], v[20:21], off
	v_or_b32_e32 v2, 40, v34
	v_mad_i64_i32 v[24:25], s[10:11], v2, s3, v[32:33]
	global_load_dwordx4 v[24:27], v[24:25], off
	v_or_b32_e32 v2, 48, v34
	v_mad_i64_i32 v[28:29], s[10:11], v2, s3, v[32:33]
	global_load_dwordx4 v[28:31], v[28:29], off
	v_or_b32_e32 v2, 56, v34
	v_mad_i64_i32 v[32:33], s[10:11], v2, s3, v[32:33]
	global_load_dwordx4 v[32:35], v[32:33], off
	v_add_u32_e32 v2, v44, v47
	s_ashr_i32 s3, s2, 31
	s_lshl_b64 s[2:3], s[2:3], 1
	s_add_u32 s2, s7, s2
	s_addc_u32 s3, s8, s3
	v_readlane_b32 s58, v253, 10
	v_readlane_b32 s59, v253, 11
	v_readlane_b32 s60, v253, 12
	v_readlane_b32 s61, v253, 13
	v_readlane_b32 s62, v253, 14
	v_readlane_b32 s63, v253, 15
	s_mov_b64 s[52:53], s[56:57]
	s_waitcnt vmcnt(0)
	ds_write2_b32 v45, v4, v5 offset1:1
	ds_write2_b32 v45, v6, v7 offset0:2 offset1:3
	v_add_u32_e32 v4, 0x420, v2
	ds_write2_b32 v2, v8, v9 offset1:1
	ds_write2_b32 v2, v10, v11 offset0:2 offset1:3
	ds_write2_b32 v4, v12, v13 offset1:1
	v_add_u32_e32 v4, 0x428, v2
	ds_write2_b32 v4, v14, v15 offset1:1
	v_add_u32_e32 v4, 0x840, v2
	v_add_u32_e32 v2, 0x848, v2
	ds_write2_b32 v2, v18, v19 offset1:1
	v_add_u32_e32 v2, 0x1080, v45
	ds_write2_b32 v2, v20, v21 offset1:1
	v_add_u32_e32 v2, 0x1088, v45
	ds_write2_b32 v2, v22, v23 offset1:1
	v_add_u32_e32 v2, 0x14a0, v45
	ds_write2_b32 v2, v24, v25 offset1:1
	v_add_u32_e32 v2, 0x14a8, v45
	ds_write2_b32 v2, v26, v27 offset1:1
	v_add_u32_e32 v2, 0x18c0, v45
	ds_write2_b32 v2, v28, v29 offset1:1
	v_add_u32_e32 v2, 0x18c8, v45
	ds_write2_b32 v2, v30, v31 offset1:1
	v_add_u32_e32 v2, 0x1ce0, v45
	ds_write2_b32 v2, v32, v33 offset1:1
	v_add_u32_e32 v2, 0x1ce8, v45
	ds_write2_b32 v4, v16, v17 offset1:1
	ds_write2_b32 v2, v34, v35 offset1:1
	s_waitcnt lgkmcnt(0)
	ds_read2_b32 v[10:11], v50 offset0:33 offset1:41
	ds_read2_b32 v[12:13], v50 offset1:8
	ds_read2_b32 v[14:15], v50 offset0:66 offset1:74
	ds_read2_b32 v[16:17], v50 offset0:99 offset1:107
	ds_read2_b32 v[18:19], v50 offset0:132 offset1:140
	ds_read2_b32 v[20:21], v50 offset0:165 offset1:173
	ds_read2_b32 v[22:23], v50 offset0:198 offset1:206
	ds_read2_b32 v[24:25], v50 offset0:231 offset1:239
	v_or_b32_e32 v26, s6, v39
	v_lshlrev_b32_e32 v2, 1, v38
	v_ashrrev_i32_e32 v27, 31, v26
	v_lshl_add_u64 v[8:9], s[2:3], 0, v[2:3]
	v_lshlrev_b64 v[26:27], 11, v[26:27]
	s_waitcnt lgkmcnt(0)
	v_cvt_pk_bf16_f32 v4, v12, v10
	v_lshl_add_u64 v[26:27], v[8:9], 0, v[26:27]
	v_or_b32_e32 v10, s6, v46
	v_cvt_pk_bf16_f32 v5, v14, v16
	v_cvt_pk_bf16_f32 v6, v18, v20
	v_cvt_pk_bf16_f32 v7, v22, v24
	global_store_dwordx4 v[26:27], v[4:7], off sc1
	v_or_b32_e32 v26, s6, v48
	v_ashrrev_i32_e32 v27, 31, v26
	v_cvt_pk_bf16_f32 v4, v13, v11
	v_ashrrev_i32_e32 v11, 31, v10
	v_lshlrev_b64 v[10:11], 11, v[10:11]
	v_lshl_add_u64 v[10:11], v[8:9], 0, v[10:11]
	v_cvt_pk_bf16_f32 v5, v15, v17
	v_cvt_pk_bf16_f32 v6, v19, v21
	v_cvt_pk_bf16_f32 v7, v23, v25
	global_store_dwordx4 v[10:11], v[4:7], off sc1
	ds_read2_b32 v[10:11], v50 offset0:16 offset1:24
	ds_read2_b32 v[12:13], v50 offset0:49 offset1:57
	ds_read2_b32 v[14:15], v50 offset0:82 offset1:90
	ds_read2_b32 v[16:17], v50 offset0:115 offset1:123
	ds_read2_b32 v[18:19], v50 offset0:148 offset1:156
	ds_read2_b32 v[20:21], v50 offset0:181 offset1:189
	ds_read2_b32 v[22:23], v50 offset0:214 offset1:222
	ds_read2_b32 v[24:25], v50 offset0:247 offset1:255
	v_lshlrev_b64 v[26:27], 11, v[26:27]
	s_waitcnt lgkmcnt(6)
	v_cvt_pk_bf16_f32 v4, v10, v12
	v_lshl_add_u64 v[26:27], v[8:9], 0, v[26:27]
	v_or_b32_e32 v10, s6, v49
	s_waitcnt lgkmcnt(4)
	v_cvt_pk_bf16_f32 v5, v14, v16
	s_waitcnt lgkmcnt(2)
	v_cvt_pk_bf16_f32 v6, v18, v20
	s_waitcnt lgkmcnt(0)
	v_cvt_pk_bf16_f32 v7, v22, v24
	global_store_dwordx4 v[26:27], v[4:7], off sc1
	s_nop 1
	v_cvt_pk_bf16_f32 v4, v11, v13
	v_ashrrev_i32_e32 v11, 31, v10
	v_lshlrev_b64 v[10:11], 11, v[10:11]
	v_lshl_add_u64 v[8:9], v[8:9], 0, v[10:11]
	v_cvt_pk_bf16_f32 v5, v15, v17
	v_cvt_pk_bf16_f32 v6, v19, v21
	v_cvt_pk_bf16_f32 v7, v23, v25
	global_store_dwordx4 v[8:9], v[4:7], off sc1
	s_waitcnt lgkmcnt(0)
	s_branch .LBB0_354

; #define GAS __attribute__((address_space(1)))
; #define LAS __attribute__((address_space(3)))
; #define LDS_WAIT() asm volatile("s_waitcnt lgkmcnt(0)" ::: "memory")
; __device__ __forceinline__ unsigned pk2(float lo, float hi) { unsigned r; asm("v_cvt_pk_bf16_f32 %0, %1, %2" : "=v"(r) : "v"(lo), "v"(hi)); return r; }
; __device__ __forceinline__ void transpose_item(const float* W, int K, int N, bf16* WT, int drow0, int kb, int n0, LAS float* scr, int lane) {
;     const int k0 = 64 * kb; const int c4 = 4 * (lane & 7); const bool ok = (n0 + c4) < N;
;     f32x4 v[8];
; #pragma unroll
;     for (int i = 0; i < 8; ++i) { const int kk = 8 * i + (lane >> 3); v[i] = ok ? *(const f32x4*)(W + (size_t)(k0 + kk) * N + n0 + c4) : (f32x4){0.f, 0.f, 0.f, 0.f}; }
; #pragma unroll
;     for (int i = 0; i < 8; ++i) { const int kk = 8 * i + (lane >> 3); LAS float* d = scr + kk * 33 + c4; d[0] = v[i][0]; d[1] = v[i][1]; d[2] = v[i][2]; d[3] = v[i][3]; }
;     LDS_WAIT(); asm volatile("" ::: "memory");
;     const int c = lane & 7;
; #pragma unroll
;     for (int j = 0; j < 4; ++j) { const int n = (lane >> 3) + 8 * j; const LAS float* s = scr + (8 * c) * 33 + n;
;         v4u o; o.x = pk2(s[0 * 33], s[1 * 33]); o.y = pk2(s[2 * 33], s[3 * 33]); o.z = pk2(s[4 * 33], s[5 * 33]); o.w = pk2(s[6 * 33], s[7 * 33]);
;         *(GAS v4u*)(WT + (size_t)(drow0 + n) * K + k0 + 8 * c) = o; }
;     LDS_WAIT(); asm volatile("" ::: "memory");
; }
; __device__ __forceinline__ void convert_item(const In& I, unsigned char* ws, int it, LAS float* scr, int lane) {
;     ...
;     { const int jk = r >> 3; r &= 7; const int kb = r >> 1, nb = r & 1;
;         transpose_item(I.nsa_w2 + (size_t)jk * 256 * 64, 256, 64, W2t + (size_t)jk * 64 * 256, 32 * nb, kb, 32 * nb, scr, lane); }
.LBB0_416:
	s_add_i32 s43, s41, 0xa800
	s_cmp_gt_i32 s43, 0x83ff
	s_mov_b64 s[2:3], -1
	s_cbranch_scc0 .LBB0_470
	s_cmpk_gt_u32 s43, 0x8eff
	s_cbranch_scc0 .LBB0_451
	s_cmpk_gt_u32 s43, 0x92ff
	s_cbranch_scc0 .LBB0_448
	s_cmpk_gt_u32 s43, 0x9fff
	s_cbranch_scc0 .LBB0_429
	s_cmpk_gt_u32 s43, 0xa3ff
	s_cbranch_scc0 .LBB0_426
	s_cmpk_gt_u32 s43, 0xa7ff
	s_cbranch_scc0 .LBB0_423
	s_lshr_b32 s68, s41, 3
	v_readlane_b32 s44, v253, 16
	s_lshl_b64 s[2:3], s[68:69], 16
	v_readlane_b32 s48, v253, 20
	v_readlane_b32 s49, v253, 21
	s_add_u32 s6, s48, s2
	s_addc_u32 s7, s49, s3
	s_lshl_b64 s[2:3], s[68:69], 15
	s_add_u32 s8, s34, s2
	s_addc_u32 s3, s35, s3
	s_and_b32 s2, s42, 32
	s_and_b32 s9, s42, 0xc0
	s_lshl_b32 s10, s2, 2
	s_add_u32 s6, s6, s10
	v_or_b32_e32 v6, s9, v39
	s_addc_u32 s7, s7, 0
	v_lshlrev_b32_e32 v2, 2, v36
	v_lshl_add_u64 v[4:5], s[6:7], 0, v[2:3]
	v_lshlrev_b32_e32 v2, 8, v6
	v_lshl_add_u64 v[28:29], v[4:5], 0, v[2:3]
	v_add_co_u32_e32 v16, vcc, s84, v28
	global_load_dwordx4 v[4:7], v[28:29], off
	global_load_dwordx4 v[8:11], v[28:29], off offset:2048
	v_addc_co_u32_e32 v17, vcc, 0, v29, vcc
	v_add_co_u32_e32 v24, vcc, s74, v28
	s_movk_i32 s6, 0x3000
	s_nop 0
	v_addc_co_u32_e32 v25, vcc, 0, v29, vcc
	global_load_dwordx4 v[12:15], v[24:25], off offset:-4096
	s_nop 0
	global_load_dwordx4 v[16:19], v[16:17], off offset:2048
	s_nop 0
	global_load_dwordx4 v[20:23], v[24:25], off
	s_nop 0
	global_load_dwordx4 v[24:27], v[24:25], off offset:2048
	v_add_co_u32_e32 v32, vcc, s6, v28
	v_add_u32_e32 v2, v44, v47
	s_nop 0
	v_addc_co_u32_e32 v33, vcc, 0, v29, vcc
	global_load_dwordx4 v[28:31], v[32:33], off
	s_nop 0
	global_load_dwordx4 v[32:35], v[32:33], off offset:2048
	s_lshl_b32 s6, s9, 1
	s_add_u32 s6, s8, s6
	s_addc_u32 s7, s3, 0
	v_readlane_b32 s45, v253, 17
	v_readlane_b32 s46, v253, 18
	v_readlane_b32 s47, v253, 19
	v_readlane_b32 s50, v253, 22
	v_readlane_b32 s51, v253, 23
	v_readlane_b32 s52, v253, 24
	v_readlane_b32 s53, v253, 25
	v_readlane_b32 s54, v253, 26
	v_readlane_b32 s55, v253, 27
	v_readlane_b32 s56, v253, 28
	v_readlane_b32 s57, v253, 29
	v_readlane_b32 s58, v253, 30
	v_readlane_b32 s59, v253, 31
	s_waitcnt vmcnt(0)
	ds_write2_b32 v45, v4, v5 offset1:1
	ds_write2_b32 v45, v6, v7 offset0:2 offset1:3
	v_add_u32_e32 v4, 0x420, v2
	ds_write2_b32 v2, v8, v9 offset1:1
	ds_write2_b32 v2, v10, v11 offset0:2 offset1:3
	ds_write2_b32 v4, v12, v13 offset1:1
	v_add_u32_e32 v4, 0x428, v2
	ds_write2_b32 v4, v14, v15 offset1:1
	v_add_u32_e32 v4, 0x840, v2
	v_add_u32_e32 v2, 0x848, v2
	ds_write2_b32 v2, v18, v19 offset1:1
	v_add_u32_e32 v2, 0x1080, v45
	ds_write2_b32 v2, v20, v21 offset1:1
	v_add_u32_e32 v2, 0x1088, v45
	ds_write2_b32 v2, v22, v23 offset1:1
	v_add_u32_e32 v2, 0x14a0, v45
	ds_write2_b32 v2, v24, v25 offset1:1
	v_add_u32_e32 v2, 0x14a8, v45
	ds_write2_b32 v2, v26, v27 offset1:1
	v_add_u32_e32 v2, 0x18c0, v45
	ds_write2_b32 v2, v28, v29 offset1:1
	v_add_u32_e32 v2, 0x18c8, v45
	ds_write2_b32 v2, v30, v31 offset1:1
	v_add_u32_e32 v2, 0x1ce0, v45
	ds_write2_b32 v2, v32, v33 offset1:1
	v_add_u32_e32 v2, 0x1ce8, v45
	ds_write2_b32 v4, v16, v17 offset1:1
	ds_write2_b32 v2, v34, v35 offset1:1
	s_waitcnt lgkmcnt(0)
	ds_read2_b32 v[10:11], v50 offset0:33 offset1:41
	ds_read2_b32 v[12:13], v50 offset1:8
	v_lshlrev_b32_e32 v2, 1, v38
	ds_read2_b32 v[14:15], v50 offset0:66 offset1:74
	ds_read2_b32 v[16:17], v50 offset0:99 offset1:107
	ds_read2_b32 v[18:19], v50 offset0:132 offset1:140
	ds_read2_b32 v[20:21], v50 offset0:165 offset1:173
	ds_read2_b32 v[22:23], v50 offset0:198 offset1:206
	ds_read2_b32 v[24:25], v50 offset0:231 offset1:239
	v_lshl_add_u64 v[4:5], s[6:7], 0, v[2:3]
	v_or_b32_e32 v2, s2, v39
	v_lshlrev_b32_e32 v2, 9, v2
	v_lshl_add_u64 v[26:27], v[4:5], 0, v[2:3]
	v_or_b32_e32 v2, s2, v46
	s_waitcnt lgkmcnt(0)
	v_cvt_pk_bf16_f32 v6, v12, v10
	v_lshlrev_b32_e32 v2, 9, v2
	v_cvt_pk_bf16_f32 v7, v14, v16
	v_cvt_pk_bf16_f32 v8, v18, v20
	v_cvt_pk_bf16_f32 v9, v22, v24
	global_store_dwordx4 v[26:27], v[6:9], off sc1
	s_nop 1
	v_cvt_pk_bf16_f32 v6, v13, v11
	v_lshl_add_u64 v[10:11], v[4:5], 0, v[2:3]
	v_cvt_pk_bf16_f32 v7, v15, v17
	v_cvt_pk_bf16_f32 v8, v19, v21
	v_cvt_pk_bf16_f32 v9, v23, v25
	global_store_dwordx4 v[10:11], v[6:9], off sc1
	ds_read2_b32 v[10:11], v50 offset0:16 offset1:24
	ds_read2_b32 v[12:13], v50 offset0:49 offset1:57
	ds_read2_b32 v[14:15], v50 offset0:82 offset1:90
	ds_read2_b32 v[16:17], v50 offset0:115 offset1:123
	ds_read2_b32 v[18:19], v50 offset0:148 offset1:156
	ds_read2_b32 v[20:21], v50 offset0:181 offset1:189
	ds_read2_b32 v[22:23], v50 offset0:214 offset1:222
	ds_read2_b32 v[24:25], v50 offset0:247 offset1:255
	v_or_b32_e32 v2, s2, v48
	v_lshlrev_b32_e32 v2, 9, v2
	v_lshl_add_u64 v[26:27], v[4:5], 0, v[2:3]
	v_or_b32_e32 v2, s2, v49
	v_lshlrev_b32_e32 v2, 9, v2
	s_waitcnt lgkmcnt(6)
	v_cvt_pk_bf16_f32 v6, v10, v12
	s_waitcnt lgkmcnt(4)
	v_cvt_pk_bf16_f32 v7, v14, v16
	s_waitcnt lgkmcnt(2)
	v_cvt_pk_bf16_f32 v8, v18, v20
	s_waitcnt lgkmcnt(0)
	v_cvt_pk_bf16_f32 v9, v22, v24
	v_lshl_add_u64 v[4:5], v[4:5], 0, v[2:3]
	global_store_dwordx4 v[26:27], v[6:9], off sc1
	s_mov_b64 s[2:3], 0
	s_nop 0
	v_cvt_pk_bf16_f32 v6, v11, v13
	v_cvt_pk_bf16_f32 v7, v15, v17
	v_cvt_pk_bf16_f32 v8, v19, v21
	v_cvt_pk_bf16_f32 v9, v23, v25
	global_store_dwordx4 v[4:5], v[6:9], off sc1
	s_waitcnt lgkmcnt(0)
; #define GAS __attribute__((address_space(1)))
; #define LAS __attribute__((address_space(3)))
; #define LDS_WAIT() asm volatile("s_waitcnt lgkmcnt(0)" ::: "memory")
; __device__ __forceinline__ unsigned pk2(float lo, float hi) { unsigned r; asm("v_cvt_pk_bf16_f32 %0, %1, %2" : "=v"(r) : "v"(lo), "v"(hi)); return r; }
; __device__ __forceinline__ void transpose_item(const float* W, int K, int N, bf16* WT, int drow0, int kb, int n0, LAS float* scr, int lane) {
;     const int k0 = 64 * kb; const int c4 = 4 * (lane & 7); const bool ok = (n0 + c4) < N;
;     f32x4 v[8];
; #pragma unroll
;     for (int i = 0; i < 8; ++i) { const int kk = 8 * i + (lane >> 3); v[i] = ok ? *(const f32x4*)(W + (size_t)(k0 + kk) * N + n0 + c4) : (f32x4){0.f, 0.f, 0.f, 0.f}; }
; #pragma unroll
;     for (int i = 0; i < 8; ++i) { const int kk = 8 * i + (lane >> 3); LAS float* d = scr + kk * 33 + c4; d[0] = v[i][0]; d[1] = v[i][1]; d[2] = v[i][2]; d[3] = v[i][3]; }
;     LDS_WAIT(); asm volatile("" ::: "memory");
;     const int c = lane & 7;
; #pragma unroll
;     for (int j = 0; j < 4; ++j) { const int n = (lane >> 3) + 8 * j; const LAS float* s = scr + (8 * c) * 33 + n;
;         v4u o; o.x = pk2(s[0 * 33], s[1 * 33]); o.y = pk2(s[2 * 33], s[3 * 33]); o.z = pk2(s[4 * 33], s[5 * 33]); o.w = pk2(s[6 * 33], s[7 * 33]);
;         *(GAS v4u*)(WT + (size_t)(drow0 + n) * K + k0 + 8 * c) = o; }
;     LDS_WAIT(); asm volatile("" ::: "memory");
; }
; __device__ __forceinline__ void convert_item(const In& I, unsigned char* ws, int it, LAS float* scr, int lane) {
;     ...
;     if (r < 4 * I_W1) { const int jk = r / I_W1; r -= jk * I_W1; const int kb = r / 8, nb = r % 8;
;         transpose_item(I.nsa_w1 + (size_t)jk * 2048 * 256, 2048, 256, W1t + (size_t)jk * 256 * 2048, 32 * nb, kb, 32 * nb, scr, lane); return; }
.LBB0_423:
	s_andn2_b64 vcc, exec, s[2:3]
	s_cbranch_vccnz .LBB0_425
	s_add_i32 s2, s41, 0x400
	s_lshr_b32 s68, s2, 8
	s_lshl_b64 s[2:3], s[68:69], 21
	v_readlane_b32 s44, v253, 16
	v_readlane_b32 s45, v253, 17
	s_add_u32 s6, s44, s2
	s_addc_u32 s7, s45, s3
	s_lshl_b64 s[2:3], s[68:69], 20
	s_add_u32 s8, s31, s2
	s_addc_u32 s3, s33, s3
	s_and_b32 s2, s42, 0xe0
	s_and_b32 s9, s40, 0x7c0
	s_lshl_b32 s10, s2, 2
	s_add_u32 s6, s6, s10
	v_or_b32_e32 v6, s9, v39
	s_addc_u32 s7, s7, 0
	v_lshlrev_b32_e32 v2, 2, v36
	v_lshl_add_u64 v[4:5], s[6:7], 0, v[2:3]
	v_lshlrev_b32_e32 v2, 10, v6
	v_lshl_add_u64 v[32:33], v[4:5], 0, v[2:3]
	v_add_co_u32_e32 v8, vcc, s74, v32
	s_movk_i32 s6, 0x4000
	s_nop 0
	v_addc_co_u32_e32 v9, vcc, 0, v33, vcc
	v_add_co_u32_e32 v12, vcc, s6, v32
	s_movk_i32 s6, 0x6000
	s_nop 0
	v_addc_co_u32_e32 v13, vcc, 0, v33, vcc
	global_load_dwordx4 v[4:7], v[32:33], off
	v_add_co_u32_e32 v16, vcc, s6, v32
	global_load_dwordx4 v[8:11], v[8:9], off
	s_nop 0
	v_addc_co_u32_e32 v17, vcc, 0, v33, vcc
	global_load_dwordx4 v[12:15], v[12:13], off
	v_add_co_u32_e32 v20, vcc, s81, v32
	global_load_dwordx4 v[16:19], v[16:17], off
	s_nop 0
	v_addc_co_u32_e32 v21, vcc, 0, v33, vcc
	s_mov_b32 s6, 0xa000
	global_load_dwordx4 v[20:23], v[20:21], off
	v_add_co_u32_e32 v24, vcc, s6, v32
	s_mov_b32 s6, 0xc000
	s_nop 0
	v_addc_co_u32_e32 v25, vcc, 0, v33, vcc
	global_load_dwordx4 v[24:27], v[24:25], off
	v_add_co_u32_e32 v28, vcc, s6, v32
	s_mov_b32 s6, 0xe000
	s_nop 0
	v_addc_co_u32_e32 v29, vcc, 0, v33, vcc
	global_load_dwordx4 v[28:31], v[28:29], off
	v_add_co_u32_e32 v32, vcc, s6, v32
	v_add_u32_e32 v2, v44, v47
	s_nop 0
	v_addc_co_u32_e32 v33, vcc, 0, v33, vcc
	global_load_dwordx4 v[32:35], v[32:33], off
	s_lshl_b32 s6, s9, 1
	s_add_u32 s6, s8, s6
	s_addc_u32 s7, s3, 0
	v_readlane_b32 s46, v253, 18
	v_readlane_b32 s47, v253, 19
	v_readlane_b32 s48, v253, 20
	v_readlane_b32 s49, v253, 21
	v_readlane_b32 s50, v253, 22
	v_readlane_b32 s51, v253, 23
	v_readlane_b32 s52, v253, 24
	v_readlane_b32 s53, v253, 25
	v_readlane_b32 s54, v253, 26
	v_readlane_b32 s55, v253, 27
	v_readlane_b32 s56, v253, 28
	v_readlane_b32 s57, v253, 29
	v_readlane_b32 s58, v253, 30
	v_readlane_b32 s59, v253, 31
	s_waitcnt vmcnt(0)
	ds_write2_b32 v45, v4, v5 offset1:1
	ds_write2_b32 v45, v6, v7 offset0:2 offset1:3
	v_add_u32_e32 v4, 0x420, v2
	ds_write2_b32 v2, v8, v9 offset1:1
	ds_write2_b32 v2, v10, v11 offset0:2 offset1:3
	ds_write2_b32 v4, v12, v13 offset1:1
	v_add_u32_e32 v4, 0x428, v2
	ds_write2_b32 v4, v14, v15 offset1:1
	v_add_u32_e32 v4, 0x840, v2
	v_add_u32_e32 v2, 0x848, v2
	ds_write2_b32 v2, v18, v19 offset1:1
	v_add_u32_e32 v2, 0x1080, v45
	ds_write2_b32 v2, v20, v21 offset1:1
	v_add_u32_e32 v2, 0x1088, v45
	ds_write2_b32 v2, v22, v23 offset1:1
	v_add_u32_e32 v2, 0x14a0, v45
	ds_write2_b32 v4, v16, v17 offset1:1
	ds_write2_b32 v2, v24, v25 offset1:1
	v_add_u32_e32 v2, 0x14a8, v45
	ds_write2_b32 v2, v26, v27 offset1:1
	v_add_u32_e32 v2, 0x18c0, v45
	ds_write2_b32 v2, v28, v29 offset1:1
	v_add_u32_e32 v2, 0x18c8, v45
	ds_write2_b32 v2, v30, v31 offset1:1
	v_add_u32_e32 v2, 0x1ce0, v45
	ds_write2_b32 v2, v32, v33 offset1:1
	v_add_u32_e32 v2, 0x1ce8, v45
	ds_write2_b32 v2, v34, v35 offset1:1
	s_waitcnt lgkmcnt(0)
	ds_read2_b32 v[10:11], v50 offset0:33 offset1:41
	ds_read2_b32 v[12:13], v50 offset1:8
	v_lshlrev_b32_e32 v2, 1, v38
	ds_read2_b32 v[14:15], v50 offset0:66 offset1:74
	ds_read2_b32 v[16:17], v50 offset0:99 offset1:107
	ds_read2_b32 v[18:19], v50 offset0:132 offset1:140
	ds_read2_b32 v[20:21], v50 offset0:165 offset1:173
	ds_read2_b32 v[22:23], v50 offset0:198 offset1:206
	ds_read2_b32 v[24:25], v50 offset0:231 offset1:239
	v_lshl_add_u64 v[4:5], s[6:7], 0, v[2:3]
	v_or_b32_e32 v2, s2, v39
	v_lshlrev_b32_e32 v2, 12, v2
	v_lshl_add_u64 v[26:27], v[4:5], 0, v[2:3]
	v_or_b32_e32 v2, s2, v46
	s_waitcnt lgkmcnt(0)
	v_cvt_pk_bf16_f32 v6, v12, v10
	v_lshlrev_b32_e32 v2, 12, v2
	v_cvt_pk_bf16_f32 v7, v14, v16
	v_cvt_pk_bf16_f32 v8, v18, v20
	v_cvt_pk_bf16_f32 v9, v22, v24
	global_store_dwordx4 v[26:27], v[6:9], off sc1
	s_nop 1
	v_cvt_pk_bf16_f32 v6, v13, v11
	v_lshl_add_u64 v[10:11], v[4:5], 0, v[2:3]
	v_cvt_pk_bf16_f32 v7, v15, v17
	v_cvt_pk_bf16_f32 v8, v19, v21
	v_cvt_pk_bf16_f32 v9, v23, v25
	global_store_dwordx4 v[10:11], v[6:9], off sc1
	ds_read2_b32 v[10:11], v50 offset0:16 offset1:24
	ds_read2_b32 v[12:13], v50 offset0:49 offset1:57
	ds_read2_b32 v[14:15], v50 offset0:82 offset1:90
	ds_read2_b32 v[16:17], v50 offset0:115 offset1:123
	ds_read2_b32 v[18:19], v50 offset0:148 offset1:156
	ds_read2_b32 v[20:21], v50 offset0:181 offset1:189
	ds_read2_b32 v[22:23], v50 offset0:214 offset1:222
	ds_read2_b32 v[24:25], v50 offset0:247 offset1:255
	v_or_b32_e32 v2, s2, v48
	v_lshlrev_b32_e32 v2, 12, v2
	v_lshl_add_u64 v[26:27], v[4:5], 0, v[2:3]
	v_or_b32_e32 v2, s2, v49
	v_lshlrev_b32_e32 v2, 12, v2
	s_waitcnt lgkmcnt(6)
	v_cvt_pk_bf16_f32 v6, v10, v12
	s_waitcnt lgkmcnt(4)
	v_cvt_pk_bf16_f32 v7, v14, v16
	s_waitcnt lgkmcnt(2)
	v_cvt_pk_bf16_f32 v8, v18, v20
	s_waitcnt lgkmcnt(0)
	v_cvt_pk_bf16_f32 v9, v22, v24
	v_lshl_add_u64 v[4:5], v[4:5], 0, v[2:3]
	global_store_dwordx4 v[26:27], v[6:9], off sc1
	s_nop 1
	v_cvt_pk_bf16_f32 v6, v11, v13
	v_cvt_pk_bf16_f32 v7, v15, v17
	v_cvt_pk_bf16_f32 v8, v19, v21
	v_cvt_pk_bf16_f32 v9, v23, v25
	global_store_dwordx4 v[4:5], v[6:9], off sc1
	s_waitcnt lgkmcnt(0)

; #define GAS __attribute__((address_space(1)))
; #define LAS __attribute__((address_space(3)))
; #define LDS_WAIT() asm volatile("s_waitcnt lgkmcnt(0)" ::: "memory")
; __device__ __forceinline__ unsigned pk2(float lo, float hi) { unsigned r; asm("v_cvt_pk_bf16_f32 %0, %1, %2" : "=v"(r) : "v"(lo), "v"(hi)); return r; }
; __device__ __forceinline__ void transpose_item(const float* W, int K, int N, bf16* WT, int drow0, int kb, int n0, LAS float* scr, int lane) {
;     const int k0 = 64 * kb; const int c4 = 4 * (lane & 7); const bool ok = (n0 + c4) < N;
;     f32x4 v[8];
; #pragma unroll
;     for (int i = 0; i < 8; ++i) { const int kk = 8 * i + (lane >> 3); v[i] = ok ? *(const f32x4*)(W + (size_t)(k0 + kk) * N + n0 + c4) : (f32x4){0.f, 0.f, 0.f, 0.f}; }
; #pragma unroll
;     for (int i = 0; i < 8; ++i) { const int kk = 8 * i + (lane >> 3); LAS float* d = scr + kk * 33 + c4; d[0] = v[i][0]; d[1] = v[i][1]; d[2] = v[i][2]; d[3] = v[i][3]; }
;     LDS_WAIT(); asm volatile("" ::: "memory");
;     const int c = lane & 7;
; #pragma unroll
;     for (int j = 0; j < 4; ++j) { const int n = (lane >> 3) + 8 * j; const LAS float* s = scr + (8 * c) * 33 + n;
;         v4u o; o.x = pk2(s[0 * 33], s[1 * 33]); o.y = pk2(s[2 * 33], s[3 * 33]); o.z = pk2(s[4 * 33], s[5 * 33]); o.w = pk2(s[6 * 33], s[7 * 33]);
;         *(GAS v4u*)(WT + (size_t)(drow0 + n) * K + k0 + 8 * c) = o; }
;     LDS_WAIT(); asm volatile("" ::: "memory");
; }
; __device__ __forceinline__ void convert_item(const In& I, unsigned char* ws, int it, LAS float* scr, int lane) {
;     ...
;     if (r < 2 * I_SQ) { const int j = r / I_SQ; r -= j * I_SQ; const int kb = r / 32, nb = r % 32;
;         transpose_item(I.fox_w_out + (size_t)j * D * D, D, D, Wfout + (size_t)j * D * D, 32 * nb, kb, 32 * nb, scr, lane); return; }
.LBB0_426:
	s_andn2_b64 vcc, exec, s[2:3]
	s_cbranch_vccnz .LBB0_428
	s_add_i32 s2, s41, 0x800
	s_lshr_b32 s68, s2, 9
	v_readlane_b32 s44, v253, 16
	s_lshl_b64 s[2:3], s[68:69], 22
	v_readlane_b32 s56, v253, 28
	v_readlane_b32 s57, v253, 29
	s_add_u32 s8, s56, s2
	s_addc_u32 s9, s57, s3
	s_lshl_b64 s[6:7], s[68:69], 21
	s_add_u32 s3, s26, s6
	s_addc_u32 s6, s27, s7
	s_and_b32 s2, s42, 0x3e0
	s_add_i32 s7, s0, 0x14000
	s_and_b32 s7, s7, 0x3c0
	s_lshl_b32 s10, s2, 2
	s_add_u32 s8, s8, s10
	v_or_b32_e32 v6, s7, v39
	s_addc_u32 s9, s9, 0
	v_lshlrev_b32_e32 v2, 2, v36
	v_lshl_add_u64 v[4:5], s[8:9], 0, v[2:3]
	v_lshlrev_b32_e32 v2, 12, v6
	v_lshl_add_u64 v[32:33], v[4:5], 0, v[2:3]
	v_add_co_u32_e32 v8, vcc, s81, v32
	global_load_dwordx4 v[4:7], v[32:33], off
	s_nop 0
	v_addc_co_u32_e32 v9, vcc, 0, v33, vcc
	v_add_co_u32_e32 v12, vcc, s79, v32
	global_load_dwordx4 v[8:11], v[8:9], off
	s_nop 0
	v_addc_co_u32_e32 v13, vcc, 0, v33, vcc
	v_add_co_u32_e32 v16, vcc, s80, v32
	global_load_dwordx4 v[12:15], v[12:13], off
	s_nop 0
	v_addc_co_u32_e32 v17, vcc, 0, v33, vcc
	v_add_co_u32_e32 v20, vcc, s85, v32
	global_load_dwordx4 v[16:19], v[16:17], off
	s_nop 0
	v_addc_co_u32_e32 v21, vcc, 0, v33, vcc
	global_load_dwordx4 v[20:23], v[20:21], off
	v_add_co_u32_e32 v24, vcc, s86, v32
	v_add_u32_e32 v2, v44, v47
	s_nop 0
	v_addc_co_u32_e32 v25, vcc, 0, v33, vcc
	global_load_dwordx4 v[24:27], v[24:25], off
	v_add_co_u32_e32 v28, vcc, s87, v32
	s_lshl_b32 s7, s7, 1
	s_nop 0
	v_addc_co_u32_e32 v29, vcc, 0, v33, vcc
	global_load_dwordx4 v[28:31], v[28:29], off
	v_add_co_u32_e32 v32, vcc, s89, v32
	s_add_u32 s8, s3, s7
	s_nop 0
	v_addc_co_u32_e32 v33, vcc, 0, v33, vcc
	global_load_dwordx4 v[32:35], v[32:33], off
	s_addc_u32 s9, s6, 0
	v_readlane_b32 s45, v253, 17
	v_readlane_b32 s46, v253, 18
	v_readlane_b32 s47, v253, 19
	v_readlane_b32 s48, v253, 20
	v_readlane_b32 s49, v253, 21
	v_readlane_b32 s50, v253, 22
	v_readlane_b32 s51, v253, 23
	v_readlane_b32 s52, v253, 24
	v_readlane_b32 s53, v253, 25
	v_readlane_b32 s54, v253, 26
	v_readlane_b32 s55, v253, 27
	v_readlane_b32 s58, v253, 30
	v_readlane_b32 s59, v253, 31
	s_waitcnt vmcnt(0)
	ds_write2_b32 v45, v4, v5 offset1:1
	ds_write2_b32 v45, v6, v7 offset0:2 offset1:3
	v_add_u32_e32 v4, 0x420, v2
	ds_write2_b32 v2, v8, v9 offset1:1
	ds_write2_b32 v2, v10, v11 offset0:2 offset1:3
	ds_write2_b32 v4, v12, v13 offset1:1
	v_add_u32_e32 v4, 0x428, v2
	ds_write2_b32 v4, v14, v15 offset1:1
	v_add_u32_e32 v4, 0x840, v2
	v_add_u32_e32 v2, 0x848, v2
	ds_write2_b32 v2, v18, v19 offset1:1
	v_add_u32_e32 v2, 0x1080, v45
	ds_write2_b32 v4, v16, v17 offset1:1
	ds_write2_b32 v2, v20, v21 offset1:1
	v_add_u32_e32 v2, 0x1088, v45
	ds_write2_b32 v2, v22, v23 offset1:1
	v_add_u32_e32 v2, 0x14a0, v45
	ds_write2_b32 v2, v24, v25 offset1:1
	v_add_u32_e32 v2, 0x14a8, v45
	ds_write2_b32 v2, v26, v27 offset1:1
	v_add_u32_e32 v2, 0x18c0, v45
	ds_write2_b32 v2, v28, v29 offset1:1
	v_add_u32_e32 v2, 0x18c8, v45
	ds_write2_b32 v2, v30, v31 offset1:1
	v_add_u32_e32 v2, 0x1ce0, v45
	ds_write2_b32 v2, v32, v33 offset1:1
	v_add_u32_e32 v2, 0x1ce8, v45
	ds_write2_b32 v2, v34, v35 offset1:1
	s_waitcnt lgkmcnt(0)
	ds_read2_b32 v[10:11], v50 offset0:33 offset1:41
	ds_read2_b32 v[12:13], v50 offset1:8
	v_lshlrev_b32_e32 v2, 1, v38
	ds_read2_b32 v[14:15], v50 offset0:66 offset1:74
	ds_read2_b32 v[16:17], v50 offset0:99 offset1:107
	ds_read2_b32 v[18:19], v50 offset0:132 offset1:140
	ds_read2_b32 v[20:21], v50 offset0:165 offset1:173
	ds_read2_b32 v[22:23], v50 offset0:198 offset1:206
	ds_read2_b32 v[24:25], v50 offset0:231 offset1:239
	v_lshl_add_u64 v[8:9], s[8:9], 0, v[2:3]
	v_or_b32_e32 v2, s2, v39
	v_lshlrev_b32_e32 v2, 11, v2
	v_lshl_add_u64 v[26:27], v[8:9], 0, v[2:3]
	v_or_b32_e32 v2, s2, v46
	s_waitcnt lgkmcnt(0)
	v_cvt_pk_bf16_f32 v4, v12, v10
	v_lshlrev_b32_e32 v2, 11, v2
	v_cvt_pk_bf16_f32 v5, v14, v16
	v_cvt_pk_bf16_f32 v6, v18, v20
	v_cvt_pk_bf16_f32 v7, v22, v24
	global_store_dwordx4 v[26:27], v[4:7], off sc1
	s_nop 1
	v_cvt_pk_bf16_f32 v4, v13, v11
	v_lshl_add_u64 v[10:11], v[8:9], 0, v[2:3]
	v_cvt_pk_bf16_f32 v5, v15, v17
	v_cvt_pk_bf16_f32 v6, v19, v21
	v_cvt_pk_bf16_f32 v7, v23, v25
	global_store_dwordx4 v[10:11], v[4:7], off sc1
	ds_read2_b32 v[10:11], v50 offset0:16 offset1:24
	ds_read2_b32 v[12:13], v50 offset0:49 offset1:57
	ds_read2_b32 v[14:15], v50 offset0:82 offset1:90
	ds_read2_b32 v[16:17], v50 offset0:115 offset1:123
	ds_read2_b32 v[18:19], v50 offset0:148 offset1:156
	ds_read2_b32 v[20:21], v50 offset0:181 offset1:189
	ds_read2_b32 v[22:23], v50 offset0:214 offset1:222
	ds_read2_b32 v[24:25], v50 offset0:247 offset1:255
	v_or_b32_e32 v2, s2, v48
	v_lshlrev_b32_e32 v2, 11, v2
	v_lshl_add_u64 v[26:27], v[8:9], 0, v[2:3]
	v_or_b32_e32 v2, s2, v49
	v_lshlrev_b32_e32 v2, 11, v2
	s_waitcnt lgkmcnt(6)
	v_cvt_pk_bf16_f32 v4, v10, v12
	s_waitcnt lgkmcnt(4)
	v_cvt_pk_bf16_f32 v5, v14, v16
	s_waitcnt lgkmcnt(2)
	v_cvt_pk_bf16_f32 v6, v18, v20
	s_waitcnt lgkmcnt(0)
	v_cvt_pk_bf16_f32 v7, v22, v24
	v_lshl_add_u64 v[8:9], v[8:9], 0, v[2:3]
	global_store_dwordx4 v[26:27], v[4:7], off sc1
	s_nop 1
	v_cvt_pk_bf16_f32 v4, v11, v13
	v_cvt_pk_bf16_f32 v5, v15, v17
	v_cvt_pk_bf16_f32 v6, v19, v21
	v_cvt_pk_bf16_f32 v7, v23, v25
	global_store_dwordx4 v[8:9], v[4:7], off sc1
	s_waitcnt lgkmcnt(0)

; #define GAS __attribute__((address_space(1)))
; #define LAS __attribute__((address_space(3)))
; #define LDS_WAIT() asm volatile("s_waitcnt lgkmcnt(0)" ::: "memory")
; __device__ __forceinline__ unsigned pk2(float lo, float hi) { unsigned r; asm("v_cvt_pk_bf16_f32 %0, %1, %2" : "=v"(r) : "v"(lo), "v"(hi)); return r; }
; __device__ __forceinline__ void transpose_item(const float* W, int K, int N, bf16* WT, int drow0, int kb, int n0, LAS float* scr, int lane) {
;     const int k0 = 64 * kb; const int c4 = 4 * (lane & 7); const bool ok = (n0 + c4) < N;
;     f32x4 v[8];
; #pragma unroll
;     for (int i = 0; i < 8; ++i) { const int kk = 8 * i + (lane >> 3); v[i] = ok ? *(const f32x4*)(W + (size_t)(k0 + kk) * N + n0 + c4) : (f32x4){0.f, 0.f, 0.f, 0.f}; }
; #pragma unroll
;     for (int i = 0; i < 8; ++i) { const int kk = 8 * i + (lane >> 3); LAS float* d = scr + kk * 33 + c4; d[0] = v[i][0]; d[1] = v[i][1]; d[2] = v[i][2]; d[3] = v[i][3]; }
;     LDS_WAIT(); asm volatile("" ::: "memory");
;     const int c = lane & 7;
; #pragma unroll
;     for (int j = 0; j < 4; ++j) { const int n = (lane >> 3) + 8 * j; const LAS float* s = scr + (8 * c) * 33 + n;
;         v4u o; o.x = pk2(s[0 * 33], s[1 * 33]); o.y = pk2(s[2 * 33], s[3 * 33]); o.z = pk2(s[4 * 33], s[5 * 33]); o.w = pk2(s[6 * 33], s[7 * 33]);
;         *(GAS v4u*)(WT + (size_t)(drow0 + n) * K + k0 + 8 * c) = o; }
;     LDS_WAIT(); asm volatile("" ::: "memory");
; }
; __device__ __forceinline__ void convert_item(const In& I, unsigned char* ws, int it, LAS float* scr, int lane) {
;     ...
;     if (r < 2 * I_SQ) { const int j = r / I_SQ; r -= j * I_SQ; const int kb = r / 32, nb = r % 32;
;         transpose_item(I.nsa_w_out + (size_t)j * D * D, D, D, Wnout + (size_t)j * D * D, 32 * nb, kb, 32 * nb, scr, lane); return; }
.LBB0_448:
	s_andn2_b64 vcc, exec, s[2:3]
	s_cbranch_vccnz .LBB0_450
	s_add_i32 s2, s41, 0x1900
	s_lshr_b32 s68, s2, 9
	v_readlane_b32 s44, v253, 16
	s_lshl_b64 s[2:3], s[68:69], 22
	v_readlane_b32 s50, v253, 22
	v_readlane_b32 s51, v253, 23
	s_add_u32 s8, s50, s2
	s_addc_u32 s9, s51, s3
	s_lshl_b64 s[6:7], s[68:69], 21
	s_add_u32 s3, s22, s6
	s_addc_u32 s6, s23, s7
	s_and_b32 s2, s42, 0x3e0
	s_add_i32 s7, s0, 0x2200
	s_and_b32 s7, s7, 0x3c0
	s_lshl_b32 s10, s2, 2
	s_add_u32 s8, s8, s10
	v_or_b32_e32 v6, s7, v39
	s_addc_u32 s9, s9, 0
	v_lshlrev_b32_e32 v2, 2, v36
	v_lshl_add_u64 v[4:5], s[8:9], 0, v[2:3]
	v_lshlrev_b32_e32 v2, 12, v6
	v_lshl_add_u64 v[32:33], v[4:5], 0, v[2:3]
	v_add_co_u32_e32 v8, vcc, s81, v32
	global_load_dwordx4 v[4:7], v[32:33], off
	s_nop 0
	v_addc_co_u32_e32 v9, vcc, 0, v33, vcc
	v_add_co_u32_e32 v12, vcc, s79, v32
	global_load_dwordx4 v[8:11], v[8:9], off
	s_nop 0
	v_addc_co_u32_e32 v13, vcc, 0, v33, vcc
	v_add_co_u32_e32 v16, vcc, s80, v32
	global_load_dwordx4 v[12:15], v[12:13], off
	s_nop 0
	v_addc_co_u32_e32 v17, vcc, 0, v33, vcc
	v_add_co_u32_e32 v20, vcc, s85, v32
	global_load_dwordx4 v[16:19], v[16:17], off
	s_nop 0
	v_addc_co_u32_e32 v21, vcc, 0, v33, vcc
	global_load_dwordx4 v[20:23], v[20:21], off
	v_add_co_u32_e32 v24, vcc, s86, v32
	v_add_u32_e32 v2, v44, v47
	s_nop 0
	v_addc_co_u32_e32 v25, vcc, 0, v33, vcc
	global_load_dwordx4 v[24:27], v[24:25], off
	v_add_co_u32_e32 v28, vcc, s87, v32
	s_lshl_b32 s7, s7, 1
	s_nop 0
	v_addc_co_u32_e32 v29, vcc, 0, v33, vcc
	global_load_dwordx4 v[28:31], v[28:29], off
	v_add_co_u32_e32 v32, vcc, s89, v32
	s_add_u32 s8, s3, s7
	s_nop 0
	v_addc_co_u32_e32 v33, vcc, 0, v33, vcc
	global_load_dwordx4 v[32:35], v[32:33], off
	s_addc_u32 s9, s6, 0
	v_readlane_b32 s45, v253, 17
	v_readlane_b32 s46, v253, 18
	v_readlane_b32 s47, v253, 19
	v_readlane_b32 s48, v253, 20
	v_readlane_b32 s49, v253, 21
	v_readlane_b32 s52, v253, 24
	v_readlane_b32 s53, v253, 25
	v_readlane_b32 s54, v253, 26
	v_readlane_b32 s55, v253, 27
	v_readlane_b32 s56, v253, 28
	v_readlane_b32 s57, v253, 29
	v_readlane_b32 s58, v253, 30
	v_readlane_b32 s59, v253, 31
	s_waitcnt vmcnt(0)
	ds_write2_b32 v45, v4, v5 offset1:1
	ds_write2_b32 v45, v6, v7 offset0:2 offset1:3
	v_add_u32_e32 v4, 0x420, v2
	ds_write2_b32 v2, v8, v9 offset1:1
	ds_write2_b32 v2, v10, v11 offset0:2 offset1:3
	ds_write2_b32 v4, v12, v13 offset1:1
	v_add_u32_e32 v4, 0x428, v2
	ds_write2_b32 v4, v14, v15 offset1:1
	v_add_u32_e32 v4, 0x840, v2
	v_add_u32_e32 v2, 0x848, v2
	ds_write2_b32 v2, v18, v19 offset1:1
	v_add_u32_e32 v2, 0x1080, v45
	ds_write2_b32 v4, v16, v17 offset1:1
	ds_write2_b32 v2, v20, v21 offset1:1
	v_add_u32_e32 v2, 0x1088, v45
	ds_write2_b32 v2, v22, v23 offset1:1
	v_add_u32_e32 v2, 0x14a0, v45
	ds_write2_b32 v2, v24, v25 offset1:1
	v_add_u32_e32 v2, 0x14a8, v45
	ds_write2_b32 v2, v26, v27 offset1:1
	v_add_u32_e32 v2, 0x18c0, v45
	ds_write2_b32 v2, v28, v29 offset1:1
	v_add_u32_e32 v2, 0x18c8, v45
	ds_write2_b32 v2, v30, v31 offset1:1
	v_add_u32_e32 v2, 0x1ce0, v45
	ds_write2_b32 v2, v32, v33 offset1:1
	v_add_u32_e32 v2, 0x1ce8, v45
	ds_write2_b32 v2, v34, v35 offset1:1
	s_waitcnt lgkmcnt(0)
	ds_read2_b32 v[10:11], v50 offset0:33 offset1:41
	ds_read2_b32 v[12:13], v50 offset1:8
	v_lshlrev_b32_e32 v2, 1, v38
	ds_read2_b32 v[14:15], v50 offset0:66 offset1:74
	ds_read2_b32 v[16:17], v50 offset0:99 offset1:107
	ds_read2_b32 v[18:19], v50 offset0:132 offset1:140
	ds_read2_b32 v[20:21], v50 offset0:165 offset1:173
	ds_read2_b32 v[22:23], v50 offset0:198 offset1:206
	ds_read2_b32 v[24:25], v50 offset0:231 offset1:239
	v_lshl_add_u64 v[8:9], s[8:9], 0, v[2:3]
	v_or_b32_e32 v2, s2, v39
	v_lshlrev_b32_e32 v2, 11, v2
	v_lshl_add_u64 v[26:27], v[8:9], 0, v[2:3]
	v_or_b32_e32 v2, s2, v46
	s_waitcnt lgkmcnt(0)
	v_cvt_pk_bf16_f32 v4, v12, v10
	v_lshlrev_b32_e32 v2, 11, v2
	v_cvt_pk_bf16_f32 v5, v14, v16
	v_cvt_pk_bf16_f32 v6, v18, v20
	v_cvt_pk_bf16_f32 v7, v22, v24
	global_store_dwordx4 v[26:27], v[4:7], off sc1
	s_nop 1
	v_cvt_pk_bf16_f32 v4, v13, v11
	v_lshl_add_u64 v[10:11], v[8:9], 0, v[2:3]
	v_cvt_pk_bf16_f32 v5, v15, v17
	v_cvt_pk_bf16_f32 v6, v19, v21
	v_cvt_pk_bf16_f32 v7, v23, v25
	global_store_dwordx4 v[10:11], v[4:7], off sc1
	ds_read2_b32 v[10:11], v50 offset0:16 offset1:24
	ds_read2_b32 v[12:13], v50 offset0:49 offset1:57
	ds_read2_b32 v[14:15], v50 offset0:82 offset1:90
	ds_read2_b32 v[16:17], v50 offset0:115 offset1:123
	ds_read2_b32 v[18:19], v50 offset0:148 offset1:156
	ds_read2_b32 v[20:21], v50 offset0:181 offset1:189
	ds_read2_b32 v[22:23], v50 offset0:214 offset1:222
	ds_read2_b32 v[24:25], v50 offset0:247 offset1:255
	v_or_b32_e32 v2, s2, v48
	v_lshlrev_b32_e32 v2, 11, v2
	v_lshl_add_u64 v[26:27], v[8:9], 0, v[2:3]
	v_or_b32_e32 v2, s2, v49
	v_lshlrev_b32_e32 v2, 11, v2
	s_waitcnt lgkmcnt(6)
	v_cvt_pk_bf16_f32 v4, v10, v12
	s_waitcnt lgkmcnt(4)
	v_cvt_pk_bf16_f32 v5, v14, v16
	s_waitcnt lgkmcnt(2)
	v_cvt_pk_bf16_f32 v6, v18, v20
	s_waitcnt lgkmcnt(0)
	v_cvt_pk_bf16_f32 v7, v22, v24
	v_lshl_add_u64 v[8:9], v[8:9], 0, v[2:3]
	global_store_dwordx4 v[26:27], v[4:7], off sc1
	s_nop 1
	v_cvt_pk_bf16_f32 v4, v11, v13
	v_cvt_pk_bf16_f32 v5, v15, v17
	v_cvt_pk_bf16_f32 v6, v19, v21
	v_cvt_pk_bf16_f32 v7, v23, v25
	global_store_dwordx4 v[8:9], v[4:7], off sc1
	s_waitcnt lgkmcnt(0)

; #define GAS __attribute__((address_space(1)))
; #define LAS __attribute__((address_space(3)))
; #define LDS_WAIT() asm volatile("s_waitcnt lgkmcnt(0)" ::: "memory")
; __device__ __forceinline__ unsigned pk2(float lo, float hi) { unsigned r; asm("v_cvt_pk_bf16_f32 %0, %1, %2" : "=v"(r) : "v"(lo), "v"(hi)); return r; }
; __device__ __forceinline__ void transpose_item(const float* W, int K, int N, bf16* WT, int drow0, int kb, int n0, LAS float* scr, int lane) {
;     const int k0 = 64 * kb; const int c4 = 4 * (lane & 7); const bool ok = (n0 + c4) < N;
;     f32x4 v[8];
; #pragma unroll
;     for (int i = 0; i < 8; ++i) { const int kk = 8 * i + (lane >> 3); v[i] = ok ? *(const f32x4*)(W + (size_t)(k0 + kk) * N + n0 + c4) : (f32x4){0.f, 0.f, 0.f, 0.f}; }
; #pragma unroll
;     for (int i = 0; i < 8; ++i) { const int kk = 8 * i + (lane >> 3); LAS float* d = scr + kk * 33 + c4; d[0] = v[i][0]; d[1] = v[i][1]; d[2] = v[i][2]; d[3] = v[i][3]; }
;     LDS_WAIT(); asm volatile("" ::: "memory");
;     const int c = lane & 7;
; #pragma unroll
;     for (int j = 0; j < 4; ++j) { const int n = (lane >> 3) + 8 * j; const LAS float* s = scr + (8 * c) * 33 + n;
;         v4u o; o.x = pk2(s[0 * 33], s[1 * 33]); o.y = pk2(s[2 * 33], s[3 * 33]); o.z = pk2(s[4 * 33], s[5 * 33]); o.w = pk2(s[6 * 33], s[7 * 33]);
;         *(GAS v4u*)(WT + (size_t)(drow0 + n) * K + k0 + 8 * c) = o; }
;     LDS_WAIT(); asm volatile("" ::: "memory");
; }
; __device__ __forceinline__ void convert_item(const In& I, unsigned char* ws, int it, LAS float* scr, int lane) {
;     ...
;     if (r < T0) { const int f = r / I_FFN; r -= f * I_FFN;
;         if (r < 2 * I_G) { const int up = r >= I_G; r -= up * I_G; const int kb = r / 88, nb = r % 88;
;             transpose_item((up ? I.w_up : I.w_gate) + (size_t)f * D * FF, D, FF, Wgu + (size_t)f * NGU * D, 256 * (nb >> 2) + 32 * (nb & 3) + 128 * up, kb, 32 * nb, scr, lane); }
;         else { r -= 2 * I_G; const int kb = r / 32, nb = r % 32; transpose_item(I.w_down + (size_t)f * FF * D, FF, D, Wd + (size_t)f * D * FF, 32 * nb, kb, 32 * nb, scr, lane); }
.LBB0_470:
	s_andn2_b64 vcc, exec, s[2:3]
	s_cbranch_vccnz .LBB0_415
	s_mul_hi_i32 s2, s43, 0x3e0f83e1
	s_lshr_b32 s3, s2, 31
	s_ashr_i32 s6, s2, 10
	s_add_i32 s6, s6, s3
	s_mul_i32 s2, s6, 0xffffef80
	s_add_i32 s7, s41, s2
	s_add_i32 s7, s7, 0xa800
	s_cmpk_gt_i32 s7, 0xaff
	s_mov_b64 s[2:3], -1
	s_cbranch_scc0 .LBB0_473
	v_readlane_b32 s44, v253, 0
	s_mul_i32 s3, s6, 0xb00000
	v_readlane_b32 s52, v253, 8
	s_mul_hi_i32 s2, s6, 0xb00000
	v_readlane_b32 s53, v253, 9
	s_add_u32 s9, s52, s3
	s_addc_u32 s11, s53, s2
	s_mul_i32 s3, s6, 0x580000
	s_mul_hi_i32 s2, s6, 0x580000
	s_add_u32 s3, s1, s3
	s_mul_i32 s10, s6, 0xffffdf00
	s_addc_u32 s8, s19, s2
	s_add_i32 s10, s0, s10
	s_add_i32 s10, s10, 0x14000
	s_and_b32 s2, s42, 0x3e0
	s_andn2_b32 s10, s10, 63
	s_add_i32 s68, s10, 0xffffea00
	s_lshl_b32 s10, s2, 2
	v_or_b32_e32 v32, s68, v39
	s_add_u32 s10, s9, s10
	s_addc_u32 s11, s11, 0
	v_lshlrev_b32_e32 v2, 2, v36
	v_ashrrev_i32_e32 v33, 31, v32
	v_or_b32_e32 v8, 8, v32
	v_or_b32_e32 v12, 16, v32
	v_lshl_add_u64 v[34:35], s[10:11], 0, v[2:3]
	v_lshlrev_b64 v[4:5], 12, v[32:33]
	v_ashrrev_i32_e32 v9, 31, v8
	v_ashrrev_i32_e32 v13, 31, v12
	v_lshl_add_u64 v[4:5], v[34:35], 0, v[4:5]
	v_lshlrev_b64 v[8:9], 12, v[8:9]
	v_lshlrev_b64 v[12:13], 12, v[12:13]
	v_or_b32_e32 v16, 24, v32
	global_load_dwordx4 v[4:7], v[4:5], off
	v_lshl_add_u64 v[8:9], v[34:35], 0, v[8:9]
	v_lshl_add_u64 v[12:13], v[34:35], 0, v[12:13]
	v_ashrrev_i32_e32 v17, 31, v16
	v_or_b32_e32 v20, 32, v32
	global_load_dwordx4 v[8:11], v[8:9], off
	v_lshlrev_b64 v[16:17], 12, v[16:17]
	global_load_dwordx4 v[12:15], v[12:13], off
	v_ashrrev_i32_e32 v21, 31, v20
	v_lshl_add_u64 v[16:17], v[34:35], 0, v[16:17]
	v_lshlrev_b64 v[20:21], 12, v[20:21]
	v_or_b32_e32 v24, 40, v32
	global_load_dwordx4 v[16:19], v[16:17], off
	v_lshl_add_u64 v[20:21], v[34:35], 0, v[20:21]
	v_ashrrev_i32_e32 v25, 31, v24
	global_load_dwordx4 v[20:23], v[20:21], off
	v_lshlrev_b64 v[24:25], 12, v[24:25]
	v_or_b32_e32 v28, 48, v32
	v_lshl_add_u64 v[24:25], v[34:35], 0, v[24:25]
	v_ashrrev_i32_e32 v29, 31, v28
	global_load_dwordx4 v[24:27], v[24:25], off
	v_lshlrev_b64 v[28:29], 12, v[28:29]
	v_or_b32_e32 v32, 56, v32
	v_lshl_add_u64 v[28:29], v[34:35], 0, v[28:29]
	v_ashrrev_i32_e32 v33, 31, v32
	global_load_dwordx4 v[28:31], v[28:29], off
	v_lshlrev_b64 v[32:33], 12, v[32:33]
	v_lshl_add_u64 v[32:33], v[34:35], 0, v[32:33]
	global_load_dwordx4 v[32:35], v[32:33], off
	v_add_u32_e32 v2, v44, v47
	s_lshl_b64 s[10:11], s[68:69], 1
	s_add_u32 s10, s3, s10
	s_addc_u32 s11, s8, s11
	v_readlane_b32 s45, v253, 1
	v_readlane_b32 s46, v253, 2
	v_readlane_b32 s47, v253, 3
	v_readlane_b32 s48, v253, 4
	v_readlane_b32 s49, v253, 5
	v_readlane_b32 s50, v253, 6
	v_readlane_b32 s51, v253, 7
	v_readlane_b32 s54, v253, 10
	v_readlane_b32 s55, v253, 11
	v_readlane_b32 s56, v253, 12
	v_readlane_b32 s57, v253, 13
	v_readlane_b32 s58, v253, 14
	v_readlane_b32 s59, v253, 15
	s_waitcnt vmcnt(0)
	ds_write2_b32 v45, v4, v5 offset1:1
	ds_write2_b32 v45, v6, v7 offset0:2 offset1:3
	v_add_u32_e32 v4, 0x420, v2
	ds_write2_b32 v2, v8, v9 offset1:1
	ds_write2_b32 v2, v10, v11 offset0:2 offset1:3
	ds_write2_b32 v4, v12, v13 offset1:1
	v_add_u32_e32 v4, 0x428, v2
	ds_write2_b32 v4, v14, v15 offset1:1
	v_add_u32_e32 v4, 0x840, v2
	v_add_u32_e32 v2, 0x848, v2
	ds_write2_b32 v2, v18, v19 offset1:1
	v_add_u32_e32 v2, 0x1080, v45
	ds_write2_b32 v4, v16, v17 offset1:1
	ds_write2_b32 v2, v20, v21 offset1:1
	v_add_u32_e32 v2, 0x1088, v45
	ds_write2_b32 v2, v22, v23 offset1:1
	v_add_u32_e32 v2, 0x14a0, v45
	ds_write2_b32 v2, v24, v25 offset1:1
	v_add_u32_e32 v2, 0x14a8, v45
	ds_write2_b32 v2, v26, v27 offset1:1
	v_add_u32_e32 v2, 0x18c0, v45
	ds_write2_b32 v2, v28, v29 offset1:1
	v_add_u32_e32 v2, 0x18c8, v45
	ds_write2_b32 v2, v30, v31 offset1:1
	v_add_u32_e32 v2, 0x1ce0, v45
	ds_write2_b32 v2, v32, v33 offset1:1
	v_add_u32_e32 v2, 0x1ce8, v45
	ds_write2_b32 v2, v34, v35 offset1:1
	s_waitcnt lgkmcnt(0)
	ds_read2_b32 v[10:11], v50 offset0:33 offset1:41
	ds_read2_b32 v[12:13], v50 offset1:8
	v_lshlrev_b32_e32 v2, 1, v38
	ds_read2_b32 v[14:15], v50 offset0:66 offset1:74
	ds_read2_b32 v[16:17], v50 offset0:99 offset1:107
	ds_read2_b32 v[18:19], v50 offset0:132 offset1:140
	ds_read2_b32 v[20:21], v50 offset0:165 offset1:173
	ds_read2_b32 v[22:23], v50 offset0:198 offset1:206
	ds_read2_b32 v[24:25], v50 offset0:231 offset1:239
	v_lshl_add_u64 v[8:9], s[10:11], 0, v[2:3]
	v_or_b32_e32 v2, s2, v39
	v_mul_u32_u24_e32 v2, 0x1600, v2
	v_lshl_add_u64 v[26:27], v[8:9], 0, v[2:3]
	v_or_b32_e32 v2, s2, v46
	s_waitcnt lgkmcnt(0)
	v_cvt_pk_bf16_f32 v4, v12, v10
	v_mul_u32_u24_e32 v2, 0x1600, v2
	v_cvt_pk_bf16_f32 v5, v14, v16
	v_cvt_pk_bf16_f32 v6, v18, v20
	v_cvt_pk_bf16_f32 v7, v22, v24
	global_store_dwordx4 v[26:27], v[4:7], off sc1
	s_nop 1
	v_cvt_pk_bf16_f32 v4, v13, v11
	v_lshl_add_u64 v[10:11], v[8:9], 0, v[2:3]
	v_cvt_pk_bf16_f32 v5, v15, v17
	v_cvt_pk_bf16_f32 v6, v19, v21
	v_cvt_pk_bf16_f32 v7, v23, v25
	global_store_dwordx4 v[10:11], v[4:7], off sc1
	ds_read2_b32 v[10:11], v50 offset0:16 offset1:24
	ds_read2_b32 v[12:13], v50 offset0:49 offset1:57
	ds_read2_b32 v[14:15], v50 offset0:82 offset1:90
	ds_read2_b32 v[16:17], v50 offset0:115 offset1:123
	ds_read2_b32 v[18:19], v50 offset0:148 offset1:156
	ds_read2_b32 v[20:21], v50 offset0:181 offset1:189
	ds_read2_b32 v[22:23], v50 offset0:214 offset1:222
	ds_read2_b32 v[24:25], v50 offset0:247 offset1:255
	v_or_b32_e32 v2, s2, v48
	v_mul_u32_u24_e32 v2, 0x1600, v2
	v_lshl_add_u64 v[26:27], v[8:9], 0, v[2:3]
	v_or_b32_e32 v2, s2, v49
	v_mul_u32_u24_e32 v2, 0x1600, v2
	s_waitcnt lgkmcnt(6)
	v_cvt_pk_bf16_f32 v4, v10, v12
	s_waitcnt lgkmcnt(4)
	v_cvt_pk_bf16_f32 v5, v14, v16
	s_waitcnt lgkmcnt(2)
	v_cvt_pk_bf16_f32 v6, v18, v20
	s_waitcnt lgkmcnt(0)
	v_cvt_pk_bf16_f32 v7, v22, v24
	v_lshl_add_u64 v[8:9], v[8:9], 0, v[2:3]
	global_store_dwordx4 v[26:27], v[4:7], off sc1
	s_mov_b64 s[2:3], 0
	s_nop 0
	v_cvt_pk_bf16_f32 v4, v11, v13
	v_cvt_pk_bf16_f32 v5, v15, v17
	v_cvt_pk_bf16_f32 v6, v19, v21
	v_cvt_pk_bf16_f32 v7, v23, v25
	global_store_dwordx4 v[8:9], v[4:7], off sc1
	s_waitcnt lgkmcnt(0)
; #define GAS __attribute__((address_space(1)))
; #define LAS __attribute__((address_space(3)))
; #define LDS_WAIT() asm volatile("s_waitcnt lgkmcnt(0)" ::: "memory")
; __device__ __forceinline__ unsigned pk2(float lo, float hi) { unsigned r; asm("v_cvt_pk_bf16_f32 %0, %1, %2" : "=v"(r) : "v"(lo), "v"(hi)); return r; }
; __device__ __forceinline__ void transpose_item(const float* W, int K, int N, bf16* WT, int drow0, int kb, int n0, LAS float* scr, int lane) {
;     const int k0 = 64 * kb; const int c4 = 4 * (lane & 7); const bool ok = (n0 + c4) < N;
;     f32x4 v[8];
; #pragma unroll
;     for (int i = 0; i < 8; ++i) { const int kk = 8 * i + (lane >> 3); v[i] = ok ? *(const f32x4*)(W + (size_t)(k0 + kk) * N + n0 + c4) : (f32x4){0.f, 0.f, 0.f, 0.f}; }
; #pragma unroll
;     for (int i = 0; i < 8; ++i) { const int kk = 8 * i + (lane >> 3); LAS float* d = scr + kk * 33 + c4; d[0] = v[i][0]; d[1] = v[i][1]; d[2] = v[i][2]; d[3] = v[i][3]; }
;     LDS_WAIT(); asm volatile("" ::: "memory");
;     const int c = lane & 7;
; #pragma unroll
;     for (int j = 0; j < 4; ++j) { const int n = (lane >> 3) + 8 * j; const LAS float* s = scr + (8 * c) * 33 + n;
;         v4u o; o.x = pk2(s[0 * 33], s[1 * 33]); o.y = pk2(s[2 * 33], s[3 * 33]); o.z = pk2(s[4 * 33], s[5 * 33]); o.w = pk2(s[6 * 33], s[7 * 33]);
;         *(GAS v4u*)(WT + (size_t)(drow0 + n) * K + k0 + 8 * c) = o; }
;     LDS_WAIT(); asm volatile("" ::: "memory");
; }
; __device__ __forceinline__ void convert_item(const In& I, unsigned char* ws, int it, LAS float* scr, int lane) {
;     ...
;         if (r < 2 * I_G) { const int up = r >= I_G; r -= up * I_G; const int kb = r / 88, nb = r % 88;
;             transpose_item((up ? I.w_up : I.w_gate) + (size_t)f * D * FF, D, FF, Wgu + (size_t)f * NGU * D, 256 * (nb >> 2) + 32 * (nb & 3) + 128 * up, kb, 32 * nb, scr, lane); }
.LBB0_473:
	s_andn2_b64 vcc, exec, s[2:3]
	s_cbranch_vccnz .LBB0_415
	s_cmpk_gt_i32 s7, 0x57f
	v_readlane_b32 s44, v253, 0
	s_cselect_b32 s2, 0xfffffa80, 0
	s_mul_i32 s3, s6, 0x1080
	v_readlane_b32 s48, v253, 4
	v_readlane_b32 s49, v253, 5
	v_readlane_b32 s50, v253, 6
	v_readlane_b32 s51, v253, 7
	s_cselect_b32 s9, 0x80, 0
	s_cselect_b32 s7, s50, s48
	s_cselect_b32 s8, s51, s49
	s_sub_i32 s2, s2, s3
	s_add_i32 s2, s41, s2
	s_add_i32 s2, s2, 0xa800
	s_mul_hi_i32 s3, s2, 0x2e8ba2e9
	s_lshr_b32 s10, s3, 31
	s_ashr_i32 s3, s3, 4
	s_add_i32 s3, s3, s10
	s_mul_i32 s10, s3, 0x58
	s_sub_i32 s2, s2, s10
	s_mul_hi_i32 s10, s6, 0xb00000
	s_mul_i32 s6, s6, 0xb00000
	s_add_u32 s12, s7, s6
	s_addc_u32 s13, s8, s10
	s_add_u32 s7, s28, s6
	s_addc_u32 s8, s29, s10
	s_lshl_b32 s10, s2, 5
	s_lshl_b32 s6, s2, 6
	s_and_b32 s2, s10, 0x60
	s_and_b32 s6, s6, 0xffffff00
	s_or_b32 s2, s2, s9
	s_ashr_i32 s11, s10, 31
	s_or_b32 s6, s2, s6
	s_lshl_b32 s2, s3, 6
	s_lshl_b64 s[10:11], s[10:11], 2
	s_add_u32 s10, s12, s10
	v_or_b32_e32 v34, s2, v39
	s_addc_u32 s11, s13, s11
	v_lshlrev_b32_e32 v2, 2, v36
	v_lshl_add_u64 v[32:33], s[10:11], 0, v[2:3]
	s_movk_i32 s3, 0x2c00
	v_or_b32_e32 v2, 8, v34
	v_mad_i64_i32 v[4:5], s[10:11], v34, s3, v[32:33]
	v_mad_i64_i32 v[8:9], s[10:11], v2, s3, v[32:33]
	v_or_b32_e32 v2, 16, v34
	global_load_dwordx4 v[4:7], v[4:5], off
	v_mad_i64_i32 v[12:13], s[10:11], v2, s3, v[32:33]
	global_load_dwordx4 v[8:11], v[8:9], off
	v_or_b32_e32 v2, 24, v34
	global_load_dwordx4 v[12:15], v[12:13], off
	v_mad_i64_i32 v[16:17], s[10:11], v2, s3, v[32:33]
	v_or_b32_e32 v2, 32, v34
	global_load_dwordx4 v[16:19], v[16:17], off
	v_mad_i64_i32 v[20:21], s[10:11], v2, s3, v[32:33]
	global_load_dwordx4 v[20:23], v[20:21], off
	v_or_b32_e32 v2, 40, v34
	v_mad_i64_i32 v[24:25], s[10:11], v2, s3, v[32:33]
	global_load_dwordx4 v[24:27], v[24:25], off
	v_or_b32_e32 v2, 48, v34
	v_mad_i64_i32 v[28:29], s[10:11], v2, s3, v[32:33]
	global_load_dwordx4 v[28:31], v[28:29], off
	v_or_b32_e32 v2, 56, v34
	v_mad_i64_i32 v[32:33], s[10:11], v2, s3, v[32:33]
	global_load_dwordx4 v[32:35], v[32:33], off
	v_add_u32_e32 v2, v44, v47
	s_ashr_i32 s3, s2, 31
	s_lshl_b64 s[2:3], s[2:3], 1
	s_add_u32 s2, s7, s2
	s_addc_u32 s3, s8, s3
	v_readlane_b32 s45, v253, 1
	v_readlane_b32 s46, v253, 2
	v_readlane_b32 s47, v253, 3
	v_readlane_b32 s52, v253, 8
	v_readlane_b32 s53, v253, 9
	v_readlane_b32 s54, v253, 10
	v_readlane_b32 s55, v253, 11
	v_readlane_b32 s56, v253, 12
	v_readlane_b32 s57, v253, 13
	v_readlane_b32 s58, v253, 14
	v_readlane_b32 s59, v253, 15
	s_waitcnt vmcnt(0)
	ds_write2_b32 v45, v4, v5 offset1:1
	ds_write2_b32 v45, v6, v7 offset0:2 offset1:3
	v_add_u32_e32 v4, 0x420, v2
	ds_write2_b32 v2, v8, v9 offset1:1
	ds_write2_b32 v2, v10, v11 offset0:2 offset1:3
	ds_write2_b32 v4, v12, v13 offset1:1
	v_add_u32_e32 v4, 0x428, v2
	ds_write2_b32 v4, v14, v15 offset1:1
	v_add_u32_e32 v4, 0x840, v2
	v_add_u32_e32 v2, 0x848, v2
	ds_write2_b32 v2, v18, v19 offset1:1
	v_add_u32_e32 v2, 0x1080, v45
	ds_write2_b32 v2, v20, v21 offset1:1
	v_add_u32_e32 v2, 0x1088, v45
	ds_write2_b32 v2, v22, v23 offset1:1
	v_add_u32_e32 v2, 0x14a0, v45
	ds_write2_b32 v2, v24, v25 offset1:1
	v_add_u32_e32 v2, 0x14a8, v45
	ds_write2_b32 v2, v26, v27 offset1:1
	v_add_u32_e32 v2, 0x18c0, v45
	ds_write2_b32 v2, v28, v29 offset1:1
	v_add_u32_e32 v2, 0x18c8, v45
	ds_write2_b32 v2, v30, v31 offset1:1
	v_add_u32_e32 v2, 0x1ce0, v45
	ds_write2_b32 v2, v32, v33 offset1:1
	v_add_u32_e32 v2, 0x1ce8, v45
	ds_write2_b32 v4, v16, v17 offset1:1
	ds_write2_b32 v2, v34, v35 offset1:1
	s_waitcnt lgkmcnt(0)
	ds_read2_b32 v[10:11], v50 offset0:33 offset1:41
	ds_read2_b32 v[12:13], v50 offset1:8
	ds_read2_b32 v[14:15], v50 offset0:66 offset1:74
	ds_read2_b32 v[16:17], v50 offset0:99 offset1:107
	ds_read2_b32 v[18:19], v50 offset0:132 offset1:140
	ds_read2_b32 v[20:21], v50 offset0:165 offset1:173
	ds_read2_b32 v[22:23], v50 offset0:198 offset1:206
	ds_read2_b32 v[24:25], v50 offset0:231 offset1:239
	v_or_b32_e32 v26, s6, v39
	v_lshlrev_b32_e32 v2, 1, v38
	v_ashrrev_i32_e32 v27, 31, v26
	v_lshl_add_u64 v[8:9], s[2:3], 0, v[2:3]
	v_lshlrev_b64 v[26:27], 11, v[26:27]
	s_waitcnt lgkmcnt(0)
	v_cvt_pk_bf16_f32 v4, v12, v10
	v_lshl_add_u64 v[26:27], v[8:9], 0, v[26:27]
	v_or_b32_e32 v10, s6, v46
	v_cvt_pk_bf16_f32 v5, v14, v16
	v_cvt_pk_bf16_f32 v6, v18, v20
	v_cvt_pk_bf16_f32 v7, v22, v24
	global_store_dwordx4 v[26:27], v[4:7], off sc1
	v_or_b32_e32 v26, s6, v48
	v_ashrrev_i32_e32 v27, 31, v26
	v_cvt_pk_bf16_f32 v4, v13, v11
	v_ashrrev_i32_e32 v11, 31, v10
	v_lshlrev_b64 v[10:11], 11, v[10:11]
	v_lshl_add_u64 v[10:11], v[8:9], 0, v[10:11]
	v_cvt_pk_bf16_f32 v5, v15, v17
	v_cvt_pk_bf16_f32 v6, v19, v21
	v_cvt_pk_bf16_f32 v7, v23, v25
	global_store_dwordx4 v[10:11], v[4:7], off sc1
	ds_read2_b32 v[10:11], v50 offset0:16 offset1:24
	ds_read2_b32 v[12:13], v50 offset0:49 offset1:57
	ds_read2_b32 v[14:15], v50 offset0:82 offset1:90
	ds_read2_b32 v[16:17], v50 offset0:115 offset1:123
	ds_read2_b32 v[18:19], v50 offset0:148 offset1:156
	ds_read2_b32 v[20:21], v50 offset0:181 offset1:189
	ds_read2_b32 v[22:23], v50 offset0:214 offset1:222
	ds_read2_b32 v[24:25], v50 offset0:247 offset1:255
	v_lshlrev_b64 v[26:27], 11, v[26:27]
	s_waitcnt lgkmcnt(6)
	v_cvt_pk_bf16_f32 v4, v10, v12
	v_lshl_add_u64 v[26:27], v[8:9], 0, v[26:27]
	v_or_b32_e32 v10, s6, v49
	s_waitcnt lgkmcnt(4)
	v_cvt_pk_bf16_f32 v5, v14, v16
	s_waitcnt lgkmcnt(2)
	v_cvt_pk_bf16_f32 v6, v18, v20
	s_waitcnt lgkmcnt(0)
	v_cvt_pk_bf16_f32 v7, v22, v24
	global_store_dwordx4 v[26:27], v[4:7], off sc1
	s_nop 1
	v_cvt_pk_bf16_f32 v4, v11, v13
	v_ashrrev_i32_e32 v11, 31, v10
	v_lshlrev_b64 v[10:11], 11, v[10:11]
	v_lshl_add_u64 v[8:9], v[8:9], 0, v[10:11]
	v_cvt_pk_bf16_f32 v5, v15, v17
	v_cvt_pk_bf16_f32 v6, v19, v21
	v_cvt_pk_bf16_f32 v7, v23, v25
	global_store_dwordx4 v[8:9], v[4:7], off sc1
	s_waitcnt lgkmcnt(0)
	s_branch .LBB0_415

; #define GAS __attribute__((address_space(1)))
; #define LAS __attribute__((address_space(3)))
; #define LDS_WAIT() asm volatile("s_waitcnt lgkmcnt(0)" ::: "memory")
; __device__ __forceinline__ unsigned pk2(float lo, float hi) { unsigned r; asm("v_cvt_pk_bf16_f32 %0, %1, %2" : "=v"(r) : "v"(lo), "v"(hi)); return r; }
; __device__ __forceinline__ void transpose_item(const float* W, int K, int N, bf16* WT, int drow0, int kb, int n0, LAS float* scr, int lane) {
;     const int k0 = 64 * kb; const int c4 = 4 * (lane & 7); const bool ok = (n0 + c4) < N;
;     f32x4 v[8];
; #pragma unroll
;     for (int i = 0; i < 8; ++i) { const int kk = 8 * i + (lane >> 3); v[i] = ok ? *(const f32x4*)(W + (size_t)(k0 + kk) * N + n0 + c4) : (f32x4){0.f, 0.f, 0.f, 0.f}; }
; #pragma unroll
;     for (int i = 0; i < 8; ++i) { const int kk = 8 * i + (lane >> 3); LAS float* d = scr + kk * 33 + c4; d[0] = v[i][0]; d[1] = v[i][1]; d[2] = v[i][2]; d[3] = v[i][3]; }
;     LDS_WAIT(); asm volatile("" ::: "memory");
;     const int c = lane & 7;
; #pragma unroll
;     for (int j = 0; j < 4; ++j) { const int n = (lane >> 3) + 8 * j; const LAS float* s = scr + (8 * c) * 33 + n;
;         v4u o; o.x = pk2(s[0 * 33], s[1 * 33]); o.y = pk2(s[2 * 33], s[3 * 33]); o.z = pk2(s[4 * 33], s[5 * 33]); o.w = pk2(s[6 * 33], s[7 * 33]);
;         *(GAS v4u*)(WT + (size_t)(drow0 + n) * K + k0 + 8 * c) = o; }
;     LDS_WAIT(); asm volatile("" ::: "memory");
; }
; __device__ __forceinline__ void convert_item(const In& I, unsigned char* ws, int it, LAS float* scr, int lane) {
;     ...
;     { const int jk = r >> 3; r &= 7; const int kb = r >> 1, nb = r & 1;
;         transpose_item(I.nsa_w2 + (size_t)jk * 256 * 64, 256, 64, W2t + (size_t)jk * 64 * 256, 32 * nb, kb, 32 * nb, scr, lane); }
.LBB0_478:
	s_add_i32 s42, s18, 0xa800
	s_cmp_gt_i32 s42, 0x83ff
	s_mov_b64 s[2:3], -1
	s_cbranch_scc0 .LBB0_532
	s_cmpk_gt_u32 s42, 0x8eff
	s_cbranch_scc0 .LBB0_513
	s_cmpk_gt_u32 s42, 0x92ff
	s_cbranch_scc0 .LBB0_510
	s_cmpk_gt_u32 s42, 0x9fff
	s_cbranch_scc0 .LBB0_491
	s_cmpk_gt_u32 s42, 0xa3ff
	s_cbranch_scc0 .LBB0_488
	s_cmpk_gt_u32 s42, 0xa7ff
	s_cbranch_scc0 .LBB0_485
	s_lshr_b32 s68, s18, 3
	v_readlane_b32 s44, v253, 16
	s_lshl_b64 s[2:3], s[68:69], 16
	v_readlane_b32 s48, v253, 20
	v_readlane_b32 s49, v253, 21
	s_add_u32 s6, s48, s2
	s_addc_u32 s7, s49, s3
	s_lshl_b64 s[2:3], s[68:69], 15
	s_add_u32 s8, s34, s2
	s_addc_u32 s3, s35, s3
	s_and_b32 s2, s40, 32
	s_and_b32 s9, s40, 0xc0
	s_lshl_b32 s10, s2, 2
	s_add_u32 s6, s6, s10
	v_or_b32_e32 v6, s9, v39
	s_addc_u32 s7, s7, 0
	v_lshlrev_b32_e32 v2, 2, v36
	v_lshl_add_u64 v[4:5], s[6:7], 0, v[2:3]
	v_lshlrev_b32_e32 v2, 8, v6
	v_lshl_add_u64 v[28:29], v[4:5], 0, v[2:3]
	global_load_dwordx4 v[4:7], v[28:29], off
	global_load_dwordx4 v[8:11], v[28:29], off offset:2048
	v_add_co_u32_e32 v16, vcc, s84, v28
	s_movk_i32 s6, 0x3000
	s_nop 0
	v_addc_co_u32_e32 v17, vcc, 0, v29, vcc
	v_add_co_u32_e32 v24, vcc, s74, v28
	v_add_u32_e32 v2, v44, v45
	s_nop 0
	v_addc_co_u32_e32 v25, vcc, 0, v29, vcc
	global_load_dwordx4 v[12:15], v[24:25], off offset:-4096
	s_nop 0
	global_load_dwordx4 v[16:19], v[16:17], off offset:2048
	s_nop 0
	global_load_dwordx4 v[20:23], v[24:25], off
	s_nop 0
	global_load_dwordx4 v[24:27], v[24:25], off offset:2048
	v_add_co_u32_e32 v32, vcc, s6, v28
	s_lshl_b32 s6, s9, 1
	s_nop 0
	v_addc_co_u32_e32 v33, vcc, 0, v29, vcc
	global_load_dwordx4 v[28:31], v[32:33], off
	s_nop 0
	global_load_dwordx4 v[32:35], v[32:33], off offset:2048
	s_add_u32 s6, s8, s6
	s_addc_u32 s7, s3, 0
	v_readlane_b32 s45, v253, 17
	v_readlane_b32 s46, v253, 18
	v_readlane_b32 s47, v253, 19
	v_readlane_b32 s50, v253, 22
	v_readlane_b32 s51, v253, 23
	v_readlane_b32 s52, v253, 24
	v_readlane_b32 s53, v253, 25
	v_readlane_b32 s54, v253, 26
	v_readlane_b32 s55, v253, 27
	v_readlane_b32 s56, v253, 28
	v_readlane_b32 s57, v253, 29
	v_readlane_b32 s58, v253, 30
	v_readlane_b32 s59, v253, 31
	s_waitcnt vmcnt(0)
	ds_write2_b32 v2, v4, v5 offset1:1
	ds_write2_b32 v2, v6, v7 offset0:2 offset1:3
	v_add_u32_e32 v4, 0x420, v2
	ds_write2_b32 v4, v8, v9 offset1:1
	v_add_u32_e32 v4, 0x428, v2
	ds_write2_b32 v4, v10, v11 offset1:1
	v_add_u32_e32 v4, 0x840, v2
	ds_write2_b32 v4, v12, v13 offset1:1
	v_add_u32_e32 v4, 0x848, v2
	ds_write2_b32 v4, v14, v15 offset1:1
	v_add_u32_e32 v4, 0xc60, v2
	ds_write2_b32 v4, v16, v17 offset1:1
	v_add_u32_e32 v4, 0xc68, v2
	ds_write2_b32 v4, v18, v19 offset1:1
	v_add_u32_e32 v4, 0x1080, v2
	ds_write2_b32 v4, v20, v21 offset1:1
	v_add_u32_e32 v4, 0x1088, v2
	ds_write2_b32 v4, v22, v23 offset1:1
	v_add_u32_e32 v4, 0x14a0, v2
	ds_write2_b32 v4, v24, v25 offset1:1
	v_add_u32_e32 v4, 0x14a8, v2
	ds_write2_b32 v4, v26, v27 offset1:1
	v_add_u32_e32 v4, 0x18c0, v2
	ds_write2_b32 v4, v28, v29 offset1:1
	v_add_u32_e32 v4, 0x18c8, v2
	ds_write2_b32 v4, v30, v31 offset1:1
	v_add_u32_e32 v4, 0x1ce0, v2
	v_add_u32_e32 v2, 0x1ce8, v2
	ds_write2_b32 v4, v32, v33 offset1:1
	ds_write2_b32 v2, v34, v35 offset1:1
	s_waitcnt lgkmcnt(0)
	ds_read2_b32 v[10:11], v49 offset0:33 offset1:41
	ds_read2_b32 v[12:13], v49 offset1:8
	v_lshlrev_b32_e32 v2, 1, v38
	ds_read2_b32 v[14:15], v49 offset0:66 offset1:74
	ds_read2_b32 v[16:17], v49 offset0:99 offset1:107
	ds_read2_b32 v[18:19], v49 offset0:132 offset1:140
	ds_read2_b32 v[20:21], v49 offset0:165 offset1:173
	ds_read2_b32 v[22:23], v49 offset0:198 offset1:206
	ds_read2_b32 v[24:25], v49 offset0:231 offset1:239
	v_lshl_add_u64 v[4:5], s[6:7], 0, v[2:3]
	v_or_b32_e32 v2, s2, v39
	v_lshlrev_b32_e32 v2, 9, v2
	v_lshl_add_u64 v[26:27], v[4:5], 0, v[2:3]
	v_or_b32_e32 v2, s2, v46
	s_waitcnt lgkmcnt(0)
	v_cvt_pk_bf16_f32 v6, v12, v10
	v_lshlrev_b32_e32 v2, 9, v2
	v_cvt_pk_bf16_f32 v7, v14, v16
	v_cvt_pk_bf16_f32 v8, v18, v20
	v_cvt_pk_bf16_f32 v9, v22, v24
	global_store_dwordx4 v[26:27], v[6:9], off sc1
	s_nop 1
	v_cvt_pk_bf16_f32 v6, v13, v11
	v_lshl_add_u64 v[10:11], v[4:5], 0, v[2:3]
	v_cvt_pk_bf16_f32 v7, v15, v17
	v_cvt_pk_bf16_f32 v8, v19, v21
	v_cvt_pk_bf16_f32 v9, v23, v25
	global_store_dwordx4 v[10:11], v[6:9], off sc1
	ds_read2_b32 v[10:11], v49 offset0:16 offset1:24
	ds_read2_b32 v[12:13], v49 offset0:49 offset1:57
	ds_read2_b32 v[14:15], v49 offset0:82 offset1:90
	ds_read2_b32 v[16:17], v49 offset0:115 offset1:123
	ds_read2_b32 v[18:19], v49 offset0:148 offset1:156
	ds_read2_b32 v[20:21], v49 offset0:181 offset1:189
	ds_read2_b32 v[22:23], v49 offset0:214 offset1:222
	ds_read2_b32 v[24:25], v49 offset0:247 offset1:255
	v_or_b32_e32 v2, s2, v47
	v_lshlrev_b32_e32 v2, 9, v2
	v_lshl_add_u64 v[26:27], v[4:5], 0, v[2:3]
	v_or_b32_e32 v2, s2, v48
	v_lshlrev_b32_e32 v2, 9, v2
	s_waitcnt lgkmcnt(6)
	v_cvt_pk_bf16_f32 v6, v10, v12
	s_waitcnt lgkmcnt(4)
	v_cvt_pk_bf16_f32 v7, v14, v16
	s_waitcnt lgkmcnt(2)
	v_cvt_pk_bf16_f32 v8, v18, v20
	s_waitcnt lgkmcnt(0)
	v_cvt_pk_bf16_f32 v9, v22, v24
	v_lshl_add_u64 v[4:5], v[4:5], 0, v[2:3]
	global_store_dwordx4 v[26:27], v[6:9], off sc1
	s_mov_b64 s[2:3], 0
	s_nop 0
	v_cvt_pk_bf16_f32 v6, v11, v13
	v_cvt_pk_bf16_f32 v7, v15, v17
	v_cvt_pk_bf16_f32 v8, v19, v21
	v_cvt_pk_bf16_f32 v9, v23, v25
	global_store_dwordx4 v[4:5], v[6:9], off sc1
	s_waitcnt lgkmcnt(0)
; #define GAS __attribute__((address_space(1)))
; #define LAS __attribute__((address_space(3)))
; #define LDS_WAIT() asm volatile("s_waitcnt lgkmcnt(0)" ::: "memory")
; __device__ __forceinline__ unsigned pk2(float lo, float hi) { unsigned r; asm("v_cvt_pk_bf16_f32 %0, %1, %2" : "=v"(r) : "v"(lo), "v"(hi)); return r; }
; __device__ __forceinline__ void transpose_item(const float* W, int K, int N, bf16* WT, int drow0, int kb, int n0, LAS float* scr, int lane) {
;     const int k0 = 64 * kb; const int c4 = 4 * (lane & 7); const bool ok = (n0 + c4) < N;
;     f32x4 v[8];
; #pragma unroll
;     for (int i = 0; i < 8; ++i) { const int kk = 8 * i + (lane >> 3); v[i] = ok ? *(const f32x4*)(W + (size_t)(k0 + kk) * N + n0 + c4) : (f32x4){0.f, 0.f, 0.f, 0.f}; }
; #pragma unroll
;     for (int i = 0; i < 8; ++i) { const int kk = 8 * i + (lane >> 3); LAS float* d = scr + kk * 33 + c4; d[0] = v[i][0]; d[1] = v[i][1]; d[2] = v[i][2]; d[3] = v[i][3]; }
;     LDS_WAIT(); asm volatile("" ::: "memory");
;     const int c = lane & 7;
; #pragma unroll
;     for (int j = 0; j < 4; ++j) { const int n = (lane >> 3) + 8 * j; const LAS float* s = scr + (8 * c) * 33 + n;
;         v4u o; o.x = pk2(s[0 * 33], s[1 * 33]); o.y = pk2(s[2 * 33], s[3 * 33]); o.z = pk2(s[4 * 33], s[5 * 33]); o.w = pk2(s[6 * 33], s[7 * 33]);
;         *(GAS v4u*)(WT + (size_t)(drow0 + n) * K + k0 + 8 * c) = o; }
;     LDS_WAIT(); asm volatile("" ::: "memory");
; }
; __device__ __forceinline__ void convert_item(const In& I, unsigned char* ws, int it, LAS float* scr, int lane) {
;     ...
;     if (r < 4 * I_W1) { const int jk = r / I_W1; r -= jk * I_W1; const int kb = r / 8, nb = r % 8;
;         transpose_item(I.nsa_w1 + (size_t)jk * 2048 * 256, 2048, 256, W1t + (size_t)jk * 256 * 2048, 32 * nb, kb, 32 * nb, scr, lane); return; }
.LBB0_485:
	s_andn2_b64 vcc, exec, s[2:3]
	s_cbranch_vccnz .LBB0_487
	s_add_i32 s2, s18, 0x400
	s_lshr_b32 s68, s2, 8
	s_lshl_b64 s[2:3], s[68:69], 21
	v_readlane_b32 s44, v253, 16
	v_readlane_b32 s45, v253, 17
	s_add_u32 s6, s44, s2
	s_addc_u32 s7, s45, s3
	s_lshl_b64 s[2:3], s[68:69], 20
	s_add_u32 s8, s31, s2
	s_addc_u32 s3, s33, s3
	s_and_b32 s2, s40, 0xe0
	s_and_b32 s9, s39, 0x7c0
	s_lshl_b32 s10, s2, 2
	s_add_u32 s6, s6, s10
	v_or_b32_e32 v6, s9, v39
	s_addc_u32 s7, s7, 0
	v_lshlrev_b32_e32 v2, 2, v36
	v_lshl_add_u64 v[4:5], s[6:7], 0, v[2:3]
	v_lshlrev_b32_e32 v2, 10, v6
	v_lshl_add_u64 v[32:33], v[4:5], 0, v[2:3]
	v_add_co_u32_e32 v8, vcc, s74, v32
	global_load_dwordx4 v[4:7], v[32:33], off
	s_nop 0
	v_addc_co_u32_e32 v9, vcc, 0, v33, vcc
	s_movk_i32 s6, 0x4000
	global_load_dwordx4 v[8:11], v[8:9], off
	v_add_co_u32_e32 v12, vcc, s6, v32
	s_movk_i32 s6, 0x6000
	s_nop 0
	v_addc_co_u32_e32 v13, vcc, 0, v33, vcc
	global_load_dwordx4 v[12:15], v[12:13], off
	v_add_co_u32_e32 v16, vcc, s6, v32
	s_mov_b32 s6, 0xa000
	s_nop 0
	v_addc_co_u32_e32 v17, vcc, 0, v33, vcc
	global_load_dwordx4 v[16:19], v[16:17], off
	v_add_co_u32_e32 v20, vcc, s81, v32
	v_add_u32_e32 v2, v44, v45
	s_nop 0
	v_addc_co_u32_e32 v21, vcc, 0, v33, vcc
	global_load_dwordx4 v[20:23], v[20:21], off
	v_add_co_u32_e32 v24, vcc, s6, v32
	s_mov_b32 s6, 0xc000
	s_nop 0
	v_addc_co_u32_e32 v25, vcc, 0, v33, vcc
	global_load_dwordx4 v[24:27], v[24:25], off
	v_add_co_u32_e32 v28, vcc, s6, v32
	s_mov_b32 s6, 0xe000
	s_nop 0
	v_addc_co_u32_e32 v29, vcc, 0, v33, vcc
	global_load_dwordx4 v[28:31], v[28:29], off
	v_add_co_u32_e32 v32, vcc, s6, v32
	s_lshl_b32 s6, s9, 1
	s_nop 0
	v_addc_co_u32_e32 v33, vcc, 0, v33, vcc
	global_load_dwordx4 v[32:35], v[32:33], off
	s_add_u32 s6, s8, s6
	s_addc_u32 s7, s3, 0
	v_readlane_b32 s46, v253, 18
	v_readlane_b32 s47, v253, 19
	v_readlane_b32 s48, v253, 20
	v_readlane_b32 s49, v253, 21
	v_readlane_b32 s50, v253, 22
	v_readlane_b32 s51, v253, 23
	v_readlane_b32 s52, v253, 24
	v_readlane_b32 s53, v253, 25
	v_readlane_b32 s54, v253, 26
	v_readlane_b32 s55, v253, 27
	v_readlane_b32 s56, v253, 28
	v_readlane_b32 s57, v253, 29
	v_readlane_b32 s58, v253, 30
	v_readlane_b32 s59, v253, 31
	s_waitcnt vmcnt(0)
	ds_write2_b32 v2, v4, v5 offset1:1
	ds_write2_b32 v2, v6, v7 offset0:2 offset1:3
	v_add_u32_e32 v4, 0x420, v2
	ds_write2_b32 v4, v8, v9 offset1:1
	v_add_u32_e32 v4, 0x428, v2
	ds_write2_b32 v4, v10, v11 offset1:1
	v_add_u32_e32 v4, 0x840, v2
	ds_write2_b32 v4, v12, v13 offset1:1
	v_add_u32_e32 v4, 0x848, v2
	ds_write2_b32 v4, v14, v15 offset1:1
	v_add_u32_e32 v4, 0xc60, v2
	ds_write2_b32 v4, v16, v17 offset1:1
	v_add_u32_e32 v4, 0xc68, v2
	ds_write2_b32 v4, v18, v19 offset1:1
	v_add_u32_e32 v4, 0x1080, v2
	ds_write2_b32 v4, v20, v21 offset1:1
	v_add_u32_e32 v4, 0x1088, v2
	ds_write2_b32 v4, v22, v23 offset1:1
	v_add_u32_e32 v4, 0x14a0, v2
	ds_write2_b32 v4, v24, v25 offset1:1
	v_add_u32_e32 v4, 0x14a8, v2
	ds_write2_b32 v4, v26, v27 offset1:1
	v_add_u32_e32 v4, 0x18c0, v2
	ds_write2_b32 v4, v28, v29 offset1:1
	v_add_u32_e32 v4, 0x18c8, v2
	ds_write2_b32 v4, v30, v31 offset1:1
	v_add_u32_e32 v4, 0x1ce0, v2
	v_add_u32_e32 v2, 0x1ce8, v2
	ds_write2_b32 v4, v32, v33 offset1:1
	ds_write2_b32 v2, v34, v35 offset1:1
	s_waitcnt lgkmcnt(0)
	ds_read2_b32 v[10:11], v49 offset0:33 offset1:41
	ds_read2_b32 v[12:13], v49 offset1:8
	v_lshlrev_b32_e32 v2, 1, v38
	ds_read2_b32 v[14:15], v49 offset0:66 offset1:74
	ds_read2_b32 v[16:17], v49 offset0:99 offset1:107
	ds_read2_b32 v[18:19], v49 offset0:132 offset1:140
	ds_read2_b32 v[20:21], v49 offset0:165 offset1:173
	ds_read2_b32 v[22:23], v49 offset0:198 offset1:206
	ds_read2_b32 v[24:25], v49 offset0:231 offset1:239
	v_lshl_add_u64 v[8:9], s[6:7], 0, v[2:3]
	v_or_b32_e32 v2, s2, v39
	v_lshlrev_b32_e32 v2, 12, v2
	v_lshl_add_u64 v[26:27], v[8:9], 0, v[2:3]
	v_or_b32_e32 v2, s2, v46
	s_waitcnt lgkmcnt(0)
	v_cvt_pk_bf16_f32 v4, v12, v10
	v_lshlrev_b32_e32 v2, 12, v2
	v_cvt_pk_bf16_f32 v5, v14, v16
	v_cvt_pk_bf16_f32 v6, v18, v20
	v_cvt_pk_bf16_f32 v7, v22, v24
	global_store_dwordx4 v[26:27], v[4:7], off sc1
	s_nop 1
	v_cvt_pk_bf16_f32 v4, v13, v11
	v_lshl_add_u64 v[10:11], v[8:9], 0, v[2:3]
	v_cvt_pk_bf16_f32 v5, v15, v17
	v_cvt_pk_bf16_f32 v6, v19, v21
	v_cvt_pk_bf16_f32 v7, v23, v25
	global_store_dwordx4 v[10:11], v[4:7], off sc1
	ds_read2_b32 v[10:11], v49 offset0:16 offset1:24
	ds_read2_b32 v[12:13], v49 offset0:49 offset1:57
	ds_read2_b32 v[14:15], v49 offset0:82 offset1:90
	ds_read2_b32 v[16:17], v49 offset0:115 offset1:123
	ds_read2_b32 v[18:19], v49 offset0:148 offset1:156
	ds_read2_b32 v[20:21], v49 offset0:181 offset1:189
	ds_read2_b32 v[22:23], v49 offset0:214 offset1:222
	ds_read2_b32 v[24:25], v49 offset0:247 offset1:255
	v_or_b32_e32 v2, s2, v47
	v_lshlrev_b32_e32 v2, 12, v2
	v_lshl_add_u64 v[26:27], v[8:9], 0, v[2:3]
	v_or_b32_e32 v2, s2, v48
	v_lshlrev_b32_e32 v2, 12, v2
	s_waitcnt lgkmcnt(6)
	v_cvt_pk_bf16_f32 v4, v10, v12
	s_waitcnt lgkmcnt(4)
	v_cvt_pk_bf16_f32 v5, v14, v16
	s_waitcnt lgkmcnt(2)
	v_cvt_pk_bf16_f32 v6, v18, v20
	s_waitcnt lgkmcnt(0)
	v_cvt_pk_bf16_f32 v7, v22, v24
	v_lshl_add_u64 v[8:9], v[8:9], 0, v[2:3]
	global_store_dwordx4 v[26:27], v[4:7], off sc1
	s_nop 1
	v_cvt_pk_bf16_f32 v4, v11, v13
	v_cvt_pk_bf16_f32 v5, v15, v17
	v_cvt_pk_bf16_f32 v6, v19, v21
	v_cvt_pk_bf16_f32 v7, v23, v25
	global_store_dwordx4 v[8:9], v[4:7], off sc1
	s_waitcnt lgkmcnt(0)

; #define GAS __attribute__((address_space(1)))
; #define LAS __attribute__((address_space(3)))
; #define LDS_WAIT() asm volatile("s_waitcnt lgkmcnt(0)" ::: "memory")
; __device__ __forceinline__ unsigned pk2(float lo, float hi) { unsigned r; asm("v_cvt_pk_bf16_f32 %0, %1, %2" : "=v"(r) : "v"(lo), "v"(hi)); return r; }
; __device__ __forceinline__ void transpose_item(const float* W, int K, int N, bf16* WT, int drow0, int kb, int n0, LAS float* scr, int lane) {
;     const int k0 = 64 * kb; const int c4 = 4 * (lane & 7); const bool ok = (n0 + c4) < N;
;     f32x4 v[8];
; #pragma unroll
;     for (int i = 0; i < 8; ++i) { const int kk = 8 * i + (lane >> 3); v[i] = ok ? *(const f32x4*)(W + (size_t)(k0 + kk) * N + n0 + c4) : (f32x4){0.f, 0.f, 0.f, 0.f}; }
; #pragma unroll
;     for (int i = 0; i < 8; ++i) { const int kk = 8 * i + (lane >> 3); LAS float* d = scr + kk * 33 + c4; d[0] = v[i][0]; d[1] = v[i][1]; d[2] = v[i][2]; d[3] = v[i][3]; }
;     LDS_WAIT(); asm volatile("" ::: "memory");
;     const int c = lane & 7;
; #pragma unroll
;     for (int j = 0; j < 4; ++j) { const int n = (lane >> 3) + 8 * j; const LAS float* s = scr + (8 * c) * 33 + n;
;         v4u o; o.x = pk2(s[0 * 33], s[1 * 33]); o.y = pk2(s[2 * 33], s[3 * 33]); o.z = pk2(s[4 * 33], s[5 * 33]); o.w = pk2(s[6 * 33], s[7 * 33]);
;         *(GAS v4u*)(WT + (size_t)(drow0 + n) * K + k0 + 8 * c) = o; }
;     LDS_WAIT(); asm volatile("" ::: "memory");
; }
; __device__ __forceinline__ void convert_item(const In& I, unsigned char* ws, int it, LAS float* scr, int lane) {
;     ...
;     if (r < 2 * I_SQ) { const int j = r / I_SQ; r -= j * I_SQ; const int kb = r / 32, nb = r % 32;
;         transpose_item(I.fox_w_out + (size_t)j * D * D, D, D, Wfout + (size_t)j * D * D, 32 * nb, kb, 32 * nb, scr, lane); return; }
.LBB0_488:
	s_andn2_b64 vcc, exec, s[2:3]
	s_cbranch_vccnz .LBB0_490
	s_add_i32 s2, s18, 0x800
	s_lshr_b32 s68, s2, 9
	v_readlane_b32 s44, v253, 16
	s_lshl_b64 s[2:3], s[68:69], 22
	v_readlane_b32 s56, v253, 28
	v_readlane_b32 s57, v253, 29
	s_add_u32 s6, s56, s2
	s_addc_u32 s7, s57, s3
	s_lshl_b64 s[2:3], s[68:69], 21
	s_add_u32 s8, s26, s2
	s_addc_u32 s3, s27, s3
	s_and_b32 s2, s40, 0x3e0
	s_add_i32 s9, s41, 0x14800
	s_and_b32 s9, s9, 0x3c0
	s_lshl_b32 s10, s2, 2
	s_add_u32 s6, s6, s10
	v_or_b32_e32 v6, s9, v39
	s_addc_u32 s7, s7, 0
	v_lshlrev_b32_e32 v2, 2, v36
	v_lshl_add_u64 v[4:5], s[6:7], 0, v[2:3]
	v_lshlrev_b32_e32 v2, 12, v6
	v_lshl_add_u64 v[32:33], v[4:5], 0, v[2:3]
	v_add_co_u32_e32 v8, vcc, s81, v32
	global_load_dwordx4 v[4:7], v[32:33], off
	s_nop 0
	v_addc_co_u32_e32 v9, vcc, 0, v33, vcc
	global_load_dwordx4 v[8:11], v[8:9], off
	v_add_co_u32_e32 v12, vcc, s79, v32
	v_add_u32_e32 v2, v44, v45
	s_nop 0
	v_addc_co_u32_e32 v13, vcc, 0, v33, vcc
	global_load_dwordx4 v[12:15], v[12:13], off
	v_add_co_u32_e32 v16, vcc, s80, v32
	s_lshl_b32 s6, s9, 1
	s_nop 0
	v_addc_co_u32_e32 v17, vcc, 0, v33, vcc
	global_load_dwordx4 v[16:19], v[16:17], off
	v_add_co_u32_e32 v20, vcc, s85, v32
	s_add_u32 s6, s8, s6
	s_nop 0
	v_addc_co_u32_e32 v21, vcc, 0, v33, vcc
	global_load_dwordx4 v[20:23], v[20:21], off
	v_add_co_u32_e32 v24, vcc, s86, v32
	s_addc_u32 s7, s3, 0
	s_nop 0
	v_addc_co_u32_e32 v25, vcc, 0, v33, vcc
	global_load_dwordx4 v[24:27], v[24:25], off
	v_add_co_u32_e32 v28, vcc, s87, v32
	v_readlane_b32 s45, v253, 17
	s_nop 0
	v_addc_co_u32_e32 v29, vcc, 0, v33, vcc
	global_load_dwordx4 v[28:31], v[28:29], off
	v_add_co_u32_e32 v32, vcc, s89, v32
	v_readlane_b32 s46, v253, 18
	s_nop 0
	v_addc_co_u32_e32 v33, vcc, 0, v33, vcc
	global_load_dwordx4 v[32:35], v[32:33], off
	v_readlane_b32 s47, v253, 19
	v_readlane_b32 s48, v253, 20
	v_readlane_b32 s49, v253, 21
	v_readlane_b32 s50, v253, 22
	v_readlane_b32 s51, v253, 23
	v_readlane_b32 s52, v253, 24
	v_readlane_b32 s53, v253, 25
	v_readlane_b32 s54, v253, 26
	v_readlane_b32 s55, v253, 27
	v_readlane_b32 s58, v253, 30
	v_readlane_b32 s59, v253, 31
	s_waitcnt vmcnt(0)
	ds_write2_b32 v2, v4, v5 offset1:1
	ds_write2_b32 v2, v6, v7 offset0:2 offset1:3
	v_add_u32_e32 v4, 0x420, v2
	ds_write2_b32 v4, v8, v9 offset1:1
	v_add_u32_e32 v4, 0x428, v2
	ds_write2_b32 v4, v10, v11 offset1:1
	v_add_u32_e32 v4, 0x840, v2
	ds_write2_b32 v4, v12, v13 offset1:1
	v_add_u32_e32 v4, 0x848, v2
	ds_write2_b32 v4, v14, v15 offset1:1
	v_add_u32_e32 v4, 0xc60, v2
	ds_write2_b32 v4, v16, v17 offset1:1
	v_add_u32_e32 v4, 0xc68, v2
	ds_write2_b32 v4, v18, v19 offset1:1
	v_add_u32_e32 v4, 0x1080, v2
	ds_write2_b32 v4, v20, v21 offset1:1
	v_add_u32_e32 v4, 0x1088, v2
	ds_write2_b32 v4, v22, v23 offset1:1
	v_add_u32_e32 v4, 0x14a0, v2
	ds_write2_b32 v4, v24, v25 offset1:1
	v_add_u32_e32 v4, 0x14a8, v2
	ds_write2_b32 v4, v26, v27 offset1:1
	v_add_u32_e32 v4, 0x18c0, v2
	ds_write2_b32 v4, v28, v29 offset1:1
	v_add_u32_e32 v4, 0x18c8, v2
	ds_write2_b32 v4, v30, v31 offset1:1
	v_add_u32_e32 v4, 0x1ce0, v2
	v_add_u32_e32 v2, 0x1ce8, v2
	ds_write2_b32 v4, v32, v33 offset1:1
	ds_write2_b32 v2, v34, v35 offset1:1
	s_waitcnt lgkmcnt(0)
	ds_read2_b32 v[10:11], v49 offset0:33 offset1:41
	ds_read2_b32 v[12:13], v49 offset1:8
	v_lshlrev_b32_e32 v2, 1, v38
	ds_read2_b32 v[14:15], v49 offset0:66 offset1:74
	ds_read2_b32 v[16:17], v49 offset0:99 offset1:107
	ds_read2_b32 v[18:19], v49 offset0:132 offset1:140
	ds_read2_b32 v[20:21], v49 offset0:165 offset1:173
	ds_read2_b32 v[22:23], v49 offset0:198 offset1:206
	ds_read2_b32 v[24:25], v49 offset0:231 offset1:239
	v_lshl_add_u64 v[8:9], s[6:7], 0, v[2:3]
	v_or_b32_e32 v2, s2, v39
	v_lshlrev_b32_e32 v2, 11, v2
	v_lshl_add_u64 v[26:27], v[8:9], 0, v[2:3]
	v_or_b32_e32 v2, s2, v46
	s_waitcnt lgkmcnt(0)
	v_cvt_pk_bf16_f32 v4, v12, v10
	v_lshlrev_b32_e32 v2, 11, v2
	v_cvt_pk_bf16_f32 v5, v14, v16
	v_cvt_pk_bf16_f32 v6, v18, v20
	v_cvt_pk_bf16_f32 v7, v22, v24
	global_store_dwordx4 v[26:27], v[4:7], off sc1
	s_nop 1
	v_cvt_pk_bf16_f32 v4, v13, v11
	v_lshl_add_u64 v[10:11], v[8:9], 0, v[2:3]
	v_cvt_pk_bf16_f32 v5, v15, v17
	v_cvt_pk_bf16_f32 v6, v19, v21
	v_cvt_pk_bf16_f32 v7, v23, v25
	global_store_dwordx4 v[10:11], v[4:7], off sc1
	ds_read2_b32 v[10:11], v49 offset0:16 offset1:24
	ds_read2_b32 v[12:13], v49 offset0:49 offset1:57
	ds_read2_b32 v[14:15], v49 offset0:82 offset1:90
	ds_read2_b32 v[16:17], v49 offset0:115 offset1:123
	ds_read2_b32 v[18:19], v49 offset0:148 offset1:156
	ds_read2_b32 v[20:21], v49 offset0:181 offset1:189
	ds_read2_b32 v[22:23], v49 offset0:214 offset1:222
	ds_read2_b32 v[24:25], v49 offset0:247 offset1:255
	v_or_b32_e32 v2, s2, v47
	v_lshlrev_b32_e32 v2, 11, v2
	v_lshl_add_u64 v[26:27], v[8:9], 0, v[2:3]
	v_or_b32_e32 v2, s2, v48
	v_lshlrev_b32_e32 v2, 11, v2
	s_waitcnt lgkmcnt(6)
	v_cvt_pk_bf16_f32 v4, v10, v12
	s_waitcnt lgkmcnt(4)
	v_cvt_pk_bf16_f32 v5, v14, v16
	s_waitcnt lgkmcnt(2)
	v_cvt_pk_bf16_f32 v6, v18, v20
	s_waitcnt lgkmcnt(0)
	v_cvt_pk_bf16_f32 v7, v22, v24
	v_lshl_add_u64 v[8:9], v[8:9], 0, v[2:3]
	global_store_dwordx4 v[26:27], v[4:7], off sc1
	s_nop 1
	v_cvt_pk_bf16_f32 v4, v11, v13
	v_cvt_pk_bf16_f32 v5, v15, v17
	v_cvt_pk_bf16_f32 v6, v19, v21
	v_cvt_pk_bf16_f32 v7, v23, v25
	global_store_dwordx4 v[8:9], v[4:7], off sc1
	s_waitcnt lgkmcnt(0)

; #define GAS __attribute__((address_space(1)))
; #define LAS __attribute__((address_space(3)))
; #define LDS_WAIT() asm volatile("s_waitcnt lgkmcnt(0)" ::: "memory")
; __device__ __forceinline__ unsigned pk2(float lo, float hi) { unsigned r; asm("v_cvt_pk_bf16_f32 %0, %1, %2" : "=v"(r) : "v"(lo), "v"(hi)); return r; }
; __device__ __forceinline__ void transpose_item(const float* W, int K, int N, bf16* WT, int drow0, int kb, int n0, LAS float* scr, int lane) {
;     const int k0 = 64 * kb; const int c4 = 4 * (lane & 7); const bool ok = (n0 + c4) < N;
;     f32x4 v[8];
; #pragma unroll
;     for (int i = 0; i < 8; ++i) { const int kk = 8 * i + (lane >> 3); v[i] = ok ? *(const f32x4*)(W + (size_t)(k0 + kk) * N + n0 + c4) : (f32x4){0.f, 0.f, 0.f, 0.f}; }
; #pragma unroll
;     for (int i = 0; i < 8; ++i) { const int kk = 8 * i + (lane >> 3); LAS float* d = scr + kk * 33 + c4; d[0] = v[i][0]; d[1] = v[i][1]; d[2] = v[i][2]; d[3] = v[i][3]; }
;     LDS_WAIT(); asm volatile("" ::: "memory");
;     const int c = lane & 7;
; #pragma unroll
;     for (int j = 0; j < 4; ++j) { const int n = (lane >> 3) + 8 * j; const LAS float* s = scr + (8 * c) * 33 + n;
;         v4u o; o.x = pk2(s[0 * 33], s[1 * 33]); o.y = pk2(s[2 * 33], s[3 * 33]); o.z = pk2(s[4 * 33], s[5 * 33]); o.w = pk2(s[6 * 33], s[7 * 33]);
;         *(GAS v4u*)(WT + (size_t)(drow0 + n) * K + k0 + 8 * c) = o; }
;     LDS_WAIT(); asm volatile("" ::: "memory");
; }
; __device__ __forceinline__ void convert_item(const In& I, unsigned char* ws, int it, LAS float* scr, int lane) {
;     ...
;     if (r < 2 * I_FIN) { const int j = r / I_FIN; r -= j * I_FIN; const int kb = r / 104, nb = r % 104;
;         transpose_item(I.fox_w_in + (size_t)j * D * FOX_IN, D, FOX_IN, Wfin + (size_t)j * FOX_IN_PAD * D, 32 * nb, kb, 32 * nb, scr, lane); return; }
.LBB0_508:
	s_or_b64 exec, exec, s[12:13]
	v_add_u32_e32 v2, v44, v45
	s_waitcnt vmcnt(0)
	ds_write2_b32 v2, v8, v9 offset1:1
	ds_write2_b32 v2, v10, v11 offset0:2 offset1:3
	v_add_u32_e32 v8, 0x420, v2
	ds_write2_b32 v8, v4, v5 offset1:1
	v_add_u32_e32 v4, 0x428, v2
	ds_write2_b32 v4, v6, v7 offset1:1
	v_add_u32_e32 v4, 0x840, v2
	ds_write2_b32 v4, v16, v17 offset1:1
	v_add_u32_e32 v4, 0x848, v2
	ds_write2_b32 v4, v18, v19 offset1:1
	v_add_u32_e32 v4, 0xc60, v2
	ds_write2_b32 v4, v12, v13 offset1:1
	v_add_u32_e32 v4, 0xc68, v2
	ds_write2_b32 v4, v14, v15 offset1:1
	v_add_u32_e32 v4, 0x1080, v2
	ds_write2_b32 v4, v24, v25 offset1:1
	v_add_u32_e32 v4, 0x1088, v2
	ds_write2_b32 v4, v26, v27 offset1:1
	v_add_u32_e32 v4, 0x14a0, v2
	ds_write2_b32 v4, v20, v21 offset1:1
	v_add_u32_e32 v4, 0x14a8, v2
	ds_write2_b32 v4, v22, v23 offset1:1
	v_add_u32_e32 v4, 0x18c0, v2
	ds_write2_b32 v4, v32, v33 offset1:1
	v_add_u32_e32 v4, 0x18c8, v2
	s_and_b64 s[2:3], s[10:11], exec
	ds_write2_b32 v4, v34, v35 offset1:1
	v_add_u32_e32 v4, 0x1ce0, v2
	v_add_u32_e32 v2, 0x1ce8, v2
	s_cselect_b32 s2, 0x680000, 0
	ds_write2_b32 v4, v28, v29 offset1:1
	ds_write2_b32 v2, v30, v31 offset1:1
	s_add_u32 s7, s24, s2
	s_waitcnt lgkmcnt(0)
	s_addc_u32 s10, s25, 0
	s_ashr_i32 s9, s8, 31
	s_lshl_b64 s[2:3], s[8:9], 1
	ds_read2_b32 v[8:9], v49 offset0:33 offset1:41
	ds_read2_b32 v[10:11], v49 offset1:8
	ds_read2_b32 v[12:13], v49 offset0:66 offset1:74
	ds_read2_b32 v[14:15], v49 offset0:99 offset1:107
	ds_read2_b32 v[16:17], v49 offset0:132 offset1:140
	ds_read2_b32 v[18:19], v49 offset0:165 offset1:173
	ds_read2_b32 v[20:21], v49 offset0:198 offset1:206
	ds_read2_b32 v[22:23], v49 offset0:231 offset1:239
	s_add_u32 s2, s7, s2
	v_or_b32_e32 v26, s6, v39
	s_addc_u32 s3, s10, s3
	v_lshlrev_b32_e32 v2, 1, v38
	v_ashrrev_i32_e32 v27, 31, v26
	v_lshl_add_u64 v[24:25], s[2:3], 0, v[2:3]
	v_lshlrev_b64 v[26:27], 11, v[26:27]
	s_waitcnt lgkmcnt(0)
	v_cvt_pk_bf16_f32 v4, v10, v8
	v_lshl_add_u64 v[26:27], v[24:25], 0, v[26:27]
	v_or_b32_e32 v8, s6, v46
	v_cvt_pk_bf16_f32 v5, v12, v14
	v_cvt_pk_bf16_f32 v6, v16, v18
	v_cvt_pk_bf16_f32 v7, v20, v22
	global_store_dwordx4 v[26:27], v[4:7], off sc1
	s_nop 1
	v_cvt_pk_bf16_f32 v4, v11, v9
	v_ashrrev_i32_e32 v9, 31, v8
	v_lshlrev_b64 v[8:9], 11, v[8:9]
	v_cvt_pk_bf16_f32 v5, v13, v15
	v_cvt_pk_bf16_f32 v6, v17, v19
	v_cvt_pk_bf16_f32 v7, v21, v23
	v_lshl_add_u64 v[8:9], v[24:25], 0, v[8:9]
	ds_read2_b32 v[10:11], v49 offset0:16 offset1:24
	ds_read2_b32 v[12:13], v49 offset0:49 offset1:57
	ds_read2_b32 v[14:15], v49 offset0:82 offset1:90
	ds_read2_b32 v[16:17], v49 offset0:115 offset1:123
	ds_read2_b32 v[18:19], v49 offset0:148 offset1:156
	ds_read2_b32 v[20:21], v49 offset0:181 offset1:189
	ds_read2_b32 v[22:23], v49 offset0:214 offset1:222
	ds_read2_b32 v[26:27], v49 offset0:247 offset1:255
	global_store_dwordx4 v[8:9], v[4:7], off sc1
	v_or_b32_e32 v8, s6, v47
	v_ashrrev_i32_e32 v9, 31, v8
	v_lshlrev_b64 v[8:9], 11, v[8:9]
	v_lshl_add_u64 v[8:9], v[24:25], 0, v[8:9]
	s_waitcnt lgkmcnt(6)
	v_cvt_pk_bf16_f32 v4, v10, v12
	s_waitcnt lgkmcnt(4)
	v_cvt_pk_bf16_f32 v5, v14, v16
	s_waitcnt lgkmcnt(2)
	v_cvt_pk_bf16_f32 v6, v18, v20
	s_waitcnt lgkmcnt(0)
	v_cvt_pk_bf16_f32 v7, v22, v26
	global_store_dwordx4 v[8:9], v[4:7], off sc1
	v_or_b32_e32 v8, s6, v48
	v_ashrrev_i32_e32 v9, 31, v8
	v_lshlrev_b64 v[8:9], 11, v[8:9]
	v_lshl_add_u64 v[8:9], v[24:25], 0, v[8:9]
	v_cvt_pk_bf16_f32 v4, v11, v13
	v_cvt_pk_bf16_f32 v5, v15, v17
	v_cvt_pk_bf16_f32 v6, v19, v21
	v_cvt_pk_bf16_f32 v7, v23, v27
	global_store_dwordx4 v[8:9], v[4:7], off sc1
	s_waitcnt lgkmcnt(0)

; #define GAS __attribute__((address_space(1)))
; #define LAS __attribute__((address_space(3)))
; #define LDS_WAIT() asm volatile("s_waitcnt lgkmcnt(0)" ::: "memory")
; __device__ __forceinline__ unsigned pk2(float lo, float hi) { unsigned r; asm("v_cvt_pk_bf16_f32 %0, %1, %2" : "=v"(r) : "v"(lo), "v"(hi)); return r; }
; __device__ __forceinline__ void transpose_item(const float* W, int K, int N, bf16* WT, int drow0, int kb, int n0, LAS float* scr, int lane) {
;     const int k0 = 64 * kb; const int c4 = 4 * (lane & 7); const bool ok = (n0 + c4) < N;
;     f32x4 v[8];
; #pragma unroll
;     for (int i = 0; i < 8; ++i) { const int kk = 8 * i + (lane >> 3); v[i] = ok ? *(const f32x4*)(W + (size_t)(k0 + kk) * N + n0 + c4) : (f32x4){0.f, 0.f, 0.f, 0.f}; }
; #pragma unroll
;     for (int i = 0; i < 8; ++i) { const int kk = 8 * i + (lane >> 3); LAS float* d = scr + kk * 33 + c4; d[0] = v[i][0]; d[1] = v[i][1]; d[2] = v[i][2]; d[3] = v[i][3]; }
;     LDS_WAIT(); asm volatile("" ::: "memory");
;     const int c = lane & 7;
; #pragma unroll
;     for (int j = 0; j < 4; ++j) { const int n = (lane >> 3) + 8 * j; const LAS float* s = scr + (8 * c) * 33 + n;
;         v4u o; o.x = pk2(s[0 * 33], s[1 * 33]); o.y = pk2(s[2 * 33], s[3 * 33]); o.z = pk2(s[4 * 33], s[5 * 33]); o.w = pk2(s[6 * 33], s[7 * 33]);
;         *(GAS v4u*)(WT + (size_t)(drow0 + n) * K + k0 + 8 * c) = o; }
;     LDS_WAIT(); asm volatile("" ::: "memory");
; }
; __device__ __forceinline__ void convert_item(const In& I, unsigned char* ws, int it, LAS float* scr, int lane) {
;     ...
;     if (r < 2 * I_SQ) { const int j = r / I_SQ; r -= j * I_SQ; const int kb = r / 32, nb = r % 32;
;         transpose_item(I.nsa_w_out + (size_t)j * D * D, D, D, Wnout + (size_t)j * D * D, 32 * nb, kb, 32 * nb, scr, lane); return; }
.LBB0_510:
	s_andn2_b64 vcc, exec, s[2:3]
	s_cbranch_vccnz .LBB0_512
	s_add_i32 s2, s18, 0x1900
	s_lshr_b32 s68, s2, 9
	v_readlane_b32 s44, v253, 16
	s_lshl_b64 s[2:3], s[68:69], 22
	v_readlane_b32 s50, v253, 22
	v_readlane_b32 s51, v253, 23
	s_add_u32 s6, s50, s2
	s_addc_u32 s7, s51, s3
	s_lshl_b64 s[2:3], s[68:69], 21
	s_add_u32 s8, s22, s2
	s_addc_u32 s3, s23, s3
	s_and_b32 s2, s40, 0x3e0
	s_add_i32 s9, s41, 0x2a00
	s_and_b32 s9, s9, 0x3c0
	s_lshl_b32 s10, s2, 2
	s_add_u32 s6, s6, s10
	v_or_b32_e32 v6, s9, v39
	s_addc_u32 s7, s7, 0
	v_lshlrev_b32_e32 v2, 2, v36
	v_lshl_add_u64 v[4:5], s[6:7], 0, v[2:3]
	v_lshlrev_b32_e32 v2, 12, v6
	v_lshl_add_u64 v[32:33], v[4:5], 0, v[2:3]
	v_add_co_u32_e32 v8, vcc, s81, v32
	global_load_dwordx4 v[4:7], v[32:33], off
	s_nop 0
	v_addc_co_u32_e32 v9, vcc, 0, v33, vcc
	global_load_dwordx4 v[8:11], v[8:9], off
	v_add_co_u32_e32 v12, vcc, s79, v32
	v_add_u32_e32 v2, v44, v45
	s_nop 0
	v_addc_co_u32_e32 v13, vcc, 0, v33, vcc
	global_load_dwordx4 v[12:15], v[12:13], off
	v_add_co_u32_e32 v16, vcc, s80, v32
	s_lshl_b32 s6, s9, 1
	s_nop 0
	v_addc_co_u32_e32 v17, vcc, 0, v33, vcc
	global_load_dwordx4 v[16:19], v[16:17], off
	v_add_co_u32_e32 v20, vcc, s85, v32
	s_add_u32 s6, s8, s6
	s_nop 0
	v_addc_co_u32_e32 v21, vcc, 0, v33, vcc
	global_load_dwordx4 v[20:23], v[20:21], off
	v_add_co_u32_e32 v24, vcc, s86, v32
	s_addc_u32 s7, s3, 0
	s_nop 0
	v_addc_co_u32_e32 v25, vcc, 0, v33, vcc
	global_load_dwordx4 v[24:27], v[24:25], off
	v_add_co_u32_e32 v28, vcc, s87, v32
	v_readlane_b32 s45, v253, 17
	s_nop 0
	v_addc_co_u32_e32 v29, vcc, 0, v33, vcc
	global_load_dwordx4 v[28:31], v[28:29], off
	v_add_co_u32_e32 v32, vcc, s89, v32
	v_readlane_b32 s46, v253, 18
	s_nop 0
	v_addc_co_u32_e32 v33, vcc, 0, v33, vcc
	global_load_dwordx4 v[32:35], v[32:33], off
	v_readlane_b32 s47, v253, 19
	v_readlane_b32 s48, v253, 20
	v_readlane_b32 s49, v253, 21
	v_readlane_b32 s52, v253, 24
	v_readlane_b32 s53, v253, 25
	v_readlane_b32 s54, v253, 26
	v_readlane_b32 s55, v253, 27
	v_readlane_b32 s56, v253, 28
	v_readlane_b32 s57, v253, 29
	v_readlane_b32 s58, v253, 30
	v_readlane_b32 s59, v253, 31
	s_waitcnt vmcnt(0)
	ds_write2_b32 v2, v4, v5 offset1:1
	ds_write2_b32 v2, v6, v7 offset0:2 offset1:3
	v_add_u32_e32 v4, 0x420, v2
	ds_write2_b32 v4, v8, v9 offset1:1
	v_add_u32_e32 v4, 0x428, v2
	ds_write2_b32 v4, v10, v11 offset1:1
	v_add_u32_e32 v4, 0x840, v2
	ds_write2_b32 v4, v12, v13 offset1:1
	v_add_u32_e32 v4, 0x848, v2
	ds_write2_b32 v4, v14, v15 offset1:1
	v_add_u32_e32 v4, 0xc60, v2
	ds_write2_b32 v4, v16, v17 offset1:1
	v_add_u32_e32 v4, 0xc68, v2
	ds_write2_b32 v4, v18, v19 offset1:1
	v_add_u32_e32 v4, 0x1080, v2
	ds_write2_b32 v4, v20, v21 offset1:1
	v_add_u32_e32 v4, 0x1088, v2
	ds_write2_b32 v4, v22, v23 offset1:1
	v_add_u32_e32 v4, 0x14a0, v2
	ds_write2_b32 v4, v24, v25 offset1:1
	v_add_u32_e32 v4, 0x14a8, v2
	ds_write2_b32 v4, v26, v27 offset1:1
	v_add_u32_e32 v4, 0x18c0, v2
	ds_write2_b32 v4, v28, v29 offset1:1
	v_add_u32_e32 v4, 0x18c8, v2
	ds_write2_b32 v4, v30, v31 offset1:1
	v_add_u32_e32 v4, 0x1ce0, v2
	v_add_u32_e32 v2, 0x1ce8, v2
	ds_write2_b32 v4, v32, v33 offset1:1
	ds_write2_b32 v2, v34, v35 offset1:1
	s_waitcnt lgkmcnt(0)
	ds_read2_b32 v[10:11], v49 offset0:33 offset1:41
	ds_read2_b32 v[12:13], v49 offset1:8
	v_lshlrev_b32_e32 v2, 1, v38
	ds_read2_b32 v[14:15], v49 offset0:66 offset1:74
	ds_read2_b32 v[16:17], v49 offset0:99 offset1:107
	ds_read2_b32 v[18:19], v49 offset0:132 offset1:140
	ds_read2_b32 v[20:21], v49 offset0:165 offset1:173
	ds_read2_b32 v[22:23], v49 offset0:198 offset1:206
	ds_read2_b32 v[24:25], v49 offset0:231 offset1:239
	v_lshl_add_u64 v[8:9], s[6:7], 0, v[2:3]
	v_or_b32_e32 v2, s2, v39
	v_lshlrev_b32_e32 v2, 11, v2
	v_lshl_add_u64 v[26:27], v[8:9], 0, v[2:3]
	v_or_b32_e32 v2, s2, v46
	s_waitcnt lgkmcnt(0)
	v_cvt_pk_bf16_f32 v4, v12, v10
	v_lshlrev_b32_e32 v2, 11, v2
	v_cvt_pk_bf16_f32 v5, v14, v16
	v_cvt_pk_bf16_f32 v6, v18, v20
	v_cvt_pk_bf16_f32 v7, v22, v24
	global_store_dwordx4 v[26:27], v[4:7], off sc1
	s_nop 1
	v_cvt_pk_bf16_f32 v4, v13, v11
	v_lshl_add_u64 v[10:11], v[8:9], 0, v[2:3]
	v_cvt_pk_bf16_f32 v5, v15, v17
	v_cvt_pk_bf16_f32 v6, v19, v21
	v_cvt_pk_bf16_f32 v7, v23, v25
	global_store_dwordx4 v[10:11], v[4:7], off sc1
	ds_read2_b32 v[10:11], v49 offset0:16 offset1:24
	ds_read2_b32 v[12:13], v49 offset0:49 offset1:57
	ds_read2_b32 v[14:15], v49 offset0:82 offset1:90
	ds_read2_b32 v[16:17], v49 offset0:115 offset1:123
	ds_read2_b32 v[18:19], v49 offset0:148 offset1:156
	ds_read2_b32 v[20:21], v49 offset0:181 offset1:189
	ds_read2_b32 v[22:23], v49 offset0:214 offset1:222
	ds_read2_b32 v[24:25], v49 offset0:247 offset1:255
	v_or_b32_e32 v2, s2, v47
	v_lshlrev_b32_e32 v2, 11, v2
	v_lshl_add_u64 v[26:27], v[8:9], 0, v[2:3]
	v_or_b32_e32 v2, s2, v48
	v_lshlrev_b32_e32 v2, 11, v2
	s_waitcnt lgkmcnt(6)
	v_cvt_pk_bf16_f32 v4, v10, v12
	s_waitcnt lgkmcnt(4)
	v_cvt_pk_bf16_f32 v5, v14, v16
	s_waitcnt lgkmcnt(2)
	v_cvt_pk_bf16_f32 v6, v18, v20
	s_waitcnt lgkmcnt(0)
	v_cvt_pk_bf16_f32 v7, v22, v24
	v_lshl_add_u64 v[8:9], v[8:9], 0, v[2:3]
	global_store_dwordx4 v[26:27], v[4:7], off sc1
	s_nop 1
	v_cvt_pk_bf16_f32 v4, v11, v13
	v_cvt_pk_bf16_f32 v5, v15, v17
	v_cvt_pk_bf16_f32 v6, v19, v21
	v_cvt_pk_bf16_f32 v7, v23, v25
	global_store_dwordx4 v[8:9], v[4:7], off sc1
	s_waitcnt lgkmcnt(0)

; #define GAS __attribute__((address_space(1)))
; #define LAS __attribute__((address_space(3)))
; #define LDS_WAIT() asm volatile("s_waitcnt lgkmcnt(0)" ::: "memory")
; __device__ __forceinline__ unsigned pk2(float lo, float hi) { unsigned r; asm("v_cvt_pk_bf16_f32 %0, %1, %2" : "=v"(r) : "v"(lo), "v"(hi)); return r; }
; __device__ __forceinline__ void transpose_item(const float* W, int K, int N, bf16* WT, int drow0, int kb, int n0, LAS float* scr, int lane) {
;     const int k0 = 64 * kb; const int c4 = 4 * (lane & 7); const bool ok = (n0 + c4) < N;
;     f32x4 v[8];
; #pragma unroll
;     for (int i = 0; i < 8; ++i) { const int kk = 8 * i + (lane >> 3); v[i] = ok ? *(const f32x4*)(W + (size_t)(k0 + kk) * N + n0 + c4) : (f32x4){0.f, 0.f, 0.f, 0.f}; }
; #pragma unroll
;     for (int i = 0; i < 8; ++i) { const int kk = 8 * i + (lane >> 3); LAS float* d = scr + kk * 33 + c4; d[0] = v[i][0]; d[1] = v[i][1]; d[2] = v[i][2]; d[3] = v[i][3]; }
;     LDS_WAIT(); asm volatile("" ::: "memory");
;     const int c = lane & 7;
; #pragma unroll
;     for (int j = 0; j < 4; ++j) { const int n = (lane >> 3) + 8 * j; const LAS float* s = scr + (8 * c) * 33 + n;
;         v4u o; o.x = pk2(s[0 * 33], s[1 * 33]); o.y = pk2(s[2 * 33], s[3 * 33]); o.z = pk2(s[4 * 33], s[5 * 33]); o.w = pk2(s[6 * 33], s[7 * 33]);
;         *(GAS v4u*)(WT + (size_t)(drow0 + n) * K + k0 + 8 * c) = o; }
;     LDS_WAIT(); asm volatile("" ::: "memory");
; }
; __device__ __forceinline__ void convert_item(const In& I, unsigned char* ws, int it, LAS float* scr, int lane) {
;     ...
;     if (r < 2 * I_NIN) { const int j = r / I_NIN; r -= j * I_NIN; const int kb = r / 88, nb = r % 88;
;         transpose_item(I.nsa_w_in + (size_t)j * D * NSA_IN, D, NSA_IN, Wnin + (size_t)j * NSA_IN_PAD * D, 32 * nb, kb, 32 * nb, scr, lane); return; }
.LBB0_530:
	s_or_b64 exec, exec, s[12:13]
	v_add_u32_e32 v2, v44, v45
	s_waitcnt vmcnt(0)
	ds_write2_b32 v2, v4, v5 offset1:1
	ds_write2_b32 v2, v6, v7 offset0:2 offset1:3
	v_add_u32_e32 v4, 0x420, v2
	ds_write2_b32 v4, v8, v9 offset1:1
	v_add_u32_e32 v4, 0x428, v2
	ds_write2_b32 v4, v10, v11 offset1:1
	v_add_u32_e32 v4, 0x840, v2
	ds_write2_b32 v4, v16, v17 offset1:1
	v_add_u32_e32 v4, 0x848, v2
	ds_write2_b32 v4, v18, v19 offset1:1
	v_add_u32_e32 v4, 0xc60, v2
	ds_write2_b32 v4, v12, v13 offset1:1
	v_add_u32_e32 v4, 0xc68, v2
	ds_write2_b32 v4, v14, v15 offset1:1
	v_add_u32_e32 v4, 0x1080, v2
	ds_write2_b32 v4, v24, v25 offset1:1
	v_add_u32_e32 v4, 0x1088, v2
	ds_write2_b32 v4, v26, v27 offset1:1
	v_add_u32_e32 v4, 0x14a0, v2
	ds_write2_b32 v4, v20, v21 offset1:1
	v_add_u32_e32 v4, 0x14a8, v2
	ds_write2_b32 v4, v22, v23 offset1:1
	v_add_u32_e32 v4, 0x18c0, v2
	ds_write2_b32 v4, v32, v33 offset1:1
	v_add_u32_e32 v4, 0x18c8, v2
	s_and_b64 s[2:3], s[10:11], exec
	ds_write2_b32 v4, v34, v35 offset1:1
	v_add_u32_e32 v4, 0x1ce0, v2
	v_add_u32_e32 v2, 0x1ce8, v2
	s_cselect_b32 s2, 0x580000, 0
	ds_write2_b32 v4, v28, v29 offset1:1
	ds_write2_b32 v2, v30, v31 offset1:1
	s_add_u32 s7, s20, s2
	s_waitcnt lgkmcnt(0)
	s_addc_u32 s10, s21, 0
	s_ashr_i32 s9, s8, 31
	s_lshl_b64 s[2:3], s[8:9], 1
	ds_read2_b32 v[8:9], v49 offset0:33 offset1:41
	ds_read2_b32 v[10:11], v49 offset1:8
	ds_read2_b32 v[12:13], v49 offset0:66 offset1:74
	ds_read2_b32 v[14:15], v49 offset0:99 offset1:107
	ds_read2_b32 v[16:17], v49 offset0:132 offset1:140
	ds_read2_b32 v[18:19], v49 offset0:165 offset1:173
	ds_read2_b32 v[20:21], v49 offset0:198 offset1:206
	ds_read2_b32 v[22:23], v49 offset0:231 offset1:239
	s_add_u32 s2, s7, s2
	v_or_b32_e32 v26, s6, v39
	s_addc_u32 s3, s10, s3
	v_lshlrev_b32_e32 v2, 1, v38
	v_ashrrev_i32_e32 v27, 31, v26
	v_lshl_add_u64 v[24:25], s[2:3], 0, v[2:3]
	v_lshlrev_b64 v[26:27], 11, v[26:27]
	s_waitcnt lgkmcnt(0)
	v_cvt_pk_bf16_f32 v4, v10, v8
	v_lshl_add_u64 v[26:27], v[24:25], 0, v[26:27]
	v_or_b32_e32 v8, s6, v46
	v_cvt_pk_bf16_f32 v5, v12, v14
	v_cvt_pk_bf16_f32 v6, v16, v18
	v_cvt_pk_bf16_f32 v7, v20, v22
	global_store_dwordx4 v[26:27], v[4:7], off sc1
	s_nop 1
	v_cvt_pk_bf16_f32 v4, v11, v9
	v_ashrrev_i32_e32 v9, 31, v8
	v_lshlrev_b64 v[8:9], 11, v[8:9]
	v_cvt_pk_bf16_f32 v5, v13, v15
	v_cvt_pk_bf16_f32 v6, v17, v19
	v_cvt_pk_bf16_f32 v7, v21, v23
	v_lshl_add_u64 v[8:9], v[24:25], 0, v[8:9]
	ds_read2_b32 v[10:11], v49 offset0:16 offset1:24
	ds_read2_b32 v[12:13], v49 offset0:49 offset1:57
	ds_read2_b32 v[14:15], v49 offset0:82 offset1:90
	ds_read2_b32 v[16:17], v49 offset0:115 offset1:123
	ds_read2_b32 v[18:19], v49 offset0:148 offset1:156
	ds_read2_b32 v[20:21], v49 offset0:181 offset1:189
	ds_read2_b32 v[22:23], v49 offset0:214 offset1:222
	ds_read2_b32 v[26:27], v49 offset0:247 offset1:255
	global_store_dwordx4 v[8:9], v[4:7], off sc1
	v_or_b32_e32 v8, s6, v47
	v_ashrrev_i32_e32 v9, 31, v8
	v_lshlrev_b64 v[8:9], 11, v[8:9]
	v_lshl_add_u64 v[8:9], v[24:25], 0, v[8:9]
	s_waitcnt lgkmcnt(6)
	v_cvt_pk_bf16_f32 v4, v10, v12
	s_waitcnt lgkmcnt(4)
	v_cvt_pk_bf16_f32 v5, v14, v16
	s_waitcnt lgkmcnt(2)
	v_cvt_pk_bf16_f32 v6, v18, v20
	s_waitcnt lgkmcnt(0)
	v_cvt_pk_bf16_f32 v7, v22, v26
	global_store_dwordx4 v[8:9], v[4:7], off sc1
	v_or_b32_e32 v8, s6, v48
	v_ashrrev_i32_e32 v9, 31, v8
	v_lshlrev_b64 v[8:9], 11, v[8:9]
	v_lshl_add_u64 v[8:9], v[24:25], 0, v[8:9]
	v_cvt_pk_bf16_f32 v4, v11, v13
	v_cvt_pk_bf16_f32 v5, v15, v17
	v_cvt_pk_bf16_f32 v6, v19, v21
	v_cvt_pk_bf16_f32 v7, v23, v27
	global_store_dwordx4 v[8:9], v[4:7], off sc1
	s_waitcnt lgkmcnt(0)

; #define GAS __attribute__((address_space(1)))
; #define LAS __attribute__((address_space(3)))
; #define LDS_WAIT() asm volatile("s_waitcnt lgkmcnt(0)" ::: "memory")
; __device__ __forceinline__ unsigned pk2(float lo, float hi) { unsigned r; asm("v_cvt_pk_bf16_f32 %0, %1, %2" : "=v"(r) : "v"(lo), "v"(hi)); return r; }
; __device__ __forceinline__ void transpose_item(const float* W, int K, int N, bf16* WT, int drow0, int kb, int n0, LAS float* scr, int lane) {
;     const int k0 = 64 * kb; const int c4 = 4 * (lane & 7); const bool ok = (n0 + c4) < N;
;     f32x4 v[8];
; #pragma unroll
;     for (int i = 0; i < 8; ++i) { const int kk = 8 * i + (lane >> 3); v[i] = ok ? *(const f32x4*)(W + (size_t)(k0 + kk) * N + n0 + c4) : (f32x4){0.f, 0.f, 0.f, 0.f}; }
; #pragma unroll
;     for (int i = 0; i < 8; ++i) { const int kk = 8 * i + (lane >> 3); LAS float* d = scr + kk * 33 + c4; d[0] = v[i][0]; d[1] = v[i][1]; d[2] = v[i][2]; d[3] = v[i][3]; }
;     LDS_WAIT(); asm volatile("" ::: "memory");
;     const int c = lane & 7;
; #pragma unroll
;     for (int j = 0; j < 4; ++j) { const int n = (lane >> 3) + 8 * j; const LAS float* s = scr + (8 * c) * 33 + n;
;         v4u o; o.x = pk2(s[0 * 33], s[1 * 33]); o.y = pk2(s[2 * 33], s[3 * 33]); o.z = pk2(s[4 * 33], s[5 * 33]); o.w = pk2(s[6 * 33], s[7 * 33]);
;         *(GAS v4u*)(WT + (size_t)(drow0 + n) * K + k0 + 8 * c) = o; }
;     LDS_WAIT(); asm volatile("" ::: "memory");
; }
; __device__ __forceinline__ void convert_item(const In& I, unsigned char* ws, int it, LAS float* scr, int lane) {
;     ...
;     if (r < T0) { const int f = r / I_FFN; r -= f * I_FFN;
;         if (r < 2 * I_G) { const int up = r >= I_G; r -= up * I_G; const int kb = r / 88, nb = r % 88;
;             transpose_item((up ? I.w_up : I.w_gate) + (size_t)f * D * FF, D, FF, Wgu + (size_t)f * NGU * D, 256 * (nb >> 2) + 32 * (nb & 3) + 128 * up, kb, 32 * nb, scr, lane); }
;         else { r -= 2 * I_G; const int kb = r / 32, nb = r % 32; transpose_item(I.w_down + (size_t)f * FF * D, FF, D, Wd + (size_t)f * D * FF, 32 * nb, kb, 32 * nb, scr, lane); }
.LBB0_532:
	s_andn2_b64 vcc, exec, s[2:3]
	s_cbranch_vccnz .LBB0_477
	s_mul_hi_i32 s2, s42, 0x3e0f83e1
	s_lshr_b32 s3, s2, 31
	s_ashr_i32 s6, s2, 10
	s_add_i32 s6, s6, s3
	s_mul_i32 s2, s6, 0xffffef80
	s_add_i32 s7, s18, s2
	s_add_i32 s7, s7, 0xa800
	s_cmpk_gt_i32 s7, 0xaff
	s_mov_b64 s[2:3], -1
	s_cbranch_scc0 .LBB0_535
	v_readlane_b32 s44, v253, 0
	s_mul_i32 s3, s6, 0xb00000
	v_readlane_b32 s52, v253, 8
	s_mul_hi_i32 s2, s6, 0xb00000
	v_readlane_b32 s53, v253, 9
	s_add_u32 s9, s52, s3
	s_addc_u32 s11, s53, s2
	s_mul_i32 s3, s6, 0x580000
	s_mul_hi_i32 s2, s6, 0x580000
	s_add_u32 s3, s1, s3
	s_mul_i32 s10, s6, 0xffffdf00
	s_addc_u32 s8, s19, s2
	s_add_i32 s10, s41, s10
	s_add_i32 s10, s10, 0x14800
	s_and_b32 s2, s40, 0x3e0
	s_andn2_b32 s10, s10, 63
	s_add_i32 s68, s10, 0xffffea00
	s_lshl_b32 s10, s2, 2
	v_or_b32_e32 v32, s68, v39
	s_add_u32 s10, s9, s10
	s_addc_u32 s11, s11, 0
	v_lshlrev_b32_e32 v2, 2, v36
	v_ashrrev_i32_e32 v33, 31, v32
	v_or_b32_e32 v8, 8, v32
	v_lshl_add_u64 v[34:35], s[10:11], 0, v[2:3]
	v_lshlrev_b64 v[4:5], 12, v[32:33]
	v_ashrrev_i32_e32 v9, 31, v8
	v_lshl_add_u64 v[4:5], v[34:35], 0, v[4:5]
	v_lshlrev_b64 v[8:9], 12, v[8:9]
	v_or_b32_e32 v12, 16, v32
	global_load_dwordx4 v[4:7], v[4:5], off
	v_lshl_add_u64 v[8:9], v[34:35], 0, v[8:9]
	v_ashrrev_i32_e32 v13, 31, v12
	global_load_dwordx4 v[8:11], v[8:9], off
	v_lshlrev_b64 v[12:13], 12, v[12:13]
	v_or_b32_e32 v16, 24, v32
	v_lshl_add_u64 v[12:13], v[34:35], 0, v[12:13]
	v_ashrrev_i32_e32 v17, 31, v16
	global_load_dwordx4 v[12:15], v[12:13], off
	v_lshlrev_b64 v[16:17], 12, v[16:17]
	v_or_b32_e32 v20, 32, v32
	v_lshl_add_u64 v[16:17], v[34:35], 0, v[16:17]
	v_ashrrev_i32_e32 v21, 31, v20
	global_load_dwordx4 v[16:19], v[16:17], off
	v_lshlrev_b64 v[20:21], 12, v[20:21]
	v_or_b32_e32 v24, 40, v32
	v_lshl_add_u64 v[20:21], v[34:35], 0, v[20:21]
	v_ashrrev_i32_e32 v25, 31, v24
	global_load_dwordx4 v[20:23], v[20:21], off
	v_lshlrev_b64 v[24:25], 12, v[24:25]
	v_or_b32_e32 v28, 48, v32
	v_lshl_add_u64 v[24:25], v[34:35], 0, v[24:25]
	v_ashrrev_i32_e32 v29, 31, v28
	global_load_dwordx4 v[24:27], v[24:25], off
	v_lshlrev_b64 v[28:29], 12, v[28:29]
	v_or_b32_e32 v32, 56, v32
	v_lshl_add_u64 v[28:29], v[34:35], 0, v[28:29]
	v_ashrrev_i32_e32 v33, 31, v32
	global_load_dwordx4 v[28:31], v[28:29], off
	v_lshlrev_b64 v[32:33], 12, v[32:33]
	v_lshl_add_u64 v[32:33], v[34:35], 0, v[32:33]
	global_load_dwordx4 v[32:35], v[32:33], off
	v_add_u32_e32 v2, v44, v45
	s_lshl_b64 s[10:11], s[68:69], 1
	s_add_u32 s10, s3, s10
	s_addc_u32 s11, s8, s11
	v_readlane_b32 s45, v253, 1
	v_readlane_b32 s46, v253, 2
	v_readlane_b32 s47, v253, 3
	v_readlane_b32 s48, v253, 4
	v_readlane_b32 s49, v253, 5
	v_readlane_b32 s50, v253, 6
	v_readlane_b32 s51, v253, 7
	v_readlane_b32 s54, v253, 10
	v_readlane_b32 s55, v253, 11
	v_readlane_b32 s56, v253, 12
	v_readlane_b32 s57, v253, 13
	v_readlane_b32 s58, v253, 14
	v_readlane_b32 s59, v253, 15
	s_waitcnt vmcnt(0)
	ds_write2_b32 v2, v4, v5 offset1:1
	ds_write2_b32 v2, v6, v7 offset0:2 offset1:3
	v_add_u32_e32 v4, 0x420, v2
	ds_write2_b32 v4, v8, v9 offset1:1
	v_add_u32_e32 v4, 0x428, v2
	ds_write2_b32 v4, v10, v11 offset1:1
	v_add_u32_e32 v4, 0x840, v2
	ds_write2_b32 v4, v12, v13 offset1:1
	v_add_u32_e32 v4, 0x848, v2
	ds_write2_b32 v4, v14, v15 offset1:1
	v_add_u32_e32 v4, 0xc60, v2
	ds_write2_b32 v4, v16, v17 offset1:1
	v_add_u32_e32 v4, 0xc68, v2
	ds_write2_b32 v4, v18, v19 offset1:1
	v_add_u32_e32 v4, 0x1080, v2
	ds_write2_b32 v4, v20, v21 offset1:1
	v_add_u32_e32 v4, 0x1088, v2
	ds_write2_b32 v4, v22, v23 offset1:1
	v_add_u32_e32 v4, 0x14a0, v2
	ds_write2_b32 v4, v24, v25 offset1:1
	v_add_u32_e32 v4, 0x14a8, v2
	ds_write2_b32 v4, v26, v27 offset1:1
	v_add_u32_e32 v4, 0x18c0, v2
	ds_write2_b32 v4, v28, v29 offset1:1
	v_add_u32_e32 v4, 0x18c8, v2
	ds_write2_b32 v4, v30, v31 offset1:1
	v_add_u32_e32 v4, 0x1ce0, v2
	v_add_u32_e32 v2, 0x1ce8, v2
	ds_write2_b32 v4, v32, v33 offset1:1
	ds_write2_b32 v2, v34, v35 offset1:1
	s_waitcnt lgkmcnt(0)
	ds_read2_b32 v[10:11], v49 offset0:33 offset1:41
	ds_read2_b32 v[12:13], v49 offset1:8
	v_lshlrev_b32_e32 v2, 1, v38
	ds_read2_b32 v[14:15], v49 offset0:66 offset1:74
	ds_read2_b32 v[16:17], v49 offset0:99 offset1:107
	ds_read2_b32 v[18:19], v49 offset0:132 offset1:140
	ds_read2_b32 v[20:21], v49 offset0:165 offset1:173
	ds_read2_b32 v[22:23], v49 offset0:198 offset1:206
	ds_read2_b32 v[24:25], v49 offset0:231 offset1:239
	v_lshl_add_u64 v[8:9], s[10:11], 0, v[2:3]
	v_or_b32_e32 v2, s2, v39
	v_mul_u32_u24_e32 v2, 0x1600, v2
	v_lshl_add_u64 v[26:27], v[8:9], 0, v[2:3]
	v_or_b32_e32 v2, s2, v46
	s_waitcnt lgkmcnt(0)
	v_cvt_pk_bf16_f32 v4, v12, v10
	v_mul_u32_u24_e32 v2, 0x1600, v2
	v_cvt_pk_bf16_f32 v5, v14, v16
	v_cvt_pk_bf16_f32 v6, v18, v20
	v_cvt_pk_bf16_f32 v7, v22, v24
	global_store_dwordx4 v[26:27], v[4:7], off sc1
	s_nop 1
	v_cvt_pk_bf16_f32 v4, v13, v11
	v_lshl_add_u64 v[10:11], v[8:9], 0, v[2:3]
	v_cvt_pk_bf16_f32 v5, v15, v17
	v_cvt_pk_bf16_f32 v6, v19, v21
	v_cvt_pk_bf16_f32 v7, v23, v25
	global_store_dwordx4 v[10:11], v[4:7], off sc1
	ds_read2_b32 v[10:11], v49 offset0:16 offset1:24
	ds_read2_b32 v[12:13], v49 offset0:49 offset1:57
	ds_read2_b32 v[14:15], v49 offset0:82 offset1:90
	ds_read2_b32 v[16:17], v49 offset0:115 offset1:123
	ds_read2_b32 v[18:19], v49 offset0:148 offset1:156
	ds_read2_b32 v[20:21], v49 offset0:181 offset1:189
	ds_read2_b32 v[22:23], v49 offset0:214 offset1:222
	ds_read2_b32 v[24:25], v49 offset0:247 offset1:255
	v_or_b32_e32 v2, s2, v47
	v_mul_u32_u24_e32 v2, 0x1600, v2
	v_lshl_add_u64 v[26:27], v[8:9], 0, v[2:3]
	v_or_b32_e32 v2, s2, v48
	v_mul_u32_u24_e32 v2, 0x1600, v2
	s_waitcnt lgkmcnt(6)
	v_cvt_pk_bf16_f32 v4, v10, v12
	s_waitcnt lgkmcnt(4)
	v_cvt_pk_bf16_f32 v5, v14, v16
	s_waitcnt lgkmcnt(2)
	v_cvt_pk_bf16_f32 v6, v18, v20
	s_waitcnt lgkmcnt(0)
	v_cvt_pk_bf16_f32 v7, v22, v24
	v_lshl_add_u64 v[8:9], v[8:9], 0, v[2:3]
	global_store_dwordx4 v[26:27], v[4:7], off sc1
	s_mov_b64 s[2:3], 0
	s_nop 0
	v_cvt_pk_bf16_f32 v4, v11, v13
	v_cvt_pk_bf16_f32 v5, v15, v17
	v_cvt_pk_bf16_f32 v6, v19, v21
	v_cvt_pk_bf16_f32 v7, v23, v25
	global_store_dwordx4 v[8:9], v[4:7], off sc1
	s_waitcnt lgkmcnt(0)
; #define GAS __attribute__((address_space(1)))
; #define LAS __attribute__((address_space(3)))
; #define LDS_WAIT() asm volatile("s_waitcnt lgkmcnt(0)" ::: "memory")
; __device__ __forceinline__ unsigned pk2(float lo, float hi) { unsigned r; asm("v_cvt_pk_bf16_f32 %0, %1, %2" : "=v"(r) : "v"(lo), "v"(hi)); return r; }
; __device__ __forceinline__ void transpose_item(const float* W, int K, int N, bf16* WT, int drow0, int kb, int n0, LAS float* scr, int lane) {
;     const int k0 = 64 * kb; const int c4 = 4 * (lane & 7); const bool ok = (n0 + c4) < N;
;     f32x4 v[8];
; #pragma unroll
;     for (int i = 0; i < 8; ++i) { const int kk = 8 * i + (lane >> 3); v[i] = ok ? *(const f32x4*)(W + (size_t)(k0 + kk) * N + n0 + c4) : (f32x4){0.f, 0.f, 0.f, 0.f}; }
; #pragma unroll
;     for (int i = 0; i < 8; ++i) { const int kk = 8 * i + (lane >> 3); LAS float* d = scr + kk * 33 + c4; d[0] = v[i][0]; d[1] = v[i][1]; d[2] = v[i][2]; d[3] = v[i][3]; }
;     LDS_WAIT(); asm volatile("" ::: "memory");
;     const int c = lane & 7;
; #pragma unroll
;     for (int j = 0; j < 4; ++j) { const int n = (lane >> 3) + 8 * j; const LAS float* s = scr + (8 * c) * 33 + n;
;         v4u o; o.x = pk2(s[0 * 33], s[1 * 33]); o.y = pk2(s[2 * 33], s[3 * 33]); o.z = pk2(s[4 * 33], s[5 * 33]); o.w = pk2(s[6 * 33], s[7 * 33]);
;         *(GAS v4u*)(WT + (size_t)(drow0 + n) * K + k0 + 8 * c) = o; }
;     LDS_WAIT(); asm volatile("" ::: "memory");
; }
; __device__ __forceinline__ void convert_item(const In& I, unsigned char* ws, int it, LAS float* scr, int lane) {
;     ...
;         if (r < 2 * I_G) { const int up = r >= I_G; r -= up * I_G; const int kb = r / 88, nb = r % 88;
;             transpose_item((up ? I.w_up : I.w_gate) + (size_t)f * D * FF, D, FF, Wgu + (size_t)f * NGU * D, 256 * (nb >> 2) + 32 * (nb & 3) + 128 * up, kb, 32 * nb, scr, lane); }
.LBB0_535:
	s_andn2_b64 vcc, exec, s[2:3]
	s_cbranch_vccnz .LBB0_477
	s_cmpk_gt_i32 s7, 0x57f
	v_readlane_b32 s44, v253, 0
	s_cselect_b32 s2, 0xfffffa80, 0
	s_mul_i32 s3, s6, 0x1080
	v_readlane_b32 s48, v253, 4
	v_readlane_b32 s49, v253, 5
	v_readlane_b32 s50, v253, 6
	v_readlane_b32 s51, v253, 7
	s_cselect_b32 s7, 0x80, 0
	s_cselect_b32 s8, s50, s48
	s_cselect_b32 s9, s51, s49
	s_sub_i32 s2, s2, s3
	s_add_i32 s2, s18, s2
	s_add_i32 s2, s2, 0xa800
	s_mul_hi_i32 s3, s2, 0x2e8ba2e9
	s_lshr_b32 s10, s3, 31
	s_ashr_i32 s3, s3, 4
	s_add_i32 s3, s3, s10
	s_mul_i32 s10, s3, 0x58
	s_sub_i32 s2, s2, s10
	s_mul_hi_i32 s10, s6, 0xb00000
	s_mul_i32 s6, s6, 0xb00000
	s_add_u32 s11, s8, s6
	s_addc_u32 s12, s9, s10
	s_add_u32 s13, s28, s6
	s_addc_u32 s10, s29, s10
	s_lshl_b32 s8, s2, 5
	s_lshl_b32 s6, s2, 6
	s_and_b32 s2, s8, 0x60
	s_and_b32 s6, s6, 0xffffff00
	s_or_b32 s2, s2, s7
	s_ashr_i32 s9, s8, 31
	s_or_b32 s6, s2, s6
	s_lshl_b32 s2, s3, 6
	s_lshl_b64 s[8:9], s[8:9], 2
	s_add_u32 s8, s11, s8
	s_addc_u32 s9, s12, s9
	v_lshlrev_b32_e32 v2, 2, v36
	v_or_b32_e32 v34, s2, v39
	v_lshl_add_u64 v[32:33], s[8:9], 0, v[2:3]
	s_movk_i32 s3, 0x2c00
	v_mad_i64_i32 v[4:5], s[8:9], v34, s3, v[32:33]
	v_or_b32_e32 v2, 8, v34
	global_load_dwordx4 v[4:7], v[4:5], off
	v_mad_i64_i32 v[8:9], s[8:9], v2, s3, v[32:33]
	global_load_dwordx4 v[8:11], v[8:9], off
	v_or_b32_e32 v2, 16, v34
	v_mad_i64_i32 v[12:13], s[8:9], v2, s3, v[32:33]
	global_load_dwordx4 v[12:15], v[12:13], off
	v_or_b32_e32 v2, 24, v34
	v_mad_i64_i32 v[16:17], s[8:9], v2, s3, v[32:33]
	global_load_dwordx4 v[16:19], v[16:17], off
	v_or_b32_e32 v2, 32, v34
	v_mad_i64_i32 v[20:21], s[8:9], v2, s3, v[32:33]
	global_load_dwordx4 v[20:23], v[20:21], off
	v_or_b32_e32 v2, 40, v34
	v_mad_i64_i32 v[24:25], s[8:9], v2, s3, v[32:33]
	global_load_dwordx4 v[24:27], v[24:25], off
	v_or_b32_e32 v2, 48, v34
	v_mad_i64_i32 v[28:29], s[8:9], v2, s3, v[32:33]
	global_load_dwordx4 v[28:31], v[28:29], off
	v_or_b32_e32 v2, 56, v34
	v_mad_i64_i32 v[32:33], s[8:9], v2, s3, v[32:33]
	global_load_dwordx4 v[32:35], v[32:33], off
	v_add_u32_e32 v2, v44, v45
	s_ashr_i32 s3, s2, 31
	s_lshl_b64 s[2:3], s[2:3], 1
	s_add_u32 s2, s13, s2
	s_addc_u32 s3, s10, s3
	v_readlane_b32 s45, v253, 1
	v_readlane_b32 s46, v253, 2
	v_readlane_b32 s47, v253, 3
	v_readlane_b32 s52, v253, 8
	v_readlane_b32 s53, v253, 9
	v_readlane_b32 s54, v253, 10
	v_readlane_b32 s55, v253, 11
	v_readlane_b32 s56, v253, 12
	v_readlane_b32 s57, v253, 13
	v_readlane_b32 s58, v253, 14
	v_readlane_b32 s59, v253, 15
	s_waitcnt vmcnt(0)
	ds_write2_b32 v2, v4, v5 offset1:1
	ds_write2_b32 v2, v6, v7 offset0:2 offset1:3
	v_add_u32_e32 v4, 0x420, v2
	ds_write2_b32 v4, v8, v9 offset1:1
	v_add_u32_e32 v4, 0x428, v2
	ds_write2_b32 v4, v10, v11 offset1:1
	v_add_u32_e32 v4, 0x840, v2
	ds_write2_b32 v4, v12, v13 offset1:1
	v_add_u32_e32 v4, 0x848, v2
	ds_write2_b32 v4, v14, v15 offset1:1
	v_add_u32_e32 v4, 0xc60, v2
	ds_write2_b32 v4, v16, v17 offset1:1
	v_add_u32_e32 v4, 0xc68, v2
	ds_write2_b32 v4, v18, v19 offset1:1
	v_add_u32_e32 v4, 0x1080, v2
	ds_write2_b32 v4, v20, v21 offset1:1
	v_add_u32_e32 v4, 0x1088, v2
	ds_write2_b32 v4, v22, v23 offset1:1
	v_add_u32_e32 v4, 0x14a0, v2
	ds_write2_b32 v4, v24, v25 offset1:1
	v_add_u32_e32 v4, 0x14a8, v2
	ds_write2_b32 v4, v26, v27 offset1:1
	v_add_u32_e32 v4, 0x18c0, v2
	ds_write2_b32 v4, v28, v29 offset1:1
	v_add_u32_e32 v4, 0x18c8, v2
	ds_write2_b32 v4, v30, v31 offset1:1
	v_add_u32_e32 v4, 0x1ce0, v2
	v_add_u32_e32 v2, 0x1ce8, v2
	ds_write2_b32 v4, v32, v33 offset1:1
	ds_write2_b32 v2, v34, v35 offset1:1
	s_waitcnt lgkmcnt(0)
	ds_read2_b32 v[10:11], v49 offset0:33 offset1:41
	ds_read2_b32 v[12:13], v49 offset1:8
	ds_read2_b32 v[14:15], v49 offset0:66 offset1:74
	ds_read2_b32 v[16:17], v49 offset0:99 offset1:107
	ds_read2_b32 v[18:19], v49 offset0:132 offset1:140
	ds_read2_b32 v[20:21], v49 offset0:165 offset1:173
	ds_read2_b32 v[22:23], v49 offset0:198 offset1:206
	ds_read2_b32 v[24:25], v49 offset0:231 offset1:239
	v_or_b32_e32 v26, s6, v39
	v_lshlrev_b32_e32 v2, 1, v38
	v_ashrrev_i32_e32 v27, 31, v26
	v_lshl_add_u64 v[8:9], s[2:3], 0, v[2:3]
	v_lshlrev_b64 v[26:27], 11, v[26:27]
	s_waitcnt lgkmcnt(0)
	v_cvt_pk_bf16_f32 v4, v12, v10
	v_lshl_add_u64 v[26:27], v[8:9], 0, v[26:27]
	v_or_b32_e32 v10, s6, v46
	v_cvt_pk_bf16_f32 v5, v14, v16
	v_cvt_pk_bf16_f32 v6, v18, v20
	v_cvt_pk_bf16_f32 v7, v22, v24
	global_store_dwordx4 v[26:27], v[4:7], off sc1
	v_or_b32_e32 v26, s6, v47
	v_ashrrev_i32_e32 v27, 31, v26
	v_cvt_pk_bf16_f32 v4, v13, v11
	v_ashrrev_i32_e32 v11, 31, v10
	v_lshlrev_b64 v[10:11], 11, v[10:11]
	v_lshl_add_u64 v[10:11], v[8:9], 0, v[10:11]
	v_cvt_pk_bf16_f32 v5, v15, v17
	v_cvt_pk_bf16_f32 v6, v19, v21
	v_cvt_pk_bf16_f32 v7, v23, v25
	global_store_dwordx4 v[10:11], v[4:7], off sc1
	ds_read2_b32 v[10:11], v49 offset0:16 offset1:24
	ds_read2_b32 v[12:13], v49 offset0:49 offset1:57
	ds_read2_b32 v[14:15], v49 offset0:82 offset1:90
	ds_read2_b32 v[16:17], v49 offset0:115 offset1:123
	ds_read2_b32 v[18:19], v49 offset0:148 offset1:156
	ds_read2_b32 v[20:21], v49 offset0:181 offset1:189
	ds_read2_b32 v[22:23], v49 offset0:214 offset1:222
	ds_read2_b32 v[24:25], v49 offset0:247 offset1:255
	v_lshlrev_b64 v[26:27], 11, v[26:27]
	s_waitcnt lgkmcnt(6)
	v_cvt_pk_bf16_f32 v4, v10, v12
	v_lshl_add_u64 v[26:27], v[8:9], 0, v[26:27]
	v_or_b32_e32 v10, s6, v48
	s_waitcnt lgkmcnt(4)
	v_cvt_pk_bf16_f32 v5, v14, v16
	s_waitcnt lgkmcnt(2)
	v_cvt_pk_bf16_f32 v6, v18, v20
	s_waitcnt lgkmcnt(0)
	v_cvt_pk_bf16_f32 v7, v22, v24
	global_store_dwordx4 v[26:27], v[4:7], off sc1
	s_nop 1
	v_cvt_pk_bf16_f32 v4, v11, v13
	v_ashrrev_i32_e32 v11, 31, v10
	v_lshlrev_b64 v[10:11], 11, v[10:11]
	v_lshl_add_u64 v[8:9], v[8:9], 0, v[10:11]
	v_cvt_pk_bf16_f32 v5, v15, v17
	v_cvt_pk_bf16_f32 v6, v19, v21
	v_cvt_pk_bf16_f32 v7, v23, v25
	global_store_dwordx4 v[8:9], v[4:7], off sc1
	s_waitcnt lgkmcnt(0)
	s_branch .LBB0_477

; #define GAS __attribute__((address_space(1)))
; #define LAS __attribute__((address_space(3)))
; #define LDS_WAIT() asm volatile("s_waitcnt lgkmcnt(0)" ::: "memory")
; __device__ __forceinline__ unsigned pk2(float lo, float hi) { unsigned r; asm("v_cvt_pk_bf16_f32 %0, %1, %2" : "=v"(r) : "v"(lo), "v"(hi)); return r; }
; __device__ __forceinline__ void transpose_item(const float* W, int K, int N, bf16* WT, int drow0, int kb, int n0, LAS float* scr, int lane) {
;     const int k0 = 64 * kb; const int c4 = 4 * (lane & 7); const bool ok = (n0 + c4) < N;
;     f32x4 v[8];
; #pragma unroll
;     for (int i = 0; i < 8; ++i) { const int kk = 8 * i + (lane >> 3); v[i] = ok ? *(const f32x4*)(W + (size_t)(k0 + kk) * N + n0 + c4) : (f32x4){0.f, 0.f, 0.f, 0.f}; }
; #pragma unroll
;     for (int i = 0; i < 8; ++i) { const int kk = 8 * i + (lane >> 3); LAS float* d = scr + kk * 33 + c4; d[0] = v[i][0]; d[1] = v[i][1]; d[2] = v[i][2]; d[3] = v[i][3]; }
;     LDS_WAIT(); asm volatile("" ::: "memory");
;     const int c = lane & 7;
; #pragma unroll
;     for (int j = 0; j < 4; ++j) { const int n = (lane >> 3) + 8 * j; const LAS float* s = scr + (8 * c) * 33 + n;
;         v4u o; o.x = pk2(s[0 * 33], s[1 * 33]); o.y = pk2(s[2 * 33], s[3 * 33]); o.z = pk2(s[4 * 33], s[5 * 33]); o.w = pk2(s[6 * 33], s[7 * 33]);
;         *(GAS v4u*)(WT + (size_t)(drow0 + n) * K + k0 + 8 * c) = o; }
;     LDS_WAIT(); asm volatile("" ::: "memory");
; }
; __device__ __forceinline__ void convert_item(const In& I, unsigned char* ws, int it, LAS float* scr, int lane) {
;     ...
;     { const int jk = r >> 3; r &= 7; const int kb = r >> 1, nb = r & 1;
;         transpose_item(I.nsa_w2 + (size_t)jk * 256 * 64, 256, 64, W2t + (size_t)jk * 64 * 256, 32 * nb, kb, 32 * nb, scr, lane); }
.LBB0_540:
	s_add_i32 s30, s14, s16
	s_add_i32 s34, s30, 0xa800
	s_cmp_gt_i32 s34, 0x83ff
	s_mov_b64 s[2:3], -1
	s_cbranch_scc0 .LBB0_594
	s_cmpk_gt_u32 s34, 0x8eff
	s_cbranch_scc0 .LBB0_575
	s_cmpk_gt_u32 s34, 0x92ff
	s_cbranch_scc0 .LBB0_572
	s_cmpk_gt_u32 s34, 0x9fff
	s_cbranch_scc0 .LBB0_553
	s_cmpk_gt_u32 s34, 0xa3ff
	s_cbranch_scc0 .LBB0_550
	s_cmpk_gt_u32 s34, 0xa7ff
	s_cbranch_scc0 .LBB0_547
	s_lshr_b32 s68, s30, 3
	v_readlane_b32 s40, v253, 16
	s_lshl_b64 s[2:3], s[68:69], 16
	v_readlane_b32 s44, v253, 20
	v_readlane_b32 s45, v253, 21
	s_add_u32 s5, s44, s2
	s_addc_u32 s6, s45, s3
	s_lshl_b64 s[2:3], s[68:69], 15
	s_add_u32 s7, s26, s2
	s_addc_u32 s8, s27, s3
	s_and_b32 s4, s33, 32
	s_and_b32 s9, s33, 0xc0
	s_lshl_b32 s2, s4, 2
	s_add_u32 s2, s5, s2
	v_or_b32_e32 v2, s9, v37
	s_addc_u32 s3, s6, 0
	v_lshlrev_b32_e32 v4, 2, v36
	v_mov_b32_e32 v5, v3
	v_lshl_add_u64 v[4:5], s[2:3], 0, v[4:5]
	v_lshlrev_b32_e32 v6, 8, v2
	v_mov_b32_e32 v7, v3
	v_lshl_add_u64 v[28:29], v[4:5], 0, v[6:7]
	global_load_dwordx4 v[4:7], v[28:29], off
	global_load_dwordx4 v[8:11], v[28:29], off offset:2048
	v_add_co_u32_e32 v16, vcc, s84, v28
	s_movk_i32 s2, 0x3000
	s_nop 0
	v_addc_co_u32_e32 v17, vcc, 0, v29, vcc
	v_add_co_u32_e32 v24, vcc, s74, v28
	v_add_u32_e32 v2, v39, v44
	s_nop 0
	v_addc_co_u32_e32 v25, vcc, 0, v29, vcc
	global_load_dwordx4 v[12:15], v[24:25], off offset:-4096
	s_nop 0
	global_load_dwordx4 v[16:19], v[16:17], off offset:2048
	s_nop 0
	global_load_dwordx4 v[20:23], v[24:25], off
	s_nop 0
	global_load_dwordx4 v[24:27], v[24:25], off offset:2048
	v_add_co_u32_e32 v32, vcc, s2, v28
	s_lshl_b32 s2, s9, 1
	s_nop 0
	v_addc_co_u32_e32 v33, vcc, 0, v29, vcc
	global_load_dwordx4 v[28:31], v[32:33], off
	s_nop 0
	global_load_dwordx4 v[32:35], v[32:33], off offset:2048
	s_add_u32 s2, s7, s2
	s_addc_u32 s3, s8, 0
	v_readlane_b32 s41, v253, 17
	v_readlane_b32 s42, v253, 18
	v_readlane_b32 s43, v253, 19
	v_readlane_b32 s46, v253, 22
	v_readlane_b32 s47, v253, 23
	v_readlane_b32 s48, v253, 24
	v_readlane_b32 s49, v253, 25
	v_readlane_b32 s50, v253, 26
	v_readlane_b32 s51, v253, 27
	v_readlane_b32 s52, v253, 28
	v_readlane_b32 s53, v253, 29
	v_readlane_b32 s54, v253, 30
	v_readlane_b32 s55, v253, 31
	s_waitcnt vmcnt(0)
	ds_write2_b32 v2, v4, v5 offset1:1
	ds_write2_b32 v2, v6, v7 offset0:2 offset1:3
	v_add_u32_e32 v4, 0x420, v2
	ds_write2_b32 v4, v8, v9 offset1:1
	v_add_u32_e32 v4, 0x428, v2
	ds_write2_b32 v4, v10, v11 offset1:1
	v_add_u32_e32 v4, 0x840, v2
	v_mov_b32_e32 v5, v3
	ds_write2_b32 v4, v12, v13 offset1:1
	v_add_u32_e32 v4, 0x848, v2
	ds_write2_b32 v4, v14, v15 offset1:1
	v_add_u32_e32 v4, 0xc60, v2
	ds_write2_b32 v4, v16, v17 offset1:1
	v_add_u32_e32 v4, 0xc68, v2
	ds_write2_b32 v4, v18, v19 offset1:1
	v_add_u32_e32 v4, 0x1080, v2
	ds_write2_b32 v4, v20, v21 offset1:1
	v_add_u32_e32 v4, 0x1088, v2
	ds_write2_b32 v4, v22, v23 offset1:1
	v_add_u32_e32 v4, 0x14a0, v2
	ds_write2_b32 v4, v24, v25 offset1:1
	v_add_u32_e32 v4, 0x14a8, v2
	ds_write2_b32 v4, v26, v27 offset1:1
	v_add_u32_e32 v4, 0x18c0, v2
	ds_write2_b32 v4, v28, v29 offset1:1
	v_add_u32_e32 v4, 0x18c8, v2
	ds_write2_b32 v4, v30, v31 offset1:1
	v_add_u32_e32 v4, 0x1ce0, v2
	v_add_u32_e32 v2, 0x1ce8, v2
	ds_write2_b32 v4, v32, v33 offset1:1
	ds_write2_b32 v2, v34, v35 offset1:1
	s_waitcnt lgkmcnt(0)
	ds_read2_b32 v[10:11], v48 offset0:33 offset1:41
	ds_read2_b32 v[12:13], v48 offset1:8
	ds_read2_b32 v[14:15], v48 offset0:66 offset1:74
	ds_read2_b32 v[16:17], v48 offset0:99 offset1:107
	ds_read2_b32 v[18:19], v48 offset0:132 offset1:140
	ds_read2_b32 v[20:21], v48 offset0:165 offset1:173
	ds_read2_b32 v[22:23], v48 offset0:198 offset1:206
	ds_read2_b32 v[24:25], v48 offset0:231 offset1:239
	v_lshlrev_b32_e32 v4, 1, v38
	v_or_b32_e32 v2, s4, v37
	v_lshl_add_u64 v[8:9], s[2:3], 0, v[4:5]
	v_lshlrev_b32_e32 v26, 9, v2
	v_mov_b32_e32 v27, v3
	s_waitcnt lgkmcnt(0)
	v_cvt_pk_bf16_f32 v4, v12, v10
	v_lshl_add_u64 v[26:27], v[8:9], 0, v[26:27]
	v_or_b32_e32 v2, s4, v45
	v_cvt_pk_bf16_f32 v5, v14, v16
	v_cvt_pk_bf16_f32 v6, v18, v20
	v_cvt_pk_bf16_f32 v7, v22, v24
	global_store_dwordx4 v[26:27], v[4:7], off sc1
	v_lshlrev_b32_e32 v10, 9, v2
	v_or_b32_e32 v2, s4, v46
	v_cvt_pk_bf16_f32 v4, v13, v11
	v_mov_b32_e32 v11, v3
	v_lshl_add_u64 v[10:11], v[8:9], 0, v[10:11]
	v_cvt_pk_bf16_f32 v5, v15, v17
	v_cvt_pk_bf16_f32 v6, v19, v21
	v_cvt_pk_bf16_f32 v7, v23, v25
	global_store_dwordx4 v[10:11], v[4:7], off sc1
	ds_read2_b32 v[10:11], v48 offset0:16 offset1:24
	ds_read2_b32 v[12:13], v48 offset0:49 offset1:57
	ds_read2_b32 v[14:15], v48 offset0:82 offset1:90
	ds_read2_b32 v[16:17], v48 offset0:115 offset1:123
	ds_read2_b32 v[18:19], v48 offset0:148 offset1:156
	ds_read2_b32 v[20:21], v48 offset0:181 offset1:189
	ds_read2_b32 v[22:23], v48 offset0:214 offset1:222
	ds_read2_b32 v[24:25], v48 offset0:247 offset1:255
	v_lshlrev_b32_e32 v26, 9, v2
	v_mov_b32_e32 v27, v3
	s_waitcnt lgkmcnt(6)
	v_cvt_pk_bf16_f32 v4, v10, v12
	v_lshl_add_u64 v[26:27], v[8:9], 0, v[26:27]
	v_or_b32_e32 v2, s4, v47
	s_waitcnt lgkmcnt(4)
	v_cvt_pk_bf16_f32 v5, v14, v16
	s_waitcnt lgkmcnt(2)
	v_cvt_pk_bf16_f32 v6, v18, v20
	s_waitcnt lgkmcnt(0)
	v_cvt_pk_bf16_f32 v7, v22, v24
	global_store_dwordx4 v[26:27], v[4:7], off sc1
	v_lshlrev_b32_e32 v10, 9, v2
	s_mov_b64 s[2:3], 0
	v_cvt_pk_bf16_f32 v4, v11, v13
	v_mov_b32_e32 v11, v3
	v_lshl_add_u64 v[8:9], v[8:9], 0, v[10:11]
	v_cvt_pk_bf16_f32 v5, v15, v17
	v_cvt_pk_bf16_f32 v6, v19, v21
	v_cvt_pk_bf16_f32 v7, v23, v25
	global_store_dwordx4 v[8:9], v[4:7], off sc1
	s_waitcnt lgkmcnt(0)
; #define GAS __attribute__((address_space(1)))
; #define LAS __attribute__((address_space(3)))
; #define LDS_WAIT() asm volatile("s_waitcnt lgkmcnt(0)" ::: "memory")
; __device__ __forceinline__ unsigned pk2(float lo, float hi) { unsigned r; asm("v_cvt_pk_bf16_f32 %0, %1, %2" : "=v"(r) : "v"(lo), "v"(hi)); return r; }
; __device__ __forceinline__ void transpose_item(const float* W, int K, int N, bf16* WT, int drow0, int kb, int n0, LAS float* scr, int lane) {
;     const int k0 = 64 * kb; const int c4 = 4 * (lane & 7); const bool ok = (n0 + c4) < N;
;     f32x4 v[8];
; #pragma unroll
;     for (int i = 0; i < 8; ++i) { const int kk = 8 * i + (lane >> 3); v[i] = ok ? *(const f32x4*)(W + (size_t)(k0 + kk) * N + n0 + c4) : (f32x4){0.f, 0.f, 0.f, 0.f}; }
; #pragma unroll
;     for (int i = 0; i < 8; ++i) { const int kk = 8 * i + (lane >> 3); LAS float* d = scr + kk * 33 + c4; d[0] = v[i][0]; d[1] = v[i][1]; d[2] = v[i][2]; d[3] = v[i][3]; }
;     LDS_WAIT(); asm volatile("" ::: "memory");
;     const int c = lane & 7;
; #pragma unroll
;     for (int j = 0; j < 4; ++j) { const int n = (lane >> 3) + 8 * j; const LAS float* s = scr + (8 * c) * 33 + n;
;         v4u o; o.x = pk2(s[0 * 33], s[1 * 33]); o.y = pk2(s[2 * 33], s[3 * 33]); o.z = pk2(s[4 * 33], s[5 * 33]); o.w = pk2(s[6 * 33], s[7 * 33]);
;         *(GAS v4u*)(WT + (size_t)(drow0 + n) * K + k0 + 8 * c) = o; }
;     LDS_WAIT(); asm volatile("" ::: "memory");
; }
; __device__ __forceinline__ void convert_item(const In& I, unsigned char* ws, int it, LAS float* scr, int lane) {
;     ...
;     if (r < 4 * I_W1) { const int jk = r / I_W1; r -= jk * I_W1; const int kb = r / 8, nb = r % 8;
;         transpose_item(I.nsa_w1 + (size_t)jk * 2048 * 256, 2048, 256, W1t + (size_t)jk * 256 * 2048, 32 * nb, kb, 32 * nb, scr, lane); return; }
.LBB0_547:
	s_andn2_b64 vcc, exec, s[2:3]
	s_cbranch_vccnz .LBB0_549
	s_add_i32 s2, s30, 0x400
	s_lshr_b32 s68, s2, 8
	s_lshl_b64 s[2:3], s[68:69], 21
	v_readlane_b32 s40, v253, 16
	v_readlane_b32 s41, v253, 17
	s_add_u32 s4, s40, s2
	s_addc_u32 s5, s41, s3
	s_lshl_b64 s[2:3], s[68:69], 20
	s_add_u32 s6, s24, s2
	s_addc_u32 s3, s25, s3
	s_and_b32 s2, s33, 0xe0
	s_and_b32 s7, s31, 0x7c0
	s_lshl_b32 s8, s2, 2
	s_add_u32 s4, s4, s8
	v_or_b32_e32 v6, s7, v37
	s_addc_u32 s5, s5, 0
	v_lshlrev_b32_e32 v2, 2, v36
	v_lshl_add_u64 v[4:5], s[4:5], 0, v[2:3]
	v_lshlrev_b32_e32 v2, 10, v6
	v_lshl_add_u64 v[32:33], v[4:5], 0, v[2:3]
	v_add_co_u32_e32 v8, vcc, s74, v32
	global_load_dwordx4 v[4:7], v[32:33], off
	s_nop 0
	v_addc_co_u32_e32 v9, vcc, 0, v33, vcc
	s_movk_i32 s4, 0x4000
	global_load_dwordx4 v[8:11], v[8:9], off
	v_add_co_u32_e32 v12, vcc, s4, v32
	s_movk_i32 s4, 0x6000
	s_nop 0
	v_addc_co_u32_e32 v13, vcc, 0, v33, vcc
	global_load_dwordx4 v[12:15], v[12:13], off
	v_add_co_u32_e32 v16, vcc, s4, v32
	s_mov_b32 s4, 0xa000
	s_nop 0
	v_addc_co_u32_e32 v17, vcc, 0, v33, vcc
	global_load_dwordx4 v[16:19], v[16:17], off
	v_add_co_u32_e32 v20, vcc, s81, v32
	v_add_u32_e32 v2, v39, v44
	s_nop 0
	v_addc_co_u32_e32 v21, vcc, 0, v33, vcc
	global_load_dwordx4 v[20:23], v[20:21], off
	v_add_co_u32_e32 v24, vcc, s4, v32
	s_mov_b32 s4, 0xc000
	s_nop 0
	v_addc_co_u32_e32 v25, vcc, 0, v33, vcc
	global_load_dwordx4 v[24:27], v[24:25], off
	v_add_co_u32_e32 v28, vcc, s4, v32
	s_mov_b32 s4, 0xe000
	s_nop 0
	v_addc_co_u32_e32 v29, vcc, 0, v33, vcc
	global_load_dwordx4 v[28:31], v[28:29], off
	v_add_co_u32_e32 v32, vcc, s4, v32
	s_lshl_b32 s4, s7, 1
	s_nop 0
	v_addc_co_u32_e32 v33, vcc, 0, v33, vcc
	global_load_dwordx4 v[32:35], v[32:33], off
	s_add_u32 s4, s6, s4
	s_addc_u32 s5, s3, 0
	v_readlane_b32 s42, v253, 18
	v_readlane_b32 s43, v253, 19
	v_readlane_b32 s44, v253, 20
	v_readlane_b32 s45, v253, 21
	v_readlane_b32 s46, v253, 22
	v_readlane_b32 s47, v253, 23
	v_readlane_b32 s48, v253, 24
	v_readlane_b32 s49, v253, 25
	v_readlane_b32 s50, v253, 26
	v_readlane_b32 s51, v253, 27
	v_readlane_b32 s52, v253, 28
	v_readlane_b32 s53, v253, 29
	v_readlane_b32 s54, v253, 30
	v_readlane_b32 s55, v253, 31
	s_waitcnt vmcnt(0)
	ds_write2_b32 v2, v4, v5 offset1:1
	ds_write2_b32 v2, v6, v7 offset0:2 offset1:3
	v_add_u32_e32 v4, 0x420, v2
	ds_write2_b32 v4, v8, v9 offset1:1
	v_add_u32_e32 v4, 0x428, v2
	ds_write2_b32 v4, v10, v11 offset1:1
	v_add_u32_e32 v4, 0x840, v2
	ds_write2_b32 v4, v12, v13 offset1:1
	v_add_u32_e32 v4, 0x848, v2
	ds_write2_b32 v4, v14, v15 offset1:1
	v_add_u32_e32 v4, 0xc60, v2
	ds_write2_b32 v4, v16, v17 offset1:1
	v_add_u32_e32 v4, 0xc68, v2
	ds_write2_b32 v4, v18, v19 offset1:1
	v_add_u32_e32 v4, 0x1080, v2
	ds_write2_b32 v4, v20, v21 offset1:1
	v_add_u32_e32 v4, 0x1088, v2
	ds_write2_b32 v4, v22, v23 offset1:1
	v_add_u32_e32 v4, 0x14a0, v2
	ds_write2_b32 v4, v24, v25 offset1:1
	v_add_u32_e32 v4, 0x14a8, v2
	ds_write2_b32 v4, v26, v27 offset1:1
	v_add_u32_e32 v4, 0x18c0, v2
	ds_write2_b32 v4, v28, v29 offset1:1
	v_add_u32_e32 v4, 0x18c8, v2
	ds_write2_b32 v4, v30, v31 offset1:1
	v_add_u32_e32 v4, 0x1ce0, v2
	v_add_u32_e32 v2, 0x1ce8, v2
	ds_write2_b32 v4, v32, v33 offset1:1
	ds_write2_b32 v2, v34, v35 offset1:1
	s_waitcnt lgkmcnt(0)
	ds_read2_b32 v[10:11], v48 offset0:33 offset1:41
	ds_read2_b32 v[12:13], v48 offset1:8
	ds_read2_b32 v[14:15], v48 offset0:66 offset1:74
	ds_read2_b32 v[16:17], v48 offset0:99 offset1:107
	ds_read2_b32 v[18:19], v48 offset0:132 offset1:140
	ds_read2_b32 v[20:21], v48 offset0:165 offset1:173
	ds_read2_b32 v[22:23], v48 offset0:198 offset1:206
	ds_read2_b32 v[24:25], v48 offset0:231 offset1:239
	v_lshlrev_b32_e32 v2, 1, v38
	v_lshl_add_u64 v[8:9], s[4:5], 0, v[2:3]
	v_or_b32_e32 v2, s2, v37
	v_lshlrev_b32_e32 v2, 12, v2
	s_waitcnt lgkmcnt(0)
	v_cvt_pk_bf16_f32 v4, v12, v10
	v_lshl_add_u64 v[26:27], v[8:9], 0, v[2:3]
	v_or_b32_e32 v2, s2, v45
	v_cvt_pk_bf16_f32 v5, v14, v16
	v_cvt_pk_bf16_f32 v6, v18, v20
	v_cvt_pk_bf16_f32 v7, v22, v24
	global_store_dwordx4 v[26:27], v[4:7], off sc1
	v_lshlrev_b32_e32 v10, 12, v2
	v_or_b32_e32 v2, s2, v46
	v_cvt_pk_bf16_f32 v4, v13, v11
	v_mov_b32_e32 v11, v3
	v_lshl_add_u64 v[10:11], v[8:9], 0, v[10:11]
	v_cvt_pk_bf16_f32 v5, v15, v17
	v_cvt_pk_bf16_f32 v6, v19, v21
	v_cvt_pk_bf16_f32 v7, v23, v25
	global_store_dwordx4 v[10:11], v[4:7], off sc1
	ds_read2_b32 v[10:11], v48 offset0:16 offset1:24
	ds_read2_b32 v[12:13], v48 offset0:49 offset1:57
	ds_read2_b32 v[14:15], v48 offset0:82 offset1:90
	ds_read2_b32 v[16:17], v48 offset0:115 offset1:123
	ds_read2_b32 v[18:19], v48 offset0:148 offset1:156
	ds_read2_b32 v[20:21], v48 offset0:181 offset1:189
	ds_read2_b32 v[22:23], v48 offset0:214 offset1:222
	ds_read2_b32 v[24:25], v48 offset0:247 offset1:255
	v_lshlrev_b32_e32 v26, 12, v2
	v_mov_b32_e32 v27, v3
	s_waitcnt lgkmcnt(6)
	v_cvt_pk_bf16_f32 v4, v10, v12
	v_lshl_add_u64 v[26:27], v[8:9], 0, v[26:27]
	v_or_b32_e32 v2, s2, v47
	s_waitcnt lgkmcnt(4)
	v_cvt_pk_bf16_f32 v5, v14, v16
	s_waitcnt lgkmcnt(2)
	v_cvt_pk_bf16_f32 v6, v18, v20
	s_waitcnt lgkmcnt(0)
	v_cvt_pk_bf16_f32 v7, v22, v24
	global_store_dwordx4 v[26:27], v[4:7], off sc1
	v_lshlrev_b32_e32 v10, 12, v2
	s_nop 0
	v_cvt_pk_bf16_f32 v4, v11, v13
	v_mov_b32_e32 v11, v3
	v_lshl_add_u64 v[8:9], v[8:9], 0, v[10:11]
	v_cvt_pk_bf16_f32 v5, v15, v17
	v_cvt_pk_bf16_f32 v6, v19, v21
	v_cvt_pk_bf16_f32 v7, v23, v25
	global_store_dwordx4 v[8:9], v[4:7], off sc1
	s_waitcnt lgkmcnt(0)

; #define GAS __attribute__((address_space(1)))
; #define LAS __attribute__((address_space(3)))
; #define LDS_WAIT() asm volatile("s_waitcnt lgkmcnt(0)" ::: "memory")
; __device__ __forceinline__ unsigned pk2(float lo, float hi) { unsigned r; asm("v_cvt_pk_bf16_f32 %0, %1, %2" : "=v"(r) : "v"(lo), "v"(hi)); return r; }
; __device__ __forceinline__ void transpose_item(const float* W, int K, int N, bf16* WT, int drow0, int kb, int n0, LAS float* scr, int lane) {
;     const int k0 = 64 * kb; const int c4 = 4 * (lane & 7); const bool ok = (n0 + c4) < N;
;     f32x4 v[8];
; #pragma unroll
;     for (int i = 0; i < 8; ++i) { const int kk = 8 * i + (lane >> 3); v[i] = ok ? *(const f32x4*)(W + (size_t)(k0 + kk) * N + n0 + c4) : (f32x4){0.f, 0.f, 0.f, 0.f}; }
; #pragma unroll
;     for (int i = 0; i < 8; ++i) { const int kk = 8 * i + (lane >> 3); LAS float* d = scr + kk * 33 + c4; d[0] = v[i][0]; d[1] = v[i][1]; d[2] = v[i][2]; d[3] = v[i][3]; }
;     LDS_WAIT(); asm volatile("" ::: "memory");
;     const int c = lane & 7;
; #pragma unroll
;     for (int j = 0; j < 4; ++j) { const int n = (lane >> 3) + 8 * j; const LAS float* s = scr + (8 * c) * 33 + n;
;         v4u o; o.x = pk2(s[0 * 33], s[1 * 33]); o.y = pk2(s[2 * 33], s[3 * 33]); o.z = pk2(s[4 * 33], s[5 * 33]); o.w = pk2(s[6 * 33], s[7 * 33]);
;         *(GAS v4u*)(WT + (size_t)(drow0 + n) * K + k0 + 8 * c) = o; }
;     LDS_WAIT(); asm volatile("" ::: "memory");
; }
; __device__ __forceinline__ void convert_item(const In& I, unsigned char* ws, int it, LAS float* scr, int lane) {
;     ...
;     if (r < 2 * I_SQ) { const int j = r / I_SQ; r -= j * I_SQ; const int kb = r / 32, nb = r % 32;
;         transpose_item(I.fox_w_out + (size_t)j * D * D, D, D, Wfout + (size_t)j * D * D, 32 * nb, kb, 32 * nb, scr, lane); return; }
.LBB0_550:
	s_andn2_b64 vcc, exec, s[2:3]
	s_cbranch_vccnz .LBB0_552
	s_add_i32 s2, s30, 0x800
	s_lshr_b32 s68, s2, 9
	v_readlane_b32 s40, v253, 16
	s_lshl_b64 s[2:3], s[68:69], 22
	v_readlane_b32 s52, v253, 28
	v_readlane_b32 s53, v253, 29
	s_add_u32 s4, s52, s2
	s_addc_u32 s5, s53, s3
	s_lshl_b64 s[2:3], s[68:69], 21
	s_add_u32 s6, s22, s2
	v_readlane_b32 s7, v253, 52
	s_addc_u32 s3, s23, s3
	s_add_i32 s7, s7, s15
	s_and_b32 s2, s33, 0x3e0
	s_addk_i32 s7, 0x1900
	s_and_b32 s7, s7, 0x3c0
	s_lshl_b32 s8, s2, 2
	s_add_u32 s4, s4, s8
	v_or_b32_e32 v6, s7, v37
	s_addc_u32 s5, s5, 0
	v_lshlrev_b32_e32 v2, 2, v36
	v_lshl_add_u64 v[4:5], s[4:5], 0, v[2:3]
	v_lshlrev_b32_e32 v2, 12, v6
	v_lshl_add_u64 v[32:33], v[4:5], 0, v[2:3]
	v_add_co_u32_e32 v8, vcc, s81, v32
	global_load_dwordx4 v[4:7], v[32:33], off
	s_nop 0
	v_addc_co_u32_e32 v9, vcc, 0, v33, vcc
	global_load_dwordx4 v[8:11], v[8:9], off
	v_add_co_u32_e32 v12, vcc, s79, v32
	v_add_u32_e32 v2, v39, v44
	s_nop 0
	v_addc_co_u32_e32 v13, vcc, 0, v33, vcc
	global_load_dwordx4 v[12:15], v[12:13], off
	v_add_co_u32_e32 v16, vcc, s80, v32
	s_lshl_b32 s4, s7, 1
	s_nop 0
	v_addc_co_u32_e32 v17, vcc, 0, v33, vcc
	global_load_dwordx4 v[16:19], v[16:17], off
	v_add_co_u32_e32 v20, vcc, s85, v32
	s_add_u32 s4, s6, s4
	s_nop 0
	v_addc_co_u32_e32 v21, vcc, 0, v33, vcc
	global_load_dwordx4 v[20:23], v[20:21], off
	v_add_co_u32_e32 v24, vcc, s86, v32
	s_addc_u32 s5, s3, 0
	s_nop 0
	v_addc_co_u32_e32 v25, vcc, 0, v33, vcc
	global_load_dwordx4 v[24:27], v[24:25], off
	v_add_co_u32_e32 v28, vcc, s87, v32
	v_readlane_b32 s41, v253, 17
	s_nop 0
	v_addc_co_u32_e32 v29, vcc, 0, v33, vcc
	global_load_dwordx4 v[28:31], v[28:29], off
	v_add_co_u32_e32 v32, vcc, s89, v32
	v_readlane_b32 s42, v253, 18
	s_nop 0
	v_addc_co_u32_e32 v33, vcc, 0, v33, vcc
	global_load_dwordx4 v[32:35], v[32:33], off
	v_readlane_b32 s43, v253, 19
	v_readlane_b32 s44, v253, 20
	v_readlane_b32 s45, v253, 21
	v_readlane_b32 s46, v253, 22
	v_readlane_b32 s47, v253, 23
	v_readlane_b32 s48, v253, 24
	v_readlane_b32 s49, v253, 25
	v_readlane_b32 s50, v253, 26
	v_readlane_b32 s51, v253, 27
	v_readlane_b32 s54, v253, 30
	v_readlane_b32 s55, v253, 31
	s_waitcnt vmcnt(0)
	ds_write2_b32 v2, v4, v5 offset1:1
	ds_write2_b32 v2, v6, v7 offset0:2 offset1:3
	v_add_u32_e32 v4, 0x420, v2
	ds_write2_b32 v4, v8, v9 offset1:1
	v_add_u32_e32 v4, 0x428, v2
	ds_write2_b32 v4, v10, v11 offset1:1
	v_add_u32_e32 v4, 0x840, v2
	ds_write2_b32 v4, v12, v13 offset1:1
	v_add_u32_e32 v4, 0x848, v2
	ds_write2_b32 v4, v14, v15 offset1:1
	v_add_u32_e32 v4, 0xc60, v2
	ds_write2_b32 v4, v16, v17 offset1:1
	v_add_u32_e32 v4, 0xc68, v2
	ds_write2_b32 v4, v18, v19 offset1:1
	v_add_u32_e32 v4, 0x1080, v2
	ds_write2_b32 v4, v20, v21 offset1:1
	v_add_u32_e32 v4, 0x1088, v2
	ds_write2_b32 v4, v22, v23 offset1:1
	v_add_u32_e32 v4, 0x14a0, v2
	ds_write2_b32 v4, v24, v25 offset1:1
	v_add_u32_e32 v4, 0x14a8, v2
	ds_write2_b32 v4, v26, v27 offset1:1
	v_add_u32_e32 v4, 0x18c0, v2
	ds_write2_b32 v4, v28, v29 offset1:1
	v_add_u32_e32 v4, 0x18c8, v2
	ds_write2_b32 v4, v30, v31 offset1:1
	v_add_u32_e32 v4, 0x1ce0, v2
	v_add_u32_e32 v2, 0x1ce8, v2
	ds_write2_b32 v4, v32, v33 offset1:1
	ds_write2_b32 v2, v34, v35 offset1:1
	s_waitcnt lgkmcnt(0)
	ds_read2_b32 v[10:11], v48 offset0:33 offset1:41
	ds_read2_b32 v[12:13], v48 offset1:8
	v_lshlrev_b32_e32 v2, 1, v38
	ds_read2_b32 v[14:15], v48 offset0:66 offset1:74
	ds_read2_b32 v[16:17], v48 offset0:99 offset1:107
	ds_read2_b32 v[18:19], v48 offset0:132 offset1:140
	ds_read2_b32 v[20:21], v48 offset0:165 offset1:173
	ds_read2_b32 v[22:23], v48 offset0:198 offset1:206
	ds_read2_b32 v[24:25], v48 offset0:231 offset1:239
	v_lshl_add_u64 v[8:9], s[4:5], 0, v[2:3]
	v_or_b32_e32 v2, s2, v37
	v_lshlrev_b32_e32 v2, 11, v2
	v_lshl_add_u64 v[26:27], v[8:9], 0, v[2:3]
	v_or_b32_e32 v2, s2, v45
	s_waitcnt lgkmcnt(0)
	v_cvt_pk_bf16_f32 v4, v12, v10
	v_lshlrev_b32_e32 v2, 11, v2
	v_cvt_pk_bf16_f32 v5, v14, v16
	v_cvt_pk_bf16_f32 v6, v18, v20
	v_cvt_pk_bf16_f32 v7, v22, v24
	global_store_dwordx4 v[26:27], v[4:7], off sc1
	s_nop 1
	v_cvt_pk_bf16_f32 v4, v13, v11
	v_lshl_add_u64 v[10:11], v[8:9], 0, v[2:3]
	v_cvt_pk_bf16_f32 v5, v15, v17
	v_cvt_pk_bf16_f32 v6, v19, v21
	v_cvt_pk_bf16_f32 v7, v23, v25
	global_store_dwordx4 v[10:11], v[4:7], off sc1
	ds_read2_b32 v[10:11], v48 offset0:16 offset1:24
	ds_read2_b32 v[12:13], v48 offset0:49 offset1:57
	ds_read2_b32 v[14:15], v48 offset0:82 offset1:90
	ds_read2_b32 v[16:17], v48 offset0:115 offset1:123
	ds_read2_b32 v[18:19], v48 offset0:148 offset1:156
	ds_read2_b32 v[20:21], v48 offset0:181 offset1:189
	ds_read2_b32 v[22:23], v48 offset0:214 offset1:222
	ds_read2_b32 v[24:25], v48 offset0:247 offset1:255
	v_or_b32_e32 v2, s2, v46
	v_lshlrev_b32_e32 v2, 11, v2
	v_lshl_add_u64 v[26:27], v[8:9], 0, v[2:3]
	v_or_b32_e32 v2, s2, v47
	v_lshlrev_b32_e32 v2, 11, v2
	s_waitcnt lgkmcnt(6)
	v_cvt_pk_bf16_f32 v4, v10, v12
	s_waitcnt lgkmcnt(4)
	v_cvt_pk_bf16_f32 v5, v14, v16
	s_waitcnt lgkmcnt(2)
	v_cvt_pk_bf16_f32 v6, v18, v20
	s_waitcnt lgkmcnt(0)
	v_cvt_pk_bf16_f32 v7, v22, v24
	v_lshl_add_u64 v[8:9], v[8:9], 0, v[2:3]
	global_store_dwordx4 v[26:27], v[4:7], off sc1
	s_nop 1
	v_cvt_pk_bf16_f32 v4, v11, v13
	v_cvt_pk_bf16_f32 v5, v15, v17
	v_cvt_pk_bf16_f32 v6, v19, v21
	v_cvt_pk_bf16_f32 v7, v23, v25
	global_store_dwordx4 v[8:9], v[4:7], off sc1
	s_waitcnt lgkmcnt(0)

; #define GAS __attribute__((address_space(1)))
; #define LAS __attribute__((address_space(3)))
; #define LDS_WAIT() asm volatile("s_waitcnt lgkmcnt(0)" ::: "memory")
; __device__ __forceinline__ unsigned pk2(float lo, float hi) { unsigned r; asm("v_cvt_pk_bf16_f32 %0, %1, %2" : "=v"(r) : "v"(lo), "v"(hi)); return r; }
; __device__ __forceinline__ void transpose_item(const float* W, int K, int N, bf16* WT, int drow0, int kb, int n0, LAS float* scr, int lane) {
;     ...
;     for (int i = 0; i < 8; ++i) { const int kk = 8 * i + (lane >> 3); v[i] = ok ? *(const f32x4*)(W + (size_t)(k0 + kk) * N + n0 + c4) : (f32x4){0.f, 0.f, 0.f, 0.f}; }
; #pragma unroll
;     for (int i = 0; i < 8; ++i) { const int kk = 8 * i + (lane >> 3); LAS float* d = scr + kk * 33 + c4; d[0] = v[i][0]; d[1] = v[i][1]; d[2] = v[i][2]; d[3] = v[i][3]; }
;     LDS_WAIT(); asm volatile("" ::: "memory");
;     const int c = lane & 7;
; #pragma unroll
;     for (int j = 0; j < 4; ++j) { const int n = (lane >> 3) + 8 * j; const LAS float* s = scr + (8 * c) * 33 + n;
;         v4u o; o.x = pk2(s[0 * 33], s[1 * 33]); o.y = pk2(s[2 * 33], s[3 * 33]); o.z = pk2(s[4 * 33], s[5 * 33]); o.w = pk2(s[6 * 33], s[7 * 33]);
;         *(GAS v4u*)(WT + (size_t)(drow0 + n) * K + k0 + 8 * c) = o; }
;     LDS_WAIT(); asm volatile("" ::: "memory");
; }
; __device__ __forceinline__ void convert_item(const In& I, unsigned char* ws, int it, LAS float* scr, int lane) {
;     ...
;     if (r < 2 * I_FIN) { const int j = r / I_FIN; r -= j * I_FIN; const int kb = r / 104, nb = r % 104;
;         transpose_item(I.fox_w_in + (size_t)j * D * FOX_IN, D, FOX_IN, Wfin + (size_t)j * FOX_IN_PAD * D, 32 * nb, kb, 32 * nb, scr, lane); return; }
.LBB0_570:
	s_or_b64 exec, exec, s[10:11]
	v_add_u32_e32 v2, v39, v44
	s_waitcnt vmcnt(0)
	ds_write2_b32 v2, v4, v5 offset1:1
	ds_write2_b32 v2, v6, v7 offset0:2 offset1:3
	v_add_u32_e32 v4, 0x420, v2
	ds_write2_b32 v4, v8, v9 offset1:1
	v_add_u32_e32 v4, 0x428, v2
	ds_write2_b32 v4, v10, v11 offset1:1
	v_add_u32_e32 v4, 0x840, v2
	ds_write2_b32 v4, v16, v17 offset1:1
	v_add_u32_e32 v4, 0x848, v2
	ds_write2_b32 v4, v18, v19 offset1:1
	v_add_u32_e32 v4, 0xc60, v2
	ds_write2_b32 v4, v12, v13 offset1:1
	v_add_u32_e32 v4, 0xc68, v2
	ds_write2_b32 v4, v14, v15 offset1:1
	v_add_u32_e32 v4, 0x1080, v2
	ds_write2_b32 v4, v24, v25 offset1:1
	v_add_u32_e32 v4, 0x1088, v2
	ds_write2_b32 v4, v26, v27 offset1:1
	v_add_u32_e32 v4, 0x14a0, v2
	ds_write2_b32 v4, v20, v21 offset1:1
	v_add_u32_e32 v4, 0x14a8, v2
	ds_write2_b32 v4, v22, v23 offset1:1
	v_add_u32_e32 v4, 0x18c0, v2
	ds_write2_b32 v4, v32, v33 offset1:1
	v_add_u32_e32 v4, 0x18c8, v2
	s_and_b64 s[2:3], s[8:9], exec
	ds_write2_b32 v4, v34, v35 offset1:1
	v_add_u32_e32 v4, 0x1ce0, v2
	v_add_u32_e32 v2, 0x1ce8, v2
	s_cselect_b32 s2, 0x680000, 0
	ds_write2_b32 v4, v28, v29 offset1:1
	ds_write2_b32 v2, v30, v31 offset1:1
	s_add_u32 s5, s20, s2
	s_waitcnt lgkmcnt(0)
	s_addc_u32 s8, s21, 0
	s_ashr_i32 s7, s6, 31
	s_lshl_b64 s[2:3], s[6:7], 1
	ds_read2_b32 v[8:9], v48 offset0:33 offset1:41
	ds_read2_b32 v[10:11], v48 offset1:8
	ds_read2_b32 v[12:13], v48 offset0:66 offset1:74
	ds_read2_b32 v[14:15], v48 offset0:99 offset1:107
	ds_read2_b32 v[16:17], v48 offset0:132 offset1:140
	ds_read2_b32 v[18:19], v48 offset0:165 offset1:173
	ds_read2_b32 v[20:21], v48 offset0:198 offset1:206
	ds_read2_b32 v[22:23], v48 offset0:231 offset1:239
	s_add_u32 s2, s5, s2
	v_or_b32_e32 v26, s4, v37
	s_addc_u32 s3, s8, s3
	v_lshlrev_b32_e32 v2, 1, v38
	v_ashrrev_i32_e32 v27, 31, v26
	v_lshl_add_u64 v[24:25], s[2:3], 0, v[2:3]
	v_lshlrev_b64 v[26:27], 11, v[26:27]
	s_waitcnt lgkmcnt(0)
	v_cvt_pk_bf16_f32 v4, v10, v8
	v_lshl_add_u64 v[26:27], v[24:25], 0, v[26:27]
	v_or_b32_e32 v8, s4, v45
	v_cvt_pk_bf16_f32 v5, v12, v14
	v_cvt_pk_bf16_f32 v6, v16, v18
	v_cvt_pk_bf16_f32 v7, v20, v22
	global_store_dwordx4 v[26:27], v[4:7], off sc1
	s_nop 1
	v_cvt_pk_bf16_f32 v4, v11, v9
	v_ashrrev_i32_e32 v9, 31, v8
	v_lshlrev_b64 v[8:9], 11, v[8:9]
	v_cvt_pk_bf16_f32 v5, v13, v15
	v_cvt_pk_bf16_f32 v6, v17, v19
	v_cvt_pk_bf16_f32 v7, v21, v23
	v_lshl_add_u64 v[8:9], v[24:25], 0, v[8:9]
	ds_read2_b32 v[10:11], v48 offset0:16 offset1:24
	ds_read2_b32 v[12:13], v48 offset0:49 offset1:57
	ds_read2_b32 v[14:15], v48 offset0:82 offset1:90
	ds_read2_b32 v[16:17], v48 offset0:115 offset1:123
	ds_read2_b32 v[18:19], v48 offset0:148 offset1:156
	ds_read2_b32 v[20:21], v48 offset0:181 offset1:189
	ds_read2_b32 v[22:23], v48 offset0:214 offset1:222
	ds_read2_b32 v[26:27], v48 offset0:247 offset1:255
	global_store_dwordx4 v[8:9], v[4:7], off sc1
	v_or_b32_e32 v8, s4, v46
	v_ashrrev_i32_e32 v9, 31, v8
	v_lshlrev_b64 v[8:9], 11, v[8:9]
	v_lshl_add_u64 v[8:9], v[24:25], 0, v[8:9]
	s_waitcnt lgkmcnt(6)
	v_cvt_pk_bf16_f32 v4, v10, v12
	s_waitcnt lgkmcnt(4)
	v_cvt_pk_bf16_f32 v5, v14, v16
	s_waitcnt lgkmcnt(2)
	v_cvt_pk_bf16_f32 v6, v18, v20
	s_waitcnt lgkmcnt(0)
	v_cvt_pk_bf16_f32 v7, v22, v26
	global_store_dwordx4 v[8:9], v[4:7], off sc1
	v_or_b32_e32 v8, s4, v47
	v_ashrrev_i32_e32 v9, 31, v8
	v_lshlrev_b64 v[8:9], 11, v[8:9]
	v_lshl_add_u64 v[8:9], v[24:25], 0, v[8:9]
	v_cvt_pk_bf16_f32 v4, v11, v13
	v_cvt_pk_bf16_f32 v5, v15, v17
	v_cvt_pk_bf16_f32 v6, v19, v21
	v_cvt_pk_bf16_f32 v7, v23, v27
	global_store_dwordx4 v[8:9], v[4:7], off sc1
	s_waitcnt lgkmcnt(0)

; #define GAS __attribute__((address_space(1)))
; #define LAS __attribute__((address_space(3)))
; #define LDS_WAIT() asm volatile("s_waitcnt lgkmcnt(0)" ::: "memory")
; __device__ __forceinline__ unsigned pk2(float lo, float hi) { unsigned r; asm("v_cvt_pk_bf16_f32 %0, %1, %2" : "=v"(r) : "v"(lo), "v"(hi)); return r; }
; __device__ __forceinline__ void transpose_item(const float* W, int K, int N, bf16* WT, int drow0, int kb, int n0, LAS float* scr, int lane) {
;     const int k0 = 64 * kb; const int c4 = 4 * (lane & 7); const bool ok = (n0 + c4) < N;
;     f32x4 v[8];
; #pragma unroll
;     for (int i = 0; i < 8; ++i) { const int kk = 8 * i + (lane >> 3); v[i] = ok ? *(const f32x4*)(W + (size_t)(k0 + kk) * N + n0 + c4) : (f32x4){0.f, 0.f, 0.f, 0.f}; }
; #pragma unroll
;     for (int i = 0; i < 8; ++i) { const int kk = 8 * i + (lane >> 3); LAS float* d = scr + kk * 33 + c4; d[0] = v[i][0]; d[1] = v[i][1]; d[2] = v[i][2]; d[3] = v[i][3]; }
;     LDS_WAIT(); asm volatile("" ::: "memory");
;     const int c = lane & 7;
; #pragma unroll
;     for (int j = 0; j < 4; ++j) { const int n = (lane >> 3) + 8 * j; const LAS float* s = scr + (8 * c) * 33 + n;
;         v4u o; o.x = pk2(s[0 * 33], s[1 * 33]); o.y = pk2(s[2 * 33], s[3 * 33]); o.z = pk2(s[4 * 33], s[5 * 33]); o.w = pk2(s[6 * 33], s[7 * 33]);
;         *(GAS v4u*)(WT + (size_t)(drow0 + n) * K + k0 + 8 * c) = o; }
;     LDS_WAIT(); asm volatile("" ::: "memory");
; }
; __device__ __forceinline__ void convert_item(const In& I, unsigned char* ws, int it, LAS float* scr, int lane) {
;     ...
;     if (r < 2 * I_SQ) { const int j = r / I_SQ; r -= j * I_SQ; const int kb = r / 32, nb = r % 32;
;         transpose_item(I.nsa_w_out + (size_t)j * D * D, D, D, Wnout + (size_t)j * D * D, 32 * nb, kb, 32 * nb, scr, lane); return; }
.LBB0_572:
	s_andn2_b64 vcc, exec, s[2:3]
	s_cbranch_vccnz .LBB0_574
	s_add_i32 s2, s30, 0x1900
	s_lshr_b32 s68, s2, 9
	v_readlane_b32 s40, v253, 16
	s_lshl_b64 s[2:3], s[68:69], 22
	v_readlane_b32 s46, v253, 22
	v_readlane_b32 s47, v253, 23
	s_add_u32 s4, s46, s2
	s_addc_u32 s5, s47, s3
	s_lshl_b64 s[2:3], s[68:69], 21
	s_add_u32 s6, s18, s2
	v_readlane_b32 s7, v253, 52
	s_addc_u32 s3, s19, s3
	s_add_i32 s7, s7, s15
	s_and_b32 s2, s33, 0x3e0
	s_add_i32 s7, s7, 0xfffefb00
	s_and_b32 s7, s7, 0x3c0
	s_lshl_b32 s8, s2, 2
	s_add_u32 s4, s4, s8
	v_or_b32_e32 v6, s7, v37
	s_addc_u32 s5, s5, 0
	v_lshlrev_b32_e32 v2, 2, v36
	v_lshl_add_u64 v[4:5], s[4:5], 0, v[2:3]
	v_lshlrev_b32_e32 v2, 12, v6
	v_lshl_add_u64 v[32:33], v[4:5], 0, v[2:3]
	v_add_co_u32_e32 v8, vcc, s81, v32
	global_load_dwordx4 v[4:7], v[32:33], off
	s_nop 0
	v_addc_co_u32_e32 v9, vcc, 0, v33, vcc
	global_load_dwordx4 v[8:11], v[8:9], off
	v_add_co_u32_e32 v12, vcc, s79, v32
	v_add_u32_e32 v2, v39, v44
	s_nop 0
	v_addc_co_u32_e32 v13, vcc, 0, v33, vcc
	global_load_dwordx4 v[12:15], v[12:13], off
	v_add_co_u32_e32 v16, vcc, s80, v32
	s_lshl_b32 s4, s7, 1
	s_nop 0
	v_addc_co_u32_e32 v17, vcc, 0, v33, vcc
	global_load_dwordx4 v[16:19], v[16:17], off
	v_add_co_u32_e32 v20, vcc, s85, v32
	s_add_u32 s4, s6, s4
	s_nop 0
	v_addc_co_u32_e32 v21, vcc, 0, v33, vcc
	global_load_dwordx4 v[20:23], v[20:21], off
	v_add_co_u32_e32 v24, vcc, s86, v32
	s_addc_u32 s5, s3, 0
	s_nop 0
	v_addc_co_u32_e32 v25, vcc, 0, v33, vcc
	global_load_dwordx4 v[24:27], v[24:25], off
	v_add_co_u32_e32 v28, vcc, s87, v32
	v_readlane_b32 s41, v253, 17
	s_nop 0
	v_addc_co_u32_e32 v29, vcc, 0, v33, vcc
	global_load_dwordx4 v[28:31], v[28:29], off
	v_add_co_u32_e32 v32, vcc, s89, v32
	v_readlane_b32 s42, v253, 18
	s_nop 0
	v_addc_co_u32_e32 v33, vcc, 0, v33, vcc
	global_load_dwordx4 v[32:35], v[32:33], off
	v_readlane_b32 s43, v253, 19
	v_readlane_b32 s44, v253, 20
	v_readlane_b32 s45, v253, 21
	v_readlane_b32 s48, v253, 24
	v_readlane_b32 s49, v253, 25
	v_readlane_b32 s50, v253, 26
	v_readlane_b32 s51, v253, 27
	v_readlane_b32 s52, v253, 28
	v_readlane_b32 s53, v253, 29
	v_readlane_b32 s54, v253, 30
	v_readlane_b32 s55, v253, 31
	s_waitcnt vmcnt(0)
	ds_write2_b32 v2, v4, v5 offset1:1
	ds_write2_b32 v2, v6, v7 offset0:2 offset1:3
	v_add_u32_e32 v4, 0x420, v2
	ds_write2_b32 v4, v8, v9 offset1:1
	v_add_u32_e32 v4, 0x428, v2
	ds_write2_b32 v4, v10, v11 offset1:1
	v_add_u32_e32 v4, 0x840, v2
	ds_write2_b32 v4, v12, v13 offset1:1
	v_add_u32_e32 v4, 0x848, v2
	ds_write2_b32 v4, v14, v15 offset1:1
	v_add_u32_e32 v4, 0xc60, v2
	ds_write2_b32 v4, v16, v17 offset1:1
	v_add_u32_e32 v4, 0xc68, v2
	ds_write2_b32 v4, v18, v19 offset1:1
	v_add_u32_e32 v4, 0x1080, v2
	ds_write2_b32 v4, v20, v21 offset1:1
	v_add_u32_e32 v4, 0x1088, v2
	ds_write2_b32 v4, v22, v23 offset1:1
	v_add_u32_e32 v4, 0x14a0, v2
	ds_write2_b32 v4, v24, v25 offset1:1
	v_add_u32_e32 v4, 0x14a8, v2
	ds_write2_b32 v4, v26, v27 offset1:1
	v_add_u32_e32 v4, 0x18c0, v2
	ds_write2_b32 v4, v28, v29 offset1:1
	v_add_u32_e32 v4, 0x18c8, v2
	ds_write2_b32 v4, v30, v31 offset1:1
	v_add_u32_e32 v4, 0x1ce0, v2
	v_add_u32_e32 v2, 0x1ce8, v2
	ds_write2_b32 v4, v32, v33 offset1:1
	ds_write2_b32 v2, v34, v35 offset1:1
	s_waitcnt lgkmcnt(0)
	ds_read2_b32 v[10:11], v48 offset0:33 offset1:41
	ds_read2_b32 v[12:13], v48 offset1:8
	v_lshlrev_b32_e32 v2, 1, v38
	ds_read2_b32 v[14:15], v48 offset0:66 offset1:74
	ds_read2_b32 v[16:17], v48 offset0:99 offset1:107
	ds_read2_b32 v[18:19], v48 offset0:132 offset1:140
	ds_read2_b32 v[20:21], v48 offset0:165 offset1:173
	ds_read2_b32 v[22:23], v48 offset0:198 offset1:206
	ds_read2_b32 v[24:25], v48 offset0:231 offset1:239
	v_lshl_add_u64 v[8:9], s[4:5], 0, v[2:3]
	v_or_b32_e32 v2, s2, v37
	v_lshlrev_b32_e32 v2, 11, v2
	v_lshl_add_u64 v[26:27], v[8:9], 0, v[2:3]
	v_or_b32_e32 v2, s2, v45
	s_waitcnt lgkmcnt(0)
	v_cvt_pk_bf16_f32 v4, v12, v10
	v_lshlrev_b32_e32 v2, 11, v2
	v_cvt_pk_bf16_f32 v5, v14, v16
	v_cvt_pk_bf16_f32 v6, v18, v20
	v_cvt_pk_bf16_f32 v7, v22, v24
	global_store_dwordx4 v[26:27], v[4:7], off sc1
	s_nop 1
	v_cvt_pk_bf16_f32 v4, v13, v11
	v_lshl_add_u64 v[10:11], v[8:9], 0, v[2:3]
	v_cvt_pk_bf16_f32 v5, v15, v17
	v_cvt_pk_bf16_f32 v6, v19, v21
	v_cvt_pk_bf16_f32 v7, v23, v25
	global_store_dwordx4 v[10:11], v[4:7], off sc1
	ds_read2_b32 v[10:11], v48 offset0:16 offset1:24
	ds_read2_b32 v[12:13], v48 offset0:49 offset1:57
	ds_read2_b32 v[14:15], v48 offset0:82 offset1:90
	ds_read2_b32 v[16:17], v48 offset0:115 offset1:123
	ds_read2_b32 v[18:19], v48 offset0:148 offset1:156
	ds_read2_b32 v[20:21], v48 offset0:181 offset1:189
	ds_read2_b32 v[22:23], v48 offset0:214 offset1:222
	ds_read2_b32 v[24:25], v48 offset0:247 offset1:255
	v_or_b32_e32 v2, s2, v46
	v_lshlrev_b32_e32 v2, 11, v2
	v_lshl_add_u64 v[26:27], v[8:9], 0, v[2:3]
	v_or_b32_e32 v2, s2, v47
	v_lshlrev_b32_e32 v2, 11, v2
	s_waitcnt lgkmcnt(6)
	v_cvt_pk_bf16_f32 v4, v10, v12
	s_waitcnt lgkmcnt(4)
	v_cvt_pk_bf16_f32 v5, v14, v16
	s_waitcnt lgkmcnt(2)
	v_cvt_pk_bf16_f32 v6, v18, v20
	s_waitcnt lgkmcnt(0)
	v_cvt_pk_bf16_f32 v7, v22, v24
	v_lshl_add_u64 v[8:9], v[8:9], 0, v[2:3]
	global_store_dwordx4 v[26:27], v[4:7], off sc1
	s_nop 1
	v_cvt_pk_bf16_f32 v4, v11, v13
	v_cvt_pk_bf16_f32 v5, v15, v17
	v_cvt_pk_bf16_f32 v6, v19, v21
	v_cvt_pk_bf16_f32 v7, v23, v25
	global_store_dwordx4 v[8:9], v[4:7], off sc1
	s_waitcnt lgkmcnt(0)

; #define GAS __attribute__((address_space(1)))
; #define LAS __attribute__((address_space(3)))
; #define LDS_WAIT() asm volatile("s_waitcnt lgkmcnt(0)" ::: "memory")
; __device__ __forceinline__ unsigned pk2(float lo, float hi) { unsigned r; asm("v_cvt_pk_bf16_f32 %0, %1, %2" : "=v"(r) : "v"(lo), "v"(hi)); return r; }
; __device__ __forceinline__ void transpose_item(const float* W, int K, int N, bf16* WT, int drow0, int kb, int n0, LAS float* scr, int lane) {
;     ...
;     for (int i = 0; i < 8; ++i) { const int kk = 8 * i + (lane >> 3); v[i] = ok ? *(const f32x4*)(W + (size_t)(k0 + kk) * N + n0 + c4) : (f32x4){0.f, 0.f, 0.f, 0.f}; }
; #pragma unroll
;     for (int i = 0; i < 8; ++i) { const int kk = 8 * i + (lane >> 3); LAS float* d = scr + kk * 33 + c4; d[0] = v[i][0]; d[1] = v[i][1]; d[2] = v[i][2]; d[3] = v[i][3]; }
;     LDS_WAIT(); asm volatile("" ::: "memory");
;     const int c = lane & 7;
; #pragma unroll
;     for (int j = 0; j < 4; ++j) { const int n = (lane >> 3) + 8 * j; const LAS float* s = scr + (8 * c) * 33 + n;
;         v4u o; o.x = pk2(s[0 * 33], s[1 * 33]); o.y = pk2(s[2 * 33], s[3 * 33]); o.z = pk2(s[4 * 33], s[5 * 33]); o.w = pk2(s[6 * 33], s[7 * 33]);
;         *(GAS v4u*)(WT + (size_t)(drow0 + n) * K + k0 + 8 * c) = o; }
;     LDS_WAIT(); asm volatile("" ::: "memory");
; }
; __device__ __forceinline__ void convert_item(const In& I, unsigned char* ws, int it, LAS float* scr, int lane) {
;     ...
;     if (r < 2 * I_NIN) { const int j = r / I_NIN; r -= j * I_NIN; const int kb = r / 88, nb = r % 88;
;         transpose_item(I.nsa_w_in + (size_t)j * D * NSA_IN, D, NSA_IN, Wnin + (size_t)j * NSA_IN_PAD * D, 32 * nb, kb, 32 * nb, scr, lane); return; }
;     ...
;     if (r < 2 * I_FIN) { const int j = r / I_FIN; r -= j * I_FIN; const int kb = r / 104, nb = r % 104;
;         transpose_item(I.fox_w_in + (size_t)j * D * FOX_IN, D, FOX_IN, Wfin + (size_t)j * FOX_IN_PAD * D, 32 * nb, kb, 32 * nb, scr, lane); return; }
.LBB0_592:
	s_or_b64 exec, exec, s[10:11]
	v_add_u32_e32 v2, v39, v44
	s_waitcnt vmcnt(0)
	ds_write2_b32 v2, v8, v9 offset1:1
	ds_write2_b32 v2, v10, v11 offset0:2 offset1:3
	v_add_u32_e32 v8, 0x420, v2
	ds_write2_b32 v8, v4, v5 offset1:1
	v_add_u32_e32 v4, 0x428, v2
	ds_write2_b32 v4, v6, v7 offset1:1
	v_add_u32_e32 v4, 0x840, v2
	ds_write2_b32 v4, v16, v17 offset1:1
	v_add_u32_e32 v4, 0x848, v2
	ds_write2_b32 v4, v18, v19 offset1:1
	v_add_u32_e32 v4, 0xc60, v2
	ds_write2_b32 v4, v12, v13 offset1:1
	v_add_u32_e32 v4, 0xc68, v2
	ds_write2_b32 v4, v14, v15 offset1:1
	v_add_u32_e32 v4, 0x1080, v2
	ds_write2_b32 v4, v24, v25 offset1:1
	v_add_u32_e32 v4, 0x1088, v2
	ds_write2_b32 v4, v26, v27 offset1:1
	v_add_u32_e32 v4, 0x14a0, v2
	ds_write2_b32 v4, v20, v21 offset1:1
	v_add_u32_e32 v4, 0x14a8, v2
	ds_write2_b32 v4, v22, v23 offset1:1
	v_add_u32_e32 v4, 0x18c0, v2
	ds_write2_b32 v4, v32, v33 offset1:1
	v_add_u32_e32 v4, 0x18c8, v2
	s_and_b64 s[2:3], s[8:9], exec
	ds_write2_b32 v4, v34, v35 offset1:1
	v_add_u32_e32 v4, 0x1ce0, v2
	v_add_u32_e32 v2, 0x1ce8, v2
	s_cselect_b32 s2, 0x580000, 0
	ds_write2_b32 v4, v28, v29 offset1:1
	ds_write2_b32 v2, v30, v31 offset1:1
	s_add_u32 s5, s13, s2
	s_waitcnt lgkmcnt(0)
	s_addc_u32 s8, s17, 0
	s_ashr_i32 s7, s6, 31
	s_lshl_b64 s[2:3], s[6:7], 1
	ds_read2_b32 v[8:9], v48 offset0:33 offset1:41
	ds_read2_b32 v[10:11], v48 offset1:8
	ds_read2_b32 v[12:13], v48 offset0:66 offset1:74
	ds_read2_b32 v[14:15], v48 offset0:99 offset1:107
	ds_read2_b32 v[16:17], v48 offset0:132 offset1:140
	ds_read2_b32 v[18:19], v48 offset0:165 offset1:173
	ds_read2_b32 v[20:21], v48 offset0:198 offset1:206
	ds_read2_b32 v[22:23], v48 offset0:231 offset1:239
	s_add_u32 s2, s5, s2
	v_or_b32_e32 v26, s4, v37
	s_addc_u32 s3, s8, s3
	v_lshlrev_b32_e32 v2, 1, v38
	v_ashrrev_i32_e32 v27, 31, v26
	v_lshl_add_u64 v[24:25], s[2:3], 0, v[2:3]
	v_lshlrev_b64 v[26:27], 11, v[26:27]
	s_waitcnt lgkmcnt(0)
	v_cvt_pk_bf16_f32 v4, v10, v8
	v_lshl_add_u64 v[26:27], v[24:25], 0, v[26:27]
	v_or_b32_e32 v8, s4, v45
	v_cvt_pk_bf16_f32 v5, v12, v14
	v_cvt_pk_bf16_f32 v6, v16, v18
	v_cvt_pk_bf16_f32 v7, v20, v22
	global_store_dwordx4 v[26:27], v[4:7], off sc1
	s_nop 1
	v_cvt_pk_bf16_f32 v4, v11, v9
	v_ashrrev_i32_e32 v9, 31, v8
	v_lshlrev_b64 v[8:9], 11, v[8:9]
	v_cvt_pk_bf16_f32 v5, v13, v15
	v_cvt_pk_bf16_f32 v6, v17, v19
	v_cvt_pk_bf16_f32 v7, v21, v23
	v_lshl_add_u64 v[8:9], v[24:25], 0, v[8:9]
	ds_read2_b32 v[10:11], v48 offset0:16 offset1:24
	ds_read2_b32 v[12:13], v48 offset0:49 offset1:57
	ds_read2_b32 v[14:15], v48 offset0:82 offset1:90
	ds_read2_b32 v[16:17], v48 offset0:115 offset1:123
	ds_read2_b32 v[18:19], v48 offset0:148 offset1:156
	ds_read2_b32 v[20:21], v48 offset0:181 offset1:189
	ds_read2_b32 v[22:23], v48 offset0:214 offset1:222
	ds_read2_b32 v[26:27], v48 offset0:247 offset1:255
	global_store_dwordx4 v[8:9], v[4:7], off sc1
	v_or_b32_e32 v8, s4, v46
	v_ashrrev_i32_e32 v9, 31, v8
	v_lshlrev_b64 v[8:9], 11, v[8:9]
	v_lshl_add_u64 v[8:9], v[24:25], 0, v[8:9]
	s_waitcnt lgkmcnt(6)
	v_cvt_pk_bf16_f32 v4, v10, v12
	s_waitcnt lgkmcnt(4)
	v_cvt_pk_bf16_f32 v5, v14, v16
	s_waitcnt lgkmcnt(2)
	v_cvt_pk_bf16_f32 v6, v18, v20
	s_waitcnt lgkmcnt(0)
	v_cvt_pk_bf16_f32 v7, v22, v26
	global_store_dwordx4 v[8:9], v[4:7], off sc1
	v_or_b32_e32 v8, s4, v47
	v_ashrrev_i32_e32 v9, 31, v8
	v_lshlrev_b64 v[8:9], 11, v[8:9]
	v_lshl_add_u64 v[8:9], v[24:25], 0, v[8:9]
	v_cvt_pk_bf16_f32 v4, v11, v13
	v_cvt_pk_bf16_f32 v5, v15, v17
	v_cvt_pk_bf16_f32 v6, v19, v21
	v_cvt_pk_bf16_f32 v7, v23, v27
	global_store_dwordx4 v[8:9], v[4:7], off sc1
	s_waitcnt lgkmcnt(0)

; #define GAS __attribute__((address_space(1)))
; #define LAS __attribute__((address_space(3)))
; #define LDS_WAIT() asm volatile("s_waitcnt lgkmcnt(0)" ::: "memory")
; __device__ __forceinline__ unsigned pk2(float lo, float hi) { unsigned r; asm("v_cvt_pk_bf16_f32 %0, %1, %2" : "=v"(r) : "v"(lo), "v"(hi)); return r; }
; __device__ __forceinline__ void transpose_item(const float* W, int K, int N, bf16* WT, int drow0, int kb, int n0, LAS float* scr, int lane) {
;     const int k0 = 64 * kb; const int c4 = 4 * (lane & 7); const bool ok = (n0 + c4) < N;
;     f32x4 v[8];
; #pragma unroll
;     for (int i = 0; i < 8; ++i) { const int kk = 8 * i + (lane >> 3); v[i] = ok ? *(const f32x4*)(W + (size_t)(k0 + kk) * N + n0 + c4) : (f32x4){0.f, 0.f, 0.f, 0.f}; }
; #pragma unroll
;     for (int i = 0; i < 8; ++i) { const int kk = 8 * i + (lane >> 3); LAS float* d = scr + kk * 33 + c4; d[0] = v[i][0]; d[1] = v[i][1]; d[2] = v[i][2]; d[3] = v[i][3]; }
;     LDS_WAIT(); asm volatile("" ::: "memory");
;     const int c = lane & 7;
; #pragma unroll
;     for (int j = 0; j < 4; ++j) { const int n = (lane >> 3) + 8 * j; const LAS float* s = scr + (8 * c) * 33 + n;
;         v4u o; o.x = pk2(s[0 * 33], s[1 * 33]); o.y = pk2(s[2 * 33], s[3 * 33]); o.z = pk2(s[4 * 33], s[5 * 33]); o.w = pk2(s[6 * 33], s[7 * 33]);
;         *(GAS v4u*)(WT + (size_t)(drow0 + n) * K + k0 + 8 * c) = o; }
;     LDS_WAIT(); asm volatile("" ::: "memory");
; }
; __device__ __forceinline__ void convert_item(const In& I, unsigned char* ws, int it, LAS float* scr, int lane) {
;     ...
;     if (r < T0) { const int f = r / I_FFN; r -= f * I_FFN;
;         if (r < 2 * I_G) { const int up = r >= I_G; r -= up * I_G; const int kb = r / 88, nb = r % 88;
;             transpose_item((up ? I.w_up : I.w_gate) + (size_t)f * D * FF, D, FF, Wgu + (size_t)f * NGU * D, 256 * (nb >> 2) + 32 * (nb & 3) + 128 * up, kb, 32 * nb, scr, lane); }
;         else { r -= 2 * I_G; const int kb = r / 32, nb = r % 32; transpose_item(I.w_down + (size_t)f * FF * D, FF, D, Wd + (size_t)f * D * FF, 32 * nb, kb, 32 * nb, scr, lane); }
.LBB0_594:
	s_andn2_b64 vcc, exec, s[2:3]
	s_cbranch_vccnz .LBB0_539
	s_mul_hi_i32 s2, s34, 0x3e0f83e1
	s_lshr_b32 s3, s2, 31
	s_ashr_i32 s6, s2, 10
	s_add_i32 s6, s6, s3
	s_mul_i32 s2, s6, 0xffffef80
	s_add_i32 s7, s30, s2
	s_add_i32 s7, s7, 0xa800
	v_add_u32_e32 v8, v39, v44
	s_mov_b64 s[2:3], -1
	s_cmpk_gt_i32 s7, 0xaff
	s_mul_hi_i32 s4, s6, 0xb00000
	s_mul_i32 s5, s6, 0xb00000
	v_lshlrev_b32_e32 v2, 2, v36
	v_add_u32_e32 v9, 0x420, v8
	v_add_u32_e32 v10, 0x428, v8
	v_add_u32_e32 v11, 0x840, v8
	v_add_u32_e32 v12, 0x848, v8
	v_add_u32_e32 v13, 0xc60, v8
	v_add_u32_e32 v14, 0xc68, v8
	v_add_u32_e32 v15, 0x1080, v8
	v_add_u32_e32 v16, 0x1088, v8
	v_add_u32_e32 v17, 0x14a0, v8
	v_add_u32_e32 v18, 0x14a8, v8
	v_add_u32_e32 v19, 0x18c0, v8
	v_add_u32_e32 v20, 0x18c8, v8
	v_add_u32_e32 v21, 0x1ce0, v8
	v_add_u32_e32 v22, 0x1ce8, v8
	v_lshlrev_b32_e32 v4, 1, v38
	s_cbranch_scc0 .LBB0_597
	v_readlane_b32 s40, v253, 0
	v_readlane_b32 s48, v253, 8
	v_readlane_b32 s49, v253, 9
	s_add_u32 s3, s48, s5
	s_addc_u32 s9, s49, s4
	s_mul_i32 s8, s6, 0x580000
	s_mul_hi_i32 s2, s6, 0x580000
	s_add_u32 s10, s1, s8
	v_readlane_b32 s34, v253, 52
	s_addc_u32 s11, s12, s2
	s_mul_i32 s8, s6, 0xffffdf00
	s_add_i32 s34, s34, s15
	s_add_i32 s8, s34, s8
	s_addk_i32 s8, 0x1900
	s_and_b32 s2, s33, 0x3e0
	s_andn2_b32 s8, s8, 63
	s_add_i32 s68, s8, 0xffffea00
	s_lshl_b32 s8, s2, 2
	v_or_b32_e32 v6, s68, v37
	s_add_u32 s8, s3, s8
	s_addc_u32 s9, s9, 0
	v_ashrrev_i32_e32 v7, 31, v6
	v_lshl_add_u64 v[62:63], s[8:9], 0, v[2:3]
	v_lshlrev_b64 v[24:25], 12, v[6:7]
	v_or_b32_e32 v28, 8, v6
	v_lshl_add_u64 v[24:25], v[62:63], 0, v[24:25]
	v_ashrrev_i32_e32 v29, 31, v28
	global_load_dwordx4 v[24:27], v[24:25], off
	v_lshlrev_b64 v[28:29], 12, v[28:29]
	v_or_b32_e32 v32, 16, v6
	v_lshl_add_u64 v[28:29], v[62:63], 0, v[28:29]
	v_ashrrev_i32_e32 v33, 31, v32
	global_load_dwordx4 v[28:31], v[28:29], off
	v_lshlrev_b64 v[32:33], 12, v[32:33]
	v_or_b32_e32 v40, 24, v6
	v_lshl_add_u64 v[32:33], v[62:63], 0, v[32:33]
	v_ashrrev_i32_e32 v41, 31, v40
	global_load_dwordx4 v[32:35], v[32:33], off
	v_lshlrev_b64 v[40:41], 12, v[40:41]
	v_or_b32_e32 v50, 32, v6
	v_lshl_add_u64 v[40:41], v[62:63], 0, v[40:41]
	v_ashrrev_i32_e32 v51, 31, v50
	global_load_dwordx4 v[40:43], v[40:41], off
	v_lshlrev_b64 v[50:51], 12, v[50:51]
	v_or_b32_e32 v54, 40, v6
	v_lshl_add_u64 v[50:51], v[62:63], 0, v[50:51]
	v_ashrrev_i32_e32 v55, 31, v54
	global_load_dwordx4 v[50:53], v[50:51], off
	v_lshlrev_b64 v[54:55], 12, v[54:55]
	v_or_b32_e32 v58, 48, v6
	v_lshl_add_u64 v[54:55], v[62:63], 0, v[54:55]
	v_ashrrev_i32_e32 v59, 31, v58
	global_load_dwordx4 v[54:57], v[54:55], off
	v_lshlrev_b64 v[58:59], 12, v[58:59]
	v_or_b32_e32 v6, 56, v6
	v_lshl_add_u64 v[58:59], v[62:63], 0, v[58:59]
	v_ashrrev_i32_e32 v7, 31, v6
	global_load_dwordx4 v[58:61], v[58:59], off
	v_lshlrev_b64 v[6:7], 12, v[6:7]
	v_lshl_add_u64 v[6:7], v[62:63], 0, v[6:7]
	global_load_dwordx4 v[62:65], v[6:7], off
	s_lshl_b64 s[8:9], s[68:69], 1
	s_add_u32 s8, s10, s8
	s_addc_u32 s9, s11, s9
	v_mov_b32_e32 v5, v3
	v_lshl_add_u64 v[6:7], s[8:9], 0, v[4:5]
	v_or_b32_e32 v5, s2, v37
	v_readlane_b32 s41, v253, 1
	v_readlane_b32 s42, v253, 2
	v_readlane_b32 s43, v253, 3
	v_readlane_b32 s44, v253, 4
	v_readlane_b32 s45, v253, 5
	v_readlane_b32 s46, v253, 6
	v_readlane_b32 s47, v253, 7
	v_readlane_b32 s50, v253, 10
	v_readlane_b32 s51, v253, 11
	v_readlane_b32 s52, v253, 12
	v_readlane_b32 s53, v253, 13
	v_readlane_b32 s54, v253, 14
	v_readlane_b32 s55, v253, 15
	s_waitcnt vmcnt(0)
	ds_write2_b32 v8, v24, v25 offset1:1
	ds_write2_b32 v8, v26, v27 offset0:2 offset1:3
	ds_write2_b32 v9, v28, v29 offset1:1
	ds_write2_b32 v10, v30, v31 offset1:1
	ds_write2_b32 v11, v32, v33 offset1:1
	ds_write2_b32 v12, v34, v35 offset1:1
	ds_write2_b32 v13, v40, v41 offset1:1
	ds_write2_b32 v14, v42, v43 offset1:1
	ds_write2_b32 v15, v50, v51 offset1:1
	ds_write2_b32 v16, v52, v53 offset1:1
	ds_write2_b32 v17, v54, v55 offset1:1
	ds_write2_b32 v18, v56, v57 offset1:1
	ds_write2_b32 v19, v58, v59 offset1:1
	ds_write2_b32 v20, v60, v61 offset1:1
	ds_write2_b32 v21, v62, v63 offset1:1
	ds_write2_b32 v22, v64, v65 offset1:1
	s_waitcnt lgkmcnt(0)
	ds_read2_b32 v[28:29], v48 offset0:33 offset1:41
	ds_read2_b32 v[30:31], v48 offset1:8
	ds_read2_b32 v[32:33], v48 offset0:66 offset1:74
	ds_read2_b32 v[34:35], v48 offset0:99 offset1:107
	ds_read2_b32 v[40:41], v48 offset0:132 offset1:140
	ds_read2_b32 v[42:43], v48 offset0:165 offset1:173
	ds_read2_b32 v[50:51], v48 offset0:198 offset1:206
	ds_read2_b32 v[52:53], v48 offset0:231 offset1:239
	v_mul_u32_u24_e32 v54, 0x1600, v5
	v_mov_b32_e32 v55, v3
	s_waitcnt lgkmcnt(0)
	v_cvt_pk_bf16_f32 v24, v30, v28
	v_lshl_add_u64 v[54:55], v[6:7], 0, v[54:55]
	v_or_b32_e32 v5, s2, v45
	v_cvt_pk_bf16_f32 v25, v32, v34
	v_cvt_pk_bf16_f32 v26, v40, v42
	v_cvt_pk_bf16_f32 v27, v50, v52
	global_store_dwordx4 v[54:55], v[24:27], off sc1
	v_mul_u32_u24_e32 v28, 0x1600, v5
	v_or_b32_e32 v5, s2, v46
	v_cvt_pk_bf16_f32 v24, v31, v29
	v_mov_b32_e32 v29, v3
	v_lshl_add_u64 v[28:29], v[6:7], 0, v[28:29]
	v_cvt_pk_bf16_f32 v25, v33, v35
	v_cvt_pk_bf16_f32 v26, v41, v43
	v_cvt_pk_bf16_f32 v27, v51, v53
	global_store_dwordx4 v[28:29], v[24:27], off sc1
	ds_read2_b32 v[28:29], v48 offset0:16 offset1:24
	ds_read2_b32 v[30:31], v48 offset0:49 offset1:57
	ds_read2_b32 v[32:33], v48 offset0:82 offset1:90
	ds_read2_b32 v[34:35], v48 offset0:115 offset1:123
	ds_read2_b32 v[40:41], v48 offset0:148 offset1:156
	ds_read2_b32 v[42:43], v48 offset0:181 offset1:189
	ds_read2_b32 v[50:51], v48 offset0:214 offset1:222
	ds_read2_b32 v[52:53], v48 offset0:247 offset1:255
	v_mul_u32_u24_e32 v54, 0x1600, v5
	v_mov_b32_e32 v55, v3
	s_waitcnt lgkmcnt(6)
	v_cvt_pk_bf16_f32 v24, v28, v30
	v_lshl_add_u64 v[54:55], v[6:7], 0, v[54:55]
	v_or_b32_e32 v5, s2, v47
	s_waitcnt lgkmcnt(4)
	v_cvt_pk_bf16_f32 v25, v32, v34
	s_waitcnt lgkmcnt(2)
	v_cvt_pk_bf16_f32 v26, v40, v42
	s_waitcnt lgkmcnt(0)
	v_cvt_pk_bf16_f32 v27, v50, v52
	global_store_dwordx4 v[54:55], v[24:27], off sc1
	v_mul_u32_u24_e32 v28, 0x1600, v5
	s_mov_b64 s[2:3], 0
	v_cvt_pk_bf16_f32 v24, v29, v31
	v_mov_b32_e32 v29, v3
	v_lshl_add_u64 v[6:7], v[6:7], 0, v[28:29]
	v_cvt_pk_bf16_f32 v25, v33, v35
	v_cvt_pk_bf16_f32 v26, v41, v43
	v_cvt_pk_bf16_f32 v27, v51, v53
	global_store_dwordx4 v[6:7], v[24:27], off sc1
	s_waitcnt lgkmcnt(0)
; #define GAS __attribute__((address_space(1)))
; #define LAS __attribute__((address_space(3)))
; #define LDS_WAIT() asm volatile("s_waitcnt lgkmcnt(0)" ::: "memory")
; __device__ __forceinline__ unsigned pk2(float lo, float hi) { unsigned r; asm("v_cvt_pk_bf16_f32 %0, %1, %2" : "=v"(r) : "v"(lo), "v"(hi)); return r; }
; __device__ __forceinline__ void transpose_item(const float* W, int K, int N, bf16* WT, int drow0, int kb, int n0, LAS float* scr, int lane) {
;     const int k0 = 64 * kb; const int c4 = 4 * (lane & 7); const bool ok = (n0 + c4) < N;
;     f32x4 v[8];
; #pragma unroll
;     for (int i = 0; i < 8; ++i) { const int kk = 8 * i + (lane >> 3); v[i] = ok ? *(const f32x4*)(W + (size_t)(k0 + kk) * N + n0 + c4) : (f32x4){0.f, 0.f, 0.f, 0.f}; }
; #pragma unroll
;     for (int i = 0; i < 8; ++i) { const int kk = 8 * i + (lane >> 3); LAS float* d = scr + kk * 33 + c4; d[0] = v[i][0]; d[1] = v[i][1]; d[2] = v[i][2]; d[3] = v[i][3]; }
;     LDS_WAIT(); asm volatile("" ::: "memory");
;     const int c = lane & 7;
; #pragma unroll
;     for (int j = 0; j < 4; ++j) { const int n = (lane >> 3) + 8 * j; const LAS float* s = scr + (8 * c) * 33 + n;
;         v4u o; o.x = pk2(s[0 * 33], s[1 * 33]); o.y = pk2(s[2 * 33], s[3 * 33]); o.z = pk2(s[4 * 33], s[5 * 33]); o.w = pk2(s[6 * 33], s[7 * 33]);
;         *(GAS v4u*)(WT + (size_t)(drow0 + n) * K + k0 + 8 * c) = o; }
;     LDS_WAIT(); asm volatile("" ::: "memory");
; }
; __device__ __forceinline__ void convert_item(const In& I, unsigned char* ws, int it, LAS float* scr, int lane) {
;     ...
;         if (r < 2 * I_G) { const int up = r >= I_G; r -= up * I_G; const int kb = r / 88, nb = r % 88;
;             transpose_item((up ? I.w_up : I.w_gate) + (size_t)f * D * FF, D, FF, Wgu + (size_t)f * NGU * D, 256 * (nb >> 2) + 32 * (nb & 3) + 128 * up, kb, 32 * nb, scr, lane); }
.LBB0_597:
	s_andn2_b64 vcc, exec, s[2:3]
	s_cbranch_vccnz .LBB0_539
	s_cmpk_gt_i32 s7, 0x57f
	v_readlane_b32 s40, v253, 0
	s_cselect_b32 s2, 0xfffffa80, 0
	s_mulk_i32 s6, 0x1080
	v_readlane_b32 s44, v253, 4
	v_readlane_b32 s45, v253, 5
	v_readlane_b32 s46, v253, 6
	v_readlane_b32 s47, v253, 7
	s_cselect_b32 s3, 0x80, 0
	s_cselect_b32 s7, s46, s44
	s_cselect_b32 s8, s47, s45
	s_sub_i32 s2, s2, s6
	s_add_i32 s2, s30, s2
	s_add_i32 s2, s2, 0xa800
	s_mul_hi_i32 s6, s2, 0x2e8ba2e9
	s_lshr_b32 s9, s6, 31
	s_ashr_i32 s6, s6, 4
	s_add_i32 s6, s6, s9
	s_mul_i32 s9, s6, 0x58
	s_sub_i32 s2, s2, s9
	s_add_u32 s7, s7, s5
	s_addc_u32 s8, s8, s4
	s_add_u32 s9, s28, s5
	s_addc_u32 s10, s29, s4
	s_lshl_b32 s4, s2, 6
	s_and_b32 s5, s4, 0xffffff00
	s_lshl_b32 s4, s2, 5
	s_and_b32 s2, s4, 0x60
	s_or_b32 s2, s2, s3
	s_or_b32 s2, s2, s5
	s_ashr_i32 s5, s4, 31
	s_lshl_b32 s6, s6, 6
	s_lshl_b64 s[4:5], s[4:5], 2
	s_add_u32 s4, s7, s4
	s_addc_u32 s5, s8, s5
	v_or_b32_e32 v5, s6, v37
	v_lshl_add_u64 v[6:7], s[4:5], 0, v[2:3]
	s_movk_i32 s3, 0x2c00
	v_mad_i64_i32 v[24:25], s[4:5], v5, s3, v[6:7]
	global_load_dwordx4 v[24:27], v[24:25], off
	v_or_b32_e32 v2, 8, v5
	v_mad_i64_i32 v[28:29], s[4:5], v2, s3, v[6:7]
	global_load_dwordx4 v[28:31], v[28:29], off
	v_or_b32_e32 v2, 16, v5
	v_mad_i64_i32 v[32:33], s[4:5], v2, s3, v[6:7]
	global_load_dwordx4 v[32:35], v[32:33], off
	v_or_b32_e32 v2, 24, v5
	v_mad_i64_i32 v[40:41], s[4:5], v2, s3, v[6:7]
	global_load_dwordx4 v[40:43], v[40:41], off
	v_or_b32_e32 v2, 32, v5
	v_mad_i64_i32 v[50:51], s[4:5], v2, s3, v[6:7]
	global_load_dwordx4 v[50:53], v[50:51], off
	v_or_b32_e32 v2, 40, v5
	v_mad_i64_i32 v[54:55], s[4:5], v2, s3, v[6:7]
	global_load_dwordx4 v[54:57], v[54:55], off
	v_or_b32_e32 v2, 48, v5
	v_mad_i64_i32 v[58:59], s[4:5], v2, s3, v[6:7]
	global_load_dwordx4 v[58:61], v[58:59], off
	v_or_b32_e32 v2, 56, v5
	v_mad_i64_i32 v[6:7], s[4:5], v2, s3, v[6:7]
	global_load_dwordx4 v[62:65], v[6:7], off
	s_ashr_i32 s7, s6, 31
	s_lshl_b64 s[4:5], s[6:7], 1
	s_add_u32 s4, s9, s4
	s_addc_u32 s5, s10, s5
	v_mov_b32_e32 v5, v3
	v_lshl_add_u64 v[4:5], s[4:5], 0, v[4:5]
	v_readlane_b32 s41, v253, 1
	v_readlane_b32 s42, v253, 2
	v_readlane_b32 s43, v253, 3
	v_readlane_b32 s48, v253, 8
	v_readlane_b32 s49, v253, 9
	v_readlane_b32 s50, v253, 10
	v_readlane_b32 s51, v253, 11
	v_readlane_b32 s52, v253, 12
	v_readlane_b32 s53, v253, 13
	v_readlane_b32 s54, v253, 14
	v_readlane_b32 s55, v253, 15
	s_waitcnt vmcnt(0)
	ds_write2_b32 v8, v24, v25 offset1:1
	ds_write2_b32 v8, v26, v27 offset0:2 offset1:3
	ds_write2_b32 v9, v28, v29 offset1:1
	ds_write2_b32 v10, v30, v31 offset1:1
	ds_write2_b32 v11, v32, v33 offset1:1
	ds_write2_b32 v12, v34, v35 offset1:1
	ds_write2_b32 v13, v40, v41 offset1:1
	ds_write2_b32 v14, v42, v43 offset1:1
	ds_write2_b32 v15, v50, v51 offset1:1
	ds_write2_b32 v16, v52, v53 offset1:1
	ds_write2_b32 v17, v54, v55 offset1:1
	ds_write2_b32 v18, v56, v57 offset1:1
	ds_write2_b32 v19, v58, v59 offset1:1
	ds_write2_b32 v20, v60, v61 offset1:1
	ds_write2_b32 v21, v62, v63 offset1:1
	ds_write2_b32 v22, v64, v65 offset1:1
	s_waitcnt lgkmcnt(0)
	ds_read2_b32 v[10:11], v48 offset0:33 offset1:41
	ds_read2_b32 v[12:13], v48 offset1:8
	ds_read2_b32 v[14:15], v48 offset0:66 offset1:74
	ds_read2_b32 v[16:17], v48 offset0:99 offset1:107
	ds_read2_b32 v[18:19], v48 offset0:132 offset1:140
	ds_read2_b32 v[20:21], v48 offset0:165 offset1:173
	ds_read2_b32 v[22:23], v48 offset0:198 offset1:206
	ds_read2_b32 v[24:25], v48 offset0:231 offset1:239
	v_or_b32_e32 v26, s2, v37
	v_ashrrev_i32_e32 v27, 31, v26
	v_lshlrev_b64 v[26:27], 11, v[26:27]
	s_waitcnt lgkmcnt(0)
	v_cvt_pk_bf16_f32 v6, v12, v10
	v_lshl_add_u64 v[26:27], v[4:5], 0, v[26:27]
	v_or_b32_e32 v10, s2, v45
	v_cvt_pk_bf16_f32 v7, v14, v16
	v_cvt_pk_bf16_f32 v8, v18, v20
	v_cvt_pk_bf16_f32 v9, v22, v24
	global_store_dwordx4 v[26:27], v[6:9], off sc1
	v_or_b32_e32 v26, s2, v46
	v_ashrrev_i32_e32 v27, 31, v26
	v_cvt_pk_bf16_f32 v6, v13, v11
	v_ashrrev_i32_e32 v11, 31, v10
	v_lshlrev_b64 v[10:11], 11, v[10:11]
	v_lshl_add_u64 v[10:11], v[4:5], 0, v[10:11]
	v_cvt_pk_bf16_f32 v7, v15, v17
	v_cvt_pk_bf16_f32 v8, v19, v21
	v_cvt_pk_bf16_f32 v9, v23, v25
	global_store_dwordx4 v[10:11], v[6:9], off sc1
	ds_read2_b32 v[10:11], v48 offset0:16 offset1:24
	ds_read2_b32 v[12:13], v48 offset0:49 offset1:57
	ds_read2_b32 v[14:15], v48 offset0:82 offset1:90
	ds_read2_b32 v[16:17], v48 offset0:115 offset1:123
	ds_read2_b32 v[18:19], v48 offset0:148 offset1:156
	ds_read2_b32 v[20:21], v48 offset0:181 offset1:189
	ds_read2_b32 v[22:23], v48 offset0:214 offset1:222
	ds_read2_b32 v[24:25], v48 offset0:247 offset1:255
	v_lshlrev_b64 v[26:27], 11, v[26:27]
	s_waitcnt lgkmcnt(6)
	v_cvt_pk_bf16_f32 v6, v10, v12
	v_lshl_add_u64 v[26:27], v[4:5], 0, v[26:27]
	v_or_b32_e32 v10, s2, v47
	s_waitcnt lgkmcnt(4)
	v_cvt_pk_bf16_f32 v7, v14, v16
	s_waitcnt lgkmcnt(2)
	v_cvt_pk_bf16_f32 v8, v18, v20
	s_waitcnt lgkmcnt(0)
	v_cvt_pk_bf16_f32 v9, v22, v24
	global_store_dwordx4 v[26:27], v[6:9], off sc1
	s_nop 1
	v_cvt_pk_bf16_f32 v6, v11, v13
	v_ashrrev_i32_e32 v11, 31, v10
	v_lshlrev_b64 v[10:11], 11, v[10:11]
	v_lshl_add_u64 v[4:5], v[4:5], 0, v[10:11]
	v_cvt_pk_bf16_f32 v7, v15, v17
	v_cvt_pk_bf16_f32 v8, v19, v21
	v_cvt_pk_bf16_f32 v9, v23, v25
	global_store_dwordx4 v[4:5], v[6:9], off sc1
	s_waitcnt lgkmcnt(0)
	s_branch .LBB0_539
